# v31: v28 + DSA nibble->LUT address 2 VALU, GEMM: loop-invariant adds hoisted, first K iteration peeled with C=0 (no accumulator zeroing)
# speedup vs baseline: 1.0071x; 1.0044x over previous
; #define PG8_STAGE(bufoff, gbase, voff) do { _Pragma("unroll") for (int _i = 0; _i < 2; ++_i) \
;         __builtin_amdgcn_global_load_lds((const unsigned*)((const char*)(gbase) + (voff)[_i]), (PG8_LAS unsigned*)(lds + (bufoff) + ldsw + _i * 8192), 16, 0, 0); } while (0)
; #define PG8_LDA(dst, b, h) do { _Pragma("unroll") for (int m = 0; m < 4; ++m) _Pragma("unroll") for (int k = 0; k < 2; ++k) dst[m][k] = *(const PG8_LAS bf16x8*)(lds + PG8_SA(b, h) + aoff + m * 2048 + k * 1024); } while (0)
; #define PG8_WAIT_V(n) asm volatile("s_waitcnt vmcnt(" #n ")" ::: "memory")
; #define PG8_WAIT_L(n) asm volatile("s_waitcnt lgkmcnt(" #n ")" ::: "memory")
; #define PG8_BAR __builtin_amdgcn_s_barrier()
; template <class Epi, class Sched, bool ALIGN_EPI = false, bool SP2 = false>
; __device__ __forceinline__ void gemm_phase(PG8_LAS unsigned char* lds, const Gemm g, const Sched& S, const Epi& E, const int wid) {
;     ...
;     f32x4 acc[2][2][4][2];
; #pragma unroll
;     for (int a = 0; a < 2; ++a)
; #pragma unroll
;         for (int b = 0; b < 2; ++b)
; #pragma unroll
;             for (int m = 0; m < 4; ++m)
; #pragma unroll
;                 for (int n = 0; n < 2; ++n) acc[a][b][m][n] = (f32x4){0.f, 0.f, 0.f, 0.f};
;     ...
;         const bool has_next = S.next(ui + 1, nxt);
;         const char* nA = has_next ? (const char*)g.A + (size_t)nxt.pm * tstepA : cA; const char* nB = has_next ? (const char*)g.Bt + (size_t)nxt.pn * tstepB : cB;
;         for (int t = 0; t < nt; t += 2) {
;             const bool last = (t == nt - 2);
;             const char* a1 = cA + (size_t)(t + 1) * kstep;
;             const char* a2 = last ? nA : cA + (size_t)(t + 2) * kstep; const char* b2 = last ? nB : cB + (size_t)(t + 2) * kstep;
;             const char* a3 = a2 + kstep; const char* b3 = b2 + kstep;
;             if (last && has_next) S.a_ready(nxt);
;             if constexpr (SP2) {
;             PG8_LDB(B0, 0, 0); PG8_LDB(B1, 0, 1); PG8_SCHED; PG8_LDA(At, 0, 0); PG8_STAGE(PG8_SA(1, 1), a1 + hstepA, voffA);
;             PG8_WAIT_V(8); PG8_WAIT_L(0); PG8_BAR; PG8_MMA(0, 0, At, B0); PG8_MMA(0, 1, At, B1); PG8_BAR; PG8_SCHED;
;             PG8_LDA(At, 0, 1); PG8_STAGE(PG8_SB(0, 0), b2, voffB); PG8_STAGE(PG8_SB(0, 1), b2 + hstepB, voffB); PG8_STAGE(PG8_SA(0, 0), a2, voffA);
;             PG8_WAIT_V(8); PG8_WAIT_L(0); PG8_BAR; PG8_MMA(1, 0, At, B0); PG8_MMA(1, 1, At, B1); PG8_BAR; PG8_SCHED;
.LBB0_348:
	s_ashr_i32 s27, s26, 31
	s_lshl_b64 s[28:29], s[26:27], 19
	s_add_u32 s28, s0, s28
	s_addc_u32 s29, s1, s29
	s_and_b64 s[30:31], s[4:5], exec
	s_cselect_b32 s7, s29, s9
	s_cselect_b32 s27, s28, s8
	s_ashr_i32 s25, s24, 31
	s_lshl_b64 s[30:31], s[24:25], 19
	s_add_u32 s30, s33, s30
	s_addc_u32 s31, s44, s31
	s_and_b64 s[40:41], s[4:5], exec
	s_cselect_b32 s25, s31, s37
	s_cselect_b32 s35, s30, s36
	s_add_u32 s8, s8, 0x40080
	s_addc_u32 s9, s9, 0
	s_add_u32 s73, s36, 0x100
	s_addc_u32 s74, s37, 0
	s_mov_b32 s75, -2
	s_waitcnt lgkmcnt(0)
	v_add_u32_e32 v252, 0x18000, v178
	v_add_u32_e32 v253, 0x1c000, v178
	ds_read_b128 v[128:131], v183
	ds_read_b128 v[150:153], v183 offset:1024
	ds_read_b128 v[154:157], v183 offset:2048
	ds_read_b128 v[158:161], v183 offset:3072
	ds_read_b128 v[162:165], v184
	ds_read_b128 v[166:169], v184 offset:1024
	ds_read_b128 v[170:173], v184 offset:2048
	ds_read_b128 v[188:191], v184 offset:3072
	s_add_u32 s36, s8, 0xfffc0080
	s_addc_u32 s37, s9, -1
	s_cmp_eq_u32 s75, 12
	s_cselect_b32 s41, s7, s37
	s_cselect_b32 s40, s27, s36
	s_cselect_b32 s37, s25, s74
	s_cselect_b32 s36, s35, s73
	s_add_i32 m0, s46, 0xc000
	ds_read_b128 v[192:195], v185
	ds_read_b128 v[196:199], v185 offset:1024
	ds_read_b128 v[200:203], v185 offset:2048
	ds_read_b128 v[204:207], v185 offset:3072
	ds_read_b128 v[208:211], v185 offset:4096
	ds_read_b128 v[212:215], v185 offset:5120
	ds_read_b128 v[216:219], v185 offset:6144
	ds_read_b128 v[220:223], v185 offset:7168
	global_load_lds_dwordx4 v142, s[8:9]
	s_add_i32 m0, s46, 0xe000
	s_nop 0
	global_load_lds_dwordx4 v144, s[8:9]
	s_waitcnt vmcnt(8) lgkmcnt(0)
	s_barrier
	s_setprio 1
	v_mfma_f32_16x16x32_bf16 v[124:127], v[128:131], v[192:195], 0
	v_mfma_f32_16x16x32_bf16 v[120:123], v[154:157], v[192:195], 0
	v_mfma_f32_16x16x32_bf16 v[108:111], v[128:131], v[200:203], 0
	v_mfma_f32_16x16x32_bf16 v[104:107], v[154:157], v[200:203], 0
	v_mfma_f32_16x16x32_bf16 v[92:95], v[128:131], v[208:211], 0
	v_mfma_f32_16x16x32_bf16 v[88:91], v[154:157], v[208:211], 0
	v_mfma_f32_16x16x32_bf16 v[76:79], v[128:131], v[216:219], 0
	v_mfma_f32_16x16x32_bf16 v[72:75], v[154:157], v[216:219], 0
	v_mfma_f32_16x16x32_bf16 v[124:127], v[150:153], v[196:199], v[124:127]
	v_mfma_f32_16x16x32_bf16 v[120:123], v[158:161], v[196:199], v[120:123]
	v_mfma_f32_16x16x32_bf16 v[108:111], v[150:153], v[204:207], v[108:111]
	v_mfma_f32_16x16x32_bf16 v[104:107], v[158:161], v[204:207], v[104:107]
	v_mfma_f32_16x16x32_bf16 v[92:95], v[150:153], v[212:215], v[92:95]
	v_mfma_f32_16x16x32_bf16 v[88:91], v[158:161], v[212:215], v[88:91]
	v_mfma_f32_16x16x32_bf16 v[76:79], v[150:153], v[220:223], v[76:79]
	v_mfma_f32_16x16x32_bf16 v[72:75], v[158:161], v[220:223], v[72:75]
	s_setprio 0
	s_setprio 1
	v_mfma_f32_16x16x32_bf16 v[116:119], v[162:165], v[192:195], 0
	v_mfma_f32_16x16x32_bf16 v[112:115], v[170:173], v[192:195], 0
	v_mfma_f32_16x16x32_bf16 v[100:103], v[162:165], v[200:203], 0
	v_mfma_f32_16x16x32_bf16 v[96:99], v[170:173], v[200:203], 0
	v_mfma_f32_16x16x32_bf16 v[84:87], v[162:165], v[208:211], 0
	v_mfma_f32_16x16x32_bf16 v[80:83], v[170:173], v[208:211], 0
	v_mfma_f32_16x16x32_bf16 v[68:71], v[162:165], v[216:219], 0
	v_mfma_f32_16x16x32_bf16 v[64:67], v[170:173], v[216:219], 0
	v_mfma_f32_16x16x32_bf16 v[116:119], v[166:169], v[196:199], v[116:119]
	v_mfma_f32_16x16x32_bf16 v[112:115], v[188:191], v[196:199], v[112:115]
	v_mfma_f32_16x16x32_bf16 v[100:103], v[166:169], v[204:207], v[100:103]
	v_mfma_f32_16x16x32_bf16 v[96:99], v[188:191], v[204:207], v[96:99]
	v_mfma_f32_16x16x32_bf16 v[84:87], v[166:169], v[212:215], v[84:87]
	v_mfma_f32_16x16x32_bf16 v[80:83], v[188:191], v[212:215], v[80:83]
	v_mfma_f32_16x16x32_bf16 v[68:71], v[166:169], v[220:223], v[68:71]
	v_mfma_f32_16x16x32_bf16 v[64:67], v[188:191], v[220:223], v[64:67]
	s_setprio 0
	s_barrier
	s_add_i32 s76, s69, s45
	s_add_u32 s98, s36, 0x80
	s_addc_u32 s99, s37, 0
	s_mov_b32 m0, s76
	ds_read_b128 v[192:195], v185 offset:16384
	ds_read_b128 v[196:199], v185 offset:17408
	ds_read_b128 v[200:203], v185 offset:18432
	ds_read_b128 v[204:207], v185 offset:19456
	ds_read_b128 v[208:211], v185 offset:20480
	ds_read_b128 v[212:215], v185 offset:21504
	ds_read_b128 v[216:219], v185 offset:22528
	ds_read_b128 v[220:223], v185 offset:23552
	global_load_lds_dwordx4 v134, s[36:37]
	s_add_i32 m0, s76, 0x2000
	s_add_u32 s76, s36, 0x40000
	s_addc_u32 s77, s37, 0
	s_add_i32 s78, s70, s45
	global_load_lds_dwordx4 v138, s[36:37]
	s_mov_b32 m0, s78
	s_add_u32 s100, s40, 0x80
	s_addc_u32 s101, s41, 0
	global_load_lds_dwordx4 v134, s[76:77]
	s_add_i32 m0, s78, 0x2000
	s_nop 0
	global_load_lds_dwordx4 v138, s[76:77]
	s_mov_b32 m0, s46
	s_nop 0
	global_load_lds_dwordx4 v132, s[40:41]
	s_mov_b32 m0, s47
	s_nop 0
	global_load_lds_dwordx4 v136, s[40:41]
	s_waitcnt vmcnt(8) lgkmcnt(0)
	s_barrier
; #define PG8_STAGE(bufoff, gbase, voff) do { _Pragma("unroll") for (int _i = 0; _i < 2; ++_i) \
;         __builtin_amdgcn_global_load_lds((const unsigned*)((const char*)(gbase) + (voff)[_i]), (PG8_LAS unsigned*)(lds + (bufoff) + ldsw + _i * 8192), 16, 0, 0); } while (0)
; #define PG8_LDA(dst, b, h) do { _Pragma("unroll") for (int m = 0; m < 4; ++m) _Pragma("unroll") for (int k = 0; k < 2; ++k) dst[m][k] = *(const PG8_LAS bf16x8*)(lds + PG8_SA(b, h) + aoff + m * 2048 + k * 1024); } while (0)
; #define PG8_LDB(dst, b, h) do { _Pragma("unroll") for (int n = 0; n < 2; ++n) _Pragma("unroll") for (int k = 0; k < 2; ++k) dst[n][k] = *(const PG8_LAS bf16x8*)(lds + PG8_SB(b, h) + boff + n * 2048 + k * 1024); } while (0)
; #define PG8_MMA(ai, bj, At, Bt) do { __builtin_amdgcn_s_setprio(1); _Pragma("unroll") for (int m = 0; m < 4; ++m) _Pragma("unroll") for (int n = 0; n < 2; ++n) _Pragma("unroll") for (int k = 0; k < 2; ++k) \
;         acc[ai][bj][m][n] = __builtin_amdgcn_mfma_f32_16x16x32_bf16(Bt[n][k], At[m][k], acc[ai][bj][m][n], 0, 0, 0); __builtin_amdgcn_s_setprio(0); } while (0)
; #define PG8_WAIT_V(n) asm volatile("s_waitcnt vmcnt(" #n ")" ::: "memory")
; #define PG8_WAIT_L(n) asm volatile("s_waitcnt lgkmcnt(" #n ")" ::: "memory")
; #define PG8_BAR __builtin_amdgcn_s_barrier()
; #define PG8_SCHED __builtin_amdgcn_sched_barrier(0)
; template <class Epi, class Sched, bool ALIGN_EPI = false, bool SP2 = false>
; __device__ __forceinline__ void gemm_phase(PG8_LAS unsigned char* lds, const Gemm g, const Sched& S, const Epi& E, const int wid) {
;     ...
;             PG8_WAIT_V(8); PG8_WAIT_L(0); PG8_BAR; PG8_MMA(0, 0, At, B0); PG8_MMA(0, 1, At, B1); PG8_BAR; PG8_SCHED;
;             PG8_LDA(At, 0, 1); PG8_STAGE(PG8_SB(0, 0), b2, voffB); PG8_STAGE(PG8_SB(0, 1), b2 + hstepB, voffB); PG8_STAGE(PG8_SA(0, 0), a2, voffA);
;             PG8_WAIT_V(8); PG8_WAIT_L(0); PG8_BAR; PG8_MMA(1, 0, At, B0); PG8_MMA(1, 1, At, B1); PG8_BAR; PG8_SCHED;
;             PG8_LDB(B0, 1, 0); PG8_LDB(B1, 1, 1); PG8_SCHED; PG8_LDA(At, 1, 0); PG8_STAGE(PG8_SA(0, 1), a2 + hstepA, voffA);
;             PG8_WAIT_V(8); PG8_WAIT_L(0); PG8_BAR; PG8_MMA(0, 0, At, B0); PG8_MMA(0, 1, At, B1); PG8_BAR; PG8_SCHED;
	s_setprio 1
	v_mfma_f32_16x16x32_bf16 v[60:63], v[128:131], v[192:195], 0
	v_mfma_f32_16x16x32_bf16 v[56:59], v[154:157], v[192:195], 0
	v_mfma_f32_16x16x32_bf16 v[44:47], v[128:131], v[200:203], 0
	v_mfma_f32_16x16x32_bf16 v[40:43], v[154:157], v[200:203], 0
	v_mfma_f32_16x16x32_bf16 v[28:31], v[128:131], v[208:211], 0
	v_mfma_f32_16x16x32_bf16 v[24:27], v[154:157], v[208:211], 0
	v_mfma_f32_16x16x32_bf16 v[12:15], v[128:131], v[216:219], 0
	v_mfma_f32_16x16x32_bf16 v[8:11], v[154:157], v[216:219], 0
	v_mfma_f32_16x16x32_bf16 v[60:63], v[150:153], v[196:199], v[60:63]
	v_mfma_f32_16x16x32_bf16 v[56:59], v[158:161], v[196:199], v[56:59]
	v_mfma_f32_16x16x32_bf16 v[44:47], v[150:153], v[204:207], v[44:47]
	v_mfma_f32_16x16x32_bf16 v[40:43], v[158:161], v[204:207], v[40:43]
	v_mfma_f32_16x16x32_bf16 v[28:31], v[150:153], v[212:215], v[28:31]
	v_mfma_f32_16x16x32_bf16 v[24:27], v[158:161], v[212:215], v[24:27]
	v_mfma_f32_16x16x32_bf16 v[12:15], v[150:153], v[220:223], v[12:15]
	v_mfma_f32_16x16x32_bf16 v[8:11], v[158:161], v[220:223], v[8:11]
	s_setprio 0
	s_setprio 1
	v_mfma_f32_16x16x32_bf16 v[52:55], v[162:165], v[192:195], 0
	v_mfma_f32_16x16x32_bf16 v[48:51], v[170:173], v[192:195], 0
	v_mfma_f32_16x16x32_bf16 v[36:39], v[162:165], v[200:203], 0
	v_mfma_f32_16x16x32_bf16 v[32:35], v[170:173], v[200:203], 0
	v_mfma_f32_16x16x32_bf16 v[20:23], v[162:165], v[208:211], 0
	v_mfma_f32_16x16x32_bf16 v[16:19], v[170:173], v[208:211], 0
	v_mfma_f32_16x16x32_bf16 v[4:7], v[162:165], v[216:219], 0
	v_mfma_f32_16x16x32_bf16 v[0:3], v[170:173], v[216:219], 0
	v_mfma_f32_16x16x32_bf16 v[52:55], v[166:169], v[196:199], v[52:55]
	v_mfma_f32_16x16x32_bf16 v[48:51], v[188:191], v[196:199], v[48:51]
	v_mfma_f32_16x16x32_bf16 v[36:39], v[166:169], v[204:207], v[36:39]
	v_mfma_f32_16x16x32_bf16 v[32:35], v[188:191], v[204:207], v[32:35]
	v_mfma_f32_16x16x32_bf16 v[20:23], v[166:169], v[212:215], v[20:23]
	v_mfma_f32_16x16x32_bf16 v[16:19], v[188:191], v[212:215], v[16:19]
	v_mfma_f32_16x16x32_bf16 v[4:7], v[166:169], v[220:223], v[4:7]
	v_mfma_f32_16x16x32_bf16 v[0:3], v[188:191], v[220:223], v[0:3]
	s_setprio 0
	s_barrier
	s_add_i32 s76, 0, 0x18000
	s_add_i32 s77, 0, 0x1c000
	ds_read_b128 v[128:131], v252
	ds_read_b128 v[150:153], v252 offset:1024
	ds_read_b128 v[154:157], v252 offset:2048
	ds_read_b128 v[158:161], v252 offset:3072
	ds_read_b128 v[162:165], v253
	ds_read_b128 v[166:169], v253 offset:1024
	ds_read_b128 v[170:173], v253 offset:2048
	ds_read_b128 v[188:191], v253 offset:3072
	s_add_u32 s40, s40, 0x40000
	s_addc_u32 s41, s41, 0
	s_mov_b32 m0, s48
	ds_read_b128 v[192:195], v185 offset:32768
	ds_read_b128 v[196:199], v185 offset:33792
	ds_read_b128 v[200:203], v185 offset:34816
	ds_read_b128 v[204:207], v185 offset:35840
	ds_read_b128 v[208:211], v185 offset:36864
	ds_read_b128 v[212:215], v185 offset:37888
	ds_read_b128 v[216:219], v185 offset:38912
	ds_read_b128 v[220:223], v185 offset:39936
	global_load_lds_dwordx4 v132, s[40:41]
	s_mov_b32 m0, s49
	s_nop 0
	global_load_lds_dwordx4 v136, s[40:41]
	s_waitcnt vmcnt(8) lgkmcnt(0)
	s_barrier
	s_setprio 1
	v_mfma_f32_16x16x32_bf16 v[124:127], v[128:131], v[192:195], v[124:127]
	v_mfma_f32_16x16x32_bf16 v[120:123], v[154:157], v[192:195], v[120:123]
	v_mfma_f32_16x16x32_bf16 v[108:111], v[128:131], v[200:203], v[108:111]
	v_mfma_f32_16x16x32_bf16 v[104:107], v[154:157], v[200:203], v[104:107]
	v_mfma_f32_16x16x32_bf16 v[92:95], v[128:131], v[208:211], v[92:95]
	v_mfma_f32_16x16x32_bf16 v[88:91], v[154:157], v[208:211], v[88:91]
	v_mfma_f32_16x16x32_bf16 v[76:79], v[128:131], v[216:219], v[76:79]
	v_mfma_f32_16x16x32_bf16 v[72:75], v[154:157], v[216:219], v[72:75]
	v_mfma_f32_16x16x32_bf16 v[124:127], v[150:153], v[196:199], v[124:127]
	v_mfma_f32_16x16x32_bf16 v[120:123], v[158:161], v[196:199], v[120:123]
	v_mfma_f32_16x16x32_bf16 v[108:111], v[150:153], v[204:207], v[108:111]
	v_mfma_f32_16x16x32_bf16 v[104:107], v[158:161], v[204:207], v[104:107]
	v_mfma_f32_16x16x32_bf16 v[92:95], v[150:153], v[212:215], v[92:95]
	v_mfma_f32_16x16x32_bf16 v[88:91], v[158:161], v[212:215], v[88:91]
	v_mfma_f32_16x16x32_bf16 v[76:79], v[150:153], v[220:223], v[76:79]
	v_mfma_f32_16x16x32_bf16 v[72:75], v[158:161], v[220:223], v[72:75]
	s_setprio 0
	s_setprio 1
	v_mfma_f32_16x16x32_bf16 v[116:119], v[162:165], v[192:195], v[116:119]
	v_mfma_f32_16x16x32_bf16 v[112:115], v[170:173], v[192:195], v[112:115]
	v_mfma_f32_16x16x32_bf16 v[100:103], v[162:165], v[200:203], v[100:103]
	v_mfma_f32_16x16x32_bf16 v[96:99], v[170:173], v[200:203], v[96:99]
	v_mfma_f32_16x16x32_bf16 v[84:87], v[162:165], v[208:211], v[84:87]
	v_mfma_f32_16x16x32_bf16 v[80:83], v[170:173], v[208:211], v[80:83]
	v_mfma_f32_16x16x32_bf16 v[68:71], v[162:165], v[216:219], v[68:71]
	v_mfma_f32_16x16x32_bf16 v[64:67], v[170:173], v[216:219], v[64:67]
	v_mfma_f32_16x16x32_bf16 v[116:119], v[166:169], v[196:199], v[116:119]
	v_mfma_f32_16x16x32_bf16 v[112:115], v[188:191], v[196:199], v[112:115]
	v_mfma_f32_16x16x32_bf16 v[100:103], v[166:169], v[204:207], v[100:103]
	v_mfma_f32_16x16x32_bf16 v[96:99], v[188:191], v[204:207], v[96:99]
	v_mfma_f32_16x16x32_bf16 v[84:87], v[166:169], v[212:215], v[84:87]
	v_mfma_f32_16x16x32_bf16 v[80:83], v[188:191], v[212:215], v[80:83]
	v_mfma_f32_16x16x32_bf16 v[68:71], v[166:169], v[220:223], v[68:71]
	v_mfma_f32_16x16x32_bf16 v[64:67], v[188:191], v[220:223], v[64:67]
	s_setprio 0
	s_barrier
; #define PG8_STAGE(bufoff, gbase, voff) do { _Pragma("unroll") for (int _i = 0; _i < 2; ++_i) \
;         __builtin_amdgcn_global_load_lds((const unsigned*)((const char*)(gbase) + (voff)[_i]), (PG8_LAS unsigned*)(lds + (bufoff) + ldsw + _i * 8192), 16, 0, 0); } while (0)
; #define PG8_LDA(dst, b, h) do { _Pragma("unroll") for (int m = 0; m < 4; ++m) _Pragma("unroll") for (int k = 0; k < 2; ++k) dst[m][k] = *(const PG8_LAS bf16x8*)(lds + PG8_SA(b, h) + aoff + m * 2048 + k * 1024); } while (0)
; #define PG8_LDB(dst, b, h) do { _Pragma("unroll") for (int n = 0; n < 2; ++n) _Pragma("unroll") for (int k = 0; k < 2; ++k) dst[n][k] = *(const PG8_LAS bf16x8*)(lds + PG8_SB(b, h) + boff + n * 2048 + k * 1024); } while (0)
; #define PG8_MMA(ai, bj, At, Bt) do { __builtin_amdgcn_s_setprio(1); _Pragma("unroll") for (int m = 0; m < 4; ++m) _Pragma("unroll") for (int n = 0; n < 2; ++n) _Pragma("unroll") for (int k = 0; k < 2; ++k) \
;         acc[ai][bj][m][n] = __builtin_amdgcn_mfma_f32_16x16x32_bf16(Bt[n][k], At[m][k], acc[ai][bj][m][n], 0, 0, 0); __builtin_amdgcn_s_setprio(0); } while (0)
; #define PG8_WAIT_V(n) asm volatile("s_waitcnt vmcnt(" #n ")" ::: "memory")
; #define PG8_BAR __builtin_amdgcn_s_barrier()
; template <class Epi, class Sched, bool ALIGN_EPI = false, bool SP2 = false>
; __device__ __forceinline__ void gemm_phase(PG8_LAS unsigned char* lds, const Gemm g, const Sched& S, const Epi& E, const int wid) {
;     ...
;         for (int t = 0; t < nt; t += 2) {
;             const bool last = (t == nt - 2);
;             const char* a1 = cA + (size_t)(t + 1) * kstep;
;             const char* a2 = last ? nA : cA + (size_t)(t + 2) * kstep; const char* b2 = last ? nB : cB + (size_t)(t + 2) * kstep;
;             const char* a3 = a2 + kstep; const char* b3 = b2 + kstep;
;             if (last && has_next) S.a_ready(nxt);
;             if constexpr (SP2) {
;             PG8_LDB(B0, 0, 0); PG8_LDB(B1, 0, 1); PG8_SCHED; PG8_LDA(At, 0, 0); PG8_STAGE(PG8_SA(1, 1), a1 + hstepA, voffA);
;             PG8_WAIT_V(8); PG8_WAIT_L(0); PG8_BAR; PG8_MMA(0, 0, At, B0); PG8_MMA(0, 1, At, B1); PG8_BAR; PG8_SCHED;
;     ...
;             PG8_LDA(At, 1, 1); PG8_STAGE(PG8_SB(1, 0), b3, voffB); PG8_STAGE(PG8_SB(1, 1), b3 + hstepB, voffB); PG8_STAGE(PG8_SA(1, 0), a3, voffA);
;             PG8_WAIT_V(8); PG8_WAIT_L(0); PG8_BAR; PG8_MMA(1, 0, At, B0); PG8_MMA(1, 1, At, B1); PG8_BAR; PG8_SCHED;
	s_add_i32 s40, s76, s45
	s_mov_b32 m0, s40
	ds_read_b128 v[192:195], v185 offset:49152
	ds_read_b128 v[196:199], v185 offset:50176
	ds_read_b128 v[200:203], v185 offset:51200
	ds_read_b128 v[204:207], v185 offset:52224
	ds_read_b128 v[208:211], v185 offset:53248
	ds_read_b128 v[212:215], v185 offset:54272
	ds_read_b128 v[216:219], v185 offset:55296
	ds_read_b128 v[220:223], v185 offset:56320
	global_load_lds_dwordx4 v134, s[98:99]
	s_add_i32 m0, s40, 0x2000
	s_add_u32 s36, s36, 0x40080
	s_addc_u32 s37, s37, 0
	s_add_i32 s40, s77, s45
	global_load_lds_dwordx4 v138, s[98:99]
	s_mov_b32 m0, s40
	s_nop 0
	global_load_lds_dwordx4 v134, s[36:37]
	s_add_i32 m0, s40, 0x2000
	s_nop 0
	global_load_lds_dwordx4 v138, s[36:37]
	s_mov_b32 m0, s64
	s_nop 0
	global_load_lds_dwordx4 v132, s[100:101]
	s_mov_b32 m0, s65
	s_nop 0
	global_load_lds_dwordx4 v136, s[100:101]
	s_waitcnt vmcnt(8) lgkmcnt(0)
	s_barrier
	s_setprio 1
	v_mfma_f32_16x16x32_bf16 v[60:63], v[128:131], v[192:195], v[60:63]
	v_mfma_f32_16x16x32_bf16 v[56:59], v[154:157], v[192:195], v[56:59]
	v_mfma_f32_16x16x32_bf16 v[44:47], v[128:131], v[200:203], v[44:47]
	v_mfma_f32_16x16x32_bf16 v[40:43], v[154:157], v[200:203], v[40:43]
	v_mfma_f32_16x16x32_bf16 v[28:31], v[128:131], v[208:211], v[28:31]
	v_mfma_f32_16x16x32_bf16 v[24:27], v[154:157], v[208:211], v[24:27]
	v_mfma_f32_16x16x32_bf16 v[12:15], v[128:131], v[216:219], v[12:15]
	v_mfma_f32_16x16x32_bf16 v[8:11], v[154:157], v[216:219], v[8:11]
	v_mfma_f32_16x16x32_bf16 v[60:63], v[150:153], v[196:199], v[60:63]
	v_mfma_f32_16x16x32_bf16 v[56:59], v[158:161], v[196:199], v[56:59]
	v_mfma_f32_16x16x32_bf16 v[44:47], v[150:153], v[204:207], v[44:47]
	v_mfma_f32_16x16x32_bf16 v[40:43], v[158:161], v[204:207], v[40:43]
	v_mfma_f32_16x16x32_bf16 v[28:31], v[150:153], v[212:215], v[28:31]
	v_mfma_f32_16x16x32_bf16 v[24:27], v[158:161], v[212:215], v[24:27]
	v_mfma_f32_16x16x32_bf16 v[12:15], v[150:153], v[220:223], v[12:15]
	v_mfma_f32_16x16x32_bf16 v[8:11], v[158:161], v[220:223], v[8:11]
	s_setprio 0
	s_setprio 1
	v_mfma_f32_16x16x32_bf16 v[52:55], v[162:165], v[192:195], v[52:55]
	v_mfma_f32_16x16x32_bf16 v[48:51], v[170:173], v[192:195], v[48:51]
	v_mfma_f32_16x16x32_bf16 v[36:39], v[162:165], v[200:203], v[36:39]
	v_mfma_f32_16x16x32_bf16 v[32:35], v[170:173], v[200:203], v[32:35]
	v_mfma_f32_16x16x32_bf16 v[20:23], v[162:165], v[208:211], v[20:23]
	v_mfma_f32_16x16x32_bf16 v[16:19], v[170:173], v[208:211], v[16:19]
	v_mfma_f32_16x16x32_bf16 v[4:7], v[162:165], v[216:219], v[4:7]
	v_mfma_f32_16x16x32_bf16 v[0:3], v[170:173], v[216:219], v[0:3]
	v_mfma_f32_16x16x32_bf16 v[52:55], v[166:169], v[196:199], v[52:55]
	v_mfma_f32_16x16x32_bf16 v[48:51], v[188:191], v[196:199], v[48:51]
	v_mfma_f32_16x16x32_bf16 v[36:39], v[166:169], v[204:207], v[36:39]
	v_mfma_f32_16x16x32_bf16 v[32:35], v[188:191], v[204:207], v[32:35]
	v_mfma_f32_16x16x32_bf16 v[20:23], v[166:169], v[212:215], v[20:23]
	v_mfma_f32_16x16x32_bf16 v[16:19], v[188:191], v[212:215], v[16:19]
	v_mfma_f32_16x16x32_bf16 v[4:7], v[166:169], v[220:223], v[4:7]
	v_mfma_f32_16x16x32_bf16 v[0:3], v[188:191], v[220:223], v[0:3]
	s_setprio 0
	s_barrier
	s_add_i32 s75, s75, 2
	s_add_u32 s8, s8, 0x100
	s_addc_u32 s9, s9, 0
	s_add_u32 s73, s73, 0x100
	s_addc_u32 s74, s74, 0
	s_cmp_gt_u32 s75, 13
.LBB0_349:
	ds_read_b128 v[128:131], v183
	ds_read_b128 v[150:153], v183 offset:1024
	ds_read_b128 v[154:157], v183 offset:2048
	ds_read_b128 v[158:161], v183 offset:3072
	ds_read_b128 v[162:165], v184
	ds_read_b128 v[166:169], v184 offset:1024
	ds_read_b128 v[170:173], v184 offset:2048
	ds_read_b128 v[188:191], v184 offset:3072
	s_add_u32 s36, s8, 0xfffc0080
	s_addc_u32 s37, s9, -1
	s_cmp_eq_u32 s75, 12
	s_cselect_b32 s41, s7, s37
	s_cselect_b32 s40, s27, s36
	s_cselect_b32 s37, s25, s74
	s_cselect_b32 s36, s35, s73
	s_add_i32 m0, s46, 0xc000
	ds_read_b128 v[192:195], v185
	ds_read_b128 v[196:199], v185 offset:1024
	ds_read_b128 v[200:203], v185 offset:2048
	ds_read_b128 v[204:207], v185 offset:3072
	ds_read_b128 v[208:211], v185 offset:4096
	ds_read_b128 v[212:215], v185 offset:5120
	ds_read_b128 v[216:219], v185 offset:6144
	ds_read_b128 v[220:223], v185 offset:7168
	global_load_lds_dwordx4 v142, s[8:9]
	s_add_i32 m0, s46, 0xe000
	s_nop 0
	global_load_lds_dwordx4 v144, s[8:9]
	s_waitcnt vmcnt(8) lgkmcnt(0)
	s_barrier
	s_setprio 1
	v_mfma_f32_16x16x32_bf16 v[124:127], v[128:131], v[192:195], v[124:127]
	v_mfma_f32_16x16x32_bf16 v[120:123], v[154:157], v[192:195], v[120:123]
	v_mfma_f32_16x16x32_bf16 v[108:111], v[128:131], v[200:203], v[108:111]
	v_mfma_f32_16x16x32_bf16 v[104:107], v[154:157], v[200:203], v[104:107]
	v_mfma_f32_16x16x32_bf16 v[92:95], v[128:131], v[208:211], v[92:95]
	v_mfma_f32_16x16x32_bf16 v[88:91], v[154:157], v[208:211], v[88:91]
	v_mfma_f32_16x16x32_bf16 v[76:79], v[128:131], v[216:219], v[76:79]
	v_mfma_f32_16x16x32_bf16 v[72:75], v[154:157], v[216:219], v[72:75]
	v_mfma_f32_16x16x32_bf16 v[124:127], v[150:153], v[196:199], v[124:127]
	v_mfma_f32_16x16x32_bf16 v[120:123], v[158:161], v[196:199], v[120:123]
	v_mfma_f32_16x16x32_bf16 v[108:111], v[150:153], v[204:207], v[108:111]
	v_mfma_f32_16x16x32_bf16 v[104:107], v[158:161], v[204:207], v[104:107]
	v_mfma_f32_16x16x32_bf16 v[92:95], v[150:153], v[212:215], v[92:95]
	v_mfma_f32_16x16x32_bf16 v[88:91], v[158:161], v[212:215], v[88:91]
	v_mfma_f32_16x16x32_bf16 v[76:79], v[150:153], v[220:223], v[76:79]
	v_mfma_f32_16x16x32_bf16 v[72:75], v[158:161], v[220:223], v[72:75]
	s_setprio 0
	s_setprio 1
	v_mfma_f32_16x16x32_bf16 v[116:119], v[162:165], v[192:195], v[116:119]
	v_mfma_f32_16x16x32_bf16 v[112:115], v[170:173], v[192:195], v[112:115]
	v_mfma_f32_16x16x32_bf16 v[100:103], v[162:165], v[200:203], v[100:103]
	v_mfma_f32_16x16x32_bf16 v[96:99], v[170:173], v[200:203], v[96:99]
	v_mfma_f32_16x16x32_bf16 v[84:87], v[162:165], v[208:211], v[84:87]
	v_mfma_f32_16x16x32_bf16 v[80:83], v[170:173], v[208:211], v[80:83]
	v_mfma_f32_16x16x32_bf16 v[68:71], v[162:165], v[216:219], v[68:71]
	v_mfma_f32_16x16x32_bf16 v[64:67], v[170:173], v[216:219], v[64:67]
	v_mfma_f32_16x16x32_bf16 v[116:119], v[166:169], v[196:199], v[116:119]
	v_mfma_f32_16x16x32_bf16 v[112:115], v[188:191], v[196:199], v[112:115]
	v_mfma_f32_16x16x32_bf16 v[100:103], v[166:169], v[204:207], v[100:103]
	v_mfma_f32_16x16x32_bf16 v[96:99], v[188:191], v[204:207], v[96:99]
	v_mfma_f32_16x16x32_bf16 v[84:87], v[166:169], v[212:215], v[84:87]
	v_mfma_f32_16x16x32_bf16 v[80:83], v[188:191], v[212:215], v[80:83]
	v_mfma_f32_16x16x32_bf16 v[68:71], v[166:169], v[220:223], v[68:71]
	v_mfma_f32_16x16x32_bf16 v[64:67], v[188:191], v[220:223], v[64:67]
	s_setprio 0
	s_barrier
; #define PG8_STAGE(bufoff, gbase, voff) do { _Pragma("unroll") for (int _i = 0; _i < 2; ++_i) \
;         __builtin_amdgcn_global_load_lds((const unsigned*)((const char*)(gbase) + (voff)[_i]), (PG8_LAS unsigned*)(lds + (bufoff) + ldsw + _i * 8192), 16, 0, 0); } while (0)
; #define PG8_LDA(dst, b, h) do { _Pragma("unroll") for (int m = 0; m < 4; ++m) _Pragma("unroll") for (int k = 0; k < 2; ++k) dst[m][k] = *(const PG8_LAS bf16x8*)(lds + PG8_SA(b, h) + aoff + m * 2048 + k * 1024); } while (0)
; #define PG8_LDB(dst, b, h) do { _Pragma("unroll") for (int n = 0; n < 2; ++n) _Pragma("unroll") for (int k = 0; k < 2; ++k) dst[n][k] = *(const PG8_LAS bf16x8*)(lds + PG8_SB(b, h) + boff + n * 2048 + k * 1024); } while (0)
; #define PG8_MMA(ai, bj, At, Bt) do { __builtin_amdgcn_s_setprio(1); _Pragma("unroll") for (int m = 0; m < 4; ++m) _Pragma("unroll") for (int n = 0; n < 2; ++n) _Pragma("unroll") for (int k = 0; k < 2; ++k) \
;         acc[ai][bj][m][n] = __builtin_amdgcn_mfma_f32_16x16x32_bf16(Bt[n][k], At[m][k], acc[ai][bj][m][n], 0, 0, 0); __builtin_amdgcn_s_setprio(0); } while (0)
; #define PG8_WAIT_V(n) asm volatile("s_waitcnt vmcnt(" #n ")" ::: "memory")
; #define PG8_WAIT_L(n) asm volatile("s_waitcnt lgkmcnt(" #n ")" ::: "memory")
; #define PG8_BAR __builtin_amdgcn_s_barrier()
; #define PG8_SCHED __builtin_amdgcn_sched_barrier(0)
; template <class Epi, class Sched, bool ALIGN_EPI = false, bool SP2 = false>
; __device__ __forceinline__ void gemm_phase(PG8_LAS unsigned char* lds, const Gemm g, const Sched& S, const Epi& E, const int wid) {
;     ...
;             PG8_LDA(At, 0, 1); PG8_STAGE(PG8_SB(0, 0), b2, voffB); PG8_STAGE(PG8_SB(0, 1), b2 + hstepB, voffB); PG8_STAGE(PG8_SA(0, 0), a2, voffA);
;             PG8_WAIT_V(8); PG8_WAIT_L(0); PG8_BAR; PG8_MMA(1, 0, At, B0); PG8_MMA(1, 1, At, B1); PG8_BAR; PG8_SCHED;
;             PG8_LDB(B0, 1, 0); PG8_LDB(B1, 1, 1); PG8_SCHED; PG8_LDA(At, 1, 0); PG8_STAGE(PG8_SA(0, 1), a2 + hstepA, voffA);
;             PG8_WAIT_V(8); PG8_WAIT_L(0); PG8_BAR; PG8_MMA(0, 0, At, B0); PG8_MMA(0, 1, At, B1); PG8_BAR; PG8_SCHED;
	s_add_i32 s76, s69, s45
	s_add_u32 s98, s36, 0x80
	s_addc_u32 s99, s37, 0
	s_mov_b32 m0, s76
	ds_read_b128 v[192:195], v185 offset:16384
	ds_read_b128 v[196:199], v185 offset:17408
	ds_read_b128 v[200:203], v185 offset:18432
	ds_read_b128 v[204:207], v185 offset:19456
	ds_read_b128 v[208:211], v185 offset:20480
	ds_read_b128 v[212:215], v185 offset:21504
	ds_read_b128 v[216:219], v185 offset:22528
	ds_read_b128 v[220:223], v185 offset:23552
	global_load_lds_dwordx4 v134, s[36:37]
	s_add_i32 m0, s76, 0x2000
	s_add_u32 s76, s36, 0x40000
	s_addc_u32 s77, s37, 0
	s_add_i32 s78, s70, s45
	global_load_lds_dwordx4 v138, s[36:37]
	s_mov_b32 m0, s78
	s_add_u32 s100, s40, 0x80
	s_addc_u32 s101, s41, 0
	global_load_lds_dwordx4 v134, s[76:77]
	s_add_i32 m0, s78, 0x2000
	s_nop 0
	global_load_lds_dwordx4 v138, s[76:77]
	s_mov_b32 m0, s46
	s_nop 0
	global_load_lds_dwordx4 v132, s[40:41]
	s_mov_b32 m0, s47
	s_nop 0
	global_load_lds_dwordx4 v136, s[40:41]
	s_waitcnt vmcnt(8) lgkmcnt(0)
	s_barrier
	s_setprio 1
	v_mfma_f32_16x16x32_bf16 v[60:63], v[128:131], v[192:195], v[60:63]
	v_mfma_f32_16x16x32_bf16 v[56:59], v[154:157], v[192:195], v[56:59]
	v_mfma_f32_16x16x32_bf16 v[44:47], v[128:131], v[200:203], v[44:47]
	v_mfma_f32_16x16x32_bf16 v[40:43], v[154:157], v[200:203], v[40:43]
	v_mfma_f32_16x16x32_bf16 v[28:31], v[128:131], v[208:211], v[28:31]
	v_mfma_f32_16x16x32_bf16 v[24:27], v[154:157], v[208:211], v[24:27]
	v_mfma_f32_16x16x32_bf16 v[12:15], v[128:131], v[216:219], v[12:15]
	v_mfma_f32_16x16x32_bf16 v[8:11], v[154:157], v[216:219], v[8:11]
	v_mfma_f32_16x16x32_bf16 v[60:63], v[150:153], v[196:199], v[60:63]
	v_mfma_f32_16x16x32_bf16 v[56:59], v[158:161], v[196:199], v[56:59]
	v_mfma_f32_16x16x32_bf16 v[44:47], v[150:153], v[204:207], v[44:47]
	v_mfma_f32_16x16x32_bf16 v[40:43], v[158:161], v[204:207], v[40:43]
	v_mfma_f32_16x16x32_bf16 v[28:31], v[150:153], v[212:215], v[28:31]
	v_mfma_f32_16x16x32_bf16 v[24:27], v[158:161], v[212:215], v[24:27]
	v_mfma_f32_16x16x32_bf16 v[12:15], v[150:153], v[220:223], v[12:15]
	v_mfma_f32_16x16x32_bf16 v[8:11], v[158:161], v[220:223], v[8:11]
	s_setprio 0
	s_setprio 1
	v_mfma_f32_16x16x32_bf16 v[52:55], v[162:165], v[192:195], v[52:55]
	v_mfma_f32_16x16x32_bf16 v[48:51], v[170:173], v[192:195], v[48:51]
	v_mfma_f32_16x16x32_bf16 v[36:39], v[162:165], v[200:203], v[36:39]
	v_mfma_f32_16x16x32_bf16 v[32:35], v[170:173], v[200:203], v[32:35]
	v_mfma_f32_16x16x32_bf16 v[20:23], v[162:165], v[208:211], v[20:23]
	v_mfma_f32_16x16x32_bf16 v[16:19], v[170:173], v[208:211], v[16:19]
	v_mfma_f32_16x16x32_bf16 v[4:7], v[162:165], v[216:219], v[4:7]
	v_mfma_f32_16x16x32_bf16 v[0:3], v[170:173], v[216:219], v[0:3]
	v_mfma_f32_16x16x32_bf16 v[52:55], v[166:169], v[196:199], v[52:55]
	v_mfma_f32_16x16x32_bf16 v[48:51], v[188:191], v[196:199], v[48:51]
	v_mfma_f32_16x16x32_bf16 v[36:39], v[166:169], v[204:207], v[36:39]
	v_mfma_f32_16x16x32_bf16 v[32:35], v[188:191], v[204:207], v[32:35]
	v_mfma_f32_16x16x32_bf16 v[20:23], v[166:169], v[212:215], v[20:23]
	v_mfma_f32_16x16x32_bf16 v[16:19], v[188:191], v[212:215], v[16:19]
	v_mfma_f32_16x16x32_bf16 v[4:7], v[166:169], v[220:223], v[4:7]
	v_mfma_f32_16x16x32_bf16 v[0:3], v[188:191], v[220:223], v[0:3]
	s_setprio 0
	s_barrier
	s_add_i32 s76, 0, 0x18000
	s_add_i32 s77, 0, 0x1c000
	ds_read_b128 v[128:131], v252
	ds_read_b128 v[150:153], v252 offset:1024
	ds_read_b128 v[154:157], v252 offset:2048
	ds_read_b128 v[158:161], v252 offset:3072
	ds_read_b128 v[162:165], v253
	ds_read_b128 v[166:169], v253 offset:1024
	ds_read_b128 v[170:173], v253 offset:2048
	ds_read_b128 v[188:191], v253 offset:3072
	s_add_u32 s40, s40, 0x40000
	s_addc_u32 s41, s41, 0
	s_mov_b32 m0, s48
	ds_read_b128 v[192:195], v185 offset:32768
	ds_read_b128 v[196:199], v185 offset:33792
	ds_read_b128 v[200:203], v185 offset:34816
	ds_read_b128 v[204:207], v185 offset:35840
	ds_read_b128 v[208:211], v185 offset:36864
	ds_read_b128 v[212:215], v185 offset:37888
	ds_read_b128 v[216:219], v185 offset:38912
	ds_read_b128 v[220:223], v185 offset:39936
	global_load_lds_dwordx4 v132, s[40:41]
	s_mov_b32 m0, s49
	s_nop 0
	global_load_lds_dwordx4 v136, s[40:41]
	s_waitcnt vmcnt(8) lgkmcnt(0)
	s_barrier
; #define PG8_STAGE(bufoff, gbase, voff) do { _Pragma("unroll") for (int _i = 0; _i < 2; ++_i) \
;         __builtin_amdgcn_global_load_lds((const unsigned*)((const char*)(gbase) + (voff)[_i]), (PG8_LAS unsigned*)(lds + (bufoff) + ldsw + _i * 8192), 16, 0, 0); } while (0)
; #define PG8_LDA(dst, b, h) do { _Pragma("unroll") for (int m = 0; m < 4; ++m) _Pragma("unroll") for (int k = 0; k < 2; ++k) dst[m][k] = *(const PG8_LAS bf16x8*)(lds + PG8_SA(b, h) + aoff + m * 2048 + k * 1024); } while (0)
; #define PG8_MMA(ai, bj, At, Bt) do { __builtin_amdgcn_s_setprio(1); _Pragma("unroll") for (int m = 0; m < 4; ++m) _Pragma("unroll") for (int n = 0; n < 2; ++n) _Pragma("unroll") for (int k = 0; k < 2; ++k) \
;         acc[ai][bj][m][n] = __builtin_amdgcn_mfma_f32_16x16x32_bf16(Bt[n][k], At[m][k], acc[ai][bj][m][n], 0, 0, 0); __builtin_amdgcn_s_setprio(0); } while (0)
; #define PG8_WAIT_V(n) asm volatile("s_waitcnt vmcnt(" #n ")" ::: "memory")
; #define PG8_WAIT_L(n) asm volatile("s_waitcnt lgkmcnt(" #n ")" ::: "memory")
; #define PG8_BAR __builtin_amdgcn_s_barrier()
; #define PG8_SCHED __builtin_amdgcn_sched_barrier(0)
; template <class Epi, class Sched, bool ALIGN_EPI = false, bool SP2 = false>
; __device__ __forceinline__ void gemm_phase(PG8_LAS unsigned char* lds, const Gemm g, const Sched& S, const Epi& E, const int wid) {
;     ...
;             PG8_WAIT_V(8); PG8_WAIT_L(0); PG8_BAR; PG8_MMA(0, 0, At, B0); PG8_MMA(0, 1, At, B1); PG8_BAR; PG8_SCHED;
;             PG8_LDA(At, 1, 1); PG8_STAGE(PG8_SB(1, 0), b3, voffB); PG8_STAGE(PG8_SB(1, 1), b3 + hstepB, voffB); PG8_STAGE(PG8_SA(1, 0), a3, voffA);
;             PG8_WAIT_V(8); PG8_WAIT_L(0); PG8_BAR; PG8_MMA(1, 0, At, B0); PG8_MMA(1, 1, At, B1); PG8_BAR; PG8_SCHED;
;     ...
;         if constexpr (ALIGN_EPI) { if (wr == 0) PG8_BAR; }
	s_setprio 1
	v_mfma_f32_16x16x32_bf16 v[124:127], v[128:131], v[192:195], v[124:127]
	v_mfma_f32_16x16x32_bf16 v[120:123], v[154:157], v[192:195], v[120:123]
	v_mfma_f32_16x16x32_bf16 v[108:111], v[128:131], v[200:203], v[108:111]
	v_mfma_f32_16x16x32_bf16 v[104:107], v[154:157], v[200:203], v[104:107]
	v_mfma_f32_16x16x32_bf16 v[92:95], v[128:131], v[208:211], v[92:95]
	v_mfma_f32_16x16x32_bf16 v[88:91], v[154:157], v[208:211], v[88:91]
	v_mfma_f32_16x16x32_bf16 v[76:79], v[128:131], v[216:219], v[76:79]
	v_mfma_f32_16x16x32_bf16 v[72:75], v[154:157], v[216:219], v[72:75]
	v_mfma_f32_16x16x32_bf16 v[124:127], v[150:153], v[196:199], v[124:127]
	v_mfma_f32_16x16x32_bf16 v[120:123], v[158:161], v[196:199], v[120:123]
	v_mfma_f32_16x16x32_bf16 v[108:111], v[150:153], v[204:207], v[108:111]
	v_mfma_f32_16x16x32_bf16 v[104:107], v[158:161], v[204:207], v[104:107]
	v_mfma_f32_16x16x32_bf16 v[92:95], v[150:153], v[212:215], v[92:95]
	v_mfma_f32_16x16x32_bf16 v[88:91], v[158:161], v[212:215], v[88:91]
	v_mfma_f32_16x16x32_bf16 v[76:79], v[150:153], v[220:223], v[76:79]
	v_mfma_f32_16x16x32_bf16 v[72:75], v[158:161], v[220:223], v[72:75]
	s_setprio 0
	s_setprio 1
	v_mfma_f32_16x16x32_bf16 v[116:119], v[162:165], v[192:195], v[116:119]
	v_mfma_f32_16x16x32_bf16 v[112:115], v[170:173], v[192:195], v[112:115]
	v_mfma_f32_16x16x32_bf16 v[100:103], v[162:165], v[200:203], v[100:103]
	v_mfma_f32_16x16x32_bf16 v[96:99], v[170:173], v[200:203], v[96:99]
	v_mfma_f32_16x16x32_bf16 v[84:87], v[162:165], v[208:211], v[84:87]
	v_mfma_f32_16x16x32_bf16 v[80:83], v[170:173], v[208:211], v[80:83]
	v_mfma_f32_16x16x32_bf16 v[68:71], v[162:165], v[216:219], v[68:71]
	v_mfma_f32_16x16x32_bf16 v[64:67], v[170:173], v[216:219], v[64:67]
	v_mfma_f32_16x16x32_bf16 v[116:119], v[166:169], v[196:199], v[116:119]
	v_mfma_f32_16x16x32_bf16 v[112:115], v[188:191], v[196:199], v[112:115]
	v_mfma_f32_16x16x32_bf16 v[100:103], v[166:169], v[204:207], v[100:103]
	v_mfma_f32_16x16x32_bf16 v[96:99], v[188:191], v[204:207], v[96:99]
	v_mfma_f32_16x16x32_bf16 v[84:87], v[166:169], v[212:215], v[84:87]
	v_mfma_f32_16x16x32_bf16 v[80:83], v[188:191], v[212:215], v[80:83]
	v_mfma_f32_16x16x32_bf16 v[68:71], v[166:169], v[220:223], v[68:71]
	v_mfma_f32_16x16x32_bf16 v[64:67], v[188:191], v[220:223], v[64:67]
	s_setprio 0
	s_barrier
	s_add_i32 s40, s76, s45
	s_mov_b32 m0, s40
	ds_read_b128 v[192:195], v185 offset:49152
	ds_read_b128 v[196:199], v185 offset:50176
	ds_read_b128 v[200:203], v185 offset:51200
	ds_read_b128 v[204:207], v185 offset:52224
	ds_read_b128 v[208:211], v185 offset:53248
	ds_read_b128 v[212:215], v185 offset:54272
	ds_read_b128 v[216:219], v185 offset:55296
	ds_read_b128 v[220:223], v185 offset:56320
	global_load_lds_dwordx4 v134, s[98:99]
	s_add_i32 m0, s40, 0x2000
	s_add_u32 s36, s36, 0x40080
	s_addc_u32 s37, s37, 0
	s_add_i32 s40, s77, s45
	global_load_lds_dwordx4 v138, s[98:99]
	s_mov_b32 m0, s40
	s_nop 0
	global_load_lds_dwordx4 v134, s[36:37]
	s_add_i32 m0, s40, 0x2000
	s_nop 0
	global_load_lds_dwordx4 v138, s[36:37]
	s_mov_b32 m0, s64
	s_nop 0
	global_load_lds_dwordx4 v132, s[100:101]
	s_mov_b32 m0, s65
	s_nop 0
	global_load_lds_dwordx4 v136, s[100:101]
	s_waitcnt vmcnt(8) lgkmcnt(0)
	s_barrier
	s_setprio 1
	v_mfma_f32_16x16x32_bf16 v[60:63], v[128:131], v[192:195], v[60:63]
	v_mfma_f32_16x16x32_bf16 v[56:59], v[154:157], v[192:195], v[56:59]
	v_mfma_f32_16x16x32_bf16 v[44:47], v[128:131], v[200:203], v[44:47]
	v_mfma_f32_16x16x32_bf16 v[40:43], v[154:157], v[200:203], v[40:43]
	v_mfma_f32_16x16x32_bf16 v[28:31], v[128:131], v[208:211], v[28:31]
	v_mfma_f32_16x16x32_bf16 v[24:27], v[154:157], v[208:211], v[24:27]
	v_mfma_f32_16x16x32_bf16 v[12:15], v[128:131], v[216:219], v[12:15]
	v_mfma_f32_16x16x32_bf16 v[8:11], v[154:157], v[216:219], v[8:11]
	v_mfma_f32_16x16x32_bf16 v[60:63], v[150:153], v[196:199], v[60:63]
	v_mfma_f32_16x16x32_bf16 v[56:59], v[158:161], v[196:199], v[56:59]
	v_mfma_f32_16x16x32_bf16 v[44:47], v[150:153], v[204:207], v[44:47]
	v_mfma_f32_16x16x32_bf16 v[40:43], v[158:161], v[204:207], v[40:43]
	v_mfma_f32_16x16x32_bf16 v[28:31], v[150:153], v[212:215], v[28:31]
	v_mfma_f32_16x16x32_bf16 v[24:27], v[158:161], v[212:215], v[24:27]
	v_mfma_f32_16x16x32_bf16 v[12:15], v[150:153], v[220:223], v[12:15]
	v_mfma_f32_16x16x32_bf16 v[8:11], v[158:161], v[220:223], v[8:11]
	s_setprio 0
	s_setprio 1
	v_mfma_f32_16x16x32_bf16 v[52:55], v[162:165], v[192:195], v[52:55]
	v_mfma_f32_16x16x32_bf16 v[48:51], v[170:173], v[192:195], v[48:51]
	v_mfma_f32_16x16x32_bf16 v[36:39], v[162:165], v[200:203], v[36:39]
	v_mfma_f32_16x16x32_bf16 v[32:35], v[170:173], v[200:203], v[32:35]
	v_mfma_f32_16x16x32_bf16 v[20:23], v[162:165], v[208:211], v[20:23]
	v_mfma_f32_16x16x32_bf16 v[16:19], v[170:173], v[208:211], v[16:19]
	v_mfma_f32_16x16x32_bf16 v[4:7], v[162:165], v[216:219], v[4:7]
	v_mfma_f32_16x16x32_bf16 v[0:3], v[170:173], v[216:219], v[0:3]
	v_mfma_f32_16x16x32_bf16 v[52:55], v[166:169], v[196:199], v[52:55]
	v_mfma_f32_16x16x32_bf16 v[48:51], v[188:191], v[196:199], v[48:51]
	v_mfma_f32_16x16x32_bf16 v[36:39], v[166:169], v[204:207], v[36:39]
	v_mfma_f32_16x16x32_bf16 v[32:35], v[188:191], v[204:207], v[32:35]
	v_mfma_f32_16x16x32_bf16 v[20:23], v[166:169], v[212:215], v[20:23]
	v_mfma_f32_16x16x32_bf16 v[16:19], v[188:191], v[212:215], v[16:19]
	v_mfma_f32_16x16x32_bf16 v[4:7], v[166:169], v[220:223], v[4:7]
	v_mfma_f32_16x16x32_bf16 v[0:3], v[188:191], v[220:223], v[0:3]
	s_setprio 0
	s_barrier
	s_add_i32 s75, s75, 2
	s_add_u32 s8, s8, 0x100
	s_addc_u32 s9, s9, 0
	s_add_u32 s73, s73, 0x100
	s_addc_u32 s74, s74, 0
	s_cmp_gt_u32 s75, 13
	s_cbranch_scc0 .LBB0_349
	s_and_b64 vcc, exec, s[20:21]
	s_cbranch_vccz .LBB0_352
	s_barrier

; #define LAS __attribute__((address_space(3)))
; template <int MODE, int DQK, int DV>
; __device__ __forceinline__ void attn_pass(LAS unsigned char* lds, const Tens& T, size_t rowbase, int q0, f32x16 (&o)[DV / 32], float& l_out, const int wave, QPre* qp = nullptr) {
;     ...
;             u32x2 mw = {0u, 0u};
;             if (MODE == AM_DSA) mw = *(const LAS u32x2*)(lds + OFF_MW + (sl * NSUB + sub) * 2048 + (wave * 32 + r) * 8);
;             f32x16 p[2];
;             const int kbase = 64 * j;
;             const bool diag = (kbase + 63 > q0 + wave * 32);
;             const bool nearb = (kbase + 63 + 128 > q0 + wave * 32);
;             constexpr bool POSTHOC = (MODE != AM_FOX);
;             constexpr float BIG = 65536.0f;
;             bool redo = (it == 0);
;             float psum;
;             for (;;) {
; #pragma unroll
;             for (int kb = 0; kb < 2; ++kb) {
;                 if (MODE == AM_FOX) {
;                     const float ctm = ct2 - m;
; #pragma unroll
;                     for (int g = 0; g < 4; ++g) {
;                         const f32x4 c = *(const LAS f32x4*)(lds + OFF_CS + (sl * NSUB + sub) * 256 + (32 * kb + 8 * g + 4 * h) * 4);
;                         p[kb][4 * g + 0] = fmaf(-LOG2E, c.x, ctm); p[kb][4 * g + 1] = fmaf(-LOG2E, c.y, ctm); p[kb][4 * g + 2] = fmaf(-LOG2E, c.z, ctm); p[kb][4 * g + 3] = fmaf(-LOG2E, c.w, ctm);
;                     }
;                 } else if (MODE == AM_DSA) {
; #pragma unroll
;                     for (int g = 0; g < 4; ++g) {
;                         const unsigned nib = __builtin_amdgcn_ubfe(mw[kb], (unsigned)(8 * g + 4 * h), 4u);
;                         const f32x4 t4 = *(const LAS f32x4*)(lds + OFF_LUT + 768 + nib * 16);
;                         p[kb][4 * g + 0] = t4.x; p[kb][4 * g + 1] = t4.y; p[kb][4 * g + 2] = t4.z; p[kb][4 * g + 3] = t4.w;
;                     }
;                     p[kb] = __builtin_amdgcn_mfma_f32_32x32x16_bf16(kone, qm, p[kb], 0, 0, 0);
;                 }
; #pragma unroll
;                 for (int s = 0; s < NSTEP; ++s) {
;                     bf16x8 a;
;                     if (s < 4) a = *(const LAS bf16x8*)(kfa[s] + sl * KSL + sub * KB_T + kb * 4096);
;                     else       a = *(const LAS bf16x8*)(kfa[s] + sl * KSL + sub * KB_T + kb * 2048);
;                     if ((MODE == AM_DIFF || MODE == AM_MLA) && s == 0)
.LBB0_1651:
	v_add_u32_e32 v32, s67, v105
	ds_read_b64 v[32:33], v32
	s_add_i32 s0, s11, 0xbf
	s_cmp_gt_u32 s0, s83
	s_cselect_b64 s[34:35], -1, 0
	s_cmp_le_u32 s0, s83
	s_waitcnt lgkmcnt(0)
	v_bfe_u32 v114, v32, v106, 4
	v_bfe_u32 v115, v32, v107, 4
	v_bfe_u32 v121, v32, v109, 4
	v_bfe_u32 v116, v33, v106, 4
	v_bfe_u32 v117, v33, v107, 4
	v_bfe_u32 v118, v33, v108, 4
	v_bfe_u32 v120, v32, v108, 4
	v_bfe_u32 v119, v33, v109, 4
	v_lshl_add_u32 v114, v114, 4, s79
	v_lshl_add_u32 v115, v115, 4, s79
	v_lshl_add_u32 v121, v121, 4, s79
	v_lshl_add_u32 v116, v116, 4, s79
	v_lshl_add_u32 v117, v117, 4, s79
	v_lshl_add_u32 v118, v118, 4, s79
	v_lshl_add_u32 v120, v120, 4, s79
	v_lshl_add_u32 v119, v119, 4, s79
	ds_read_b128 v[32:35], v114
	ds_read_b128 v[36:39], v115
	ds_read_b128 v[40:43], v120
	ds_read_b128 v[44:47], v121
	ds_read_b128 v[188:191], v96
	ds_read_b128 v[192:195], v97
	ds_read_b128 v[196:199], v98
	ds_read_b128 v[200:203], v99
	ds_read_b128 v[48:51], v116
	ds_read_b128 v[52:55], v117
	ds_read_b128 v[56:59], v118
	ds_read_b128 v[60:63], v119
	ds_read_b128 v[204:207], v96 offset:4096
	ds_read_b128 v[208:211], v97 offset:4096
	ds_read_b128 v[212:215], v98 offset:4096
	s_waitcnt lgkmcnt(11)
	v_mfma_f32_32x32x16_bf16 v[32:47], v[68:71], v[64:67], v[32:47]
	ds_read_b128 v[216:219], v99 offset:4096
	v_add_u32_e32 v113, 0x80, v110
	s_waitcnt lgkmcnt(11)
	v_mfma_f32_32x32x16_bf16 v[32:47], v[188:191], v[72:75], v[32:47]
	s_waitcnt lgkmcnt(10)
	v_mfma_f32_32x32x16_bf16 v[32:47], v[192:195], v[76:79], v[32:47]
	s_waitcnt lgkmcnt(9)
	v_mfma_f32_32x32x16_bf16 v[32:47], v[196:199], v[80:83], v[32:47]
	s_waitcnt lgkmcnt(8)
	v_mfma_f32_32x32x16_bf16 v[32:47], v[200:203], v[84:87], v[32:47]
	s_waitcnt lgkmcnt(4)
	v_mfma_f32_32x32x16_bf16 v[48:63], v[68:71], v[64:67], v[48:63]
	s_waitcnt lgkmcnt(3)
	v_mfma_f32_32x32x16_bf16 v[48:63], v[204:207], v[72:75], v[48:63]
	s_waitcnt lgkmcnt(2)
	v_mfma_f32_32x32x16_bf16 v[48:63], v[208:211], v[76:79], v[48:63]
	s_waitcnt lgkmcnt(1)
	v_mfma_f32_32x32x16_bf16 v[48:63], v[212:215], v[80:83], v[48:63]
	s_waitcnt lgkmcnt(0)
	v_mfma_f32_32x32x16_bf16 v[48:63], v[216:219], v[84:87], v[48:63]
	ds_read_b64_tr_b16 v[156:157], v101
	ds_read_b64_tr_b16 v[158:159], v101 offset:1024
	ds_read_b64_tr_b16 v[160:161], v101 offset:2048
	ds_read_b64_tr_b16 v[162:163], v101 offset:3072
	ds_read_b64_tr_b16 v[164:165], v101 offset:4096
	ds_read_b64_tr_b16 v[166:167], v101 offset:5120
	ds_read_b64_tr_b16 v[168:169], v101 offset:6144
	ds_read_b64_tr_b16 v[170:171], v101 offset:7168
	ds_read_b64_tr_b16 v[172:173], v102
	ds_read_b64_tr_b16 v[174:175], v102 offset:1024
	ds_read_b64_tr_b16 v[176:177], v102 offset:2048
	ds_read_b64_tr_b16 v[178:179], v102 offset:3072
	ds_read_b64_tr_b16 v[180:181], v102 offset:4096
	ds_read_b64_tr_b16 v[182:183], v102 offset:5120
	ds_read_b64_tr_b16 v[184:185], v102 offset:6144
	ds_read_b64_tr_b16 v[186:187], v102 offset:7168
	s_cbranch_scc1 .LBB0_1653
; template <int MODE, int DQK, int DV>
; __device__ __forceinline__ void attn_pass(LAS unsigned char* lds, const Tens& T, size_t rowbase, int q0, f32x16 (&o)[DV / 32], float& l_out, const int wave, QPre* qp = nullptr) {
;     ...
;             if (MODE == AM_DSA || MODE == AM_DIFF) {
;                 if (nearb) {
;                     int dq = tq - kbase - 4 * h; asm volatile("" : "+v"(dq));
; #pragma unroll
;                     for (int kb = 0; kb < 2; ++kb)
; #pragma unroll
;                         for (int rg = 0; rg < 16; ++rg) { int dist = dq - (32 * kb + (rg & 3) + 8 * (rg >> 2)); dist = dist < 0 ? 0 : (dist > 128 ? 128 : dist); p[kb][rg] += lut[dist]; }
;                 }
	v_mov_b32_e32 v146, v113
	s_add_i32 s0, 0, 0x1f800
	v_add_u32_e32 v123, -1, v146
	v_add_u32_e32 v124, -2, v146
	v_add_u32_e32 v125, -3, v146
	v_add_u32_e32 v126, -8, v146
	v_add_u32_e32 v127, -9, v146
	v_add_u32_e32 v128, -10, v146
	v_add_u32_e32 v129, -11, v146
	v_add_u32_e32 v130, -16, v146
	v_subrev_u32_e32 v131, 17, v146
	v_subrev_u32_e32 v132, 18, v146
	v_subrev_u32_e32 v133, 19, v146
	v_subrev_u32_e32 v134, 24, v146
	v_subrev_u32_e32 v135, 25, v146
	v_subrev_u32_e32 v136, 26, v146
	v_subrev_u32_e32 v137, 27, v146
	v_subrev_u32_e32 v138, 32, v146
	v_subrev_u32_e32 v139, 33, v146
	v_subrev_u32_e32 v140, 34, v146
	v_subrev_u32_e32 v141, 35, v146
	v_subrev_u32_e32 v142, 40, v146
	v_subrev_u32_e32 v143, 41, v146
	v_subrev_u32_e32 v144, 42, v146
	v_subrev_u32_e32 v145, 43, v146
	v_subrev_u32_e32 v147, 48, v146
	v_subrev_u32_e32 v148, 49, v146
	v_subrev_u32_e32 v149, 50, v146
	v_subrev_u32_e32 v150, 51, v146
	v_subrev_u32_e32 v151, 56, v146
	v_subrev_u32_e32 v152, 57, v146
	v_subrev_u32_e32 v153, 58, v146
	v_med3_i32 v122, v146, 0, v93
	v_med3_i32 v123, v123, 0, v93
	v_med3_i32 v124, v124, 0, v93
	v_med3_i32 v125, v125, 0, v93
	v_med3_i32 v126, v126, 0, v93
	v_med3_i32 v127, v127, 0, v93
	v_med3_i32 v128, v128, 0, v93
	v_med3_i32 v129, v129, 0, v93
	v_med3_i32 v130, v130, 0, v93
	v_med3_i32 v131, v131, 0, v93
	v_med3_i32 v132, v132, 0, v93
	v_med3_i32 v133, v133, 0, v93
	v_med3_i32 v134, v134, 0, v93
	v_med3_i32 v135, v135, 0, v93
	v_med3_i32 v136, v136, 0, v93
	v_med3_i32 v137, v137, 0, v93
	v_med3_i32 v138, v138, 0, v93
	v_med3_i32 v139, v139, 0, v93
	v_med3_i32 v140, v140, 0, v93
	v_med3_i32 v141, v141, 0, v93
	v_med3_i32 v142, v142, 0, v93
	v_med3_i32 v143, v143, 0, v93
	v_med3_i32 v144, v144, 0, v93
	v_med3_i32 v145, v145, 0, v93
	v_med3_i32 v147, v147, 0, v93
	v_med3_i32 v148, v148, 0, v93
	v_med3_i32 v149, v149, 0, v93
	v_med3_i32 v150, v150, 0, v93
	v_med3_i32 v151, v151, 0, v93
	v_med3_i32 v152, v152, 0, v93
	v_med3_i32 v153, v153, 0, v93
	v_subrev_u32_e32 v146, 59, v146
	v_lshl_add_u32 v122, v122, 2, s0
	v_lshl_add_u32 v123, v123, 2, s0
	v_lshl_add_u32 v124, v124, 2, s0
	v_lshl_add_u32 v125, v125, 2, s0
	v_lshl_add_u32 v126, v126, 2, s0
	v_lshl_add_u32 v127, v127, 2, s0
	v_lshl_add_u32 v128, v128, 2, s0
	v_lshl_add_u32 v129, v129, 2, s0
	v_lshl_add_u32 v130, v130, 2, s0
	v_lshl_add_u32 v131, v131, 2, s0
	v_lshl_add_u32 v132, v132, 2, s0
	v_lshl_add_u32 v133, v133, 2, s0
	v_lshl_add_u32 v134, v134, 2, s0
	v_lshl_add_u32 v135, v135, 2, s0
	v_lshl_add_u32 v136, v136, 2, s0
	v_lshl_add_u32 v137, v137, 2, s0
	v_lshl_add_u32 v138, v138, 2, s0
	v_lshl_add_u32 v139, v139, 2, s0
	v_lshl_add_u32 v140, v140, 2, s0
	v_lshl_add_u32 v141, v141, 2, s0
	v_lshl_add_u32 v142, v142, 2, s0
	v_lshl_add_u32 v143, v143, 2, s0
	v_lshl_add_u32 v144, v144, 2, s0
	v_lshl_add_u32 v145, v145, 2, s0
	v_lshl_add_u32 v147, v147, 2, s0
	v_lshl_add_u32 v148, v148, 2, s0
	v_lshl_add_u32 v149, v149, 2, s0
	v_lshl_add_u32 v150, v150, 2, s0
	v_lshl_add_u32 v151, v151, 2, s0
	v_lshl_add_u32 v152, v152, 2, s0
	v_lshl_add_u32 v153, v153, 2, s0
	v_med3_i32 v146, v146, 0, v93
	ds_read_b32 v122, v122
	ds_read_b32 v123, v123
	ds_read_b32 v124, v124
	ds_read_b32 v125, v125
	ds_read_b32 v126, v126
	ds_read_b32 v127, v127
	ds_read_b32 v128, v128
	ds_read_b32 v129, v129
	ds_read_b32 v130, v130
	ds_read_b32 v131, v131
	ds_read_b32 v132, v132
	ds_read_b32 v133, v133
	ds_read_b32 v134, v134
	ds_read_b32 v135, v135
	ds_read_b32 v136, v136
	ds_read_b32 v137, v137
	ds_read_b32 v138, v138
	ds_read_b32 v139, v139
	ds_read_b32 v140, v140
	ds_read_b32 v141, v141
	ds_read_b32 v142, v142
	ds_read_b32 v143, v143
	ds_read_b32 v144, v144
	ds_read_b32 v145, v145
	v_lshl_add_u32 v154, v146, 2, s0
	ds_read_b32 v146, v147
	ds_read_b32 v147, v148
	ds_read_b32 v148, v149
	ds_read_b32 v149, v150
	ds_read_b32 v150, v151
	ds_read_b32 v151, v152
	ds_read_b32 v152, v153
	ds_read_b32 v153, v154
	s_waitcnt lgkmcnt(14)
	v_pk_add_f32 v[44:45], v[44:45], v[134:135]
	v_pk_add_f32 v[46:47], v[46:47], v[136:137]
	v_pk_add_f32 v[42:43], v[42:43], v[132:133]
	v_pk_add_f32 v[40:41], v[40:41], v[130:131]
	v_pk_add_f32 v[38:39], v[38:39], v[128:129]
	v_pk_add_f32 v[36:37], v[36:37], v[126:127]
	v_pk_add_f32 v[34:35], v[34:35], v[124:125]
	v_pk_add_f32 v[32:33], v[32:33], v[122:123]
	s_waitcnt lgkmcnt(0)
	v_pk_add_f32 v[62:63], v[62:63], v[152:153]
	v_pk_add_f32 v[60:61], v[60:61], v[150:151]
	v_pk_add_f32 v[58:59], v[58:59], v[148:149]
	v_pk_add_f32 v[56:57], v[56:57], v[146:147]
	v_pk_add_f32 v[54:55], v[54:55], v[144:145]
	v_pk_add_f32 v[52:53], v[52:53], v[142:143]
	v_pk_add_f32 v[50:51], v[50:51], v[140:141]
	v_pk_add_f32 v[48:49], v[48:49], v[138:139]

; #define LAS __attribute__((address_space(3)))
; template <int MODE, int DQK, int DV>
; __device__ __forceinline__ void attn_pass(LAS unsigned char* lds, const Tens& T, size_t rowbase, int q0, f32x16 (&o)[DV / 32], float& l_out, const int wave, QPre* qp = nullptr) {
;     ...
;             u32x2 mw = {0u, 0u};
;             if (MODE == AM_DSA) mw = *(const LAS u32x2*)(lds + OFF_MW + (sl * NSUB + sub) * 2048 + (wave * 32 + r) * 8);
;             f32x16 p[2];
;             const int kbase = 64 * j;
;             const bool diag = (kbase + 63 > q0 + wave * 32);
;             const bool nearb = (kbase + 63 + 128 > q0 + wave * 32);
;             constexpr bool POSTHOC = (MODE != AM_FOX);
;             constexpr float BIG = 65536.0f;
;             bool redo = (it == 0);
;             float psum;
;             for (;;) {
; #pragma unroll
;             for (int kb = 0; kb < 2; ++kb) {
;                 if (MODE == AM_FOX) {
;                     const float ctm = ct2 - m;
; #pragma unroll
;                     for (int g = 0; g < 4; ++g) {
;                         const f32x4 c = *(const LAS f32x4*)(lds + OFF_CS + (sl * NSUB + sub) * 256 + (32 * kb + 8 * g + 4 * h) * 4);
;                         p[kb][4 * g + 0] = fmaf(-LOG2E, c.x, ctm); p[kb][4 * g + 1] = fmaf(-LOG2E, c.y, ctm); p[kb][4 * g + 2] = fmaf(-LOG2E, c.z, ctm); p[kb][4 * g + 3] = fmaf(-LOG2E, c.w, ctm);
;                     }
;                 } else if (MODE == AM_DSA) {
; #pragma unroll
;                     for (int g = 0; g < 4; ++g) {
;                         const unsigned nib = __builtin_amdgcn_ubfe(mw[kb], (unsigned)(8 * g + 4 * h), 4u);
;                         const f32x4 t4 = *(const LAS f32x4*)(lds + OFF_LUT + 768 + nib * 16);
;                         p[kb][4 * g + 0] = t4.x; p[kb][4 * g + 1] = t4.y; p[kb][4 * g + 2] = t4.z; p[kb][4 * g + 3] = t4.w;
;                     }
;                     p[kb] = __builtin_amdgcn_mfma_f32_32x32x16_bf16(kone, qm, p[kb], 0, 0, 0);
;                 }
; #pragma unroll
;                 for (int s = 0; s < NSTEP; ++s) {
;                     bf16x8 a;
;                     if (s < 4) a = *(const LAS bf16x8*)(kfa[s] + sl * KSL + sub * KB_T + kb * 4096);
;                     else       a = *(const LAS bf16x8*)(kfa[s] + sl * KSL + sub * KB_T + kb * 2048);
;                     if ((MODE == AM_DIFF || MODE == AM_MLA) && s == 0)
.LBB0_1658:
	v_add_u32_e32 v32, s68, v105
	ds_read_b64 v[32:33], v32
	s_cmp_gt_i32 s11, s8
	s_cselect_b64 s[34:35], -1, 0
	s_cmp_le_i32 s11, s8
	v_add_u32_e32 v113, 64, v110
	s_waitcnt lgkmcnt(0)
	v_bfe_u32 v114, v32, v106, 4
	v_bfe_u32 v115, v32, v107, 4
	v_bfe_u32 v121, v32, v109, 4
	v_bfe_u32 v116, v33, v106, 4
	v_bfe_u32 v117, v33, v107, 4
	v_bfe_u32 v118, v33, v108, 4
	v_bfe_u32 v120, v32, v108, 4
	v_bfe_u32 v119, v33, v109, 4
	v_lshl_add_u32 v114, v114, 4, s79
	v_lshl_add_u32 v115, v115, 4, s79
	v_lshl_add_u32 v121, v121, 4, s79
	v_lshl_add_u32 v116, v116, 4, s79
	v_lshl_add_u32 v117, v117, 4, s79
	v_lshl_add_u32 v118, v118, 4, s79
	v_lshl_add_u32 v120, v120, 4, s79
	v_lshl_add_u32 v119, v119, 4, s79
	ds_read_b128 v[32:35], v114
	ds_read_b128 v[36:39], v115
	ds_read_b128 v[40:43], v120
	ds_read_b128 v[44:47], v121
	ds_read_b128 v[188:191], v96 offset:8192
	ds_read_b128 v[192:195], v97 offset:8192
	ds_read_b128 v[196:199], v98 offset:8192
	ds_read_b128 v[200:203], v99 offset:8192
	ds_read_b128 v[48:51], v116
	ds_read_b128 v[52:55], v117
	ds_read_b128 v[56:59], v118
	ds_read_b128 v[60:63], v119
	ds_read_b128 v[204:207], v96 offset:12288
	ds_read_b128 v[208:211], v97 offset:12288
	ds_read_b128 v[212:215], v98 offset:12288
	s_waitcnt lgkmcnt(11)
	v_mfma_f32_32x32x16_bf16 v[32:47], v[68:71], v[64:67], v[32:47]
	ds_read_b128 v[216:219], v99 offset:12288
	s_waitcnt lgkmcnt(11)
	v_mfma_f32_32x32x16_bf16 v[32:47], v[188:191], v[72:75], v[32:47]
	s_waitcnt lgkmcnt(10)
	v_mfma_f32_32x32x16_bf16 v[32:47], v[192:195], v[76:79], v[32:47]
	s_waitcnt lgkmcnt(9)
	v_mfma_f32_32x32x16_bf16 v[32:47], v[196:199], v[80:83], v[32:47]
	s_waitcnt lgkmcnt(8)
	v_mfma_f32_32x32x16_bf16 v[32:47], v[200:203], v[84:87], v[32:47]
	s_waitcnt lgkmcnt(4)
	v_mfma_f32_32x32x16_bf16 v[48:63], v[68:71], v[64:67], v[48:63]
	s_waitcnt lgkmcnt(3)
	v_mfma_f32_32x32x16_bf16 v[48:63], v[204:207], v[72:75], v[48:63]
	s_waitcnt lgkmcnt(2)
	v_mfma_f32_32x32x16_bf16 v[48:63], v[208:211], v[76:79], v[48:63]
	s_waitcnt lgkmcnt(1)
	v_mfma_f32_32x32x16_bf16 v[48:63], v[212:215], v[80:83], v[48:63]
	s_waitcnt lgkmcnt(0)
	v_mfma_f32_32x32x16_bf16 v[48:63], v[216:219], v[84:87], v[48:63]
	ds_read_b64_tr_b16 v[156:157], v101 offset:8192
	ds_read_b64_tr_b16 v[158:159], v101 offset:9216
	ds_read_b64_tr_b16 v[160:161], v101 offset:10240
	ds_read_b64_tr_b16 v[162:163], v101 offset:11264
	ds_read_b64_tr_b16 v[164:165], v101 offset:12288
	ds_read_b64_tr_b16 v[166:167], v101 offset:13312
	ds_read_b64_tr_b16 v[168:169], v101 offset:14336
	ds_read_b64_tr_b16 v[170:171], v101 offset:15360
	ds_read_b64_tr_b16 v[172:173], v102 offset:8192
	ds_read_b64_tr_b16 v[174:175], v102 offset:9216
	ds_read_b64_tr_b16 v[176:177], v102 offset:10240
	ds_read_b64_tr_b16 v[178:179], v102 offset:11264
	ds_read_b64_tr_b16 v[180:181], v102 offset:12288
	ds_read_b64_tr_b16 v[182:183], v102 offset:13312
	ds_read_b64_tr_b16 v[184:185], v102 offset:14336
	ds_read_b64_tr_b16 v[186:187], v102 offset:15360
	s_cbranch_scc1 .LBB0_1660
; template <int MODE, int DQK, int DV>
; __device__ __forceinline__ void attn_pass(LAS unsigned char* lds, const Tens& T, size_t rowbase, int q0, f32x16 (&o)[DV / 32], float& l_out, const int wave, QPre* qp = nullptr) {
;     ...
;             if (MODE == AM_DSA || MODE == AM_DIFF) {
;                 if (nearb) {
;                     int dq = tq - kbase - 4 * h; asm volatile("" : "+v"(dq));
; #pragma unroll
;                     for (int kb = 0; kb < 2; ++kb)
; #pragma unroll
;                         for (int rg = 0; rg < 16; ++rg) { int dist = dq - (32 * kb + (rg & 3) + 8 * (rg >> 2)); dist = dist < 0 ? 0 : (dist > 128 ? 128 : dist); p[kb][rg] += lut[dist]; }
;                 }
	v_mov_b32_e32 v146, v113
	s_add_i32 s0, 0, 0x1f800
	v_add_u32_e32 v123, -1, v146
	v_add_u32_e32 v124, -2, v146
	v_add_u32_e32 v125, -3, v146
	v_add_u32_e32 v126, -8, v146
	v_add_u32_e32 v127, -9, v146
	v_add_u32_e32 v128, -10, v146
	v_add_u32_e32 v129, -11, v146
	v_add_u32_e32 v130, -16, v146
	v_subrev_u32_e32 v131, 17, v146
	v_subrev_u32_e32 v132, 18, v146
	v_subrev_u32_e32 v133, 19, v146
	v_subrev_u32_e32 v134, 24, v146
	v_subrev_u32_e32 v135, 25, v146
	v_subrev_u32_e32 v136, 26, v146
	v_subrev_u32_e32 v137, 27, v146
	v_subrev_u32_e32 v138, 32, v146
	v_subrev_u32_e32 v139, 33, v146
	v_subrev_u32_e32 v140, 34, v146
	v_subrev_u32_e32 v141, 35, v146
	v_subrev_u32_e32 v142, 40, v146
	v_subrev_u32_e32 v143, 41, v146
	v_subrev_u32_e32 v144, 42, v146
	v_subrev_u32_e32 v145, 43, v146
	v_subrev_u32_e32 v147, 48, v146
	v_subrev_u32_e32 v148, 49, v146
	v_subrev_u32_e32 v149, 50, v146
	v_subrev_u32_e32 v150, 51, v146
	v_subrev_u32_e32 v151, 56, v146
	v_subrev_u32_e32 v152, 57, v146
	v_subrev_u32_e32 v153, 58, v146
	v_med3_i32 v122, v146, 0, v93
	v_med3_i32 v123, v123, 0, v93
	v_med3_i32 v124, v124, 0, v93
	v_med3_i32 v125, v125, 0, v93
	v_med3_i32 v126, v126, 0, v93
	v_med3_i32 v127, v127, 0, v93
	v_med3_i32 v128, v128, 0, v93
	v_med3_i32 v129, v129, 0, v93
	v_med3_i32 v130, v130, 0, v93
	v_med3_i32 v131, v131, 0, v93
	v_med3_i32 v132, v132, 0, v93
	v_med3_i32 v133, v133, 0, v93
	v_med3_i32 v134, v134, 0, v93
	v_med3_i32 v135, v135, 0, v93
	v_med3_i32 v136, v136, 0, v93
	v_med3_i32 v137, v137, 0, v93
	v_med3_i32 v138, v138, 0, v93
	v_med3_i32 v139, v139, 0, v93
	v_med3_i32 v140, v140, 0, v93
	v_med3_i32 v141, v141, 0, v93
	v_med3_i32 v142, v142, 0, v93
	v_med3_i32 v143, v143, 0, v93
	v_med3_i32 v144, v144, 0, v93
	v_med3_i32 v145, v145, 0, v93
	v_med3_i32 v147, v147, 0, v93
	v_med3_i32 v148, v148, 0, v93
	v_med3_i32 v149, v149, 0, v93
	v_med3_i32 v150, v150, 0, v93
	v_med3_i32 v151, v151, 0, v93
	v_med3_i32 v152, v152, 0, v93
	v_med3_i32 v153, v153, 0, v93
	v_subrev_u32_e32 v146, 59, v146
	v_lshl_add_u32 v122, v122, 2, s0
	v_lshl_add_u32 v123, v123, 2, s0
	v_lshl_add_u32 v124, v124, 2, s0
	v_lshl_add_u32 v125, v125, 2, s0
	v_lshl_add_u32 v126, v126, 2, s0
	v_lshl_add_u32 v127, v127, 2, s0
	v_lshl_add_u32 v128, v128, 2, s0
	v_lshl_add_u32 v129, v129, 2, s0
	v_lshl_add_u32 v130, v130, 2, s0
	v_lshl_add_u32 v131, v131, 2, s0
	v_lshl_add_u32 v132, v132, 2, s0
	v_lshl_add_u32 v133, v133, 2, s0
	v_lshl_add_u32 v134, v134, 2, s0
	v_lshl_add_u32 v135, v135, 2, s0
	v_lshl_add_u32 v136, v136, 2, s0
	v_lshl_add_u32 v137, v137, 2, s0
	v_lshl_add_u32 v138, v138, 2, s0
	v_lshl_add_u32 v139, v139, 2, s0
	v_lshl_add_u32 v140, v140, 2, s0
	v_lshl_add_u32 v141, v141, 2, s0
	v_lshl_add_u32 v142, v142, 2, s0
	v_lshl_add_u32 v143, v143, 2, s0
	v_lshl_add_u32 v144, v144, 2, s0
	v_lshl_add_u32 v145, v145, 2, s0
	v_lshl_add_u32 v147, v147, 2, s0
	v_lshl_add_u32 v148, v148, 2, s0
	v_lshl_add_u32 v149, v149, 2, s0
	v_lshl_add_u32 v150, v150, 2, s0
	v_lshl_add_u32 v151, v151, 2, s0
	v_lshl_add_u32 v152, v152, 2, s0
	v_lshl_add_u32 v153, v153, 2, s0
	v_med3_i32 v146, v146, 0, v93
	ds_read_b32 v122, v122
	ds_read_b32 v123, v123
	ds_read_b32 v124, v124
	ds_read_b32 v125, v125
	ds_read_b32 v126, v126
	ds_read_b32 v127, v127
	ds_read_b32 v128, v128
	ds_read_b32 v129, v129
	ds_read_b32 v130, v130
	ds_read_b32 v131, v131
	ds_read_b32 v132, v132
	ds_read_b32 v133, v133
	ds_read_b32 v134, v134
	ds_read_b32 v135, v135
	ds_read_b32 v136, v136
	ds_read_b32 v137, v137
	ds_read_b32 v138, v138
	ds_read_b32 v139, v139
	ds_read_b32 v140, v140
	ds_read_b32 v141, v141
	ds_read_b32 v142, v142
	ds_read_b32 v143, v143
	ds_read_b32 v144, v144
	ds_read_b32 v145, v145
	v_lshl_add_u32 v154, v146, 2, s0
	ds_read_b32 v146, v147
	ds_read_b32 v147, v148
	ds_read_b32 v148, v149
	ds_read_b32 v149, v150
	ds_read_b32 v150, v151
	ds_read_b32 v151, v152
	ds_read_b32 v152, v153
	ds_read_b32 v153, v154
	s_waitcnt lgkmcnt(14)
	v_pk_add_f32 v[44:45], v[44:45], v[134:135]
	v_pk_add_f32 v[46:47], v[46:47], v[136:137]
	v_pk_add_f32 v[42:43], v[42:43], v[132:133]
	v_pk_add_f32 v[40:41], v[40:41], v[130:131]
	v_pk_add_f32 v[38:39], v[38:39], v[128:129]
	v_pk_add_f32 v[36:37], v[36:37], v[126:127]
	v_pk_add_f32 v[34:35], v[34:35], v[124:125]
	v_pk_add_f32 v[32:33], v[32:33], v[122:123]
	s_waitcnt lgkmcnt(0)
	v_pk_add_f32 v[62:63], v[62:63], v[152:153]
	v_pk_add_f32 v[60:61], v[60:61], v[150:151]
	v_pk_add_f32 v[58:59], v[58:59], v[148:149]
	v_pk_add_f32 v[56:57], v[56:57], v[146:147]
	v_pk_add_f32 v[54:55], v[54:55], v[144:145]
	v_pk_add_f32 v[52:53], v[52:53], v[142:143]
	v_pk_add_f32 v[50:51], v[50:51], v[140:141]
	v_pk_add_f32 v[48:49], v[48:49], v[138:139]

; #define LAS __attribute__((address_space(3)))
; template <int MODE, int DQK, int DV>
; __device__ __forceinline__ void attn_pass(LAS unsigned char* lds, const Tens& T, size_t rowbase, int q0, f32x16 (&o)[DV / 32], float& l_out, const int wave, QPre* qp = nullptr) {
;     ...
;             u32x2 mw = {0u, 0u};
;             if (MODE == AM_DSA) mw = *(const LAS u32x2*)(lds + OFF_MW + (sl * NSUB + sub) * 2048 + (wave * 32 + r) * 8);
;             f32x16 p[2];
;             const int kbase = 64 * j;
;             const bool diag = (kbase + 63 > q0 + wave * 32);
;             const bool nearb = (kbase + 63 + 128 > q0 + wave * 32);
;             constexpr bool POSTHOC = (MODE != AM_FOX);
;             constexpr float BIG = 65536.0f;
;             bool redo = (it == 0);
;             float psum;
;             for (;;) {
; #pragma unroll
;             for (int kb = 0; kb < 2; ++kb) {
;                 if (MODE == AM_FOX) {
;                     const float ctm = ct2 - m;
; #pragma unroll
;                     for (int g = 0; g < 4; ++g) {
;                         const f32x4 c = *(const LAS f32x4*)(lds + OFF_CS + (sl * NSUB + sub) * 256 + (32 * kb + 8 * g + 4 * h) * 4);
;                         p[kb][4 * g + 0] = fmaf(-LOG2E, c.x, ctm); p[kb][4 * g + 1] = fmaf(-LOG2E, c.y, ctm); p[kb][4 * g + 2] = fmaf(-LOG2E, c.z, ctm); p[kb][4 * g + 3] = fmaf(-LOG2E, c.w, ctm);
;                     }
;                 } else if (MODE == AM_DSA) {
; #pragma unroll
;                     for (int g = 0; g < 4; ++g) {
;                         const unsigned nib = __builtin_amdgcn_ubfe(mw[kb], (unsigned)(8 * g + 4 * h), 4u);
;                         const f32x4 t4 = *(const LAS f32x4*)(lds + OFF_LUT + 768 + nib * 16);
;                         p[kb][4 * g + 0] = t4.x; p[kb][4 * g + 1] = t4.y; p[kb][4 * g + 2] = t4.z; p[kb][4 * g + 3] = t4.w;
;                     }
;                     p[kb] = __builtin_amdgcn_mfma_f32_32x32x16_bf16(kone, qm, p[kb], 0, 0, 0);
;                 }
; #pragma unroll
;                 for (int s = 0; s < NSTEP; ++s) {
;                     bf16x8 a;
;                     if (s < 4) a = *(const LAS bf16x8*)(kfa[s] + sl * KSL + sub * KB_T + kb * 4096);
;                     else       a = *(const LAS bf16x8*)(kfa[s] + sl * KSL + sub * KB_T + kb * 2048);
;                     if ((MODE == AM_DIFF || MODE == AM_MLA) && s == 0)
.LBB0_1666:
	v_add_u32_e32 v32, s69, v105
	ds_read_b64 v[32:33], v32
	s_add_i32 s1, s11, 0x13f
	s_cmp_gt_u32 s1, s83
	s_cselect_b64 s[34:35], -1, 0
	s_cmp_le_u32 s1, s83
	s_waitcnt lgkmcnt(0)
	v_bfe_u32 v113, v32, v106, 4
	v_bfe_u32 v114, v32, v107, 4
	v_bfe_u32 v120, v32, v109, 4
	v_bfe_u32 v115, v33, v106, 4
	v_bfe_u32 v116, v33, v107, 4
	v_bfe_u32 v117, v33, v108, 4
	v_bfe_u32 v119, v32, v108, 4
	v_bfe_u32 v118, v33, v109, 4
	v_lshl_add_u32 v113, v113, 4, s79
	v_lshl_add_u32 v114, v114, 4, s79
	v_lshl_add_u32 v120, v120, 4, s79
	v_lshl_add_u32 v115, v115, 4, s79
	v_lshl_add_u32 v116, v116, 4, s79
	v_lshl_add_u32 v117, v117, 4, s79
	v_lshl_add_u32 v119, v119, 4, s79
	v_lshl_add_u32 v118, v118, 4, s79
	ds_read_b128 v[32:35], v113
	ds_read_b128 v[36:39], v114
	ds_read_b128 v[40:43], v119
	ds_read_b128 v[44:47], v120
	ds_read_b128 v[188:191], v96 offset:16384
	ds_read_b128 v[192:195], v97 offset:16384
	ds_read_b128 v[196:199], v98 offset:16384
	ds_read_b128 v[200:203], v99 offset:16384
	ds_read_b128 v[48:51], v115
	ds_read_b128 v[52:55], v116
	ds_read_b128 v[56:59], v117
	ds_read_b128 v[60:63], v118
	ds_read_b128 v[204:207], v96 offset:20480
	ds_read_b128 v[208:211], v97 offset:20480
	ds_read_b128 v[212:215], v98 offset:20480
	s_waitcnt lgkmcnt(11)
	v_mfma_f32_32x32x16_bf16 v[32:47], v[68:71], v[64:67], v[32:47]
	ds_read_b128 v[216:219], v99 offset:20480
	s_waitcnt lgkmcnt(11)
	v_mfma_f32_32x32x16_bf16 v[32:47], v[188:191], v[72:75], v[32:47]
	s_waitcnt lgkmcnt(10)
	v_mfma_f32_32x32x16_bf16 v[32:47], v[192:195], v[76:79], v[32:47]
	s_waitcnt lgkmcnt(9)
	v_mfma_f32_32x32x16_bf16 v[32:47], v[196:199], v[80:83], v[32:47]
	s_waitcnt lgkmcnt(8)
	v_mfma_f32_32x32x16_bf16 v[32:47], v[200:203], v[84:87], v[32:47]
	s_waitcnt lgkmcnt(4)
	v_mfma_f32_32x32x16_bf16 v[48:63], v[68:71], v[64:67], v[48:63]
	s_waitcnt lgkmcnt(3)
	v_mfma_f32_32x32x16_bf16 v[48:63], v[204:207], v[72:75], v[48:63]
	s_waitcnt lgkmcnt(2)
	v_mfma_f32_32x32x16_bf16 v[48:63], v[208:211], v[76:79], v[48:63]
	s_waitcnt lgkmcnt(1)
	v_mfma_f32_32x32x16_bf16 v[48:63], v[212:215], v[80:83], v[48:63]
	s_waitcnt lgkmcnt(0)
	v_mfma_f32_32x32x16_bf16 v[48:63], v[216:219], v[84:87], v[48:63]
	ds_read_b64_tr_b16 v[156:157], v101 offset:16384
	ds_read_b64_tr_b16 v[158:159], v101 offset:17408
	ds_read_b64_tr_b16 v[160:161], v101 offset:18432
	ds_read_b64_tr_b16 v[162:163], v101 offset:19456
	ds_read_b64_tr_b16 v[164:165], v101 offset:20480
	ds_read_b64_tr_b16 v[166:167], v101 offset:21504
	ds_read_b64_tr_b16 v[168:169], v101 offset:22528
	ds_read_b64_tr_b16 v[170:171], v101 offset:23552
	ds_read_b64_tr_b16 v[172:173], v102 offset:16384
	ds_read_b64_tr_b16 v[174:175], v102 offset:17408
	ds_read_b64_tr_b16 v[176:177], v102 offset:18432
	ds_read_b64_tr_b16 v[178:179], v102 offset:19456
	ds_read_b64_tr_b16 v[180:181], v102 offset:20480
	ds_read_b64_tr_b16 v[182:183], v102 offset:21504
	ds_read_b64_tr_b16 v[184:185], v102 offset:22528
	ds_read_b64_tr_b16 v[186:187], v102 offset:23552
	s_cbranch_scc1 .LBB0_1668
; template <int MODE, int DQK, int DV>
; __device__ __forceinline__ void attn_pass(LAS unsigned char* lds, const Tens& T, size_t rowbase, int q0, f32x16 (&o)[DV / 32], float& l_out, const int wave, QPre* qp = nullptr) {
;     ...
;             if (MODE == AM_DSA || MODE == AM_DIFF) {
;                 if (nearb) {
;                     int dq = tq - kbase - 4 * h; asm volatile("" : "+v"(dq));
; #pragma unroll
;                     for (int kb = 0; kb < 2; ++kb)
; #pragma unroll
;                         for (int rg = 0; rg < 16; ++rg) { int dist = dq - (32 * kb + (rg & 3) + 8 * (rg >> 2)); dist = dist < 0 ? 0 : (dist > 128 ? 128 : dist); p[kb][rg] += lut[dist]; }
;                 }
	v_mov_b32_e32 v121, v110
	s_add_i32 s1, 0, 0x1f800
	v_add_u32_e32 v123, -1, v121
	v_add_u32_e32 v124, -2, v121
	v_add_u32_e32 v125, -3, v121
	v_add_u32_e32 v126, -8, v121
	v_add_u32_e32 v127, -9, v121
	v_add_u32_e32 v128, -10, v121
	v_add_u32_e32 v129, -11, v121
	v_add_u32_e32 v130, -16, v121
	v_subrev_u32_e32 v131, 17, v121
	v_subrev_u32_e32 v132, 18, v121
	v_subrev_u32_e32 v133, 19, v121
	v_subrev_u32_e32 v134, 24, v121
	v_subrev_u32_e32 v135, 25, v121
	v_subrev_u32_e32 v136, 26, v121
	v_subrev_u32_e32 v137, 27, v121
	v_subrev_u32_e32 v138, 32, v121
	v_subrev_u32_e32 v139, 33, v121
	v_subrev_u32_e32 v140, 34, v121
	v_subrev_u32_e32 v141, 35, v121
	v_subrev_u32_e32 v142, 40, v121
	v_subrev_u32_e32 v143, 41, v121
	v_subrev_u32_e32 v144, 42, v121
	v_subrev_u32_e32 v145, 43, v121
	v_subrev_u32_e32 v146, 48, v121
	v_subrev_u32_e32 v147, 49, v121
	v_subrev_u32_e32 v148, 50, v121
	v_subrev_u32_e32 v149, 51, v121
	v_subrev_u32_e32 v150, 56, v121
	v_subrev_u32_e32 v151, 57, v121
	v_subrev_u32_e32 v152, 58, v121
	v_med3_i32 v122, v121, 0, v93
	v_med3_i32 v123, v123, 0, v93
	v_med3_i32 v124, v124, 0, v93
	v_med3_i32 v125, v125, 0, v93
	v_med3_i32 v126, v126, 0, v93
	v_med3_i32 v127, v127, 0, v93
	v_med3_i32 v128, v128, 0, v93
	v_med3_i32 v129, v129, 0, v93
	v_med3_i32 v130, v130, 0, v93
	v_med3_i32 v131, v131, 0, v93
	v_med3_i32 v132, v132, 0, v93
	v_med3_i32 v133, v133, 0, v93
	v_med3_i32 v134, v134, 0, v93
	v_med3_i32 v135, v135, 0, v93
	v_med3_i32 v136, v136, 0, v93
	v_med3_i32 v137, v137, 0, v93
	v_med3_i32 v138, v138, 0, v93
	v_med3_i32 v139, v139, 0, v93
	v_med3_i32 v140, v140, 0, v93
	v_med3_i32 v141, v141, 0, v93
	v_med3_i32 v142, v142, 0, v93
	v_med3_i32 v143, v143, 0, v93
	v_med3_i32 v144, v144, 0, v93
	v_med3_i32 v145, v145, 0, v93
	v_med3_i32 v146, v146, 0, v93
	v_med3_i32 v147, v147, 0, v93
	v_med3_i32 v148, v148, 0, v93
	v_med3_i32 v149, v149, 0, v93
	v_med3_i32 v150, v150, 0, v93
	v_med3_i32 v151, v151, 0, v93
	v_med3_i32 v152, v152, 0, v93
	v_subrev_u32_e32 v121, 59, v121
	v_lshl_add_u32 v122, v122, 2, s1
	v_lshl_add_u32 v123, v123, 2, s1
	v_lshl_add_u32 v124, v124, 2, s1
	v_lshl_add_u32 v125, v125, 2, s1
	v_lshl_add_u32 v126, v126, 2, s1
	v_lshl_add_u32 v127, v127, 2, s1
	v_lshl_add_u32 v128, v128, 2, s1
	v_lshl_add_u32 v129, v129, 2, s1
	v_lshl_add_u32 v130, v130, 2, s1
	v_lshl_add_u32 v131, v131, 2, s1
	v_lshl_add_u32 v132, v132, 2, s1
	v_lshl_add_u32 v133, v133, 2, s1
	v_lshl_add_u32 v134, v134, 2, s1
	v_lshl_add_u32 v135, v135, 2, s1
	v_lshl_add_u32 v136, v136, 2, s1
	v_lshl_add_u32 v137, v137, 2, s1
	v_lshl_add_u32 v138, v138, 2, s1
	v_lshl_add_u32 v139, v139, 2, s1
	v_lshl_add_u32 v140, v140, 2, s1
	v_lshl_add_u32 v141, v141, 2, s1
	v_lshl_add_u32 v142, v142, 2, s1
	v_lshl_add_u32 v143, v143, 2, s1
	v_lshl_add_u32 v144, v144, 2, s1
	v_lshl_add_u32 v145, v145, 2, s1
	v_lshl_add_u32 v146, v146, 2, s1
	v_lshl_add_u32 v147, v147, 2, s1
	v_lshl_add_u32 v148, v148, 2, s1
	v_lshl_add_u32 v149, v149, 2, s1
	v_lshl_add_u32 v150, v150, 2, s1
	v_lshl_add_u32 v151, v151, 2, s1
	v_lshl_add_u32 v152, v152, 2, s1
	v_med3_i32 v121, v121, 0, v93
	ds_read_b32 v122, v122
	ds_read_b32 v123, v123
	ds_read_b32 v124, v124
	ds_read_b32 v125, v125
	ds_read_b32 v126, v126
	ds_read_b32 v127, v127
	ds_read_b32 v128, v128
	ds_read_b32 v129, v129
	ds_read_b32 v130, v130
	ds_read_b32 v131, v131
	ds_read_b32 v132, v132
	ds_read_b32 v133, v133
	ds_read_b32 v134, v134
	ds_read_b32 v135, v135
	ds_read_b32 v136, v136
	ds_read_b32 v137, v137
	ds_read_b32 v138, v138
	ds_read_b32 v139, v139
	ds_read_b32 v140, v140
	ds_read_b32 v141, v141
	ds_read_b32 v142, v142
	ds_read_b32 v143, v143
	ds_read_b32 v144, v144
	ds_read_b32 v145, v145
	v_lshl_add_u32 v121, v121, 2, s1
	ds_read_b32 v146, v146
	ds_read_b32 v147, v147
	ds_read_b32 v148, v148
	ds_read_b32 v149, v149
	ds_read_b32 v150, v150
	ds_read_b32 v151, v151
	ds_read_b32 v152, v152
	ds_read_b32 v153, v121
	s_waitcnt lgkmcnt(14)
	v_pk_add_f32 v[44:45], v[44:45], v[134:135]
	v_pk_add_f32 v[46:47], v[46:47], v[136:137]
	v_pk_add_f32 v[42:43], v[42:43], v[132:133]
	v_pk_add_f32 v[40:41], v[40:41], v[130:131]
	v_pk_add_f32 v[38:39], v[38:39], v[128:129]
	v_pk_add_f32 v[36:37], v[36:37], v[126:127]
	v_pk_add_f32 v[34:35], v[34:35], v[124:125]
	v_pk_add_f32 v[32:33], v[32:33], v[122:123]
	s_waitcnt lgkmcnt(0)
	v_pk_add_f32 v[62:63], v[62:63], v[152:153]
	v_pk_add_f32 v[60:61], v[60:61], v[150:151]
	v_pk_add_f32 v[58:59], v[58:59], v[148:149]
	v_pk_add_f32 v[56:57], v[56:57], v[146:147]
	v_pk_add_f32 v[54:55], v[54:55], v[144:145]
	v_pk_add_f32 v[52:53], v[52:53], v[142:143]
	v_pk_add_f32 v[50:51], v[50:51], v[140:141]
	v_pk_add_f32 v[48:49], v[48:49], v[138:139]

; #define LAS __attribute__((address_space(3)))
; template <int MODE, int DQK, int DV>
; __device__ __forceinline__ void attn_pass(LAS unsigned char* lds, const Tens& T, size_t rowbase, int q0, f32x16 (&o)[DV / 32], float& l_out, const int wave, QPre* qp = nullptr) {
;     ...
;             u32x2 mw = {0u, 0u};
;             if (MODE == AM_DSA) mw = *(const LAS u32x2*)(lds + OFF_MW + (sl * NSUB + sub) * 2048 + (wave * 32 + r) * 8);
;             f32x16 p[2];
;             const int kbase = 64 * j;
;             const bool diag = (kbase + 63 > q0 + wave * 32);
;             const bool nearb = (kbase + 63 + 128 > q0 + wave * 32);
;             constexpr bool POSTHOC = (MODE != AM_FOX);
;             constexpr float BIG = 65536.0f;
;             bool redo = (it == 0);
;             float psum;
;             for (;;) {
; #pragma unroll
;             for (int kb = 0; kb < 2; ++kb) {
;                 if (MODE == AM_FOX) {
;                     const float ctm = ct2 - m;
; #pragma unroll
;                     for (int g = 0; g < 4; ++g) {
;                         const f32x4 c = *(const LAS f32x4*)(lds + OFF_CS + (sl * NSUB + sub) * 256 + (32 * kb + 8 * g + 4 * h) * 4);
;                         p[kb][4 * g + 0] = fmaf(-LOG2E, c.x, ctm); p[kb][4 * g + 1] = fmaf(-LOG2E, c.y, ctm); p[kb][4 * g + 2] = fmaf(-LOG2E, c.z, ctm); p[kb][4 * g + 3] = fmaf(-LOG2E, c.w, ctm);
;                     }
;                 } else if (MODE == AM_DSA) {
; #pragma unroll
;                     for (int g = 0; g < 4; ++g) {
;                         const unsigned nib = __builtin_amdgcn_ubfe(mw[kb], (unsigned)(8 * g + 4 * h), 4u);
;                         const f32x4 t4 = *(const LAS f32x4*)(lds + OFF_LUT + 768 + nib * 16);
;                         p[kb][4 * g + 0] = t4.x; p[kb][4 * g + 1] = t4.y; p[kb][4 * g + 2] = t4.z; p[kb][4 * g + 3] = t4.w;
;                     }
;                     p[kb] = __builtin_amdgcn_mfma_f32_32x32x16_bf16(kone, qm, p[kb], 0, 0, 0);
;                 }
; #pragma unroll
;                 for (int s = 0; s < NSTEP; ++s) {
;                     bf16x8 a;
;                     if (s < 4) a = *(const LAS bf16x8*)(kfa[s] + sl * KSL + sub * KB_T + kb * 4096);
;                     else       a = *(const LAS bf16x8*)(kfa[s] + sl * KSL + sub * KB_T + kb * 2048);
;                     if ((MODE == AM_DIFF || MODE == AM_MLA) && s == 0)
.LBB0_1670:
	v_add_u32_e32 v32, s70, v105
	ds_read_b64 v[32:33], v32
	s_add_i32 s0, s11, 0x17f
	s_cmp_gt_u32 s0, s83
	s_cselect_b64 s[34:35], -1, 0
	s_cmp_le_u32 s0, s83
	s_waitcnt lgkmcnt(0)
	v_bfe_u32 v114, v32, v106, 4
	v_bfe_u32 v115, v32, v107, 4
	v_bfe_u32 v121, v32, v109, 4
	v_bfe_u32 v116, v33, v106, 4
	v_bfe_u32 v117, v33, v107, 4
	v_bfe_u32 v118, v33, v108, 4
	v_bfe_u32 v120, v32, v108, 4
	v_bfe_u32 v119, v33, v109, 4
	v_lshl_add_u32 v114, v114, 4, s79
	v_lshl_add_u32 v115, v115, 4, s79
	v_lshl_add_u32 v121, v121, 4, s79
	v_lshl_add_u32 v116, v116, 4, s79
	v_lshl_add_u32 v117, v117, 4, s79
	v_lshl_add_u32 v118, v118, 4, s79
	v_lshl_add_u32 v120, v120, 4, s79
	v_lshl_add_u32 v119, v119, 4, s79
	ds_read_b128 v[32:35], v114
	ds_read_b128 v[36:39], v115
	ds_read_b128 v[40:43], v120
	ds_read_b128 v[44:47], v121
	ds_read_b128 v[188:191], v96 offset:24576
	ds_read_b128 v[192:195], v97 offset:24576
	ds_read_b128 v[196:199], v98 offset:24576
	ds_read_b128 v[200:203], v99 offset:24576
	ds_read_b128 v[48:51], v116
	ds_read_b128 v[52:55], v117
	ds_read_b128 v[56:59], v118
	ds_read_b128 v[60:63], v119
	ds_read_b128 v[204:207], v96 offset:28672
	ds_read_b128 v[208:211], v97 offset:28672
	ds_read_b128 v[212:215], v98 offset:28672
	s_waitcnt lgkmcnt(11)
	v_mfma_f32_32x32x16_bf16 v[32:47], v[68:71], v[64:67], v[32:47]
	ds_read_b128 v[216:219], v99 offset:28672
	v_subrev_u32_e32 v113, 64, v110
	s_waitcnt lgkmcnt(11)
	v_mfma_f32_32x32x16_bf16 v[32:47], v[188:191], v[72:75], v[32:47]
	s_waitcnt lgkmcnt(10)
	v_mfma_f32_32x32x16_bf16 v[32:47], v[192:195], v[76:79], v[32:47]
	s_waitcnt lgkmcnt(9)
	v_mfma_f32_32x32x16_bf16 v[32:47], v[196:199], v[80:83], v[32:47]
	s_waitcnt lgkmcnt(8)
	v_mfma_f32_32x32x16_bf16 v[32:47], v[200:203], v[84:87], v[32:47]
	s_waitcnt lgkmcnt(4)
	v_mfma_f32_32x32x16_bf16 v[48:63], v[68:71], v[64:67], v[48:63]
	s_waitcnt lgkmcnt(3)
	v_mfma_f32_32x32x16_bf16 v[48:63], v[204:207], v[72:75], v[48:63]
	s_waitcnt lgkmcnt(2)
	v_mfma_f32_32x32x16_bf16 v[48:63], v[208:211], v[76:79], v[48:63]
	s_waitcnt lgkmcnt(1)
	v_mfma_f32_32x32x16_bf16 v[48:63], v[212:215], v[80:83], v[48:63]
	s_waitcnt lgkmcnt(0)
	v_mfma_f32_32x32x16_bf16 v[48:63], v[216:219], v[84:87], v[48:63]
	ds_read_b64_tr_b16 v[156:157], v101 offset:24576
	ds_read_b64_tr_b16 v[158:159], v101 offset:25600
	ds_read_b64_tr_b16 v[160:161], v101 offset:26624
	ds_read_b64_tr_b16 v[162:163], v101 offset:27648
	ds_read_b64_tr_b16 v[164:165], v101 offset:28672
	ds_read_b64_tr_b16 v[166:167], v101 offset:29696
	ds_read_b64_tr_b16 v[168:169], v101 offset:30720
	ds_read_b64_tr_b16 v[170:171], v101 offset:31744
	ds_read_b64_tr_b16 v[172:173], v102 offset:24576
	ds_read_b64_tr_b16 v[174:175], v102 offset:25600
	ds_read_b64_tr_b16 v[176:177], v102 offset:26624
	ds_read_b64_tr_b16 v[178:179], v102 offset:27648
	ds_read_b64_tr_b16 v[180:181], v102 offset:28672
	ds_read_b64_tr_b16 v[182:183], v102 offset:29696
	ds_read_b64_tr_b16 v[184:185], v102 offset:30720
	ds_read_b64_tr_b16 v[186:187], v102 offset:31744
	s_cbranch_scc1 .LBB0_1672
; template <int MODE, int DQK, int DV>
; __device__ __forceinline__ void attn_pass(LAS unsigned char* lds, const Tens& T, size_t rowbase, int q0, f32x16 (&o)[DV / 32], float& l_out, const int wave, QPre* qp = nullptr) {
;     ...
;             if (MODE == AM_DSA || MODE == AM_DIFF) {
;                 if (nearb) {
;                     int dq = tq - kbase - 4 * h; asm volatile("" : "+v"(dq));
; #pragma unroll
;                     for (int kb = 0; kb < 2; ++kb)
; #pragma unroll
;                         for (int rg = 0; rg < 16; ++rg) { int dist = dq - (32 * kb + (rg & 3) + 8 * (rg >> 2)); dist = dist < 0 ? 0 : (dist > 128 ? 128 : dist); p[kb][rg] += lut[dist]; }
;                 }
	v_mov_b32_e32 v146, v113
	s_add_i32 s0, 0, 0x1f800
	v_add_u32_e32 v123, -1, v146
	v_add_u32_e32 v124, -2, v146
	v_add_u32_e32 v125, -3, v146
	v_add_u32_e32 v126, -8, v146
	v_add_u32_e32 v127, -9, v146
	v_add_u32_e32 v128, -10, v146
	v_add_u32_e32 v129, -11, v146
	v_add_u32_e32 v130, -16, v146
	v_subrev_u32_e32 v131, 17, v146
	v_subrev_u32_e32 v132, 18, v146
	v_subrev_u32_e32 v133, 19, v146
	v_subrev_u32_e32 v134, 24, v146
	v_subrev_u32_e32 v135, 25, v146
	v_subrev_u32_e32 v136, 26, v146
	v_subrev_u32_e32 v137, 27, v146
	v_subrev_u32_e32 v138, 32, v146
	v_subrev_u32_e32 v139, 33, v146
	v_subrev_u32_e32 v140, 34, v146
	v_subrev_u32_e32 v141, 35, v146
	v_subrev_u32_e32 v142, 40, v146
	v_subrev_u32_e32 v143, 41, v146
	v_subrev_u32_e32 v144, 42, v146
	v_subrev_u32_e32 v145, 43, v146
	v_subrev_u32_e32 v147, 48, v146
	v_subrev_u32_e32 v148, 49, v146
	v_subrev_u32_e32 v149, 50, v146
	v_subrev_u32_e32 v150, 51, v146
	v_subrev_u32_e32 v151, 56, v146
	v_subrev_u32_e32 v152, 57, v146
	v_subrev_u32_e32 v153, 58, v146
	v_med3_i32 v122, v146, 0, v93
	v_med3_i32 v123, v123, 0, v93
	v_med3_i32 v124, v124, 0, v93
	v_med3_i32 v125, v125, 0, v93
	v_med3_i32 v126, v126, 0, v93
	v_med3_i32 v127, v127, 0, v93
	v_med3_i32 v128, v128, 0, v93
	v_med3_i32 v129, v129, 0, v93
	v_med3_i32 v130, v130, 0, v93
	v_med3_i32 v131, v131, 0, v93
	v_med3_i32 v132, v132, 0, v93
	v_med3_i32 v133, v133, 0, v93
	v_med3_i32 v134, v134, 0, v93
	v_med3_i32 v135, v135, 0, v93
	v_med3_i32 v136, v136, 0, v93
	v_med3_i32 v137, v137, 0, v93
	v_med3_i32 v138, v138, 0, v93
	v_med3_i32 v139, v139, 0, v93
	v_med3_i32 v140, v140, 0, v93
	v_med3_i32 v141, v141, 0, v93
	v_med3_i32 v142, v142, 0, v93
	v_med3_i32 v143, v143, 0, v93
	v_med3_i32 v144, v144, 0, v93
	v_med3_i32 v145, v145, 0, v93
	v_med3_i32 v147, v147, 0, v93
	v_med3_i32 v148, v148, 0, v93
	v_med3_i32 v149, v149, 0, v93
	v_med3_i32 v150, v150, 0, v93
	v_med3_i32 v151, v151, 0, v93
	v_med3_i32 v152, v152, 0, v93
	v_med3_i32 v153, v153, 0, v93
	v_subrev_u32_e32 v146, 59, v146
	v_lshl_add_u32 v122, v122, 2, s0
	v_lshl_add_u32 v123, v123, 2, s0
	v_lshl_add_u32 v124, v124, 2, s0
	v_lshl_add_u32 v125, v125, 2, s0
	v_lshl_add_u32 v126, v126, 2, s0
	v_lshl_add_u32 v127, v127, 2, s0
	v_lshl_add_u32 v128, v128, 2, s0
	v_lshl_add_u32 v129, v129, 2, s0
	v_lshl_add_u32 v130, v130, 2, s0
	v_lshl_add_u32 v131, v131, 2, s0
	v_lshl_add_u32 v132, v132, 2, s0
	v_lshl_add_u32 v133, v133, 2, s0
	v_lshl_add_u32 v134, v134, 2, s0
	v_lshl_add_u32 v135, v135, 2, s0
	v_lshl_add_u32 v136, v136, 2, s0
	v_lshl_add_u32 v137, v137, 2, s0
	v_lshl_add_u32 v138, v138, 2, s0
	v_lshl_add_u32 v139, v139, 2, s0
	v_lshl_add_u32 v140, v140, 2, s0
	v_lshl_add_u32 v141, v141, 2, s0
	v_lshl_add_u32 v142, v142, 2, s0
	v_lshl_add_u32 v143, v143, 2, s0
	v_lshl_add_u32 v144, v144, 2, s0
	v_lshl_add_u32 v145, v145, 2, s0
	v_lshl_add_u32 v147, v147, 2, s0
	v_lshl_add_u32 v148, v148, 2, s0
	v_lshl_add_u32 v149, v149, 2, s0
	v_lshl_add_u32 v150, v150, 2, s0
	v_lshl_add_u32 v151, v151, 2, s0
	v_lshl_add_u32 v152, v152, 2, s0
	v_lshl_add_u32 v153, v153, 2, s0
	v_med3_i32 v146, v146, 0, v93
	ds_read_b32 v122, v122
	ds_read_b32 v123, v123
	ds_read_b32 v124, v124
	ds_read_b32 v125, v125
	ds_read_b32 v126, v126
	ds_read_b32 v127, v127
	ds_read_b32 v128, v128
	ds_read_b32 v129, v129
	ds_read_b32 v130, v130
	ds_read_b32 v131, v131
	ds_read_b32 v132, v132
	ds_read_b32 v133, v133
	ds_read_b32 v134, v134
	ds_read_b32 v135, v135
	ds_read_b32 v136, v136
	ds_read_b32 v137, v137
	ds_read_b32 v138, v138
	ds_read_b32 v139, v139
	ds_read_b32 v140, v140
	ds_read_b32 v141, v141
	ds_read_b32 v142, v142
	ds_read_b32 v143, v143
	ds_read_b32 v144, v144
	ds_read_b32 v145, v145
	v_lshl_add_u32 v154, v146, 2, s0
	ds_read_b32 v146, v147
	ds_read_b32 v147, v148
	ds_read_b32 v148, v149
	ds_read_b32 v149, v150
	ds_read_b32 v150, v151
	ds_read_b32 v151, v152
	ds_read_b32 v152, v153
	ds_read_b32 v153, v154
	s_waitcnt lgkmcnt(14)
	v_pk_add_f32 v[44:45], v[44:45], v[134:135]
	v_pk_add_f32 v[46:47], v[46:47], v[136:137]
	v_pk_add_f32 v[42:43], v[42:43], v[132:133]
	v_pk_add_f32 v[40:41], v[40:41], v[130:131]
	v_pk_add_f32 v[38:39], v[38:39], v[128:129]
	v_pk_add_f32 v[36:37], v[36:37], v[126:127]
	v_pk_add_f32 v[34:35], v[34:35], v[124:125]
	v_pk_add_f32 v[32:33], v[32:33], v[122:123]
	s_waitcnt lgkmcnt(0)
	v_pk_add_f32 v[62:63], v[62:63], v[152:153]
	v_pk_add_f32 v[60:61], v[60:61], v[150:151]
	v_pk_add_f32 v[58:59], v[58:59], v[148:149]
	v_pk_add_f32 v[56:57], v[56:57], v[146:147]
	v_pk_add_f32 v[54:55], v[54:55], v[144:145]
	v_pk_add_f32 v[52:53], v[52:53], v[142:143]
	v_pk_add_f32 v[50:51], v[50:51], v[140:141]
	v_pk_add_f32 v[48:49], v[48:49], v[138:139]

; #define LAS __attribute__((address_space(3)))
; template <int MODE, int DQK, int DV>
; __device__ __forceinline__ void attn_pass(LAS unsigned char* lds, const Tens& T, size_t rowbase, int q0, f32x16 (&o)[DV / 32], float& l_out, const int wave, QPre* qp = nullptr) {
;     ...
;             u32x2 mw = {0u, 0u};
;             if (MODE == AM_DSA) mw = *(const LAS u32x2*)(lds + OFF_MW + (sl * NSUB + sub) * 2048 + (wave * 32 + r) * 8);
;             f32x16 p[2];
;             const int kbase = 64 * j;
;             const bool diag = (kbase + 63 > q0 + wave * 32);
;             const bool nearb = (kbase + 63 + 128 > q0 + wave * 32);
;             constexpr bool POSTHOC = (MODE != AM_FOX);
;             constexpr float BIG = 65536.0f;
;             bool redo = (it == 0);
;             float psum;
;             for (;;) {
; #pragma unroll
;             for (int kb = 0; kb < 2; ++kb) {
;                 if (MODE == AM_FOX) {
;                     const float ctm = ct2 - m;
; #pragma unroll
;                     for (int g = 0; g < 4; ++g) {
;                         const f32x4 c = *(const LAS f32x4*)(lds + OFF_CS + (sl * NSUB + sub) * 256 + (32 * kb + 8 * g + 4 * h) * 4);
;                         p[kb][4 * g + 0] = fmaf(-LOG2E, c.x, ctm); p[kb][4 * g + 1] = fmaf(-LOG2E, c.y, ctm); p[kb][4 * g + 2] = fmaf(-LOG2E, c.z, ctm); p[kb][4 * g + 3] = fmaf(-LOG2E, c.w, ctm);
;                     }
;                 } else if (MODE == AM_DSA) {
; #pragma unroll
;                     for (int g = 0; g < 4; ++g) {
;                         const unsigned nib = __builtin_amdgcn_ubfe(mw[kb], (unsigned)(8 * g + 4 * h), 4u);
;                         const f32x4 t4 = *(const LAS f32x4*)(lds + OFF_LUT + 768 + nib * 16);
;                         p[kb][4 * g + 0] = t4.x; p[kb][4 * g + 1] = t4.y; p[kb][4 * g + 2] = t4.z; p[kb][4 * g + 3] = t4.w;
;                     }
;                     p[kb] = __builtin_amdgcn_mfma_f32_32x32x16_bf16(kone, qm, p[kb], 0, 0, 0);
;                 }
; #pragma unroll
;                 for (int s = 0; s < NSTEP; ++s) {
;                     bf16x8 a;
;                     if (s < 4) a = *(const LAS bf16x8*)(kfa[s] + sl * KSL + sub * KB_T + kb * 4096);
;                     else       a = *(const LAS bf16x8*)(kfa[s] + sl * KSL + sub * KB_T + kb * 2048);
;                     if ((MODE == AM_DIFF || MODE == AM_MLA) && s == 0)
.LBB0_1678:
	v_add_u32_e32 v32, s71, v105
	ds_read_b64 v[32:33], v32
	s_add_i32 s1, s11, 0x1bf
	s_cmp_gt_u32 s1, s83
	s_cselect_b64 s[30:31], -1, 0
	s_cmp_le_u32 s1, s83
	s_waitcnt lgkmcnt(0)
	v_bfe_u32 v114, v32, v106, 4
	v_bfe_u32 v115, v32, v107, 4
	v_bfe_u32 v121, v32, v109, 4
	v_bfe_u32 v116, v33, v106, 4
	v_bfe_u32 v117, v33, v107, 4
	v_bfe_u32 v118, v33, v108, 4
	v_bfe_u32 v120, v32, v108, 4
	v_bfe_u32 v119, v33, v109, 4
	v_lshl_add_u32 v114, v114, 4, s79
	v_lshl_add_u32 v115, v115, 4, s79
	v_lshl_add_u32 v121, v121, 4, s79
	v_lshl_add_u32 v116, v116, 4, s79
	v_lshl_add_u32 v117, v117, 4, s79
	v_lshl_add_u32 v118, v118, 4, s79
	v_lshl_add_u32 v120, v120, 4, s79
	v_lshl_add_u32 v119, v119, 4, s79
	ds_read_b128 v[32:35], v114
	ds_read_b128 v[36:39], v115
	ds_read_b128 v[40:43], v120
	ds_read_b128 v[44:47], v121
	ds_read_b128 v[188:191], v96 offset:32768
	ds_read_b128 v[192:195], v97 offset:32768
	ds_read_b128 v[196:199], v98 offset:32768
	ds_read_b128 v[200:203], v99 offset:32768
	ds_read_b128 v[48:51], v116
	ds_read_b128 v[52:55], v117
	ds_read_b128 v[56:59], v118
	ds_read_b128 v[60:63], v119
	ds_read_b128 v[204:207], v96 offset:36864
	ds_read_b128 v[208:211], v97 offset:36864
	ds_read_b128 v[212:215], v98 offset:36864
	s_waitcnt lgkmcnt(11)
	v_mfma_f32_32x32x16_bf16 v[32:47], v[68:71], v[64:67], v[32:47]
	ds_read_b128 v[216:219], v99 offset:36864
	v_add_u32_e32 v113, 0xffffff80, v110
	s_waitcnt lgkmcnt(11)
	v_mfma_f32_32x32x16_bf16 v[32:47], v[188:191], v[72:75], v[32:47]
	s_waitcnt lgkmcnt(10)
	v_mfma_f32_32x32x16_bf16 v[32:47], v[192:195], v[76:79], v[32:47]
	s_waitcnt lgkmcnt(9)
	v_mfma_f32_32x32x16_bf16 v[32:47], v[196:199], v[80:83], v[32:47]
	s_waitcnt lgkmcnt(8)
	v_mfma_f32_32x32x16_bf16 v[32:47], v[200:203], v[84:87], v[32:47]
	s_waitcnt lgkmcnt(4)
	v_mfma_f32_32x32x16_bf16 v[48:63], v[68:71], v[64:67], v[48:63]
	s_waitcnt lgkmcnt(3)
	v_mfma_f32_32x32x16_bf16 v[48:63], v[204:207], v[72:75], v[48:63]
	s_waitcnt lgkmcnt(2)
	v_mfma_f32_32x32x16_bf16 v[48:63], v[208:211], v[76:79], v[48:63]
	s_waitcnt lgkmcnt(1)
	v_mfma_f32_32x32x16_bf16 v[48:63], v[212:215], v[80:83], v[48:63]
	s_waitcnt lgkmcnt(0)
	v_mfma_f32_32x32x16_bf16 v[48:63], v[216:219], v[84:87], v[48:63]
	ds_read_b64_tr_b16 v[156:157], v101 offset:32768
	ds_read_b64_tr_b16 v[158:159], v101 offset:33792
	ds_read_b64_tr_b16 v[160:161], v101 offset:34816
	ds_read_b64_tr_b16 v[162:163], v101 offset:35840
	ds_read_b64_tr_b16 v[164:165], v101 offset:36864
	ds_read_b64_tr_b16 v[166:167], v101 offset:37888
	ds_read_b64_tr_b16 v[168:169], v101 offset:38912
	ds_read_b64_tr_b16 v[170:171], v101 offset:39936
	ds_read_b64_tr_b16 v[172:173], v102 offset:32768
	ds_read_b64_tr_b16 v[174:175], v102 offset:33792
	ds_read_b64_tr_b16 v[176:177], v102 offset:34816
	ds_read_b64_tr_b16 v[178:179], v102 offset:35840
	ds_read_b64_tr_b16 v[180:181], v102 offset:36864
	ds_read_b64_tr_b16 v[182:183], v102 offset:37888
	ds_read_b64_tr_b16 v[184:185], v102 offset:38912
	ds_read_b64_tr_b16 v[186:187], v102 offset:39936
	s_cbranch_scc1 .LBB0_1680
; template <int MODE, int DQK, int DV>
; __device__ __forceinline__ void attn_pass(LAS unsigned char* lds, const Tens& T, size_t rowbase, int q0, f32x16 (&o)[DV / 32], float& l_out, const int wave, QPre* qp = nullptr) {
;     ...
;             if (MODE == AM_DSA || MODE == AM_DIFF) {
;                 if (nearb) {
;                     int dq = tq - kbase - 4 * h; asm volatile("" : "+v"(dq));
; #pragma unroll
;                     for (int kb = 0; kb < 2; ++kb)
; #pragma unroll
;                         for (int rg = 0; rg < 16; ++rg) { int dist = dq - (32 * kb + (rg & 3) + 8 * (rg >> 2)); dist = dist < 0 ? 0 : (dist > 128 ? 128 : dist); p[kb][rg] += lut[dist]; }
;                 }
	v_mov_b32_e32 v146, v113
	s_add_i32 s1, 0, 0x1f800
	v_add_u32_e32 v123, -1, v146
	v_add_u32_e32 v124, -2, v146
	v_add_u32_e32 v125, -3, v146
	v_add_u32_e32 v126, -8, v146
	v_add_u32_e32 v127, -9, v146
	v_add_u32_e32 v128, -10, v146
	v_add_u32_e32 v129, -11, v146
	v_add_u32_e32 v130, -16, v146
	v_subrev_u32_e32 v131, 17, v146
	v_subrev_u32_e32 v132, 18, v146
	v_subrev_u32_e32 v133, 19, v146
	v_subrev_u32_e32 v134, 24, v146
	v_subrev_u32_e32 v135, 25, v146
	v_subrev_u32_e32 v136, 26, v146
	v_subrev_u32_e32 v137, 27, v146
	v_subrev_u32_e32 v138, 32, v146
	v_subrev_u32_e32 v139, 33, v146
	v_subrev_u32_e32 v140, 34, v146
	v_subrev_u32_e32 v141, 35, v146
	v_subrev_u32_e32 v142, 40, v146
	v_subrev_u32_e32 v143, 41, v146
	v_subrev_u32_e32 v144, 42, v146
	v_subrev_u32_e32 v145, 43, v146
	v_subrev_u32_e32 v147, 48, v146
	v_subrev_u32_e32 v148, 49, v146
	v_subrev_u32_e32 v149, 50, v146
	v_subrev_u32_e32 v150, 51, v146
	v_subrev_u32_e32 v151, 56, v146
	v_subrev_u32_e32 v152, 57, v146
	v_subrev_u32_e32 v153, 58, v146
	v_med3_i32 v122, v146, 0, v93
	v_med3_i32 v123, v123, 0, v93
	v_med3_i32 v124, v124, 0, v93
	v_med3_i32 v125, v125, 0, v93
	v_med3_i32 v126, v126, 0, v93
	v_med3_i32 v127, v127, 0, v93
	v_med3_i32 v128, v128, 0, v93
	v_med3_i32 v129, v129, 0, v93
	v_med3_i32 v130, v130, 0, v93
	v_med3_i32 v131, v131, 0, v93
	v_med3_i32 v132, v132, 0, v93
	v_med3_i32 v133, v133, 0, v93
	v_med3_i32 v134, v134, 0, v93
	v_med3_i32 v135, v135, 0, v93
	v_med3_i32 v136, v136, 0, v93
	v_med3_i32 v137, v137, 0, v93
	v_med3_i32 v138, v138, 0, v93
	v_med3_i32 v139, v139, 0, v93
	v_med3_i32 v140, v140, 0, v93
	v_med3_i32 v141, v141, 0, v93
	v_med3_i32 v142, v142, 0, v93
	v_med3_i32 v143, v143, 0, v93
	v_med3_i32 v144, v144, 0, v93
	v_med3_i32 v145, v145, 0, v93
	v_med3_i32 v147, v147, 0, v93
	v_med3_i32 v148, v148, 0, v93
	v_med3_i32 v149, v149, 0, v93
	v_med3_i32 v150, v150, 0, v93
	v_med3_i32 v151, v151, 0, v93
	v_med3_i32 v152, v152, 0, v93
	v_med3_i32 v153, v153, 0, v93
	v_subrev_u32_e32 v146, 59, v146
	v_lshl_add_u32 v122, v122, 2, s1
	v_lshl_add_u32 v123, v123, 2, s1
	v_lshl_add_u32 v124, v124, 2, s1
	v_lshl_add_u32 v125, v125, 2, s1
	v_lshl_add_u32 v126, v126, 2, s1
	v_lshl_add_u32 v127, v127, 2, s1
	v_lshl_add_u32 v128, v128, 2, s1
	v_lshl_add_u32 v129, v129, 2, s1
	v_lshl_add_u32 v130, v130, 2, s1
	v_lshl_add_u32 v131, v131, 2, s1
	v_lshl_add_u32 v132, v132, 2, s1
	v_lshl_add_u32 v133, v133, 2, s1
	v_lshl_add_u32 v134, v134, 2, s1
	v_lshl_add_u32 v135, v135, 2, s1
	v_lshl_add_u32 v136, v136, 2, s1
	v_lshl_add_u32 v137, v137, 2, s1
	v_lshl_add_u32 v138, v138, 2, s1
	v_lshl_add_u32 v139, v139, 2, s1
	v_lshl_add_u32 v140, v140, 2, s1
	v_lshl_add_u32 v141, v141, 2, s1
	v_lshl_add_u32 v142, v142, 2, s1
	v_lshl_add_u32 v143, v143, 2, s1
	v_lshl_add_u32 v144, v144, 2, s1
	v_lshl_add_u32 v145, v145, 2, s1
	v_lshl_add_u32 v147, v147, 2, s1
	v_lshl_add_u32 v148, v148, 2, s1
	v_lshl_add_u32 v149, v149, 2, s1
	v_lshl_add_u32 v150, v150, 2, s1
	v_lshl_add_u32 v151, v151, 2, s1
	v_lshl_add_u32 v152, v152, 2, s1
	v_lshl_add_u32 v153, v153, 2, s1
	v_med3_i32 v146, v146, 0, v93
	ds_read_b32 v122, v122
	ds_read_b32 v123, v123
	ds_read_b32 v124, v124
	ds_read_b32 v125, v125
	ds_read_b32 v126, v126
	ds_read_b32 v127, v127
	ds_read_b32 v128, v128
	ds_read_b32 v129, v129
	ds_read_b32 v130, v130
	ds_read_b32 v131, v131
	ds_read_b32 v132, v132
	ds_read_b32 v133, v133
	ds_read_b32 v134, v134
	ds_read_b32 v135, v135
	ds_read_b32 v136, v136
	ds_read_b32 v137, v137
	ds_read_b32 v138, v138
	ds_read_b32 v139, v139
	ds_read_b32 v140, v140
	ds_read_b32 v141, v141
	ds_read_b32 v142, v142
	ds_read_b32 v143, v143
	ds_read_b32 v144, v144
	ds_read_b32 v145, v145
	v_lshl_add_u32 v154, v146, 2, s1
	ds_read_b32 v146, v147
	ds_read_b32 v147, v148
	ds_read_b32 v148, v149
	ds_read_b32 v149, v150
	ds_read_b32 v150, v151
	ds_read_b32 v151, v152
	ds_read_b32 v152, v153
	ds_read_b32 v153, v154
	s_waitcnt lgkmcnt(14)
	v_pk_add_f32 v[44:45], v[44:45], v[134:135]
	v_pk_add_f32 v[46:47], v[46:47], v[136:137]
	v_pk_add_f32 v[42:43], v[42:43], v[132:133]
	v_pk_add_f32 v[40:41], v[40:41], v[130:131]
	v_pk_add_f32 v[38:39], v[38:39], v[128:129]
	v_pk_add_f32 v[36:37], v[36:37], v[126:127]
	v_pk_add_f32 v[34:35], v[34:35], v[124:125]
	v_pk_add_f32 v[32:33], v[32:33], v[122:123]
	s_waitcnt lgkmcnt(0)
	v_pk_add_f32 v[62:63], v[62:63], v[152:153]
	v_pk_add_f32 v[60:61], v[60:61], v[150:151]
	v_pk_add_f32 v[58:59], v[58:59], v[148:149]
	v_pk_add_f32 v[56:57], v[56:57], v[146:147]
	v_pk_add_f32 v[54:55], v[54:55], v[144:145]
	v_pk_add_f32 v[52:53], v[52:53], v[142:143]
	v_pk_add_f32 v[50:51], v[50:51], v[140:141]
	v_pk_add_f32 v[48:49], v[48:49], v[138:139]

; #define LAS __attribute__((address_space(3)))
; template <int MODE, int DQK, int DV>
; __device__ __forceinline__ void attn_pass(LAS unsigned char* lds, const Tens& T, size_t rowbase, int q0, f32x16 (&o)[DV / 32], float& l_out, const int wave, QPre* qp = nullptr) {
;     ...
;             u32x2 mw = {0u, 0u};
;             if (MODE == AM_DSA) mw = *(const LAS u32x2*)(lds + OFF_MW + (sl * NSUB + sub) * 2048 + (wave * 32 + r) * 8);
;             f32x16 p[2];
;             const int kbase = 64 * j;
;             const bool diag = (kbase + 63 > q0 + wave * 32);
;             const bool nearb = (kbase + 63 + 128 > q0 + wave * 32);
;             constexpr bool POSTHOC = (MODE != AM_FOX);
;             constexpr float BIG = 65536.0f;
;             bool redo = (it == 0);
;             float psum;
;             for (;;) {
; #pragma unroll
;             for (int kb = 0; kb < 2; ++kb) {
;                 if (MODE == AM_FOX) {
;                     const float ctm = ct2 - m;
; #pragma unroll
;                     for (int g = 0; g < 4; ++g) {
;                         const f32x4 c = *(const LAS f32x4*)(lds + OFF_CS + (sl * NSUB + sub) * 256 + (32 * kb + 8 * g + 4 * h) * 4);
;                         p[kb][4 * g + 0] = fmaf(-LOG2E, c.x, ctm); p[kb][4 * g + 1] = fmaf(-LOG2E, c.y, ctm); p[kb][4 * g + 2] = fmaf(-LOG2E, c.z, ctm); p[kb][4 * g + 3] = fmaf(-LOG2E, c.w, ctm);
;                     }
;                 } else if (MODE == AM_DSA) {
; #pragma unroll
;                     for (int g = 0; g < 4; ++g) {
;                         const unsigned nib = __builtin_amdgcn_ubfe(mw[kb], (unsigned)(8 * g + 4 * h), 4u);
;                         const f32x4 t4 = *(const LAS f32x4*)(lds + OFF_LUT + 768 + nib * 16);
;                         p[kb][4 * g + 0] = t4.x; p[kb][4 * g + 1] = t4.y; p[kb][4 * g + 2] = t4.z; p[kb][4 * g + 3] = t4.w;
;                     }
;                     p[kb] = __builtin_amdgcn_mfma_f32_32x32x16_bf16(kone, qm, p[kb], 0, 0, 0);
;                 }
; #pragma unroll
;                 for (int s = 0; s < NSTEP; ++s) {
;                     bf16x8 a;
;                     if (s < 4) a = *(const LAS bf16x8*)(kfa[s] + sl * KSL + sub * KB_T + kb * 4096);
;                     else       a = *(const LAS bf16x8*)(kfa[s] + sl * KSL + sub * KB_T + kb * 2048);
;                     if ((MODE == AM_DIFF || MODE == AM_MLA) && s == 0)
.LBB0_1682:
	v_add_u32_e32 v32, s72, v105
	ds_read_b64 v[32:33], v32
	s_add_i32 s0, s11, 0x1ff
	s_cmp_gt_u32 s0, s83
	s_cselect_b64 s[30:31], -1, 0
	s_cmp_le_u32 s0, s83
	s_waitcnt lgkmcnt(0)
	v_bfe_u32 v114, v32, v106, 4
	v_bfe_u32 v115, v32, v107, 4
	v_bfe_u32 v121, v32, v109, 4
	v_bfe_u32 v116, v33, v106, 4
	v_bfe_u32 v117, v33, v107, 4
	v_bfe_u32 v118, v33, v108, 4
	v_bfe_u32 v120, v32, v108, 4
	v_bfe_u32 v119, v33, v109, 4
	v_lshl_add_u32 v114, v114, 4, s79
	v_lshl_add_u32 v115, v115, 4, s79
	v_lshl_add_u32 v121, v121, 4, s79
	v_lshl_add_u32 v116, v116, 4, s79
	v_lshl_add_u32 v117, v117, 4, s79
	v_lshl_add_u32 v118, v118, 4, s79
	v_lshl_add_u32 v120, v120, 4, s79
	v_lshl_add_u32 v119, v119, 4, s79
	ds_read_b128 v[32:35], v114
	ds_read_b128 v[36:39], v115
	ds_read_b128 v[40:43], v120
	ds_read_b128 v[44:47], v121
	ds_read_b128 v[188:191], v96 offset:40960
	ds_read_b128 v[192:195], v97 offset:40960
	ds_read_b128 v[196:199], v98 offset:40960
	ds_read_b128 v[200:203], v99 offset:40960
	ds_read_b128 v[48:51], v116
	ds_read_b128 v[52:55], v117
	ds_read_b128 v[56:59], v118
	ds_read_b128 v[60:63], v119
	ds_read_b128 v[204:207], v96 offset:45056
	ds_read_b128 v[208:211], v97 offset:45056
	ds_read_b128 v[212:215], v98 offset:45056
	s_waitcnt lgkmcnt(11)
	v_mfma_f32_32x32x16_bf16 v[32:47], v[68:71], v[64:67], v[32:47]
	ds_read_b128 v[216:219], v99 offset:45056
	v_add_u32_e32 v113, 0xffffff40, v110
	s_waitcnt lgkmcnt(11)
	v_mfma_f32_32x32x16_bf16 v[32:47], v[188:191], v[72:75], v[32:47]
	s_waitcnt lgkmcnt(10)
	v_mfma_f32_32x32x16_bf16 v[32:47], v[192:195], v[76:79], v[32:47]
	s_waitcnt lgkmcnt(9)
	v_mfma_f32_32x32x16_bf16 v[32:47], v[196:199], v[80:83], v[32:47]
	s_waitcnt lgkmcnt(8)
	v_mfma_f32_32x32x16_bf16 v[32:47], v[200:203], v[84:87], v[32:47]
	s_waitcnt lgkmcnt(4)
	v_mfma_f32_32x32x16_bf16 v[48:63], v[68:71], v[64:67], v[48:63]
	s_waitcnt lgkmcnt(3)
	v_mfma_f32_32x32x16_bf16 v[48:63], v[204:207], v[72:75], v[48:63]
	s_waitcnt lgkmcnt(2)
	v_mfma_f32_32x32x16_bf16 v[48:63], v[208:211], v[76:79], v[48:63]
	s_waitcnt lgkmcnt(1)
	v_mfma_f32_32x32x16_bf16 v[48:63], v[212:215], v[80:83], v[48:63]
	s_waitcnt lgkmcnt(0)
	v_mfma_f32_32x32x16_bf16 v[48:63], v[216:219], v[84:87], v[48:63]
	ds_read_b64_tr_b16 v[156:157], v101 offset:40960
	ds_read_b64_tr_b16 v[158:159], v101 offset:41984
	ds_read_b64_tr_b16 v[160:161], v101 offset:43008
	ds_read_b64_tr_b16 v[162:163], v101 offset:44032
	ds_read_b64_tr_b16 v[164:165], v101 offset:45056
	ds_read_b64_tr_b16 v[166:167], v101 offset:46080
	ds_read_b64_tr_b16 v[168:169], v101 offset:47104
	ds_read_b64_tr_b16 v[170:171], v101 offset:48128
	ds_read_b64_tr_b16 v[172:173], v102 offset:40960
	ds_read_b64_tr_b16 v[174:175], v102 offset:41984
	ds_read_b64_tr_b16 v[176:177], v102 offset:43008
	ds_read_b64_tr_b16 v[178:179], v102 offset:44032
	ds_read_b64_tr_b16 v[180:181], v102 offset:45056
	ds_read_b64_tr_b16 v[182:183], v102 offset:46080
	ds_read_b64_tr_b16 v[184:185], v102 offset:47104
	ds_read_b64_tr_b16 v[186:187], v102 offset:48128
	s_cbranch_scc1 .LBB0_1684
; template <int MODE, int DQK, int DV>
; __device__ __forceinline__ void attn_pass(LAS unsigned char* lds, const Tens& T, size_t rowbase, int q0, f32x16 (&o)[DV / 32], float& l_out, const int wave, QPre* qp = nullptr) {
;     ...
;             if (MODE == AM_DSA || MODE == AM_DIFF) {
;                 if (nearb) {
;                     int dq = tq - kbase - 4 * h; asm volatile("" : "+v"(dq));
; #pragma unroll
;                     for (int kb = 0; kb < 2; ++kb)
; #pragma unroll
;                         for (int rg = 0; rg < 16; ++rg) { int dist = dq - (32 * kb + (rg & 3) + 8 * (rg >> 2)); dist = dist < 0 ? 0 : (dist > 128 ? 128 : dist); p[kb][rg] += lut[dist]; }
;                 }
	v_mov_b32_e32 v146, v113
	s_add_i32 s0, 0, 0x1f800
	v_add_u32_e32 v123, -1, v146
	v_add_u32_e32 v124, -2, v146
	v_add_u32_e32 v125, -3, v146
	v_add_u32_e32 v126, -8, v146
	v_add_u32_e32 v127, -9, v146
	v_add_u32_e32 v128, -10, v146
	v_add_u32_e32 v129, -11, v146
	v_add_u32_e32 v130, -16, v146
	v_subrev_u32_e32 v131, 17, v146
	v_subrev_u32_e32 v132, 18, v146
	v_subrev_u32_e32 v133, 19, v146
	v_subrev_u32_e32 v134, 24, v146
	v_subrev_u32_e32 v135, 25, v146
	v_subrev_u32_e32 v136, 26, v146
	v_subrev_u32_e32 v137, 27, v146
	v_subrev_u32_e32 v138, 32, v146
	v_subrev_u32_e32 v139, 33, v146
	v_subrev_u32_e32 v140, 34, v146
	v_subrev_u32_e32 v141, 35, v146
	v_subrev_u32_e32 v142, 40, v146
	v_subrev_u32_e32 v143, 41, v146
	v_subrev_u32_e32 v144, 42, v146
	v_subrev_u32_e32 v145, 43, v146
	v_subrev_u32_e32 v147, 48, v146
	v_subrev_u32_e32 v148, 49, v146
	v_subrev_u32_e32 v149, 50, v146
	v_subrev_u32_e32 v150, 51, v146
	v_subrev_u32_e32 v151, 56, v146
	v_subrev_u32_e32 v152, 57, v146
	v_subrev_u32_e32 v153, 58, v146
	v_med3_i32 v122, v146, 0, v93
	v_med3_i32 v123, v123, 0, v93
	v_med3_i32 v124, v124, 0, v93
	v_med3_i32 v125, v125, 0, v93
	v_med3_i32 v126, v126, 0, v93
	v_med3_i32 v127, v127, 0, v93
	v_med3_i32 v128, v128, 0, v93
	v_med3_i32 v129, v129, 0, v93
	v_med3_i32 v130, v130, 0, v93
	v_med3_i32 v131, v131, 0, v93
	v_med3_i32 v132, v132, 0, v93
	v_med3_i32 v133, v133, 0, v93
	v_med3_i32 v134, v134, 0, v93
	v_med3_i32 v135, v135, 0, v93
	v_med3_i32 v136, v136, 0, v93
	v_med3_i32 v137, v137, 0, v93
	v_med3_i32 v138, v138, 0, v93
	v_med3_i32 v139, v139, 0, v93
	v_med3_i32 v140, v140, 0, v93
	v_med3_i32 v141, v141, 0, v93
	v_med3_i32 v142, v142, 0, v93
	v_med3_i32 v143, v143, 0, v93
	v_med3_i32 v144, v144, 0, v93
	v_med3_i32 v145, v145, 0, v93
	v_med3_i32 v147, v147, 0, v93
	v_med3_i32 v148, v148, 0, v93
	v_med3_i32 v149, v149, 0, v93
	v_med3_i32 v150, v150, 0, v93
	v_med3_i32 v151, v151, 0, v93
	v_med3_i32 v152, v152, 0, v93
	v_med3_i32 v153, v153, 0, v93
	v_subrev_u32_e32 v146, 59, v146
	v_lshl_add_u32 v122, v122, 2, s0
	v_lshl_add_u32 v123, v123, 2, s0
	v_lshl_add_u32 v124, v124, 2, s0
	v_lshl_add_u32 v125, v125, 2, s0
	v_lshl_add_u32 v126, v126, 2, s0
	v_lshl_add_u32 v127, v127, 2, s0
	v_lshl_add_u32 v128, v128, 2, s0
	v_lshl_add_u32 v129, v129, 2, s0
	v_lshl_add_u32 v130, v130, 2, s0
	v_lshl_add_u32 v131, v131, 2, s0
	v_lshl_add_u32 v132, v132, 2, s0
	v_lshl_add_u32 v133, v133, 2, s0
	v_lshl_add_u32 v134, v134, 2, s0
	v_lshl_add_u32 v135, v135, 2, s0
	v_lshl_add_u32 v136, v136, 2, s0
	v_lshl_add_u32 v137, v137, 2, s0
	v_lshl_add_u32 v138, v138, 2, s0
	v_lshl_add_u32 v139, v139, 2, s0
	v_lshl_add_u32 v140, v140, 2, s0
	v_lshl_add_u32 v141, v141, 2, s0
	v_lshl_add_u32 v142, v142, 2, s0
	v_lshl_add_u32 v143, v143, 2, s0
	v_lshl_add_u32 v144, v144, 2, s0
	v_lshl_add_u32 v145, v145, 2, s0
	v_lshl_add_u32 v147, v147, 2, s0
	v_lshl_add_u32 v148, v148, 2, s0
	v_lshl_add_u32 v149, v149, 2, s0
	v_lshl_add_u32 v150, v150, 2, s0
	v_lshl_add_u32 v151, v151, 2, s0
	v_lshl_add_u32 v152, v152, 2, s0
	v_lshl_add_u32 v153, v153, 2, s0
	v_med3_i32 v146, v146, 0, v93
	ds_read_b32 v122, v122
	ds_read_b32 v123, v123
	ds_read_b32 v124, v124
	ds_read_b32 v125, v125
	ds_read_b32 v126, v126
	ds_read_b32 v127, v127
	ds_read_b32 v128, v128
	ds_read_b32 v129, v129
	ds_read_b32 v130, v130
	ds_read_b32 v131, v131
	ds_read_b32 v132, v132
	ds_read_b32 v133, v133
	ds_read_b32 v134, v134
	ds_read_b32 v135, v135
	ds_read_b32 v136, v136
	ds_read_b32 v137, v137
	ds_read_b32 v138, v138
	ds_read_b32 v139, v139
	ds_read_b32 v140, v140
	ds_read_b32 v141, v141
	ds_read_b32 v142, v142
	ds_read_b32 v143, v143
	ds_read_b32 v144, v144
	ds_read_b32 v145, v145
	v_lshl_add_u32 v154, v146, 2, s0
	ds_read_b32 v146, v147
	ds_read_b32 v147, v148
	ds_read_b32 v148, v149
	ds_read_b32 v149, v150
	ds_read_b32 v150, v151
	ds_read_b32 v151, v152
	ds_read_b32 v152, v153
	ds_read_b32 v153, v154
	s_waitcnt lgkmcnt(14)
	v_pk_add_f32 v[44:45], v[44:45], v[134:135]
	v_pk_add_f32 v[46:47], v[46:47], v[136:137]
	v_pk_add_f32 v[42:43], v[42:43], v[132:133]
	v_pk_add_f32 v[40:41], v[40:41], v[130:131]
	v_pk_add_f32 v[38:39], v[38:39], v[128:129]
	v_pk_add_f32 v[36:37], v[36:37], v[126:127]
	v_pk_add_f32 v[34:35], v[34:35], v[124:125]
	v_pk_add_f32 v[32:33], v[32:33], v[122:123]
	s_waitcnt lgkmcnt(0)
	v_pk_add_f32 v[62:63], v[62:63], v[152:153]
	v_pk_add_f32 v[60:61], v[60:61], v[150:151]
	v_pk_add_f32 v[58:59], v[58:59], v[148:149]
	v_pk_add_f32 v[56:57], v[56:57], v[146:147]
	v_pk_add_f32 v[54:55], v[54:55], v[144:145]
	v_pk_add_f32 v[52:53], v[52:53], v[142:143]
	v_pk_add_f32 v[50:51], v[50:51], v[140:141]
	v_pk_add_f32 v[48:49], v[48:49], v[138:139]

; #define PG8_STAGE(bufoff, gbase, voff) do { _Pragma("unroll") for (int _i = 0; _i < 2; ++_i) \
;         __builtin_amdgcn_global_load_lds((const unsigned*)((const char*)(gbase) + (voff)[_i]), (PG8_LAS unsigned*)(lds + (bufoff) + ldsw + _i * 8192), 16, 0, 0); } while (0)
; #define PG8_LDA(dst, b, h) do { _Pragma("unroll") for (int m = 0; m < 4; ++m) _Pragma("unroll") for (int k = 0; k < 2; ++k) dst[m][k] = *(const PG8_LAS bf16x8*)(lds + PG8_SA(b, h) + aoff + m * 2048 + k * 1024); } while (0)
; #define PG8_LDB(dst, b, h) do { _Pragma("unroll") for (int n = 0; n < 2; ++n) _Pragma("unroll") for (int k = 0; k < 2; ++k) dst[n][k] = *(const PG8_LAS bf16x8*)(lds + PG8_SB(b, h) + boff + n * 2048 + k * 1024); } while (0)
; #define PG8_MMA(ai, bj, At, Bt) do { __builtin_amdgcn_s_setprio(1); _Pragma("unroll") for (int m = 0; m < 4; ++m) _Pragma("unroll") for (int n = 0; n < 2; ++n) _Pragma("unroll") for (int k = 0; k < 2; ++k) \
;         acc[ai][bj][m][n] = __builtin_amdgcn_mfma_f32_16x16x32_bf16(Bt[n][k], At[m][k], acc[ai][bj][m][n], 0, 0, 0); __builtin_amdgcn_s_setprio(0); } while (0)
; template <class Epi, class Sched, bool ALIGN_EPI = false, bool SP2 = false>
; __device__ __forceinline__ void gemm_phase(PG8_LAS unsigned char* lds, const Gemm g, const Sched& S, const Epi& E, const int wid) {
;     ...
;         const bool has_next = S.next(ui + 1, nxt);
;         const char* nA = has_next ? (const char*)g.A + (size_t)nxt.pm * tstepA : cA; const char* nB = has_next ? (const char*)g.Bt + (size_t)nxt.pn * tstepB : cB;
;         for (int t = 0; t < nt; t += 2) {
;             const bool last = (t == nt - 2);
;             const char* a1 = cA + (size_t)(t + 1) * kstep;
;             const char* a2 = last ? nA : cA + (size_t)(t + 2) * kstep; const char* b2 = last ? nB : cB + (size_t)(t + 2) * kstep;
;             const char* a3 = a2 + kstep; const char* b3 = b2 + kstep;
;             if (last && has_next) S.a_ready(nxt);
;             if constexpr (SP2) {
;             PG8_LDB(B0, 0, 0); PG8_LDB(B1, 0, 1); PG8_SCHED; PG8_LDA(At, 0, 0); PG8_STAGE(PG8_SA(1, 1), a1 + hstepA, voffA);
;             PG8_WAIT_V(8); PG8_WAIT_L(0); PG8_BAR; PG8_MMA(0, 0, At, B0); PG8_MMA(0, 1, At, B1); PG8_BAR; PG8_SCHED;
;             PG8_LDA(At, 0, 1); PG8_STAGE(PG8_SB(0, 0), b2, voffB); PG8_STAGE(PG8_SB(0, 1), b2 + hstepB, voffB); PG8_STAGE(PG8_SA(0, 0), a2, voffA);
.LBB0_1779:
	s_ashr_i32 s21, s20, 31
	s_lshl_b64 s[22:23], s[20:21], 19
	s_add_u32 s22, s0, s22
	s_addc_u32 s23, s1, s23
	s_and_b64 s[24:25], s[4:5], exec
	s_cselect_b32 s21, s23, s31
	s_cselect_b32 s27, s22, s30
	s_ashr_i32 s19, s18, 31
	s_lshl_b64 s[24:25], s[18:19], 19
	s_add_u32 s24, s33, s24
	s_addc_u32 s25, s38, s25
	s_and_b64 s[36:37], s[4:5], exec
	s_cselect_b32 s19, s25, s35
	s_cselect_b32 s29, s24, s34
	s_add_u32 s30, s30, 0x40080
	s_addc_u32 s31, s31, 0
	s_add_u32 s68, s34, 0x100
	s_addc_u32 s69, s35, 0
	s_mov_b32 s70, -2
	s_waitcnt lgkmcnt(0)
	v_add_u32_e32 v252, 0x18000, v189
	v_add_u32_e32 v253, 0x1c000, v189
	ds_read_b128 v[128:131], v190
	ds_read_b128 v[132:135], v190 offset:1024
	ds_read_b128 v[136:139], v190 offset:2048
	ds_read_b128 v[140:143], v190 offset:3072
	ds_read_b128 v[144:147], v191
	ds_read_b128 v[148:151], v191 offset:1024
	ds_read_b128 v[172:175], v191 offset:2048
	ds_read_b128 v[176:179], v191 offset:3072
	s_add_u32 s34, s30, 0xfffc0080
	s_addc_u32 s35, s31, -1
	s_cmp_eq_u32 s70, 12
	s_cselect_b32 s37, s21, s35
	s_cselect_b32 s36, s27, s34
	s_cselect_b32 s35, s19, s69
	s_cselect_b32 s34, s29, s68
	s_add_i32 m0, s40, 0xc000
	ds_read_b128 v[180:183], v192
	ds_read_b128 v[184:187], v192 offset:1024
	ds_read_b128 v[194:197], v192 offset:2048
	ds_read_b128 v[198:201], v192 offset:3072
	ds_read_b128 v[202:205], v192 offset:4096
	ds_read_b128 v[206:209], v192 offset:5120
	ds_read_b128 v[210:213], v192 offset:6144
	ds_read_b128 v[214:217], v192 offset:7168
	global_load_lds_dwordx4 v164, s[30:31]
	s_add_i32 m0, s40, 0xe000
	s_nop 0
	global_load_lds_dwordx4 v166, s[30:31]
	s_waitcnt vmcnt(8) lgkmcnt(0)
	s_barrier
	s_setprio 1
	v_mfma_f32_16x16x32_bf16 v[124:127], v[128:131], v[180:183], 0
	v_mfma_f32_16x16x32_bf16 v[120:123], v[136:139], v[180:183], 0
	v_mfma_f32_16x16x32_bf16 v[108:111], v[128:131], v[194:197], 0
	v_mfma_f32_16x16x32_bf16 v[104:107], v[136:139], v[194:197], 0
	v_mfma_f32_16x16x32_bf16 v[92:95], v[128:131], v[202:205], 0
	v_mfma_f32_16x16x32_bf16 v[88:91], v[136:139], v[202:205], 0
	v_mfma_f32_16x16x32_bf16 v[76:79], v[128:131], v[210:213], 0
	v_mfma_f32_16x16x32_bf16 v[72:75], v[136:139], v[210:213], 0
	v_mfma_f32_16x16x32_bf16 v[124:127], v[132:135], v[184:187], v[124:127]
	v_mfma_f32_16x16x32_bf16 v[120:123], v[140:143], v[184:187], v[120:123]
	v_mfma_f32_16x16x32_bf16 v[108:111], v[132:135], v[198:201], v[108:111]
	v_mfma_f32_16x16x32_bf16 v[104:107], v[140:143], v[198:201], v[104:107]
	v_mfma_f32_16x16x32_bf16 v[92:95], v[132:135], v[206:209], v[92:95]
	v_mfma_f32_16x16x32_bf16 v[88:91], v[140:143], v[206:209], v[88:91]
	v_mfma_f32_16x16x32_bf16 v[76:79], v[132:135], v[214:217], v[76:79]
	v_mfma_f32_16x16x32_bf16 v[72:75], v[140:143], v[214:217], v[72:75]
	s_setprio 0
	s_setprio 1
	v_mfma_f32_16x16x32_bf16 v[116:119], v[144:147], v[180:183], 0
	v_mfma_f32_16x16x32_bf16 v[112:115], v[172:175], v[180:183], 0
	v_mfma_f32_16x16x32_bf16 v[100:103], v[144:147], v[194:197], 0
	v_mfma_f32_16x16x32_bf16 v[96:99], v[172:175], v[194:197], 0
	v_mfma_f32_16x16x32_bf16 v[84:87], v[144:147], v[202:205], 0
	v_mfma_f32_16x16x32_bf16 v[80:83], v[172:175], v[202:205], 0
	v_mfma_f32_16x16x32_bf16 v[68:71], v[144:147], v[210:213], 0
	v_mfma_f32_16x16x32_bf16 v[64:67], v[172:175], v[210:213], 0
	v_mfma_f32_16x16x32_bf16 v[116:119], v[148:151], v[184:187], v[116:119]
	v_mfma_f32_16x16x32_bf16 v[112:115], v[176:179], v[184:187], v[112:115]
	v_mfma_f32_16x16x32_bf16 v[100:103], v[148:151], v[198:201], v[100:103]
	v_mfma_f32_16x16x32_bf16 v[96:99], v[176:179], v[198:201], v[96:99]
	v_mfma_f32_16x16x32_bf16 v[84:87], v[148:151], v[206:209], v[84:87]
	v_mfma_f32_16x16x32_bf16 v[80:83], v[176:179], v[206:209], v[80:83]
	v_mfma_f32_16x16x32_bf16 v[68:71], v[148:151], v[214:217], v[68:71]
	v_mfma_f32_16x16x32_bf16 v[64:67], v[176:179], v[214:217], v[64:67]
	s_setprio 0
	s_barrier
	s_add_i32 s71, s65, s39
	s_add_u32 s98, s34, 0x80
	s_addc_u32 s99, s35, 0
	s_mov_b32 m0, s71
	ds_read_b128 v[180:183], v192 offset:16384
	ds_read_b128 v[184:187], v192 offset:17408
	ds_read_b128 v[194:197], v192 offset:18432
	ds_read_b128 v[198:201], v192 offset:19456
	ds_read_b128 v[202:205], v192 offset:20480
	ds_read_b128 v[206:209], v192 offset:21504
	ds_read_b128 v[210:213], v192 offset:22528
	ds_read_b128 v[214:217], v192 offset:23552
	global_load_lds_dwordx4 v154, s[34:35]
	s_add_i32 m0, s71, 0x2000
	s_add_u32 s72, s34, 0x40000
	s_addc_u32 s73, s35, 0
	s_add_i32 s71, s66, s39
	global_load_lds_dwordx4 v158, s[34:35]
	s_mov_b32 m0, s71
	s_add_u32 s100, s36, 0x80
	s_addc_u32 s101, s37, 0
	global_load_lds_dwordx4 v154, s[72:73]
	s_add_i32 m0, s71, 0x2000
	s_nop 0
	global_load_lds_dwordx4 v158, s[72:73]
	s_mov_b32 m0, s40
	s_nop 0
	global_load_lds_dwordx4 v152, s[36:37]
	s_mov_b32 m0, s41
	s_nop 0
	global_load_lds_dwordx4 v156, s[36:37]
	s_waitcnt vmcnt(8) lgkmcnt(0)
	s_barrier
; #define PG8_STAGE(bufoff, gbase, voff) do { _Pragma("unroll") for (int _i = 0; _i < 2; ++_i) \
;         __builtin_amdgcn_global_load_lds((const unsigned*)((const char*)(gbase) + (voff)[_i]), (PG8_LAS unsigned*)(lds + (bufoff) + ldsw + _i * 8192), 16, 0, 0); } while (0)
; #define PG8_LDA(dst, b, h) do { _Pragma("unroll") for (int m = 0; m < 4; ++m) _Pragma("unroll") for (int k = 0; k < 2; ++k) dst[m][k] = *(const PG8_LAS bf16x8*)(lds + PG8_SA(b, h) + aoff + m * 2048 + k * 1024); } while (0)
; #define PG8_LDB(dst, b, h) do { _Pragma("unroll") for (int n = 0; n < 2; ++n) _Pragma("unroll") for (int k = 0; k < 2; ++k) dst[n][k] = *(const PG8_LAS bf16x8*)(lds + PG8_SB(b, h) + boff + n * 2048 + k * 1024); } while (0)
; #define PG8_MMA(ai, bj, At, Bt) do { __builtin_amdgcn_s_setprio(1); _Pragma("unroll") for (int m = 0; m < 4; ++m) _Pragma("unroll") for (int n = 0; n < 2; ++n) _Pragma("unroll") for (int k = 0; k < 2; ++k) \
;         acc[ai][bj][m][n] = __builtin_amdgcn_mfma_f32_16x16x32_bf16(Bt[n][k], At[m][k], acc[ai][bj][m][n], 0, 0, 0); __builtin_amdgcn_s_setprio(0); } while (0)
; #define PG8_WAIT_V(n) asm volatile("s_waitcnt vmcnt(" #n ")" ::: "memory")
; #define PG8_WAIT_L(n) asm volatile("s_waitcnt lgkmcnt(" #n ")" ::: "memory")
; #define PG8_BAR __builtin_amdgcn_s_barrier()
; #define PG8_SCHED __builtin_amdgcn_sched_barrier(0)
; template <class Epi, class Sched, bool ALIGN_EPI = false, bool SP2 = false>
; __device__ __forceinline__ void gemm_phase(PG8_LAS unsigned char* lds, const Gemm g, const Sched& S, const Epi& E, const int wid) {
;     ...
;             PG8_WAIT_V(8); PG8_WAIT_L(0); PG8_BAR; PG8_MMA(1, 0, At, B0); PG8_MMA(1, 1, At, B1); PG8_BAR; PG8_SCHED;
;             PG8_LDB(B0, 1, 0); PG8_LDB(B1, 1, 1); PG8_SCHED; PG8_LDA(At, 1, 0); PG8_STAGE(PG8_SA(0, 1), a2 + hstepA, voffA);
;             PG8_WAIT_V(8); PG8_WAIT_L(0); PG8_BAR; PG8_MMA(0, 0, At, B0); PG8_MMA(0, 1, At, B1); PG8_BAR; PG8_SCHED;
	s_setprio 1
	v_mfma_f32_16x16x32_bf16 v[60:63], v[128:131], v[180:183], 0
	v_mfma_f32_16x16x32_bf16 v[56:59], v[136:139], v[180:183], 0
	v_mfma_f32_16x16x32_bf16 v[44:47], v[128:131], v[194:197], 0
	v_mfma_f32_16x16x32_bf16 v[40:43], v[136:139], v[194:197], 0
	v_mfma_f32_16x16x32_bf16 v[28:31], v[128:131], v[202:205], 0
	v_mfma_f32_16x16x32_bf16 v[24:27], v[136:139], v[202:205], 0
	v_mfma_f32_16x16x32_bf16 v[12:15], v[128:131], v[210:213], 0
	v_mfma_f32_16x16x32_bf16 v[8:11], v[136:139], v[210:213], 0
	v_mfma_f32_16x16x32_bf16 v[60:63], v[132:135], v[184:187], v[60:63]
	v_mfma_f32_16x16x32_bf16 v[56:59], v[140:143], v[184:187], v[56:59]
	v_mfma_f32_16x16x32_bf16 v[44:47], v[132:135], v[198:201], v[44:47]
	v_mfma_f32_16x16x32_bf16 v[40:43], v[140:143], v[198:201], v[40:43]
	v_mfma_f32_16x16x32_bf16 v[28:31], v[132:135], v[206:209], v[28:31]
	v_mfma_f32_16x16x32_bf16 v[24:27], v[140:143], v[206:209], v[24:27]
	v_mfma_f32_16x16x32_bf16 v[12:15], v[132:135], v[214:217], v[12:15]
	v_mfma_f32_16x16x32_bf16 v[8:11], v[140:143], v[214:217], v[8:11]
	s_setprio 0
	s_setprio 1
	v_mfma_f32_16x16x32_bf16 v[52:55], v[144:147], v[180:183], 0
	v_mfma_f32_16x16x32_bf16 v[48:51], v[172:175], v[180:183], 0
	v_mfma_f32_16x16x32_bf16 v[36:39], v[144:147], v[194:197], 0
	v_mfma_f32_16x16x32_bf16 v[32:35], v[172:175], v[194:197], 0
	v_mfma_f32_16x16x32_bf16 v[20:23], v[144:147], v[202:205], 0
	v_mfma_f32_16x16x32_bf16 v[16:19], v[172:175], v[202:205], 0
	v_mfma_f32_16x16x32_bf16 v[4:7], v[144:147], v[210:213], 0
	v_mfma_f32_16x16x32_bf16 v[0:3], v[172:175], v[210:213], 0
	v_mfma_f32_16x16x32_bf16 v[52:55], v[148:151], v[184:187], v[52:55]
	v_mfma_f32_16x16x32_bf16 v[48:51], v[176:179], v[184:187], v[48:51]
	v_mfma_f32_16x16x32_bf16 v[36:39], v[148:151], v[198:201], v[36:39]
	v_mfma_f32_16x16x32_bf16 v[32:35], v[176:179], v[198:201], v[32:35]
	v_mfma_f32_16x16x32_bf16 v[20:23], v[148:151], v[206:209], v[20:23]
	v_mfma_f32_16x16x32_bf16 v[16:19], v[176:179], v[206:209], v[16:19]
	v_mfma_f32_16x16x32_bf16 v[4:7], v[148:151], v[214:217], v[4:7]
	v_mfma_f32_16x16x32_bf16 v[0:3], v[176:179], v[214:217], v[0:3]
	s_setprio 0
	s_barrier
	s_add_i32 s71, 0, 0x18000
	s_add_i32 s72, 0, 0x1c000
	ds_read_b128 v[128:131], v252
	ds_read_b128 v[132:135], v252 offset:1024
	ds_read_b128 v[136:139], v252 offset:2048
	ds_read_b128 v[140:143], v252 offset:3072
	ds_read_b128 v[144:147], v253
	ds_read_b128 v[148:151], v253 offset:1024
	ds_read_b128 v[172:175], v253 offset:2048
	ds_read_b128 v[176:179], v253 offset:3072
	s_add_u32 s36, s36, 0x40000
	s_addc_u32 s37, s37, 0
	s_mov_b32 m0, s44
	ds_read_b128 v[180:183], v192 offset:32768
	ds_read_b128 v[184:187], v192 offset:33792
	ds_read_b128 v[194:197], v192 offset:34816
	ds_read_b128 v[198:201], v192 offset:35840
	ds_read_b128 v[202:205], v192 offset:36864
	ds_read_b128 v[206:209], v192 offset:37888
	ds_read_b128 v[210:213], v192 offset:38912
	ds_read_b128 v[214:217], v192 offset:39936
	global_load_lds_dwordx4 v152, s[36:37]
	s_mov_b32 m0, s45
	s_nop 0
	global_load_lds_dwordx4 v156, s[36:37]
	s_waitcnt vmcnt(8) lgkmcnt(0)
	s_barrier
	s_setprio 1
	v_mfma_f32_16x16x32_bf16 v[124:127], v[128:131], v[180:183], v[124:127]
	v_mfma_f32_16x16x32_bf16 v[120:123], v[136:139], v[180:183], v[120:123]
	v_mfma_f32_16x16x32_bf16 v[108:111], v[128:131], v[194:197], v[108:111]
	v_mfma_f32_16x16x32_bf16 v[104:107], v[136:139], v[194:197], v[104:107]
	v_mfma_f32_16x16x32_bf16 v[92:95], v[128:131], v[202:205], v[92:95]
	v_mfma_f32_16x16x32_bf16 v[88:91], v[136:139], v[202:205], v[88:91]
	v_mfma_f32_16x16x32_bf16 v[76:79], v[128:131], v[210:213], v[76:79]
	v_mfma_f32_16x16x32_bf16 v[72:75], v[136:139], v[210:213], v[72:75]
	v_mfma_f32_16x16x32_bf16 v[124:127], v[132:135], v[184:187], v[124:127]
	v_mfma_f32_16x16x32_bf16 v[120:123], v[140:143], v[184:187], v[120:123]
	v_mfma_f32_16x16x32_bf16 v[108:111], v[132:135], v[198:201], v[108:111]
	v_mfma_f32_16x16x32_bf16 v[104:107], v[140:143], v[198:201], v[104:107]
	v_mfma_f32_16x16x32_bf16 v[92:95], v[132:135], v[206:209], v[92:95]
	v_mfma_f32_16x16x32_bf16 v[88:91], v[140:143], v[206:209], v[88:91]
	v_mfma_f32_16x16x32_bf16 v[76:79], v[132:135], v[214:217], v[76:79]
	v_mfma_f32_16x16x32_bf16 v[72:75], v[140:143], v[214:217], v[72:75]
	s_setprio 0
	s_setprio 1
	v_mfma_f32_16x16x32_bf16 v[116:119], v[144:147], v[180:183], v[116:119]
	v_mfma_f32_16x16x32_bf16 v[112:115], v[172:175], v[180:183], v[112:115]
	v_mfma_f32_16x16x32_bf16 v[100:103], v[144:147], v[194:197], v[100:103]
	v_mfma_f32_16x16x32_bf16 v[96:99], v[172:175], v[194:197], v[96:99]
	v_mfma_f32_16x16x32_bf16 v[84:87], v[144:147], v[202:205], v[84:87]
	v_mfma_f32_16x16x32_bf16 v[80:83], v[172:175], v[202:205], v[80:83]
	v_mfma_f32_16x16x32_bf16 v[68:71], v[144:147], v[210:213], v[68:71]
	v_mfma_f32_16x16x32_bf16 v[64:67], v[172:175], v[210:213], v[64:67]
	v_mfma_f32_16x16x32_bf16 v[116:119], v[148:151], v[184:187], v[116:119]
	v_mfma_f32_16x16x32_bf16 v[112:115], v[176:179], v[184:187], v[112:115]
	v_mfma_f32_16x16x32_bf16 v[100:103], v[148:151], v[198:201], v[100:103]
	v_mfma_f32_16x16x32_bf16 v[96:99], v[176:179], v[198:201], v[96:99]
	v_mfma_f32_16x16x32_bf16 v[84:87], v[148:151], v[206:209], v[84:87]
	v_mfma_f32_16x16x32_bf16 v[80:83], v[176:179], v[206:209], v[80:83]
	v_mfma_f32_16x16x32_bf16 v[68:71], v[148:151], v[214:217], v[68:71]
	v_mfma_f32_16x16x32_bf16 v[64:67], v[176:179], v[214:217], v[64:67]
	s_setprio 0
	s_barrier
; #define PG8_STAGE(bufoff, gbase, voff) do { _Pragma("unroll") for (int _i = 0; _i < 2; ++_i) \
;         __builtin_amdgcn_global_load_lds((const unsigned*)((const char*)(gbase) + (voff)[_i]), (PG8_LAS unsigned*)(lds + (bufoff) + ldsw + _i * 8192), 16, 0, 0); } while (0)
; #define PG8_LDA(dst, b, h) do { _Pragma("unroll") for (int m = 0; m < 4; ++m) _Pragma("unroll") for (int k = 0; k < 2; ++k) dst[m][k] = *(const PG8_LAS bf16x8*)(lds + PG8_SA(b, h) + aoff + m * 2048 + k * 1024); } while (0)
; #define PG8_LDB(dst, b, h) do { _Pragma("unroll") for (int n = 0; n < 2; ++n) _Pragma("unroll") for (int k = 0; k < 2; ++k) dst[n][k] = *(const PG8_LAS bf16x8*)(lds + PG8_SB(b, h) + boff + n * 2048 + k * 1024); } while (0)
; #define PG8_MMA(ai, bj, At, Bt) do { __builtin_amdgcn_s_setprio(1); _Pragma("unroll") for (int m = 0; m < 4; ++m) _Pragma("unroll") for (int n = 0; n < 2; ++n) _Pragma("unroll") for (int k = 0; k < 2; ++k) \
;         acc[ai][bj][m][n] = __builtin_amdgcn_mfma_f32_16x16x32_bf16(Bt[n][k], At[m][k], acc[ai][bj][m][n], 0, 0, 0); __builtin_amdgcn_s_setprio(0); } while (0)
; #define PG8_WAIT_V(n) asm volatile("s_waitcnt vmcnt(" #n ")" ::: "memory")
; #define PG8_BAR __builtin_amdgcn_s_barrier()
; template <class Epi, class Sched, bool ALIGN_EPI = false, bool SP2 = false>
; __device__ __forceinline__ void gemm_phase(PG8_LAS unsigned char* lds, const Gemm g, const Sched& S, const Epi& E, const int wid) {
;     ...
;         for (int t = 0; t < nt; t += 2) {
;             const bool last = (t == nt - 2);
;             const char* a1 = cA + (size_t)(t + 1) * kstep;
;             const char* a2 = last ? nA : cA + (size_t)(t + 2) * kstep; const char* b2 = last ? nB : cB + (size_t)(t + 2) * kstep;
;             const char* a3 = a2 + kstep; const char* b3 = b2 + kstep;
;             if (last && has_next) S.a_ready(nxt);
;             if constexpr (SP2) {
;             PG8_LDB(B0, 0, 0); PG8_LDB(B1, 0, 1); PG8_SCHED; PG8_LDA(At, 0, 0); PG8_STAGE(PG8_SA(1, 1), a1 + hstepA, voffA);
;             PG8_WAIT_V(8); PG8_WAIT_L(0); PG8_BAR; PG8_MMA(0, 0, At, B0); PG8_MMA(0, 1, At, B1); PG8_BAR; PG8_SCHED;
;     ...
;             PG8_LDA(At, 1, 1); PG8_STAGE(PG8_SB(1, 0), b3, voffB); PG8_STAGE(PG8_SB(1, 1), b3 + hstepB, voffB); PG8_STAGE(PG8_SA(1, 0), a3, voffA);
;             PG8_WAIT_V(8); PG8_WAIT_L(0); PG8_BAR; PG8_MMA(1, 0, At, B0); PG8_MMA(1, 1, At, B1); PG8_BAR; PG8_SCHED;
	s_add_i32 s36, s71, s39
	s_mov_b32 m0, s36
	ds_read_b128 v[180:183], v192 offset:49152
	ds_read_b128 v[184:187], v192 offset:50176
	ds_read_b128 v[194:197], v192 offset:51200
	ds_read_b128 v[198:201], v192 offset:52224
	ds_read_b128 v[202:205], v192 offset:53248
	ds_read_b128 v[206:209], v192 offset:54272
	ds_read_b128 v[210:213], v192 offset:55296
	ds_read_b128 v[214:217], v192 offset:56320
	global_load_lds_dwordx4 v154, s[98:99]
	s_add_i32 m0, s36, 0x2000
	s_add_u32 s34, s34, 0x40080
	s_addc_u32 s35, s35, 0
	s_add_i32 s36, s72, s39
	global_load_lds_dwordx4 v158, s[98:99]
	s_mov_b32 m0, s36
	s_nop 0
	global_load_lds_dwordx4 v154, s[34:35]
	s_add_i32 m0, s36, 0x2000
	s_nop 0
	global_load_lds_dwordx4 v158, s[34:35]
	s_mov_b32 m0, s47
	s_nop 0
	global_load_lds_dwordx4 v152, s[100:101]
	s_mov_b32 m0, s48
	s_nop 0
	global_load_lds_dwordx4 v156, s[100:101]
	s_waitcnt vmcnt(8) lgkmcnt(0)
	s_barrier
	s_setprio 1
	v_mfma_f32_16x16x32_bf16 v[60:63], v[128:131], v[180:183], v[60:63]
	v_mfma_f32_16x16x32_bf16 v[56:59], v[136:139], v[180:183], v[56:59]
	v_mfma_f32_16x16x32_bf16 v[44:47], v[128:131], v[194:197], v[44:47]
	v_mfma_f32_16x16x32_bf16 v[40:43], v[136:139], v[194:197], v[40:43]
	v_mfma_f32_16x16x32_bf16 v[28:31], v[128:131], v[202:205], v[28:31]
	v_mfma_f32_16x16x32_bf16 v[24:27], v[136:139], v[202:205], v[24:27]
	v_mfma_f32_16x16x32_bf16 v[12:15], v[128:131], v[210:213], v[12:15]
	v_mfma_f32_16x16x32_bf16 v[8:11], v[136:139], v[210:213], v[8:11]
	v_mfma_f32_16x16x32_bf16 v[60:63], v[132:135], v[184:187], v[60:63]
	v_mfma_f32_16x16x32_bf16 v[56:59], v[140:143], v[184:187], v[56:59]
	v_mfma_f32_16x16x32_bf16 v[44:47], v[132:135], v[198:201], v[44:47]
	v_mfma_f32_16x16x32_bf16 v[40:43], v[140:143], v[198:201], v[40:43]
	v_mfma_f32_16x16x32_bf16 v[28:31], v[132:135], v[206:209], v[28:31]
	v_mfma_f32_16x16x32_bf16 v[24:27], v[140:143], v[206:209], v[24:27]
	v_mfma_f32_16x16x32_bf16 v[12:15], v[132:135], v[214:217], v[12:15]
	v_mfma_f32_16x16x32_bf16 v[8:11], v[140:143], v[214:217], v[8:11]
	s_setprio 0
	s_setprio 1
	v_mfma_f32_16x16x32_bf16 v[52:55], v[144:147], v[180:183], v[52:55]
	v_mfma_f32_16x16x32_bf16 v[48:51], v[172:175], v[180:183], v[48:51]
	v_mfma_f32_16x16x32_bf16 v[36:39], v[144:147], v[194:197], v[36:39]
	v_mfma_f32_16x16x32_bf16 v[32:35], v[172:175], v[194:197], v[32:35]
	v_mfma_f32_16x16x32_bf16 v[20:23], v[144:147], v[202:205], v[20:23]
	v_mfma_f32_16x16x32_bf16 v[16:19], v[172:175], v[202:205], v[16:19]
	v_mfma_f32_16x16x32_bf16 v[4:7], v[144:147], v[210:213], v[4:7]
	v_mfma_f32_16x16x32_bf16 v[0:3], v[172:175], v[210:213], v[0:3]
	v_mfma_f32_16x16x32_bf16 v[52:55], v[148:151], v[184:187], v[52:55]
	v_mfma_f32_16x16x32_bf16 v[48:51], v[176:179], v[184:187], v[48:51]
	v_mfma_f32_16x16x32_bf16 v[36:39], v[148:151], v[198:201], v[36:39]
	v_mfma_f32_16x16x32_bf16 v[32:35], v[176:179], v[198:201], v[32:35]
	v_mfma_f32_16x16x32_bf16 v[20:23], v[148:151], v[206:209], v[20:23]
	v_mfma_f32_16x16x32_bf16 v[16:19], v[176:179], v[206:209], v[16:19]
	v_mfma_f32_16x16x32_bf16 v[4:7], v[148:151], v[214:217], v[4:7]
	v_mfma_f32_16x16x32_bf16 v[0:3], v[176:179], v[214:217], v[0:3]
	s_setprio 0
	s_barrier
	s_add_i32 s70, s70, 2
	s_add_u32 s30, s30, 0x100
	s_addc_u32 s31, s31, 0
	s_add_u32 s68, s68, 0x100
	s_addc_u32 s69, s69, 0
	s_cmp_gt_u32 s70, 13
.LBB0_1780:
	ds_read_b128 v[128:131], v190
	ds_read_b128 v[132:135], v190 offset:1024
	ds_read_b128 v[136:139], v190 offset:2048
	ds_read_b128 v[140:143], v190 offset:3072
	ds_read_b128 v[144:147], v191
	ds_read_b128 v[148:151], v191 offset:1024
	ds_read_b128 v[172:175], v191 offset:2048
	ds_read_b128 v[176:179], v191 offset:3072
	s_add_u32 s34, s30, 0xfffc0080
	s_addc_u32 s35, s31, -1
	s_cmp_eq_u32 s70, 12
	s_cselect_b32 s37, s21, s35
	s_cselect_b32 s36, s27, s34
	s_cselect_b32 s35, s19, s69
	s_cselect_b32 s34, s29, s68
	s_add_i32 m0, s40, 0xc000
	ds_read_b128 v[180:183], v192
	ds_read_b128 v[184:187], v192 offset:1024
	ds_read_b128 v[194:197], v192 offset:2048
	ds_read_b128 v[198:201], v192 offset:3072
	ds_read_b128 v[202:205], v192 offset:4096
	ds_read_b128 v[206:209], v192 offset:5120
	ds_read_b128 v[210:213], v192 offset:6144
	ds_read_b128 v[214:217], v192 offset:7168
	global_load_lds_dwordx4 v164, s[30:31]
	s_add_i32 m0, s40, 0xe000
	s_nop 0
	global_load_lds_dwordx4 v166, s[30:31]
	s_waitcnt vmcnt(8) lgkmcnt(0)
	s_barrier
	s_setprio 1
	v_mfma_f32_16x16x32_bf16 v[124:127], v[128:131], v[180:183], v[124:127]
	v_mfma_f32_16x16x32_bf16 v[120:123], v[136:139], v[180:183], v[120:123]
	v_mfma_f32_16x16x32_bf16 v[108:111], v[128:131], v[194:197], v[108:111]
	v_mfma_f32_16x16x32_bf16 v[104:107], v[136:139], v[194:197], v[104:107]
	v_mfma_f32_16x16x32_bf16 v[92:95], v[128:131], v[202:205], v[92:95]
	v_mfma_f32_16x16x32_bf16 v[88:91], v[136:139], v[202:205], v[88:91]
	v_mfma_f32_16x16x32_bf16 v[76:79], v[128:131], v[210:213], v[76:79]
	v_mfma_f32_16x16x32_bf16 v[72:75], v[136:139], v[210:213], v[72:75]
	v_mfma_f32_16x16x32_bf16 v[124:127], v[132:135], v[184:187], v[124:127]
	v_mfma_f32_16x16x32_bf16 v[120:123], v[140:143], v[184:187], v[120:123]
	v_mfma_f32_16x16x32_bf16 v[108:111], v[132:135], v[198:201], v[108:111]
	v_mfma_f32_16x16x32_bf16 v[104:107], v[140:143], v[198:201], v[104:107]
	v_mfma_f32_16x16x32_bf16 v[92:95], v[132:135], v[206:209], v[92:95]
	v_mfma_f32_16x16x32_bf16 v[88:91], v[140:143], v[206:209], v[88:91]
	v_mfma_f32_16x16x32_bf16 v[76:79], v[132:135], v[214:217], v[76:79]
	v_mfma_f32_16x16x32_bf16 v[72:75], v[140:143], v[214:217], v[72:75]
	s_setprio 0
	s_setprio 1
	v_mfma_f32_16x16x32_bf16 v[116:119], v[144:147], v[180:183], v[116:119]
	v_mfma_f32_16x16x32_bf16 v[112:115], v[172:175], v[180:183], v[112:115]
	v_mfma_f32_16x16x32_bf16 v[100:103], v[144:147], v[194:197], v[100:103]
	v_mfma_f32_16x16x32_bf16 v[96:99], v[172:175], v[194:197], v[96:99]
	v_mfma_f32_16x16x32_bf16 v[84:87], v[144:147], v[202:205], v[84:87]
	v_mfma_f32_16x16x32_bf16 v[80:83], v[172:175], v[202:205], v[80:83]
	v_mfma_f32_16x16x32_bf16 v[68:71], v[144:147], v[210:213], v[68:71]
	v_mfma_f32_16x16x32_bf16 v[64:67], v[172:175], v[210:213], v[64:67]
	v_mfma_f32_16x16x32_bf16 v[116:119], v[148:151], v[184:187], v[116:119]
	v_mfma_f32_16x16x32_bf16 v[112:115], v[176:179], v[184:187], v[112:115]
	v_mfma_f32_16x16x32_bf16 v[100:103], v[148:151], v[198:201], v[100:103]
	v_mfma_f32_16x16x32_bf16 v[96:99], v[176:179], v[198:201], v[96:99]
	v_mfma_f32_16x16x32_bf16 v[84:87], v[148:151], v[206:209], v[84:87]
	v_mfma_f32_16x16x32_bf16 v[80:83], v[176:179], v[206:209], v[80:83]
	v_mfma_f32_16x16x32_bf16 v[68:71], v[148:151], v[214:217], v[68:71]
	v_mfma_f32_16x16x32_bf16 v[64:67], v[176:179], v[214:217], v[64:67]
	s_setprio 0
	s_barrier
; #define PG8_STAGE(bufoff, gbase, voff) do { _Pragma("unroll") for (int _i = 0; _i < 2; ++_i) \
;         __builtin_amdgcn_global_load_lds((const unsigned*)((const char*)(gbase) + (voff)[_i]), (PG8_LAS unsigned*)(lds + (bufoff) + ldsw + _i * 8192), 16, 0, 0); } while (0)
; #define PG8_LDA(dst, b, h) do { _Pragma("unroll") for (int m = 0; m < 4; ++m) _Pragma("unroll") for (int k = 0; k < 2; ++k) dst[m][k] = *(const PG8_LAS bf16x8*)(lds + PG8_SA(b, h) + aoff + m * 2048 + k * 1024); } while (0)
; #define PG8_LDB(dst, b, h) do { _Pragma("unroll") for (int n = 0; n < 2; ++n) _Pragma("unroll") for (int k = 0; k < 2; ++k) dst[n][k] = *(const PG8_LAS bf16x8*)(lds + PG8_SB(b, h) + boff + n * 2048 + k * 1024); } while (0)
; #define PG8_MMA(ai, bj, At, Bt) do { __builtin_amdgcn_s_setprio(1); _Pragma("unroll") for (int m = 0; m < 4; ++m) _Pragma("unroll") for (int n = 0; n < 2; ++n) _Pragma("unroll") for (int k = 0; k < 2; ++k) \
;         acc[ai][bj][m][n] = __builtin_amdgcn_mfma_f32_16x16x32_bf16(Bt[n][k], At[m][k], acc[ai][bj][m][n], 0, 0, 0); __builtin_amdgcn_s_setprio(0); } while (0)
; #define PG8_WAIT_V(n) asm volatile("s_waitcnt vmcnt(" #n ")" ::: "memory")
; #define PG8_WAIT_L(n) asm volatile("s_waitcnt lgkmcnt(" #n ")" ::: "memory")
; #define PG8_BAR __builtin_amdgcn_s_barrier()
; #define PG8_SCHED __builtin_amdgcn_sched_barrier(0)
; template <class Epi, class Sched, bool ALIGN_EPI = false, bool SP2 = false>
; __device__ __forceinline__ void gemm_phase(PG8_LAS unsigned char* lds, const Gemm g, const Sched& S, const Epi& E, const int wid) {
;     ...
;             PG8_LDA(At, 0, 1); PG8_STAGE(PG8_SB(0, 0), b2, voffB); PG8_STAGE(PG8_SB(0, 1), b2 + hstepB, voffB); PG8_STAGE(PG8_SA(0, 0), a2, voffA);
;             PG8_WAIT_V(8); PG8_WAIT_L(0); PG8_BAR; PG8_MMA(1, 0, At, B0); PG8_MMA(1, 1, At, B1); PG8_BAR; PG8_SCHED;
;             PG8_LDB(B0, 1, 0); PG8_LDB(B1, 1, 1); PG8_SCHED; PG8_LDA(At, 1, 0); PG8_STAGE(PG8_SA(0, 1), a2 + hstepA, voffA);
;             PG8_WAIT_V(8); PG8_WAIT_L(0); PG8_BAR; PG8_MMA(0, 0, At, B0); PG8_MMA(0, 1, At, B1); PG8_BAR; PG8_SCHED;
	s_add_i32 s71, s65, s39
	s_add_u32 s98, s34, 0x80
	s_addc_u32 s99, s35, 0
	s_mov_b32 m0, s71
	ds_read_b128 v[180:183], v192 offset:16384
	ds_read_b128 v[184:187], v192 offset:17408
	ds_read_b128 v[194:197], v192 offset:18432
	ds_read_b128 v[198:201], v192 offset:19456
	ds_read_b128 v[202:205], v192 offset:20480
	ds_read_b128 v[206:209], v192 offset:21504
	ds_read_b128 v[210:213], v192 offset:22528
	ds_read_b128 v[214:217], v192 offset:23552
	global_load_lds_dwordx4 v154, s[34:35]
	s_add_i32 m0, s71, 0x2000
	s_add_u32 s72, s34, 0x40000
	s_addc_u32 s73, s35, 0
	s_add_i32 s71, s66, s39
	global_load_lds_dwordx4 v158, s[34:35]
	s_mov_b32 m0, s71
	s_add_u32 s100, s36, 0x80
	s_addc_u32 s101, s37, 0
	global_load_lds_dwordx4 v154, s[72:73]
	s_add_i32 m0, s71, 0x2000
	s_nop 0
	global_load_lds_dwordx4 v158, s[72:73]
	s_mov_b32 m0, s40
	s_nop 0
	global_load_lds_dwordx4 v152, s[36:37]
	s_mov_b32 m0, s41
	s_nop 0
	global_load_lds_dwordx4 v156, s[36:37]
	s_waitcnt vmcnt(8) lgkmcnt(0)
	s_barrier
	s_setprio 1
	v_mfma_f32_16x16x32_bf16 v[60:63], v[128:131], v[180:183], v[60:63]
	v_mfma_f32_16x16x32_bf16 v[56:59], v[136:139], v[180:183], v[56:59]
	v_mfma_f32_16x16x32_bf16 v[44:47], v[128:131], v[194:197], v[44:47]
	v_mfma_f32_16x16x32_bf16 v[40:43], v[136:139], v[194:197], v[40:43]
	v_mfma_f32_16x16x32_bf16 v[28:31], v[128:131], v[202:205], v[28:31]
	v_mfma_f32_16x16x32_bf16 v[24:27], v[136:139], v[202:205], v[24:27]
	v_mfma_f32_16x16x32_bf16 v[12:15], v[128:131], v[210:213], v[12:15]
	v_mfma_f32_16x16x32_bf16 v[8:11], v[136:139], v[210:213], v[8:11]
	v_mfma_f32_16x16x32_bf16 v[60:63], v[132:135], v[184:187], v[60:63]
	v_mfma_f32_16x16x32_bf16 v[56:59], v[140:143], v[184:187], v[56:59]
	v_mfma_f32_16x16x32_bf16 v[44:47], v[132:135], v[198:201], v[44:47]
	v_mfma_f32_16x16x32_bf16 v[40:43], v[140:143], v[198:201], v[40:43]
	v_mfma_f32_16x16x32_bf16 v[28:31], v[132:135], v[206:209], v[28:31]
	v_mfma_f32_16x16x32_bf16 v[24:27], v[140:143], v[206:209], v[24:27]
	v_mfma_f32_16x16x32_bf16 v[12:15], v[132:135], v[214:217], v[12:15]
	v_mfma_f32_16x16x32_bf16 v[8:11], v[140:143], v[214:217], v[8:11]
	s_setprio 0
	s_setprio 1
	v_mfma_f32_16x16x32_bf16 v[52:55], v[144:147], v[180:183], v[52:55]
	v_mfma_f32_16x16x32_bf16 v[48:51], v[172:175], v[180:183], v[48:51]
	v_mfma_f32_16x16x32_bf16 v[36:39], v[144:147], v[194:197], v[36:39]
	v_mfma_f32_16x16x32_bf16 v[32:35], v[172:175], v[194:197], v[32:35]
	v_mfma_f32_16x16x32_bf16 v[20:23], v[144:147], v[202:205], v[20:23]
	v_mfma_f32_16x16x32_bf16 v[16:19], v[172:175], v[202:205], v[16:19]
	v_mfma_f32_16x16x32_bf16 v[4:7], v[144:147], v[210:213], v[4:7]
	v_mfma_f32_16x16x32_bf16 v[0:3], v[172:175], v[210:213], v[0:3]
	v_mfma_f32_16x16x32_bf16 v[52:55], v[148:151], v[184:187], v[52:55]
	v_mfma_f32_16x16x32_bf16 v[48:51], v[176:179], v[184:187], v[48:51]
	v_mfma_f32_16x16x32_bf16 v[36:39], v[148:151], v[198:201], v[36:39]
	v_mfma_f32_16x16x32_bf16 v[32:35], v[176:179], v[198:201], v[32:35]
	v_mfma_f32_16x16x32_bf16 v[20:23], v[148:151], v[206:209], v[20:23]
	v_mfma_f32_16x16x32_bf16 v[16:19], v[176:179], v[206:209], v[16:19]
	v_mfma_f32_16x16x32_bf16 v[4:7], v[148:151], v[214:217], v[4:7]
	v_mfma_f32_16x16x32_bf16 v[0:3], v[176:179], v[214:217], v[0:3]
	s_setprio 0
	s_barrier
	s_add_i32 s71, 0, 0x18000
	s_add_i32 s72, 0, 0x1c000
	ds_read_b128 v[128:131], v252
	ds_read_b128 v[132:135], v252 offset:1024
	ds_read_b128 v[136:139], v252 offset:2048
	ds_read_b128 v[140:143], v252 offset:3072
	ds_read_b128 v[144:147], v253
	ds_read_b128 v[148:151], v253 offset:1024
	ds_read_b128 v[172:175], v253 offset:2048
	ds_read_b128 v[176:179], v253 offset:3072
	s_add_u32 s36, s36, 0x40000
	s_addc_u32 s37, s37, 0
	s_mov_b32 m0, s44
	ds_read_b128 v[180:183], v192 offset:32768
	ds_read_b128 v[184:187], v192 offset:33792
	ds_read_b128 v[194:197], v192 offset:34816
	ds_read_b128 v[198:201], v192 offset:35840
	ds_read_b128 v[202:205], v192 offset:36864
	ds_read_b128 v[206:209], v192 offset:37888
	ds_read_b128 v[210:213], v192 offset:38912
	ds_read_b128 v[214:217], v192 offset:39936
	global_load_lds_dwordx4 v152, s[36:37]
	s_mov_b32 m0, s45
	s_nop 0
	global_load_lds_dwordx4 v156, s[36:37]
	s_waitcnt vmcnt(8) lgkmcnt(0)
	s_barrier
; #define PG8_STAGE(bufoff, gbase, voff) do { _Pragma("unroll") for (int _i = 0; _i < 2; ++_i) \
;         __builtin_amdgcn_global_load_lds((const unsigned*)((const char*)(gbase) + (voff)[_i]), (PG8_LAS unsigned*)(lds + (bufoff) + ldsw + _i * 8192), 16, 0, 0); } while (0)
; #define PG8_LDA(dst, b, h) do { _Pragma("unroll") for (int m = 0; m < 4; ++m) _Pragma("unroll") for (int k = 0; k < 2; ++k) dst[m][k] = *(const PG8_LAS bf16x8*)(lds + PG8_SA(b, h) + aoff + m * 2048 + k * 1024); } while (0)
; #define PG8_MMA(ai, bj, At, Bt) do { __builtin_amdgcn_s_setprio(1); _Pragma("unroll") for (int m = 0; m < 4; ++m) _Pragma("unroll") for (int n = 0; n < 2; ++n) _Pragma("unroll") for (int k = 0; k < 2; ++k) \
;         acc[ai][bj][m][n] = __builtin_amdgcn_mfma_f32_16x16x32_bf16(Bt[n][k], At[m][k], acc[ai][bj][m][n], 0, 0, 0); __builtin_amdgcn_s_setprio(0); } while (0)
; #define PG8_WAIT_V(n) asm volatile("s_waitcnt vmcnt(" #n ")" ::: "memory")
; #define PG8_WAIT_L(n) asm volatile("s_waitcnt lgkmcnt(" #n ")" ::: "memory")
; #define PG8_BAR __builtin_amdgcn_s_barrier()
; #define PG8_SCHED __builtin_amdgcn_sched_barrier(0)
; template <class Epi, class Sched, bool ALIGN_EPI = false, bool SP2 = false>
; __device__ __forceinline__ void gemm_phase(PG8_LAS unsigned char* lds, const Gemm g, const Sched& S, const Epi& E, const int wid) {
;     ...
;             PG8_WAIT_V(8); PG8_WAIT_L(0); PG8_BAR; PG8_MMA(0, 0, At, B0); PG8_MMA(0, 1, At, B1); PG8_BAR; PG8_SCHED;
;             PG8_LDA(At, 1, 1); PG8_STAGE(PG8_SB(1, 0), b3, voffB); PG8_STAGE(PG8_SB(1, 1), b3 + hstepB, voffB); PG8_STAGE(PG8_SA(1, 0), a3, voffA);
;             PG8_WAIT_V(8); PG8_WAIT_L(0); PG8_BAR; PG8_MMA(1, 0, At, B0); PG8_MMA(1, 1, At, B1); PG8_BAR; PG8_SCHED;
;     ...
;         if constexpr (ALIGN_EPI) { if (wr == 0) PG8_BAR; }
	s_setprio 1
	v_mfma_f32_16x16x32_bf16 v[124:127], v[128:131], v[180:183], v[124:127]
	v_mfma_f32_16x16x32_bf16 v[120:123], v[136:139], v[180:183], v[120:123]
	v_mfma_f32_16x16x32_bf16 v[108:111], v[128:131], v[194:197], v[108:111]
	v_mfma_f32_16x16x32_bf16 v[104:107], v[136:139], v[194:197], v[104:107]
	v_mfma_f32_16x16x32_bf16 v[92:95], v[128:131], v[202:205], v[92:95]
	v_mfma_f32_16x16x32_bf16 v[88:91], v[136:139], v[202:205], v[88:91]
	v_mfma_f32_16x16x32_bf16 v[76:79], v[128:131], v[210:213], v[76:79]
	v_mfma_f32_16x16x32_bf16 v[72:75], v[136:139], v[210:213], v[72:75]
	v_mfma_f32_16x16x32_bf16 v[124:127], v[132:135], v[184:187], v[124:127]
	v_mfma_f32_16x16x32_bf16 v[120:123], v[140:143], v[184:187], v[120:123]
	v_mfma_f32_16x16x32_bf16 v[108:111], v[132:135], v[198:201], v[108:111]
	v_mfma_f32_16x16x32_bf16 v[104:107], v[140:143], v[198:201], v[104:107]
	v_mfma_f32_16x16x32_bf16 v[92:95], v[132:135], v[206:209], v[92:95]
	v_mfma_f32_16x16x32_bf16 v[88:91], v[140:143], v[206:209], v[88:91]
	v_mfma_f32_16x16x32_bf16 v[76:79], v[132:135], v[214:217], v[76:79]
	v_mfma_f32_16x16x32_bf16 v[72:75], v[140:143], v[214:217], v[72:75]
	s_setprio 0
	s_setprio 1
	v_mfma_f32_16x16x32_bf16 v[116:119], v[144:147], v[180:183], v[116:119]
	v_mfma_f32_16x16x32_bf16 v[112:115], v[172:175], v[180:183], v[112:115]
	v_mfma_f32_16x16x32_bf16 v[100:103], v[144:147], v[194:197], v[100:103]
	v_mfma_f32_16x16x32_bf16 v[96:99], v[172:175], v[194:197], v[96:99]
	v_mfma_f32_16x16x32_bf16 v[84:87], v[144:147], v[202:205], v[84:87]
	v_mfma_f32_16x16x32_bf16 v[80:83], v[172:175], v[202:205], v[80:83]
	v_mfma_f32_16x16x32_bf16 v[68:71], v[144:147], v[210:213], v[68:71]
	v_mfma_f32_16x16x32_bf16 v[64:67], v[172:175], v[210:213], v[64:67]
	v_mfma_f32_16x16x32_bf16 v[116:119], v[148:151], v[184:187], v[116:119]
	v_mfma_f32_16x16x32_bf16 v[112:115], v[176:179], v[184:187], v[112:115]
	v_mfma_f32_16x16x32_bf16 v[100:103], v[148:151], v[198:201], v[100:103]
	v_mfma_f32_16x16x32_bf16 v[96:99], v[176:179], v[198:201], v[96:99]
	v_mfma_f32_16x16x32_bf16 v[84:87], v[148:151], v[206:209], v[84:87]
	v_mfma_f32_16x16x32_bf16 v[80:83], v[176:179], v[206:209], v[80:83]
	v_mfma_f32_16x16x32_bf16 v[68:71], v[148:151], v[214:217], v[68:71]
	v_mfma_f32_16x16x32_bf16 v[64:67], v[176:179], v[214:217], v[64:67]
	s_setprio 0
	s_barrier
	s_add_i32 s36, s71, s39
	s_mov_b32 m0, s36
	ds_read_b128 v[180:183], v192 offset:49152
	ds_read_b128 v[184:187], v192 offset:50176
	ds_read_b128 v[194:197], v192 offset:51200
	ds_read_b128 v[198:201], v192 offset:52224
	ds_read_b128 v[202:205], v192 offset:53248
	ds_read_b128 v[206:209], v192 offset:54272
	ds_read_b128 v[210:213], v192 offset:55296
	ds_read_b128 v[214:217], v192 offset:56320
	global_load_lds_dwordx4 v154, s[98:99]
	s_add_i32 m0, s36, 0x2000
	s_add_u32 s34, s34, 0x40080
	s_addc_u32 s35, s35, 0
	s_add_i32 s36, s72, s39
	global_load_lds_dwordx4 v158, s[98:99]
	s_mov_b32 m0, s36
	s_nop 0
	global_load_lds_dwordx4 v154, s[34:35]
	s_add_i32 m0, s36, 0x2000
	s_nop 0
	global_load_lds_dwordx4 v158, s[34:35]
	s_mov_b32 m0, s47
	s_nop 0
	global_load_lds_dwordx4 v152, s[100:101]
	s_mov_b32 m0, s48
	s_nop 0
	global_load_lds_dwordx4 v156, s[100:101]
	s_waitcnt vmcnt(8) lgkmcnt(0)
	s_barrier
	s_setprio 1
	v_mfma_f32_16x16x32_bf16 v[60:63], v[128:131], v[180:183], v[60:63]
	v_mfma_f32_16x16x32_bf16 v[56:59], v[136:139], v[180:183], v[56:59]
	v_mfma_f32_16x16x32_bf16 v[44:47], v[128:131], v[194:197], v[44:47]
	v_mfma_f32_16x16x32_bf16 v[40:43], v[136:139], v[194:197], v[40:43]
	v_mfma_f32_16x16x32_bf16 v[28:31], v[128:131], v[202:205], v[28:31]
	v_mfma_f32_16x16x32_bf16 v[24:27], v[136:139], v[202:205], v[24:27]
	v_mfma_f32_16x16x32_bf16 v[12:15], v[128:131], v[210:213], v[12:15]
	v_mfma_f32_16x16x32_bf16 v[8:11], v[136:139], v[210:213], v[8:11]
	v_mfma_f32_16x16x32_bf16 v[60:63], v[132:135], v[184:187], v[60:63]
	v_mfma_f32_16x16x32_bf16 v[56:59], v[140:143], v[184:187], v[56:59]
	v_mfma_f32_16x16x32_bf16 v[44:47], v[132:135], v[198:201], v[44:47]
	v_mfma_f32_16x16x32_bf16 v[40:43], v[140:143], v[198:201], v[40:43]
	v_mfma_f32_16x16x32_bf16 v[28:31], v[132:135], v[206:209], v[28:31]
	v_mfma_f32_16x16x32_bf16 v[24:27], v[140:143], v[206:209], v[24:27]
	v_mfma_f32_16x16x32_bf16 v[12:15], v[132:135], v[214:217], v[12:15]
	v_mfma_f32_16x16x32_bf16 v[8:11], v[140:143], v[214:217], v[8:11]
	s_setprio 0
	s_setprio 1
	v_mfma_f32_16x16x32_bf16 v[52:55], v[144:147], v[180:183], v[52:55]
	v_mfma_f32_16x16x32_bf16 v[48:51], v[172:175], v[180:183], v[48:51]
	v_mfma_f32_16x16x32_bf16 v[36:39], v[144:147], v[194:197], v[36:39]
	v_mfma_f32_16x16x32_bf16 v[32:35], v[172:175], v[194:197], v[32:35]
	v_mfma_f32_16x16x32_bf16 v[20:23], v[144:147], v[202:205], v[20:23]
	v_mfma_f32_16x16x32_bf16 v[16:19], v[172:175], v[202:205], v[16:19]
	v_mfma_f32_16x16x32_bf16 v[4:7], v[144:147], v[210:213], v[4:7]
	v_mfma_f32_16x16x32_bf16 v[0:3], v[172:175], v[210:213], v[0:3]
	v_mfma_f32_16x16x32_bf16 v[52:55], v[148:151], v[184:187], v[52:55]
	v_mfma_f32_16x16x32_bf16 v[48:51], v[176:179], v[184:187], v[48:51]
	v_mfma_f32_16x16x32_bf16 v[36:39], v[148:151], v[198:201], v[36:39]
	v_mfma_f32_16x16x32_bf16 v[32:35], v[176:179], v[198:201], v[32:35]
	v_mfma_f32_16x16x32_bf16 v[20:23], v[148:151], v[206:209], v[20:23]
	v_mfma_f32_16x16x32_bf16 v[16:19], v[176:179], v[206:209], v[16:19]
	v_mfma_f32_16x16x32_bf16 v[4:7], v[148:151], v[214:217], v[4:7]
	v_mfma_f32_16x16x32_bf16 v[0:3], v[176:179], v[214:217], v[0:3]
	s_setprio 0
	s_barrier
	s_add_i32 s70, s70, 2
	s_add_u32 s30, s30, 0x100
	s_addc_u32 s31, s31, 0
	s_add_u32 s68, s68, 0x100
	s_addc_u32 s69, s69, 0
	s_cmp_gt_u32 s70, 13
	s_cbranch_scc0 .LBB0_1780
	s_and_b64 vcc, exec, s[16:17]
	s_cbranch_vccz .LBB0_1783
	s_barrier

; #define PG8_STAGE(bufoff, gbase, voff) do { _Pragma("unroll") for (int _i = 0; _i < 2; ++_i) \
;         __builtin_amdgcn_global_load_lds((const unsigned*)((const char*)(gbase) + (voff)[_i]), (PG8_LAS unsigned*)(lds + (bufoff) + ldsw + _i * 8192), 16, 0, 0); } while (0)
; #define PG8_LDA(dst, b, h) do { _Pragma("unroll") for (int m = 0; m < 4; ++m) _Pragma("unroll") for (int k = 0; k < 2; ++k) dst[m][k] = *(const PG8_LAS bf16x8*)(lds + PG8_SA(b, h) + aoff + m * 2048 + k * 1024); } while (0)
; #define PG8_LDB(dst, b, h) do { _Pragma("unroll") for (int n = 0; n < 2; ++n) _Pragma("unroll") for (int k = 0; k < 2; ++k) dst[n][k] = *(const PG8_LAS bf16x8*)(lds + PG8_SB(b, h) + boff + n * 2048 + k * 1024); } while (0)
; #define PG8_MMA(ai, bj, At, Bt) do { __builtin_amdgcn_s_setprio(1); _Pragma("unroll") for (int m = 0; m < 4; ++m) _Pragma("unroll") for (int n = 0; n < 2; ++n) _Pragma("unroll") for (int k = 0; k < 2; ++k) \
;         acc[ai][bj][m][n] = __builtin_amdgcn_mfma_f32_16x16x32_bf16(Bt[n][k], At[m][k], acc[ai][bj][m][n], 0, 0, 0); __builtin_amdgcn_s_setprio(0); } while (0)
; template <class Epi, class Sched, bool ALIGN_EPI = false, bool SP2 = false>
; __device__ __forceinline__ void gemm_phase(PG8_LAS unsigned char* lds, const Gemm g, const Sched& S, const Epi& E, const int wid) {
;     ...
;         const bool has_next = S.next(ui + 1, nxt);
;         const char* nA = has_next ? (const char*)g.A + (size_t)nxt.pm * tstepA : cA; const char* nB = has_next ? (const char*)g.Bt + (size_t)nxt.pn * tstepB : cB;
;         for (int t = 0; t < nt; t += 2) {
;             const bool last = (t == nt - 2);
;             const char* a1 = cA + (size_t)(t + 1) * kstep;
;             const char* a2 = last ? nA : cA + (size_t)(t + 2) * kstep; const char* b2 = last ? nB : cB + (size_t)(t + 2) * kstep;
;             const char* a3 = a2 + kstep; const char* b3 = b2 + kstep;
;             if (last && has_next) S.a_ready(nxt);
;             if constexpr (SP2) {
;             PG8_LDB(B0, 0, 0); PG8_LDB(B1, 0, 1); PG8_SCHED; PG8_LDA(At, 0, 0); PG8_STAGE(PG8_SA(1, 1), a1 + hstepA, voffA);
;             PG8_WAIT_V(8); PG8_WAIT_L(0); PG8_BAR; PG8_MMA(0, 0, At, B0); PG8_MMA(0, 1, At, B1); PG8_BAR; PG8_SCHED;
;             PG8_LDA(At, 0, 1); PG8_STAGE(PG8_SB(0, 0), b2, voffB); PG8_STAGE(PG8_SB(0, 1), b2 + hstepB, voffB); PG8_STAGE(PG8_SA(0, 0), a2, voffA);
.LBB0_1866:
	s_ashr_i32 s17, s16, 31
	s_lshl_b64 s[18:19], s[16:17], 19
	s_add_u32 s18, s0, s18
	s_addc_u32 s19, s1, s19
	s_and_b64 s[20:21], s[2:3], exec
	s_cselect_b32 s17, s19, s25
	s_cselect_b32 s49, s18, s24
	s_ashr_i32 s15, s14, 31
	s_lshl_b64 s[20:21], s[14:15], 19
	s_add_u32 s20, s30, s20
	s_addc_u32 s21, s31, s21
	s_and_b64 s[28:29], s[2:3], exec
	s_cselect_b32 s15, s21, s27
	s_cselect_b32 s64, s20, s26
	s_add_u32 s24, s24, 0x40080
	s_addc_u32 s25, s25, 0
	s_add_u32 s65, s26, 0x100
	s_addc_u32 s66, s27, 0
	s_mov_b32 s67, -2
	v_add_u32_e32 v252, 0x18000, v165
	v_add_u32_e32 v253, 0x1c000, v165
	ds_read_b128 v[148:151], v166
	ds_read_b128 v[152:155], v166 offset:1024
	ds_read_b128 v[156:159], v166 offset:2048
	ds_read_b128 v[160:163], v166 offset:3072
	ds_read_b128 v[172:175], v167
	ds_read_b128 v[176:179], v167 offset:1024
	ds_read_b128 v[180:183], v167 offset:2048
	ds_read_b128 v[184:187], v167 offset:3072
	s_add_u32 s26, s24, 0xfffc0080
	s_addc_u32 s27, s25, -1
	s_cmp_eq_u32 s67, 12
	s_cselect_b32 s29, s17, s27
	s_cselect_b32 s28, s49, s26
	s_cselect_b32 s27, s15, s66
	s_cselect_b32 s26, s64, s65
	s_add_i32 m0, s36, 0xc000
	ds_read_b128 v[188:191], v168
	ds_read_b128 v[192:195], v168 offset:1024
	ds_read_b128 v[196:199], v168 offset:2048
	ds_read_b128 v[200:203], v168 offset:3072
	ds_read_b128 v[204:207], v168 offset:4096
	ds_read_b128 v[208:211], v168 offset:5120
	ds_read_b128 v[212:215], v168 offset:6144
	ds_read_b128 v[216:219], v168 offset:7168
	global_load_lds_dwordx4 v140, s[24:25]
	s_add_i32 m0, s36, 0xe000
	s_nop 0
	global_load_lds_dwordx4 v142, s[24:25]
	s_waitcnt vmcnt(8) lgkmcnt(0)
	s_barrier
	s_setprio 1
	v_mfma_f32_16x16x32_bf16 v[124:127], v[148:151], v[188:191], 0
	v_mfma_f32_16x16x32_bf16 v[116:119], v[156:159], v[188:191], 0
	v_mfma_f32_16x16x32_bf16 v[108:111], v[148:151], v[196:199], 0
	v_mfma_f32_16x16x32_bf16 v[100:103], v[156:159], v[196:199], 0
	v_mfma_f32_16x16x32_bf16 v[92:95], v[148:151], v[204:207], 0
	v_mfma_f32_16x16x32_bf16 v[84:87], v[156:159], v[204:207], 0
	v_mfma_f32_16x16x32_bf16 v[76:79], v[148:151], v[212:215], 0
	v_mfma_f32_16x16x32_bf16 v[68:71], v[156:159], v[212:215], 0
	v_mfma_f32_16x16x32_bf16 v[124:127], v[152:155], v[192:195], v[124:127]
	v_mfma_f32_16x16x32_bf16 v[116:119], v[160:163], v[192:195], v[116:119]
	v_mfma_f32_16x16x32_bf16 v[108:111], v[152:155], v[200:203], v[108:111]
	v_mfma_f32_16x16x32_bf16 v[100:103], v[160:163], v[200:203], v[100:103]
	v_mfma_f32_16x16x32_bf16 v[92:95], v[152:155], v[208:211], v[92:95]
	v_mfma_f32_16x16x32_bf16 v[84:87], v[160:163], v[208:211], v[84:87]
	v_mfma_f32_16x16x32_bf16 v[76:79], v[152:155], v[216:219], v[76:79]
	v_mfma_f32_16x16x32_bf16 v[68:71], v[160:163], v[216:219], v[68:71]
	s_setprio 0
	s_setprio 1
	v_mfma_f32_16x16x32_bf16 v[120:123], v[172:175], v[188:191], 0
	v_mfma_f32_16x16x32_bf16 v[112:115], v[180:183], v[188:191], 0
	v_mfma_f32_16x16x32_bf16 v[104:107], v[172:175], v[196:199], 0
	v_mfma_f32_16x16x32_bf16 v[96:99], v[180:183], v[196:199], 0
	v_mfma_f32_16x16x32_bf16 v[88:91], v[172:175], v[204:207], 0
	v_mfma_f32_16x16x32_bf16 v[80:83], v[180:183], v[204:207], 0
	v_mfma_f32_16x16x32_bf16 v[72:75], v[172:175], v[212:215], 0
	v_mfma_f32_16x16x32_bf16 v[64:67], v[180:183], v[212:215], 0
	v_mfma_f32_16x16x32_bf16 v[120:123], v[176:179], v[192:195], v[120:123]
	v_mfma_f32_16x16x32_bf16 v[112:115], v[184:187], v[192:195], v[112:115]
	v_mfma_f32_16x16x32_bf16 v[104:107], v[176:179], v[200:203], v[104:107]
	v_mfma_f32_16x16x32_bf16 v[96:99], v[184:187], v[200:203], v[96:99]
	v_mfma_f32_16x16x32_bf16 v[88:91], v[176:179], v[208:211], v[88:91]
	v_mfma_f32_16x16x32_bf16 v[80:83], v[184:187], v[208:211], v[80:83]
	v_mfma_f32_16x16x32_bf16 v[72:75], v[176:179], v[216:219], v[72:75]
	v_mfma_f32_16x16x32_bf16 v[64:67], v[184:187], v[216:219], v[64:67]
	s_setprio 0
	s_barrier
	s_add_i32 s68, s45, s33
	s_add_u32 s98, s26, 0x80
	s_addc_u32 s99, s27, 0
	s_mov_b32 m0, s68
	ds_read_b128 v[188:191], v168 offset:16384
	ds_read_b128 v[192:195], v168 offset:17408
	ds_read_b128 v[196:199], v168 offset:18432
	ds_read_b128 v[200:203], v168 offset:19456
	ds_read_b128 v[204:207], v168 offset:20480
	ds_read_b128 v[208:211], v168 offset:21504
	ds_read_b128 v[212:215], v168 offset:22528
	ds_read_b128 v[216:219], v168 offset:23552
	global_load_lds_dwordx4 v132, s[26:27]
	s_add_i32 m0, s68, 0x2000
	s_add_u32 s68, s26, 0x40000
	s_addc_u32 s69, s27, 0
	s_add_i32 s70, s46, s33
	global_load_lds_dwordx4 v128, s[26:27]
	s_mov_b32 m0, s70
	s_add_u32 s100, s28, 0x80
	s_addc_u32 s101, s29, 0
	global_load_lds_dwordx4 v132, s[68:69]
	s_add_i32 m0, s70, 0x2000
	s_nop 0
	global_load_lds_dwordx4 v128, s[68:69]
	s_mov_b32 m0, s36
	s_nop 0
	global_load_lds_dwordx4 v134, s[28:29]
	s_mov_b32 m0, s37
	s_nop 0
	global_load_lds_dwordx4 v130, s[28:29]
	s_waitcnt vmcnt(8) lgkmcnt(0)
	s_barrier
; #define PG8_STAGE(bufoff, gbase, voff) do { _Pragma("unroll") for (int _i = 0; _i < 2; ++_i) \
;         __builtin_amdgcn_global_load_lds((const unsigned*)((const char*)(gbase) + (voff)[_i]), (PG8_LAS unsigned*)(lds + (bufoff) + ldsw + _i * 8192), 16, 0, 0); } while (0)
; #define PG8_LDA(dst, b, h) do { _Pragma("unroll") for (int m = 0; m < 4; ++m) _Pragma("unroll") for (int k = 0; k < 2; ++k) dst[m][k] = *(const PG8_LAS bf16x8*)(lds + PG8_SA(b, h) + aoff + m * 2048 + k * 1024); } while (0)
; #define PG8_LDB(dst, b, h) do { _Pragma("unroll") for (int n = 0; n < 2; ++n) _Pragma("unroll") for (int k = 0; k < 2; ++k) dst[n][k] = *(const PG8_LAS bf16x8*)(lds + PG8_SB(b, h) + boff + n * 2048 + k * 1024); } while (0)
; #define PG8_MMA(ai, bj, At, Bt) do { __builtin_amdgcn_s_setprio(1); _Pragma("unroll") for (int m = 0; m < 4; ++m) _Pragma("unroll") for (int n = 0; n < 2; ++n) _Pragma("unroll") for (int k = 0; k < 2; ++k) \
;         acc[ai][bj][m][n] = __builtin_amdgcn_mfma_f32_16x16x32_bf16(Bt[n][k], At[m][k], acc[ai][bj][m][n], 0, 0, 0); __builtin_amdgcn_s_setprio(0); } while (0)
; #define PG8_WAIT_V(n) asm volatile("s_waitcnt vmcnt(" #n ")" ::: "memory")
; #define PG8_WAIT_L(n) asm volatile("s_waitcnt lgkmcnt(" #n ")" ::: "memory")
; #define PG8_BAR __builtin_amdgcn_s_barrier()
; #define PG8_SCHED __builtin_amdgcn_sched_barrier(0)
; template <class Epi, class Sched, bool ALIGN_EPI = false, bool SP2 = false>
; __device__ __forceinline__ void gemm_phase(PG8_LAS unsigned char* lds, const Gemm g, const Sched& S, const Epi& E, const int wid) {
;     ...
;             PG8_WAIT_V(8); PG8_WAIT_L(0); PG8_BAR; PG8_MMA(1, 0, At, B0); PG8_MMA(1, 1, At, B1); PG8_BAR; PG8_SCHED;
;             PG8_LDB(B0, 1, 0); PG8_LDB(B1, 1, 1); PG8_SCHED; PG8_LDA(At, 1, 0); PG8_STAGE(PG8_SA(0, 1), a2 + hstepA, voffA);
;             PG8_WAIT_V(8); PG8_WAIT_L(0); PG8_BAR; PG8_MMA(0, 0, At, B0); PG8_MMA(0, 1, At, B1); PG8_BAR; PG8_SCHED;
	s_setprio 1
	v_mfma_f32_16x16x32_bf16 v[60:63], v[148:151], v[188:191], 0
	v_mfma_f32_16x16x32_bf16 v[52:55], v[156:159], v[188:191], 0
	v_mfma_f32_16x16x32_bf16 v[44:47], v[148:151], v[196:199], 0
	v_mfma_f32_16x16x32_bf16 v[36:39], v[156:159], v[196:199], 0
	v_mfma_f32_16x16x32_bf16 v[28:31], v[148:151], v[204:207], 0
	v_mfma_f32_16x16x32_bf16 v[20:23], v[156:159], v[204:207], 0
	v_mfma_f32_16x16x32_bf16 v[12:15], v[148:151], v[212:215], 0
	v_mfma_f32_16x16x32_bf16 v[4:7], v[156:159], v[212:215], 0
	v_mfma_f32_16x16x32_bf16 v[60:63], v[152:155], v[192:195], v[60:63]
	v_mfma_f32_16x16x32_bf16 v[52:55], v[160:163], v[192:195], v[52:55]
	v_mfma_f32_16x16x32_bf16 v[44:47], v[152:155], v[200:203], v[44:47]
	v_mfma_f32_16x16x32_bf16 v[36:39], v[160:163], v[200:203], v[36:39]
	v_mfma_f32_16x16x32_bf16 v[28:31], v[152:155], v[208:211], v[28:31]
	v_mfma_f32_16x16x32_bf16 v[20:23], v[160:163], v[208:211], v[20:23]
	v_mfma_f32_16x16x32_bf16 v[12:15], v[152:155], v[216:219], v[12:15]
	v_mfma_f32_16x16x32_bf16 v[4:7], v[160:163], v[216:219], v[4:7]
	s_setprio 0
	s_setprio 1
	v_mfma_f32_16x16x32_bf16 v[56:59], v[172:175], v[188:191], 0
	v_mfma_f32_16x16x32_bf16 v[48:51], v[180:183], v[188:191], 0
	v_mfma_f32_16x16x32_bf16 v[40:43], v[172:175], v[196:199], 0
	v_mfma_f32_16x16x32_bf16 v[32:35], v[180:183], v[196:199], 0
	v_mfma_f32_16x16x32_bf16 v[24:27], v[172:175], v[204:207], 0
	v_mfma_f32_16x16x32_bf16 v[16:19], v[180:183], v[204:207], 0
	v_mfma_f32_16x16x32_bf16 v[8:11], v[172:175], v[212:215], 0
	v_mfma_f32_16x16x32_bf16 v[0:3], v[180:183], v[212:215], 0
	v_mfma_f32_16x16x32_bf16 v[56:59], v[176:179], v[192:195], v[56:59]
	v_mfma_f32_16x16x32_bf16 v[48:51], v[184:187], v[192:195], v[48:51]
	v_mfma_f32_16x16x32_bf16 v[40:43], v[176:179], v[200:203], v[40:43]
	v_mfma_f32_16x16x32_bf16 v[32:35], v[184:187], v[200:203], v[32:35]
	v_mfma_f32_16x16x32_bf16 v[24:27], v[176:179], v[208:211], v[24:27]
	v_mfma_f32_16x16x32_bf16 v[16:19], v[184:187], v[208:211], v[16:19]
	v_mfma_f32_16x16x32_bf16 v[8:11], v[176:179], v[216:219], v[8:11]
	v_mfma_f32_16x16x32_bf16 v[0:3], v[184:187], v[216:219], v[0:3]
	s_setprio 0
	s_barrier
	s_add_i32 s68, 0, 0x18000
	s_add_i32 s69, 0, 0x1c000
	ds_read_b128 v[148:151], v252
	ds_read_b128 v[152:155], v252 offset:1024
	ds_read_b128 v[156:159], v252 offset:2048
	ds_read_b128 v[160:163], v252 offset:3072
	ds_read_b128 v[172:175], v253
	ds_read_b128 v[176:179], v253 offset:1024
	ds_read_b128 v[180:183], v253 offset:2048
	ds_read_b128 v[184:187], v253 offset:3072
	s_add_u32 s28, s28, 0x40000
	s_addc_u32 s29, s29, 0
	s_mov_b32 m0, s38
	ds_read_b128 v[188:191], v168 offset:32768
	ds_read_b128 v[192:195], v168 offset:33792
	ds_read_b128 v[196:199], v168 offset:34816
	ds_read_b128 v[200:203], v168 offset:35840
	ds_read_b128 v[204:207], v168 offset:36864
	ds_read_b128 v[208:211], v168 offset:37888
	ds_read_b128 v[212:215], v168 offset:38912
	ds_read_b128 v[216:219], v168 offset:39936
	global_load_lds_dwordx4 v134, s[28:29]
	s_mov_b32 m0, s39
	s_nop 0
	global_load_lds_dwordx4 v130, s[28:29]
	s_waitcnt vmcnt(8) lgkmcnt(0)
	s_barrier
	s_setprio 1
	v_mfma_f32_16x16x32_bf16 v[124:127], v[148:151], v[188:191], v[124:127]
	v_mfma_f32_16x16x32_bf16 v[116:119], v[156:159], v[188:191], v[116:119]
	v_mfma_f32_16x16x32_bf16 v[108:111], v[148:151], v[196:199], v[108:111]
	v_mfma_f32_16x16x32_bf16 v[100:103], v[156:159], v[196:199], v[100:103]
	v_mfma_f32_16x16x32_bf16 v[92:95], v[148:151], v[204:207], v[92:95]
	v_mfma_f32_16x16x32_bf16 v[84:87], v[156:159], v[204:207], v[84:87]
	v_mfma_f32_16x16x32_bf16 v[76:79], v[148:151], v[212:215], v[76:79]
	v_mfma_f32_16x16x32_bf16 v[68:71], v[156:159], v[212:215], v[68:71]
	v_mfma_f32_16x16x32_bf16 v[124:127], v[152:155], v[192:195], v[124:127]
	v_mfma_f32_16x16x32_bf16 v[116:119], v[160:163], v[192:195], v[116:119]
	v_mfma_f32_16x16x32_bf16 v[108:111], v[152:155], v[200:203], v[108:111]
	v_mfma_f32_16x16x32_bf16 v[100:103], v[160:163], v[200:203], v[100:103]
	v_mfma_f32_16x16x32_bf16 v[92:95], v[152:155], v[208:211], v[92:95]
	v_mfma_f32_16x16x32_bf16 v[84:87], v[160:163], v[208:211], v[84:87]
	v_mfma_f32_16x16x32_bf16 v[76:79], v[152:155], v[216:219], v[76:79]
	v_mfma_f32_16x16x32_bf16 v[68:71], v[160:163], v[216:219], v[68:71]
	s_setprio 0
	s_setprio 1
	v_mfma_f32_16x16x32_bf16 v[120:123], v[172:175], v[188:191], v[120:123]
	v_mfma_f32_16x16x32_bf16 v[112:115], v[180:183], v[188:191], v[112:115]
	v_mfma_f32_16x16x32_bf16 v[104:107], v[172:175], v[196:199], v[104:107]
	v_mfma_f32_16x16x32_bf16 v[96:99], v[180:183], v[196:199], v[96:99]
	v_mfma_f32_16x16x32_bf16 v[88:91], v[172:175], v[204:207], v[88:91]
	v_mfma_f32_16x16x32_bf16 v[80:83], v[180:183], v[204:207], v[80:83]
	v_mfma_f32_16x16x32_bf16 v[72:75], v[172:175], v[212:215], v[72:75]
	v_mfma_f32_16x16x32_bf16 v[64:67], v[180:183], v[212:215], v[64:67]
	v_mfma_f32_16x16x32_bf16 v[120:123], v[176:179], v[192:195], v[120:123]
	v_mfma_f32_16x16x32_bf16 v[112:115], v[184:187], v[192:195], v[112:115]
	v_mfma_f32_16x16x32_bf16 v[104:107], v[176:179], v[200:203], v[104:107]
	v_mfma_f32_16x16x32_bf16 v[96:99], v[184:187], v[200:203], v[96:99]
	v_mfma_f32_16x16x32_bf16 v[88:91], v[176:179], v[208:211], v[88:91]
	v_mfma_f32_16x16x32_bf16 v[80:83], v[184:187], v[208:211], v[80:83]
	v_mfma_f32_16x16x32_bf16 v[72:75], v[176:179], v[216:219], v[72:75]
	v_mfma_f32_16x16x32_bf16 v[64:67], v[184:187], v[216:219], v[64:67]
	s_setprio 0
	s_barrier
; #define PG8_STAGE(bufoff, gbase, voff) do { _Pragma("unroll") for (int _i = 0; _i < 2; ++_i) \
;         __builtin_amdgcn_global_load_lds((const unsigned*)((const char*)(gbase) + (voff)[_i]), (PG8_LAS unsigned*)(lds + (bufoff) + ldsw + _i * 8192), 16, 0, 0); } while (0)
; #define PG8_LDA(dst, b, h) do { _Pragma("unroll") for (int m = 0; m < 4; ++m) _Pragma("unroll") for (int k = 0; k < 2; ++k) dst[m][k] = *(const PG8_LAS bf16x8*)(lds + PG8_SA(b, h) + aoff + m * 2048 + k * 1024); } while (0)
; #define PG8_LDB(dst, b, h) do { _Pragma("unroll") for (int n = 0; n < 2; ++n) _Pragma("unroll") for (int k = 0; k < 2; ++k) dst[n][k] = *(const PG8_LAS bf16x8*)(lds + PG8_SB(b, h) + boff + n * 2048 + k * 1024); } while (0)
; #define PG8_MMA(ai, bj, At, Bt) do { __builtin_amdgcn_s_setprio(1); _Pragma("unroll") for (int m = 0; m < 4; ++m) _Pragma("unroll") for (int n = 0; n < 2; ++n) _Pragma("unroll") for (int k = 0; k < 2; ++k) \
;         acc[ai][bj][m][n] = __builtin_amdgcn_mfma_f32_16x16x32_bf16(Bt[n][k], At[m][k], acc[ai][bj][m][n], 0, 0, 0); __builtin_amdgcn_s_setprio(0); } while (0)
; #define PG8_WAIT_V(n) asm volatile("s_waitcnt vmcnt(" #n ")" ::: "memory")
; #define PG8_BAR __builtin_amdgcn_s_barrier()
; template <class Epi, class Sched, bool ALIGN_EPI = false, bool SP2 = false>
; __device__ __forceinline__ void gemm_phase(PG8_LAS unsigned char* lds, const Gemm g, const Sched& S, const Epi& E, const int wid) {
;     ...
;         for (int t = 0; t < nt; t += 2) {
;             const bool last = (t == nt - 2);
;             const char* a1 = cA + (size_t)(t + 1) * kstep;
;             const char* a2 = last ? nA : cA + (size_t)(t + 2) * kstep; const char* b2 = last ? nB : cB + (size_t)(t + 2) * kstep;
;             const char* a3 = a2 + kstep; const char* b3 = b2 + kstep;
;             if (last && has_next) S.a_ready(nxt);
;             if constexpr (SP2) {
;             PG8_LDB(B0, 0, 0); PG8_LDB(B1, 0, 1); PG8_SCHED; PG8_LDA(At, 0, 0); PG8_STAGE(PG8_SA(1, 1), a1 + hstepA, voffA);
;             PG8_WAIT_V(8); PG8_WAIT_L(0); PG8_BAR; PG8_MMA(0, 0, At, B0); PG8_MMA(0, 1, At, B1); PG8_BAR; PG8_SCHED;
;     ...
;             PG8_LDA(At, 1, 1); PG8_STAGE(PG8_SB(1, 0), b3, voffB); PG8_STAGE(PG8_SB(1, 1), b3 + hstepB, voffB); PG8_STAGE(PG8_SA(1, 0), a3, voffA);
;             PG8_WAIT_V(8); PG8_WAIT_L(0); PG8_BAR; PG8_MMA(1, 0, At, B0); PG8_MMA(1, 1, At, B1); PG8_BAR; PG8_SCHED;
	s_add_i32 s28, s68, s33
	s_mov_b32 m0, s28
	ds_read_b128 v[188:191], v168 offset:49152
	ds_read_b128 v[192:195], v168 offset:50176
	ds_read_b128 v[196:199], v168 offset:51200
	ds_read_b128 v[200:203], v168 offset:52224
	ds_read_b128 v[204:207], v168 offset:53248
	ds_read_b128 v[208:211], v168 offset:54272
	ds_read_b128 v[212:215], v168 offset:55296
	ds_read_b128 v[216:219], v168 offset:56320
	global_load_lds_dwordx4 v132, s[98:99]
	s_add_i32 m0, s28, 0x2000
	s_add_u32 s26, s26, 0x40080
	s_addc_u32 s27, s27, 0
	s_add_i32 s28, s69, s33
	global_load_lds_dwordx4 v128, s[98:99]
	s_mov_b32 m0, s28
	s_nop 0
	global_load_lds_dwordx4 v132, s[26:27]
	s_add_i32 m0, s28, 0x2000
	s_nop 0
	global_load_lds_dwordx4 v128, s[26:27]
	s_mov_b32 m0, s40
	s_nop 0
	global_load_lds_dwordx4 v134, s[100:101]
	s_mov_b32 m0, s41
	s_nop 0
	global_load_lds_dwordx4 v130, s[100:101]
	s_waitcnt vmcnt(8) lgkmcnt(0)
	s_barrier
	s_setprio 1
	v_mfma_f32_16x16x32_bf16 v[60:63], v[148:151], v[188:191], v[60:63]
	v_mfma_f32_16x16x32_bf16 v[52:55], v[156:159], v[188:191], v[52:55]
	v_mfma_f32_16x16x32_bf16 v[44:47], v[148:151], v[196:199], v[44:47]
	v_mfma_f32_16x16x32_bf16 v[36:39], v[156:159], v[196:199], v[36:39]
	v_mfma_f32_16x16x32_bf16 v[28:31], v[148:151], v[204:207], v[28:31]
	v_mfma_f32_16x16x32_bf16 v[20:23], v[156:159], v[204:207], v[20:23]
	v_mfma_f32_16x16x32_bf16 v[12:15], v[148:151], v[212:215], v[12:15]
	v_mfma_f32_16x16x32_bf16 v[4:7], v[156:159], v[212:215], v[4:7]
	v_mfma_f32_16x16x32_bf16 v[60:63], v[152:155], v[192:195], v[60:63]
	v_mfma_f32_16x16x32_bf16 v[52:55], v[160:163], v[192:195], v[52:55]
	v_mfma_f32_16x16x32_bf16 v[44:47], v[152:155], v[200:203], v[44:47]
	v_mfma_f32_16x16x32_bf16 v[36:39], v[160:163], v[200:203], v[36:39]
	v_mfma_f32_16x16x32_bf16 v[28:31], v[152:155], v[208:211], v[28:31]
	v_mfma_f32_16x16x32_bf16 v[20:23], v[160:163], v[208:211], v[20:23]
	v_mfma_f32_16x16x32_bf16 v[12:15], v[152:155], v[216:219], v[12:15]
	v_mfma_f32_16x16x32_bf16 v[4:7], v[160:163], v[216:219], v[4:7]
	s_setprio 0
	s_setprio 1
	v_mfma_f32_16x16x32_bf16 v[56:59], v[172:175], v[188:191], v[56:59]
	v_mfma_f32_16x16x32_bf16 v[48:51], v[180:183], v[188:191], v[48:51]
	v_mfma_f32_16x16x32_bf16 v[40:43], v[172:175], v[196:199], v[40:43]
	v_mfma_f32_16x16x32_bf16 v[32:35], v[180:183], v[196:199], v[32:35]
	v_mfma_f32_16x16x32_bf16 v[24:27], v[172:175], v[204:207], v[24:27]
	v_mfma_f32_16x16x32_bf16 v[16:19], v[180:183], v[204:207], v[16:19]
	v_mfma_f32_16x16x32_bf16 v[8:11], v[172:175], v[212:215], v[8:11]
	v_mfma_f32_16x16x32_bf16 v[0:3], v[180:183], v[212:215], v[0:3]
	v_mfma_f32_16x16x32_bf16 v[56:59], v[176:179], v[192:195], v[56:59]
	v_mfma_f32_16x16x32_bf16 v[48:51], v[184:187], v[192:195], v[48:51]
	v_mfma_f32_16x16x32_bf16 v[40:43], v[176:179], v[200:203], v[40:43]
	v_mfma_f32_16x16x32_bf16 v[32:35], v[184:187], v[200:203], v[32:35]
	v_mfma_f32_16x16x32_bf16 v[24:27], v[176:179], v[208:211], v[24:27]
	v_mfma_f32_16x16x32_bf16 v[16:19], v[184:187], v[208:211], v[16:19]
	v_mfma_f32_16x16x32_bf16 v[8:11], v[176:179], v[216:219], v[8:11]
	v_mfma_f32_16x16x32_bf16 v[0:3], v[184:187], v[216:219], v[0:3]
	s_setprio 0
	s_barrier
	s_add_i32 s67, s67, 2
	s_add_u32 s24, s24, 0x100
	s_addc_u32 s25, s25, 0
	s_add_u32 s65, s65, 0x100
	s_addc_u32 s66, s66, 0
	s_cmp_gt_u32 s67, 13
.LBB0_1867:
	ds_read_b128 v[148:151], v166
	ds_read_b128 v[152:155], v166 offset:1024
	ds_read_b128 v[156:159], v166 offset:2048
	ds_read_b128 v[160:163], v166 offset:3072
	ds_read_b128 v[172:175], v167
	ds_read_b128 v[176:179], v167 offset:1024
	ds_read_b128 v[180:183], v167 offset:2048
	ds_read_b128 v[184:187], v167 offset:3072
	s_add_u32 s26, s24, 0xfffc0080
	s_addc_u32 s27, s25, -1
	s_cmp_eq_u32 s67, 12
	s_cselect_b32 s29, s17, s27
	s_cselect_b32 s28, s49, s26
	s_cselect_b32 s27, s15, s66
	s_cselect_b32 s26, s64, s65
	s_add_i32 m0, s36, 0xc000
	ds_read_b128 v[188:191], v168
	ds_read_b128 v[192:195], v168 offset:1024
	ds_read_b128 v[196:199], v168 offset:2048
	ds_read_b128 v[200:203], v168 offset:3072
	ds_read_b128 v[204:207], v168 offset:4096
	ds_read_b128 v[208:211], v168 offset:5120
	ds_read_b128 v[212:215], v168 offset:6144
	ds_read_b128 v[216:219], v168 offset:7168
	global_load_lds_dwordx4 v140, s[24:25]
	s_add_i32 m0, s36, 0xe000
	s_nop 0
	global_load_lds_dwordx4 v142, s[24:25]
	s_waitcnt vmcnt(8) lgkmcnt(0)
	s_barrier
	s_setprio 1
	v_mfma_f32_16x16x32_bf16 v[124:127], v[148:151], v[188:191], v[124:127]
	v_mfma_f32_16x16x32_bf16 v[116:119], v[156:159], v[188:191], v[116:119]
	v_mfma_f32_16x16x32_bf16 v[108:111], v[148:151], v[196:199], v[108:111]
	v_mfma_f32_16x16x32_bf16 v[100:103], v[156:159], v[196:199], v[100:103]
	v_mfma_f32_16x16x32_bf16 v[92:95], v[148:151], v[204:207], v[92:95]
	v_mfma_f32_16x16x32_bf16 v[84:87], v[156:159], v[204:207], v[84:87]
	v_mfma_f32_16x16x32_bf16 v[76:79], v[148:151], v[212:215], v[76:79]
	v_mfma_f32_16x16x32_bf16 v[68:71], v[156:159], v[212:215], v[68:71]
	v_mfma_f32_16x16x32_bf16 v[124:127], v[152:155], v[192:195], v[124:127]
	v_mfma_f32_16x16x32_bf16 v[116:119], v[160:163], v[192:195], v[116:119]
	v_mfma_f32_16x16x32_bf16 v[108:111], v[152:155], v[200:203], v[108:111]
	v_mfma_f32_16x16x32_bf16 v[100:103], v[160:163], v[200:203], v[100:103]
	v_mfma_f32_16x16x32_bf16 v[92:95], v[152:155], v[208:211], v[92:95]
	v_mfma_f32_16x16x32_bf16 v[84:87], v[160:163], v[208:211], v[84:87]
	v_mfma_f32_16x16x32_bf16 v[76:79], v[152:155], v[216:219], v[76:79]
	v_mfma_f32_16x16x32_bf16 v[68:71], v[160:163], v[216:219], v[68:71]
	s_setprio 0
	s_setprio 1
	v_mfma_f32_16x16x32_bf16 v[120:123], v[172:175], v[188:191], v[120:123]
	v_mfma_f32_16x16x32_bf16 v[112:115], v[180:183], v[188:191], v[112:115]
	v_mfma_f32_16x16x32_bf16 v[104:107], v[172:175], v[196:199], v[104:107]
	v_mfma_f32_16x16x32_bf16 v[96:99], v[180:183], v[196:199], v[96:99]
	v_mfma_f32_16x16x32_bf16 v[88:91], v[172:175], v[204:207], v[88:91]
	v_mfma_f32_16x16x32_bf16 v[80:83], v[180:183], v[204:207], v[80:83]
	v_mfma_f32_16x16x32_bf16 v[72:75], v[172:175], v[212:215], v[72:75]
	v_mfma_f32_16x16x32_bf16 v[64:67], v[180:183], v[212:215], v[64:67]
	v_mfma_f32_16x16x32_bf16 v[120:123], v[176:179], v[192:195], v[120:123]
	v_mfma_f32_16x16x32_bf16 v[112:115], v[184:187], v[192:195], v[112:115]
	v_mfma_f32_16x16x32_bf16 v[104:107], v[176:179], v[200:203], v[104:107]
	v_mfma_f32_16x16x32_bf16 v[96:99], v[184:187], v[200:203], v[96:99]
	v_mfma_f32_16x16x32_bf16 v[88:91], v[176:179], v[208:211], v[88:91]
	v_mfma_f32_16x16x32_bf16 v[80:83], v[184:187], v[208:211], v[80:83]
	v_mfma_f32_16x16x32_bf16 v[72:75], v[176:179], v[216:219], v[72:75]
	v_mfma_f32_16x16x32_bf16 v[64:67], v[184:187], v[216:219], v[64:67]
	s_setprio 0
	s_barrier
; #define PG8_STAGE(bufoff, gbase, voff) do { _Pragma("unroll") for (int _i = 0; _i < 2; ++_i) \
;         __builtin_amdgcn_global_load_lds((const unsigned*)((const char*)(gbase) + (voff)[_i]), (PG8_LAS unsigned*)(lds + (bufoff) + ldsw + _i * 8192), 16, 0, 0); } while (0)
; #define PG8_LDA(dst, b, h) do { _Pragma("unroll") for (int m = 0; m < 4; ++m) _Pragma("unroll") for (int k = 0; k < 2; ++k) dst[m][k] = *(const PG8_LAS bf16x8*)(lds + PG8_SA(b, h) + aoff + m * 2048 + k * 1024); } while (0)
; #define PG8_LDB(dst, b, h) do { _Pragma("unroll") for (int n = 0; n < 2; ++n) _Pragma("unroll") for (int k = 0; k < 2; ++k) dst[n][k] = *(const PG8_LAS bf16x8*)(lds + PG8_SB(b, h) + boff + n * 2048 + k * 1024); } while (0)
; #define PG8_MMA(ai, bj, At, Bt) do { __builtin_amdgcn_s_setprio(1); _Pragma("unroll") for (int m = 0; m < 4; ++m) _Pragma("unroll") for (int n = 0; n < 2; ++n) _Pragma("unroll") for (int k = 0; k < 2; ++k) \
;         acc[ai][bj][m][n] = __builtin_amdgcn_mfma_f32_16x16x32_bf16(Bt[n][k], At[m][k], acc[ai][bj][m][n], 0, 0, 0); __builtin_amdgcn_s_setprio(0); } while (0)
; #define PG8_WAIT_V(n) asm volatile("s_waitcnt vmcnt(" #n ")" ::: "memory")
; #define PG8_WAIT_L(n) asm volatile("s_waitcnt lgkmcnt(" #n ")" ::: "memory")
; #define PG8_BAR __builtin_amdgcn_s_barrier()
; #define PG8_SCHED __builtin_amdgcn_sched_barrier(0)
; template <class Epi, class Sched, bool ALIGN_EPI = false, bool SP2 = false>
; __device__ __forceinline__ void gemm_phase(PG8_LAS unsigned char* lds, const Gemm g, const Sched& S, const Epi& E, const int wid) {
;     ...
;             PG8_LDA(At, 0, 1); PG8_STAGE(PG8_SB(0, 0), b2, voffB); PG8_STAGE(PG8_SB(0, 1), b2 + hstepB, voffB); PG8_STAGE(PG8_SA(0, 0), a2, voffA);
;             PG8_WAIT_V(8); PG8_WAIT_L(0); PG8_BAR; PG8_MMA(1, 0, At, B0); PG8_MMA(1, 1, At, B1); PG8_BAR; PG8_SCHED;
;             PG8_LDB(B0, 1, 0); PG8_LDB(B1, 1, 1); PG8_SCHED; PG8_LDA(At, 1, 0); PG8_STAGE(PG8_SA(0, 1), a2 + hstepA, voffA);
;             PG8_WAIT_V(8); PG8_WAIT_L(0); PG8_BAR; PG8_MMA(0, 0, At, B0); PG8_MMA(0, 1, At, B1); PG8_BAR; PG8_SCHED;
	s_add_i32 s68, s45, s33
	s_add_u32 s98, s26, 0x80
	s_addc_u32 s99, s27, 0
	s_mov_b32 m0, s68
	ds_read_b128 v[188:191], v168 offset:16384
	ds_read_b128 v[192:195], v168 offset:17408
	ds_read_b128 v[196:199], v168 offset:18432
	ds_read_b128 v[200:203], v168 offset:19456
	ds_read_b128 v[204:207], v168 offset:20480
	ds_read_b128 v[208:211], v168 offset:21504
	ds_read_b128 v[212:215], v168 offset:22528
	ds_read_b128 v[216:219], v168 offset:23552
	global_load_lds_dwordx4 v132, s[26:27]
	s_add_i32 m0, s68, 0x2000
	s_add_u32 s68, s26, 0x40000
	s_addc_u32 s69, s27, 0
	s_add_i32 s70, s46, s33
	global_load_lds_dwordx4 v128, s[26:27]
	s_mov_b32 m0, s70
	s_add_u32 s100, s28, 0x80
	s_addc_u32 s101, s29, 0
	global_load_lds_dwordx4 v132, s[68:69]
	s_add_i32 m0, s70, 0x2000
	s_nop 0
	global_load_lds_dwordx4 v128, s[68:69]
	s_mov_b32 m0, s36
	s_nop 0
	global_load_lds_dwordx4 v134, s[28:29]
	s_mov_b32 m0, s37
	s_nop 0
	global_load_lds_dwordx4 v130, s[28:29]
	s_waitcnt vmcnt(8) lgkmcnt(0)
	s_barrier
	s_setprio 1
	v_mfma_f32_16x16x32_bf16 v[60:63], v[148:151], v[188:191], v[60:63]
	v_mfma_f32_16x16x32_bf16 v[52:55], v[156:159], v[188:191], v[52:55]
	v_mfma_f32_16x16x32_bf16 v[44:47], v[148:151], v[196:199], v[44:47]
	v_mfma_f32_16x16x32_bf16 v[36:39], v[156:159], v[196:199], v[36:39]
	v_mfma_f32_16x16x32_bf16 v[28:31], v[148:151], v[204:207], v[28:31]
	v_mfma_f32_16x16x32_bf16 v[20:23], v[156:159], v[204:207], v[20:23]
	v_mfma_f32_16x16x32_bf16 v[12:15], v[148:151], v[212:215], v[12:15]
	v_mfma_f32_16x16x32_bf16 v[4:7], v[156:159], v[212:215], v[4:7]
	v_mfma_f32_16x16x32_bf16 v[60:63], v[152:155], v[192:195], v[60:63]
	v_mfma_f32_16x16x32_bf16 v[52:55], v[160:163], v[192:195], v[52:55]
	v_mfma_f32_16x16x32_bf16 v[44:47], v[152:155], v[200:203], v[44:47]
	v_mfma_f32_16x16x32_bf16 v[36:39], v[160:163], v[200:203], v[36:39]
	v_mfma_f32_16x16x32_bf16 v[28:31], v[152:155], v[208:211], v[28:31]
	v_mfma_f32_16x16x32_bf16 v[20:23], v[160:163], v[208:211], v[20:23]
	v_mfma_f32_16x16x32_bf16 v[12:15], v[152:155], v[216:219], v[12:15]
	v_mfma_f32_16x16x32_bf16 v[4:7], v[160:163], v[216:219], v[4:7]
	s_setprio 0
	s_setprio 1
	v_mfma_f32_16x16x32_bf16 v[56:59], v[172:175], v[188:191], v[56:59]
	v_mfma_f32_16x16x32_bf16 v[48:51], v[180:183], v[188:191], v[48:51]
	v_mfma_f32_16x16x32_bf16 v[40:43], v[172:175], v[196:199], v[40:43]
	v_mfma_f32_16x16x32_bf16 v[32:35], v[180:183], v[196:199], v[32:35]
	v_mfma_f32_16x16x32_bf16 v[24:27], v[172:175], v[204:207], v[24:27]
	v_mfma_f32_16x16x32_bf16 v[16:19], v[180:183], v[204:207], v[16:19]
	v_mfma_f32_16x16x32_bf16 v[8:11], v[172:175], v[212:215], v[8:11]
	v_mfma_f32_16x16x32_bf16 v[0:3], v[180:183], v[212:215], v[0:3]
	v_mfma_f32_16x16x32_bf16 v[56:59], v[176:179], v[192:195], v[56:59]
	v_mfma_f32_16x16x32_bf16 v[48:51], v[184:187], v[192:195], v[48:51]
	v_mfma_f32_16x16x32_bf16 v[40:43], v[176:179], v[200:203], v[40:43]
	v_mfma_f32_16x16x32_bf16 v[32:35], v[184:187], v[200:203], v[32:35]
	v_mfma_f32_16x16x32_bf16 v[24:27], v[176:179], v[208:211], v[24:27]
	v_mfma_f32_16x16x32_bf16 v[16:19], v[184:187], v[208:211], v[16:19]
	v_mfma_f32_16x16x32_bf16 v[8:11], v[176:179], v[216:219], v[8:11]
	v_mfma_f32_16x16x32_bf16 v[0:3], v[184:187], v[216:219], v[0:3]
	s_setprio 0
	s_barrier
	s_add_i32 s68, 0, 0x18000
	s_add_i32 s69, 0, 0x1c000
	ds_read_b128 v[148:151], v252
	ds_read_b128 v[152:155], v252 offset:1024
	ds_read_b128 v[156:159], v252 offset:2048
	ds_read_b128 v[160:163], v252 offset:3072
	ds_read_b128 v[172:175], v253
	ds_read_b128 v[176:179], v253 offset:1024
	ds_read_b128 v[180:183], v253 offset:2048
	ds_read_b128 v[184:187], v253 offset:3072
	s_add_u32 s28, s28, 0x40000
	s_addc_u32 s29, s29, 0
	s_mov_b32 m0, s38
	ds_read_b128 v[188:191], v168 offset:32768
	ds_read_b128 v[192:195], v168 offset:33792
	ds_read_b128 v[196:199], v168 offset:34816
	ds_read_b128 v[200:203], v168 offset:35840
	ds_read_b128 v[204:207], v168 offset:36864
	ds_read_b128 v[208:211], v168 offset:37888
	ds_read_b128 v[212:215], v168 offset:38912
	ds_read_b128 v[216:219], v168 offset:39936
	global_load_lds_dwordx4 v134, s[28:29]
	s_mov_b32 m0, s39
	s_nop 0
	global_load_lds_dwordx4 v130, s[28:29]
	s_waitcnt vmcnt(8) lgkmcnt(0)
	s_barrier
; #define PG8_STAGE(bufoff, gbase, voff) do { _Pragma("unroll") for (int _i = 0; _i < 2; ++_i) \
;         __builtin_amdgcn_global_load_lds((const unsigned*)((const char*)(gbase) + (voff)[_i]), (PG8_LAS unsigned*)(lds + (bufoff) + ldsw + _i * 8192), 16, 0, 0); } while (0)
; #define PG8_LDA(dst, b, h) do { _Pragma("unroll") for (int m = 0; m < 4; ++m) _Pragma("unroll") for (int k = 0; k < 2; ++k) dst[m][k] = *(const PG8_LAS bf16x8*)(lds + PG8_SA(b, h) + aoff + m * 2048 + k * 1024); } while (0)
; #define PG8_MMA(ai, bj, At, Bt) do { __builtin_amdgcn_s_setprio(1); _Pragma("unroll") for (int m = 0; m < 4; ++m) _Pragma("unroll") for (int n = 0; n < 2; ++n) _Pragma("unroll") for (int k = 0; k < 2; ++k) \
;         acc[ai][bj][m][n] = __builtin_amdgcn_mfma_f32_16x16x32_bf16(Bt[n][k], At[m][k], acc[ai][bj][m][n], 0, 0, 0); __builtin_amdgcn_s_setprio(0); } while (0)
; #define PG8_WAIT_V(n) asm volatile("s_waitcnt vmcnt(" #n ")" ::: "memory")
; #define PG8_WAIT_L(n) asm volatile("s_waitcnt lgkmcnt(" #n ")" ::: "memory")
; #define PG8_BAR __builtin_amdgcn_s_barrier()
; #define PG8_SCHED __builtin_amdgcn_sched_barrier(0)
; template <class Epi, class Sched, bool ALIGN_EPI = false, bool SP2 = false>
; __device__ __forceinline__ void gemm_phase(PG8_LAS unsigned char* lds, const Gemm g, const Sched& S, const Epi& E, const int wid) {
;     ...
;             PG8_WAIT_V(8); PG8_WAIT_L(0); PG8_BAR; PG8_MMA(0, 0, At, B0); PG8_MMA(0, 1, At, B1); PG8_BAR; PG8_SCHED;
;             PG8_LDA(At, 1, 1); PG8_STAGE(PG8_SB(1, 0), b3, voffB); PG8_STAGE(PG8_SB(1, 1), b3 + hstepB, voffB); PG8_STAGE(PG8_SA(1, 0), a3, voffA);
;             PG8_WAIT_V(8); PG8_WAIT_L(0); PG8_BAR; PG8_MMA(1, 0, At, B0); PG8_MMA(1, 1, At, B1); PG8_BAR; PG8_SCHED;
;     ...
;         if constexpr (ALIGN_EPI) { if (wr == 0) PG8_BAR; }
	s_setprio 1
	v_mfma_f32_16x16x32_bf16 v[124:127], v[148:151], v[188:191], v[124:127]
	v_mfma_f32_16x16x32_bf16 v[116:119], v[156:159], v[188:191], v[116:119]
	v_mfma_f32_16x16x32_bf16 v[108:111], v[148:151], v[196:199], v[108:111]
	v_mfma_f32_16x16x32_bf16 v[100:103], v[156:159], v[196:199], v[100:103]
	v_mfma_f32_16x16x32_bf16 v[92:95], v[148:151], v[204:207], v[92:95]
	v_mfma_f32_16x16x32_bf16 v[84:87], v[156:159], v[204:207], v[84:87]
	v_mfma_f32_16x16x32_bf16 v[76:79], v[148:151], v[212:215], v[76:79]
	v_mfma_f32_16x16x32_bf16 v[68:71], v[156:159], v[212:215], v[68:71]
	v_mfma_f32_16x16x32_bf16 v[124:127], v[152:155], v[192:195], v[124:127]
	v_mfma_f32_16x16x32_bf16 v[116:119], v[160:163], v[192:195], v[116:119]
	v_mfma_f32_16x16x32_bf16 v[108:111], v[152:155], v[200:203], v[108:111]
	v_mfma_f32_16x16x32_bf16 v[100:103], v[160:163], v[200:203], v[100:103]
	v_mfma_f32_16x16x32_bf16 v[92:95], v[152:155], v[208:211], v[92:95]
	v_mfma_f32_16x16x32_bf16 v[84:87], v[160:163], v[208:211], v[84:87]
	v_mfma_f32_16x16x32_bf16 v[76:79], v[152:155], v[216:219], v[76:79]
	v_mfma_f32_16x16x32_bf16 v[68:71], v[160:163], v[216:219], v[68:71]
	s_setprio 0
	s_setprio 1
	v_mfma_f32_16x16x32_bf16 v[120:123], v[172:175], v[188:191], v[120:123]
	v_mfma_f32_16x16x32_bf16 v[112:115], v[180:183], v[188:191], v[112:115]
	v_mfma_f32_16x16x32_bf16 v[104:107], v[172:175], v[196:199], v[104:107]
	v_mfma_f32_16x16x32_bf16 v[96:99], v[180:183], v[196:199], v[96:99]
	v_mfma_f32_16x16x32_bf16 v[88:91], v[172:175], v[204:207], v[88:91]
	v_mfma_f32_16x16x32_bf16 v[80:83], v[180:183], v[204:207], v[80:83]
	v_mfma_f32_16x16x32_bf16 v[72:75], v[172:175], v[212:215], v[72:75]
	v_mfma_f32_16x16x32_bf16 v[64:67], v[180:183], v[212:215], v[64:67]
	v_mfma_f32_16x16x32_bf16 v[120:123], v[176:179], v[192:195], v[120:123]
	v_mfma_f32_16x16x32_bf16 v[112:115], v[184:187], v[192:195], v[112:115]
	v_mfma_f32_16x16x32_bf16 v[104:107], v[176:179], v[200:203], v[104:107]
	v_mfma_f32_16x16x32_bf16 v[96:99], v[184:187], v[200:203], v[96:99]
	v_mfma_f32_16x16x32_bf16 v[88:91], v[176:179], v[208:211], v[88:91]
	v_mfma_f32_16x16x32_bf16 v[80:83], v[184:187], v[208:211], v[80:83]
	v_mfma_f32_16x16x32_bf16 v[72:75], v[176:179], v[216:219], v[72:75]
	v_mfma_f32_16x16x32_bf16 v[64:67], v[184:187], v[216:219], v[64:67]
	s_setprio 0
	s_barrier
	s_add_i32 s28, s68, s33
	s_mov_b32 m0, s28
	ds_read_b128 v[188:191], v168 offset:49152
	ds_read_b128 v[192:195], v168 offset:50176
	ds_read_b128 v[196:199], v168 offset:51200
	ds_read_b128 v[200:203], v168 offset:52224
	ds_read_b128 v[204:207], v168 offset:53248
	ds_read_b128 v[208:211], v168 offset:54272
	ds_read_b128 v[212:215], v168 offset:55296
	ds_read_b128 v[216:219], v168 offset:56320
	global_load_lds_dwordx4 v132, s[98:99]
	s_add_i32 m0, s28, 0x2000
	s_add_u32 s26, s26, 0x40080
	s_addc_u32 s27, s27, 0
	s_add_i32 s28, s69, s33
	global_load_lds_dwordx4 v128, s[98:99]
	s_mov_b32 m0, s28
	s_nop 0
	global_load_lds_dwordx4 v132, s[26:27]
	s_add_i32 m0, s28, 0x2000
	s_nop 0
	global_load_lds_dwordx4 v128, s[26:27]
	s_mov_b32 m0, s40
	s_nop 0
	global_load_lds_dwordx4 v134, s[100:101]
	s_mov_b32 m0, s41
	s_nop 0
	global_load_lds_dwordx4 v130, s[100:101]
	s_waitcnt vmcnt(8) lgkmcnt(0)
	s_barrier
	s_setprio 1
	v_mfma_f32_16x16x32_bf16 v[60:63], v[148:151], v[188:191], v[60:63]
	v_mfma_f32_16x16x32_bf16 v[52:55], v[156:159], v[188:191], v[52:55]
	v_mfma_f32_16x16x32_bf16 v[44:47], v[148:151], v[196:199], v[44:47]
	v_mfma_f32_16x16x32_bf16 v[36:39], v[156:159], v[196:199], v[36:39]
	v_mfma_f32_16x16x32_bf16 v[28:31], v[148:151], v[204:207], v[28:31]
	v_mfma_f32_16x16x32_bf16 v[20:23], v[156:159], v[204:207], v[20:23]
	v_mfma_f32_16x16x32_bf16 v[12:15], v[148:151], v[212:215], v[12:15]
	v_mfma_f32_16x16x32_bf16 v[4:7], v[156:159], v[212:215], v[4:7]
	v_mfma_f32_16x16x32_bf16 v[60:63], v[152:155], v[192:195], v[60:63]
	v_mfma_f32_16x16x32_bf16 v[52:55], v[160:163], v[192:195], v[52:55]
	v_mfma_f32_16x16x32_bf16 v[44:47], v[152:155], v[200:203], v[44:47]
	v_mfma_f32_16x16x32_bf16 v[36:39], v[160:163], v[200:203], v[36:39]
	v_mfma_f32_16x16x32_bf16 v[28:31], v[152:155], v[208:211], v[28:31]
	v_mfma_f32_16x16x32_bf16 v[20:23], v[160:163], v[208:211], v[20:23]
	v_mfma_f32_16x16x32_bf16 v[12:15], v[152:155], v[216:219], v[12:15]
	v_mfma_f32_16x16x32_bf16 v[4:7], v[160:163], v[216:219], v[4:7]
	s_setprio 0
	s_setprio 1
	v_mfma_f32_16x16x32_bf16 v[56:59], v[172:175], v[188:191], v[56:59]
	v_mfma_f32_16x16x32_bf16 v[48:51], v[180:183], v[188:191], v[48:51]
	v_mfma_f32_16x16x32_bf16 v[40:43], v[172:175], v[196:199], v[40:43]
	v_mfma_f32_16x16x32_bf16 v[32:35], v[180:183], v[196:199], v[32:35]
	v_mfma_f32_16x16x32_bf16 v[24:27], v[172:175], v[204:207], v[24:27]
	v_mfma_f32_16x16x32_bf16 v[16:19], v[180:183], v[204:207], v[16:19]
	v_mfma_f32_16x16x32_bf16 v[8:11], v[172:175], v[212:215], v[8:11]
	v_mfma_f32_16x16x32_bf16 v[0:3], v[180:183], v[212:215], v[0:3]
	v_mfma_f32_16x16x32_bf16 v[56:59], v[176:179], v[192:195], v[56:59]
	v_mfma_f32_16x16x32_bf16 v[48:51], v[184:187], v[192:195], v[48:51]
	v_mfma_f32_16x16x32_bf16 v[40:43], v[176:179], v[200:203], v[40:43]
	v_mfma_f32_16x16x32_bf16 v[32:35], v[184:187], v[200:203], v[32:35]
	v_mfma_f32_16x16x32_bf16 v[24:27], v[176:179], v[208:211], v[24:27]
	v_mfma_f32_16x16x32_bf16 v[16:19], v[184:187], v[208:211], v[16:19]
	v_mfma_f32_16x16x32_bf16 v[8:11], v[176:179], v[216:219], v[8:11]
	v_mfma_f32_16x16x32_bf16 v[0:3], v[184:187], v[216:219], v[0:3]
	s_setprio 0
	s_barrier
	s_add_i32 s67, s67, 2
	s_add_u32 s24, s24, 0x100
	s_addc_u32 s25, s25, 0
	s_add_u32 s65, s65, 0x100
	s_addc_u32 s66, s66, 0
	s_cmp_gt_u32 s67, 13
	s_cbranch_scc0 .LBB0_1867
	s_and_b64 vcc, exec, s[12:13]
	s_cbranch_vccz .LBB0_1870
	s_barrier

; #define PG8_STAGE(bufoff, gbase, voff) do { _Pragma("unroll") for (int _i = 0; _i < 2; ++_i) \
;         __builtin_amdgcn_global_load_lds((const unsigned*)((const char*)(gbase) + (voff)[_i]), (PG8_LAS unsigned*)(lds + (bufoff) + ldsw + _i * 8192), 16, 0, 0); } while (0)
; #define PG8_LDA(dst, b, h) do { _Pragma("unroll") for (int m = 0; m < 4; ++m) _Pragma("unroll") for (int k = 0; k < 2; ++k) dst[m][k] = *(const PG8_LAS bf16x8*)(lds + PG8_SA(b, h) + aoff + m * 2048 + k * 1024); } while (0)
; #define PG8_LDB(dst, b, h) do { _Pragma("unroll") for (int n = 0; n < 2; ++n) _Pragma("unroll") for (int k = 0; k < 2; ++k) dst[n][k] = *(const PG8_LAS bf16x8*)(lds + PG8_SB(b, h) + boff + n * 2048 + k * 1024); } while (0)
; #define PG8_MMA(ai, bj, At, Bt) do { __builtin_amdgcn_s_setprio(1); _Pragma("unroll") for (int m = 0; m < 4; ++m) _Pragma("unroll") for (int n = 0; n < 2; ++n) _Pragma("unroll") for (int k = 0; k < 2; ++k) \
;         acc[ai][bj][m][n] = __builtin_amdgcn_mfma_f32_16x16x32_bf16(Bt[n][k], At[m][k], acc[ai][bj][m][n], 0, 0, 0); __builtin_amdgcn_s_setprio(0); } while (0)
; #define PG8_WAIT_V(n) asm volatile("s_waitcnt vmcnt(" #n ")" ::: "memory")
; #define PG8_BAR __builtin_amdgcn_s_barrier()
; template <class Epi, class Sched, bool ALIGN_EPI = false, bool SP2 = false>
; __device__ __forceinline__ void gemm_phase(PG8_LAS unsigned char* lds, const Gemm g, const Sched& S, const Epi& E, const int wid) {
;     ...
;         for (int t = 0; t < nt; t += 2) {
;             const bool last = (t == nt - 2);
;             const char* a1 = cA + (size_t)(t + 1) * kstep;
;             const char* a2 = last ? nA : cA + (size_t)(t + 2) * kstep; const char* b2 = last ? nB : cB + (size_t)(t + 2) * kstep;
;             const char* a3 = a2 + kstep; const char* b3 = b2 + kstep;
;             if (last && has_next) S.a_ready(nxt);
;             if constexpr (SP2) {
;             PG8_LDB(B0, 0, 0); PG8_LDB(B1, 0, 1); PG8_SCHED; PG8_LDA(At, 0, 0); PG8_STAGE(PG8_SA(1, 1), a1 + hstepA, voffA);
;             PG8_WAIT_V(8); PG8_WAIT_L(0); PG8_BAR; PG8_MMA(0, 0, At, B0); PG8_MMA(0, 1, At, B1); PG8_BAR; PG8_SCHED;
;             PG8_LDA(At, 0, 1); PG8_STAGE(PG8_SB(0, 0), b2, voffB); PG8_STAGE(PG8_SB(0, 1), b2 + hstepB, voffB); PG8_STAGE(PG8_SA(0, 0), a2, voffA);
;             PG8_WAIT_V(8); PG8_WAIT_L(0); PG8_BAR; PG8_MMA(1, 0, At, B0); PG8_MMA(1, 1, At, B1); PG8_BAR; PG8_SCHED;
.LBB0_1951:
	s_add_u32 s66, s24, 0x100
	s_addc_u32 s67, s25, 0
	s_mov_b32 s68, -2
	s_waitcnt lgkmcnt(0)
	v_add_u32_e32 v252, 0x18000, v189
	v_add_u32_e32 v253, 0x1c000, v189
	ds_read_b128 v[128:131], v190
	ds_read_b128 v[132:135], v190 offset:1024
	ds_read_b128 v[136:139], v190 offset:2048
	ds_read_b128 v[140:143], v190 offset:3072
	ds_read_b128 v[144:147], v191
	ds_read_b128 v[148:151], v191 offset:1024
	ds_read_b128 v[172:175], v191 offset:2048
	ds_read_b128 v[176:179], v191 offset:3072
	s_add_u32 s24, s22, 0x100
	s_addc_u32 s25, s23, 0
	s_cmp_eq_u32 s68, 40
	s_cselect_b32 s29, s7, s25
	s_cselect_b32 s28, s6, s24
	s_cselect_b32 s27, s21, s67
	s_cselect_b32 s26, s20, s66
	s_add_i32 m0, s34, 0xc000
	ds_read_b128 v[180:183], v192
	ds_read_b128 v[184:187], v192 offset:1024
	ds_read_b128 v[194:197], v192 offset:2048
	ds_read_b128 v[198:201], v192 offset:3072
	ds_read_b128 v[202:205], v192 offset:4096
	ds_read_b128 v[206:209], v192 offset:5120
	ds_read_b128 v[210:213], v192 offset:6144
	ds_read_b128 v[214:217], v192 offset:7168
	global_load_lds_dwordx4 v164, s[22:23]
	s_add_i32 m0, s34, 0xe000
	s_nop 0
	global_load_lds_dwordx4 v166, s[22:23]
	s_waitcnt vmcnt(8) lgkmcnt(0)
	s_barrier
	s_setprio 1
	v_mfma_f32_16x16x32_bf16 v[124:127], v[128:131], v[180:183], 0
	v_mfma_f32_16x16x32_bf16 v[120:123], v[136:139], v[180:183], 0
	v_mfma_f32_16x16x32_bf16 v[108:111], v[128:131], v[194:197], 0
	v_mfma_f32_16x16x32_bf16 v[104:107], v[136:139], v[194:197], 0
	v_mfma_f32_16x16x32_bf16 v[92:95], v[128:131], v[202:205], 0
	v_mfma_f32_16x16x32_bf16 v[88:91], v[136:139], v[202:205], 0
	v_mfma_f32_16x16x32_bf16 v[76:79], v[128:131], v[210:213], 0
	v_mfma_f32_16x16x32_bf16 v[72:75], v[136:139], v[210:213], 0
	v_mfma_f32_16x16x32_bf16 v[124:127], v[132:135], v[184:187], v[124:127]
	v_mfma_f32_16x16x32_bf16 v[120:123], v[140:143], v[184:187], v[120:123]
	v_mfma_f32_16x16x32_bf16 v[108:111], v[132:135], v[198:201], v[108:111]
	v_mfma_f32_16x16x32_bf16 v[104:107], v[140:143], v[198:201], v[104:107]
	v_mfma_f32_16x16x32_bf16 v[92:95], v[132:135], v[206:209], v[92:95]
	v_mfma_f32_16x16x32_bf16 v[88:91], v[140:143], v[206:209], v[88:91]
	v_mfma_f32_16x16x32_bf16 v[76:79], v[132:135], v[214:217], v[76:79]
	v_mfma_f32_16x16x32_bf16 v[72:75], v[140:143], v[214:217], v[72:75]
	s_setprio 0
	s_setprio 1
	v_mfma_f32_16x16x32_bf16 v[116:119], v[144:147], v[180:183], 0
	v_mfma_f32_16x16x32_bf16 v[112:115], v[172:175], v[180:183], 0
	v_mfma_f32_16x16x32_bf16 v[100:103], v[144:147], v[194:197], 0
	v_mfma_f32_16x16x32_bf16 v[96:99], v[172:175], v[194:197], 0
	v_mfma_f32_16x16x32_bf16 v[84:87], v[144:147], v[202:205], 0
	v_mfma_f32_16x16x32_bf16 v[80:83], v[172:175], v[202:205], 0
	v_mfma_f32_16x16x32_bf16 v[68:71], v[144:147], v[210:213], 0
	v_mfma_f32_16x16x32_bf16 v[64:67], v[172:175], v[210:213], 0
	v_mfma_f32_16x16x32_bf16 v[116:119], v[148:151], v[184:187], v[116:119]
	v_mfma_f32_16x16x32_bf16 v[112:115], v[176:179], v[184:187], v[112:115]
	v_mfma_f32_16x16x32_bf16 v[100:103], v[148:151], v[198:201], v[100:103]
	v_mfma_f32_16x16x32_bf16 v[96:99], v[176:179], v[198:201], v[96:99]
	v_mfma_f32_16x16x32_bf16 v[84:87], v[148:151], v[206:209], v[84:87]
	v_mfma_f32_16x16x32_bf16 v[80:83], v[176:179], v[206:209], v[80:83]
	v_mfma_f32_16x16x32_bf16 v[68:71], v[148:151], v[214:217], v[68:71]
	v_mfma_f32_16x16x32_bf16 v[64:67], v[176:179], v[214:217], v[64:67]
	s_setprio 0
	s_barrier
	s_add_i32 s22, s45, s33
	s_add_u32 s98, s26, 0x80
	s_addc_u32 s99, s27, 0
	s_mov_b32 m0, s22
	ds_read_b128 v[180:183], v192 offset:16384
	ds_read_b128 v[184:187], v192 offset:17408
	ds_read_b128 v[194:197], v192 offset:18432
	ds_read_b128 v[198:201], v192 offset:19456
	ds_read_b128 v[202:205], v192 offset:20480
	ds_read_b128 v[206:209], v192 offset:21504
	ds_read_b128 v[210:213], v192 offset:22528
	ds_read_b128 v[214:217], v192 offset:23552
	global_load_lds_dwordx4 v154, s[26:27]
	s_add_i32 m0, s22, 0x2000
	s_add_u32 s22, s26, 0xb0000
	s_addc_u32 s23, s27, 0
	s_add_i32 s69, s46, s33
	global_load_lds_dwordx4 v158, s[26:27]
	s_mov_b32 m0, s69
	s_add_u32 s100, s28, 0x80
	s_addc_u32 s101, s29, 0
	global_load_lds_dwordx4 v154, s[22:23]
	s_add_i32 m0, s69, 0x2000
	s_nop 0
	global_load_lds_dwordx4 v158, s[22:23]
	s_mov_b32 m0, s34
	s_nop 0
	global_load_lds_dwordx4 v152, s[28:29]
	s_mov_b32 m0, s35
	s_nop 0
	global_load_lds_dwordx4 v156, s[28:29]
	s_waitcnt vmcnt(8) lgkmcnt(0)
	s_barrier
	s_setprio 1
	v_mfma_f32_16x16x32_bf16 v[60:63], v[128:131], v[180:183], 0
	v_mfma_f32_16x16x32_bf16 v[56:59], v[136:139], v[180:183], 0
	v_mfma_f32_16x16x32_bf16 v[44:47], v[128:131], v[194:197], 0
	v_mfma_f32_16x16x32_bf16 v[40:43], v[136:139], v[194:197], 0
	v_mfma_f32_16x16x32_bf16 v[28:31], v[128:131], v[202:205], 0
	v_mfma_f32_16x16x32_bf16 v[24:27], v[136:139], v[202:205], 0
	v_mfma_f32_16x16x32_bf16 v[12:15], v[128:131], v[210:213], 0
	v_mfma_f32_16x16x32_bf16 v[8:11], v[136:139], v[210:213], 0
	v_mfma_f32_16x16x32_bf16 v[60:63], v[132:135], v[184:187], v[60:63]
	v_mfma_f32_16x16x32_bf16 v[56:59], v[140:143], v[184:187], v[56:59]
	v_mfma_f32_16x16x32_bf16 v[44:47], v[132:135], v[198:201], v[44:47]
	v_mfma_f32_16x16x32_bf16 v[40:43], v[140:143], v[198:201], v[40:43]
	v_mfma_f32_16x16x32_bf16 v[28:31], v[132:135], v[206:209], v[28:31]
	v_mfma_f32_16x16x32_bf16 v[24:27], v[140:143], v[206:209], v[24:27]
	v_mfma_f32_16x16x32_bf16 v[12:15], v[132:135], v[214:217], v[12:15]
	v_mfma_f32_16x16x32_bf16 v[8:11], v[140:143], v[214:217], v[8:11]
	s_setprio 0
	s_setprio 1
	v_mfma_f32_16x16x32_bf16 v[52:55], v[144:147], v[180:183], 0
	v_mfma_f32_16x16x32_bf16 v[48:51], v[172:175], v[180:183], 0
	v_mfma_f32_16x16x32_bf16 v[36:39], v[144:147], v[194:197], 0
	v_mfma_f32_16x16x32_bf16 v[32:35], v[172:175], v[194:197], 0
	v_mfma_f32_16x16x32_bf16 v[20:23], v[144:147], v[202:205], 0
	v_mfma_f32_16x16x32_bf16 v[16:19], v[172:175], v[202:205], 0
	v_mfma_f32_16x16x32_bf16 v[4:7], v[144:147], v[210:213], 0
	v_mfma_f32_16x16x32_bf16 v[0:3], v[172:175], v[210:213], 0
	v_mfma_f32_16x16x32_bf16 v[52:55], v[148:151], v[184:187], v[52:55]
	v_mfma_f32_16x16x32_bf16 v[48:51], v[176:179], v[184:187], v[48:51]
	v_mfma_f32_16x16x32_bf16 v[36:39], v[148:151], v[198:201], v[36:39]
	v_mfma_f32_16x16x32_bf16 v[32:35], v[176:179], v[198:201], v[32:35]
	v_mfma_f32_16x16x32_bf16 v[20:23], v[148:151], v[206:209], v[20:23]
	v_mfma_f32_16x16x32_bf16 v[16:19], v[176:179], v[206:209], v[16:19]
	v_mfma_f32_16x16x32_bf16 v[4:7], v[148:151], v[214:217], v[4:7]
	v_mfma_f32_16x16x32_bf16 v[0:3], v[176:179], v[214:217], v[0:3]
	s_setprio 0
	s_barrier
; #define PG8_STAGE(bufoff, gbase, voff) do { _Pragma("unroll") for (int _i = 0; _i < 2; ++_i) \
;         __builtin_amdgcn_global_load_lds((const unsigned*)((const char*)(gbase) + (voff)[_i]), (PG8_LAS unsigned*)(lds + (bufoff) + ldsw + _i * 8192), 16, 0, 0); } while (0)
; #define PG8_LDA(dst, b, h) do { _Pragma("unroll") for (int m = 0; m < 4; ++m) _Pragma("unroll") for (int k = 0; k < 2; ++k) dst[m][k] = *(const PG8_LAS bf16x8*)(lds + PG8_SA(b, h) + aoff + m * 2048 + k * 1024); } while (0)
; #define PG8_LDB(dst, b, h) do { _Pragma("unroll") for (int n = 0; n < 2; ++n) _Pragma("unroll") for (int k = 0; k < 2; ++k) dst[n][k] = *(const PG8_LAS bf16x8*)(lds + PG8_SB(b, h) + boff + n * 2048 + k * 1024); } while (0)
; #define PG8_MMA(ai, bj, At, Bt) do { __builtin_amdgcn_s_setprio(1); _Pragma("unroll") for (int m = 0; m < 4; ++m) _Pragma("unroll") for (int n = 0; n < 2; ++n) _Pragma("unroll") for (int k = 0; k < 2; ++k) \
;         acc[ai][bj][m][n] = __builtin_amdgcn_mfma_f32_16x16x32_bf16(Bt[n][k], At[m][k], acc[ai][bj][m][n], 0, 0, 0); __builtin_amdgcn_s_setprio(0); } while (0)
; #define PG8_WAIT_V(n) asm volatile("s_waitcnt vmcnt(" #n ")" ::: "memory")
; #define PG8_WAIT_L(n) asm volatile("s_waitcnt lgkmcnt(" #n ")" ::: "memory")
; #define PG8_BAR __builtin_amdgcn_s_barrier()
; #define PG8_SCHED __builtin_amdgcn_sched_barrier(0)
; template <class Epi, class Sched, bool ALIGN_EPI = false, bool SP2 = false>
; __device__ __forceinline__ void gemm_phase(PG8_LAS unsigned char* lds, const Gemm g, const Sched& S, const Epi& E, const int wid) {
;     ...
;             PG8_LDB(B0, 1, 0); PG8_LDB(B1, 1, 1); PG8_SCHED; PG8_LDA(At, 1, 0); PG8_STAGE(PG8_SA(0, 1), a2 + hstepA, voffA);
;             PG8_WAIT_V(8); PG8_WAIT_L(0); PG8_BAR; PG8_MMA(0, 0, At, B0); PG8_MMA(0, 1, At, B1); PG8_BAR; PG8_SCHED;
;             PG8_LDA(At, 1, 1); PG8_STAGE(PG8_SB(1, 0), b3, voffB); PG8_STAGE(PG8_SB(1, 1), b3 + hstepB, voffB); PG8_STAGE(PG8_SA(1, 0), a3, voffA);
;             PG8_WAIT_V(8); PG8_WAIT_L(0); PG8_BAR; PG8_MMA(1, 0, At, B0); PG8_MMA(1, 1, At, B1); PG8_BAR; PG8_SCHED;
	s_add_i32 s69, 0, 0x18000
	s_add_i32 s70, 0, 0x1c000
	ds_read_b128 v[128:131], v252
	ds_read_b128 v[132:135], v252 offset:1024
	ds_read_b128 v[136:139], v252 offset:2048
	ds_read_b128 v[140:143], v252 offset:3072
	ds_read_b128 v[144:147], v253
	ds_read_b128 v[148:151], v253 offset:1024
	ds_read_b128 v[172:175], v253 offset:2048
	ds_read_b128 v[176:179], v253 offset:3072
	s_add_u32 s22, s28, 0xb0000
	s_addc_u32 s23, s29, 0
	s_mov_b32 m0, s36
	ds_read_b128 v[180:183], v192 offset:32768
	ds_read_b128 v[184:187], v192 offset:33792
	ds_read_b128 v[194:197], v192 offset:34816
	ds_read_b128 v[198:201], v192 offset:35840
	ds_read_b128 v[202:205], v192 offset:36864
	ds_read_b128 v[206:209], v192 offset:37888
	ds_read_b128 v[210:213], v192 offset:38912
	ds_read_b128 v[214:217], v192 offset:39936
	global_load_lds_dwordx4 v152, s[22:23]
	s_mov_b32 m0, s37
	s_nop 0
	global_load_lds_dwordx4 v156, s[22:23]
	s_waitcnt vmcnt(8) lgkmcnt(0)
	s_barrier
	s_setprio 1
	v_mfma_f32_16x16x32_bf16 v[124:127], v[128:131], v[180:183], v[124:127]
	v_mfma_f32_16x16x32_bf16 v[120:123], v[136:139], v[180:183], v[120:123]
	v_mfma_f32_16x16x32_bf16 v[108:111], v[128:131], v[194:197], v[108:111]
	v_mfma_f32_16x16x32_bf16 v[104:107], v[136:139], v[194:197], v[104:107]
	v_mfma_f32_16x16x32_bf16 v[92:95], v[128:131], v[202:205], v[92:95]
	v_mfma_f32_16x16x32_bf16 v[88:91], v[136:139], v[202:205], v[88:91]
	v_mfma_f32_16x16x32_bf16 v[76:79], v[128:131], v[210:213], v[76:79]
	v_mfma_f32_16x16x32_bf16 v[72:75], v[136:139], v[210:213], v[72:75]
	v_mfma_f32_16x16x32_bf16 v[124:127], v[132:135], v[184:187], v[124:127]
	v_mfma_f32_16x16x32_bf16 v[120:123], v[140:143], v[184:187], v[120:123]
	v_mfma_f32_16x16x32_bf16 v[108:111], v[132:135], v[198:201], v[108:111]
	v_mfma_f32_16x16x32_bf16 v[104:107], v[140:143], v[198:201], v[104:107]
	v_mfma_f32_16x16x32_bf16 v[92:95], v[132:135], v[206:209], v[92:95]
	v_mfma_f32_16x16x32_bf16 v[88:91], v[140:143], v[206:209], v[88:91]
	v_mfma_f32_16x16x32_bf16 v[76:79], v[132:135], v[214:217], v[76:79]
	v_mfma_f32_16x16x32_bf16 v[72:75], v[140:143], v[214:217], v[72:75]
	s_setprio 0
	s_setprio 1
	v_mfma_f32_16x16x32_bf16 v[116:119], v[144:147], v[180:183], v[116:119]
	v_mfma_f32_16x16x32_bf16 v[112:115], v[172:175], v[180:183], v[112:115]
	v_mfma_f32_16x16x32_bf16 v[100:103], v[144:147], v[194:197], v[100:103]
	v_mfma_f32_16x16x32_bf16 v[96:99], v[172:175], v[194:197], v[96:99]
	v_mfma_f32_16x16x32_bf16 v[84:87], v[144:147], v[202:205], v[84:87]
	v_mfma_f32_16x16x32_bf16 v[80:83], v[172:175], v[202:205], v[80:83]
	v_mfma_f32_16x16x32_bf16 v[68:71], v[144:147], v[210:213], v[68:71]
	v_mfma_f32_16x16x32_bf16 v[64:67], v[172:175], v[210:213], v[64:67]
	v_mfma_f32_16x16x32_bf16 v[116:119], v[148:151], v[184:187], v[116:119]
	v_mfma_f32_16x16x32_bf16 v[112:115], v[176:179], v[184:187], v[112:115]
	v_mfma_f32_16x16x32_bf16 v[100:103], v[148:151], v[198:201], v[100:103]
	v_mfma_f32_16x16x32_bf16 v[96:99], v[176:179], v[198:201], v[96:99]
	v_mfma_f32_16x16x32_bf16 v[84:87], v[148:151], v[206:209], v[84:87]
	v_mfma_f32_16x16x32_bf16 v[80:83], v[176:179], v[206:209], v[80:83]
	v_mfma_f32_16x16x32_bf16 v[68:71], v[148:151], v[214:217], v[68:71]
	v_mfma_f32_16x16x32_bf16 v[64:67], v[176:179], v[214:217], v[64:67]
	s_setprio 0
	s_barrier
	s_add_i32 s22, s69, s33
	s_mov_b32 m0, s22
	ds_read_b128 v[180:183], v192 offset:49152
	ds_read_b128 v[184:187], v192 offset:50176
	ds_read_b128 v[194:197], v192 offset:51200
	ds_read_b128 v[198:201], v192 offset:52224
	ds_read_b128 v[202:205], v192 offset:53248
	ds_read_b128 v[206:209], v192 offset:54272
	ds_read_b128 v[210:213], v192 offset:55296
	ds_read_b128 v[214:217], v192 offset:56320
	global_load_lds_dwordx4 v154, s[98:99]
	s_add_i32 m0, s22, 0x2000
	s_add_u32 s22, s26, 0xb0080
	s_addc_u32 s23, s27, 0
	s_add_i32 s26, s70, s33
	global_load_lds_dwordx4 v158, s[98:99]
	s_mov_b32 m0, s26
	s_nop 0
	global_load_lds_dwordx4 v154, s[22:23]
	s_add_i32 m0, s26, 0x2000
	s_nop 0
	global_load_lds_dwordx4 v158, s[22:23]
	s_mov_b32 m0, s39
	s_nop 0
	global_load_lds_dwordx4 v152, s[100:101]
	s_mov_b32 m0, s40
	s_nop 0
	global_load_lds_dwordx4 v156, s[100:101]
	s_waitcnt vmcnt(8) lgkmcnt(0)
	s_barrier
	s_setprio 1
	v_mfma_f32_16x16x32_bf16 v[60:63], v[128:131], v[180:183], v[60:63]
	v_mfma_f32_16x16x32_bf16 v[56:59], v[136:139], v[180:183], v[56:59]
	v_mfma_f32_16x16x32_bf16 v[44:47], v[128:131], v[194:197], v[44:47]
	v_mfma_f32_16x16x32_bf16 v[40:43], v[136:139], v[194:197], v[40:43]
	v_mfma_f32_16x16x32_bf16 v[28:31], v[128:131], v[202:205], v[28:31]
	v_mfma_f32_16x16x32_bf16 v[24:27], v[136:139], v[202:205], v[24:27]
	v_mfma_f32_16x16x32_bf16 v[12:15], v[128:131], v[210:213], v[12:15]
	v_mfma_f32_16x16x32_bf16 v[8:11], v[136:139], v[210:213], v[8:11]
	v_mfma_f32_16x16x32_bf16 v[60:63], v[132:135], v[184:187], v[60:63]
	v_mfma_f32_16x16x32_bf16 v[56:59], v[140:143], v[184:187], v[56:59]
	v_mfma_f32_16x16x32_bf16 v[44:47], v[132:135], v[198:201], v[44:47]
	v_mfma_f32_16x16x32_bf16 v[40:43], v[140:143], v[198:201], v[40:43]
	v_mfma_f32_16x16x32_bf16 v[28:31], v[132:135], v[206:209], v[28:31]
	v_mfma_f32_16x16x32_bf16 v[24:27], v[140:143], v[206:209], v[24:27]
	v_mfma_f32_16x16x32_bf16 v[12:15], v[132:135], v[214:217], v[12:15]
	v_mfma_f32_16x16x32_bf16 v[8:11], v[140:143], v[214:217], v[8:11]
	s_setprio 0
	s_setprio 1
	v_mfma_f32_16x16x32_bf16 v[52:55], v[144:147], v[180:183], v[52:55]
	v_mfma_f32_16x16x32_bf16 v[48:51], v[172:175], v[180:183], v[48:51]
	v_mfma_f32_16x16x32_bf16 v[36:39], v[144:147], v[194:197], v[36:39]
	v_mfma_f32_16x16x32_bf16 v[32:35], v[172:175], v[194:197], v[32:35]
	v_mfma_f32_16x16x32_bf16 v[20:23], v[144:147], v[202:205], v[20:23]
	v_mfma_f32_16x16x32_bf16 v[16:19], v[172:175], v[202:205], v[16:19]
	v_mfma_f32_16x16x32_bf16 v[4:7], v[144:147], v[210:213], v[4:7]
	v_mfma_f32_16x16x32_bf16 v[0:3], v[172:175], v[210:213], v[0:3]
	v_mfma_f32_16x16x32_bf16 v[52:55], v[148:151], v[184:187], v[52:55]
	v_mfma_f32_16x16x32_bf16 v[48:51], v[176:179], v[184:187], v[48:51]
	v_mfma_f32_16x16x32_bf16 v[36:39], v[148:151], v[198:201], v[36:39]
	v_mfma_f32_16x16x32_bf16 v[32:35], v[176:179], v[198:201], v[32:35]
	v_mfma_f32_16x16x32_bf16 v[20:23], v[148:151], v[206:209], v[20:23]
	v_mfma_f32_16x16x32_bf16 v[16:19], v[176:179], v[206:209], v[16:19]
	v_mfma_f32_16x16x32_bf16 v[4:7], v[148:151], v[214:217], v[4:7]
	v_mfma_f32_16x16x32_bf16 v[0:3], v[176:179], v[214:217], v[0:3]
	s_setprio 0
	s_barrier
	s_add_i32 s68, s68, 2
	s_add_u32 s66, s66, 0x100
	s_addc_u32 s67, s67, 0
	s_cmp_gt_u32 s68, 41
	s_mov_b64 s[22:23], s[24:25]
; #define PG8_STAGE(bufoff, gbase, voff) do { _Pragma("unroll") for (int _i = 0; _i < 2; ++_i) \
;         __builtin_amdgcn_global_load_lds((const unsigned*)((const char*)(gbase) + (voff)[_i]), (PG8_LAS unsigned*)(lds + (bufoff) + ldsw + _i * 8192), 16, 0, 0); } while (0)
; #define PG8_LDA(dst, b, h) do { _Pragma("unroll") for (int m = 0; m < 4; ++m) _Pragma("unroll") for (int k = 0; k < 2; ++k) dst[m][k] = *(const PG8_LAS bf16x8*)(lds + PG8_SA(b, h) + aoff + m * 2048 + k * 1024); } while (0)
; #define PG8_LDB(dst, b, h) do { _Pragma("unroll") for (int n = 0; n < 2; ++n) _Pragma("unroll") for (int k = 0; k < 2; ++k) dst[n][k] = *(const PG8_LAS bf16x8*)(lds + PG8_SB(b, h) + boff + n * 2048 + k * 1024); } while (0)
; #define PG8_MMA(ai, bj, At, Bt) do { __builtin_amdgcn_s_setprio(1); _Pragma("unroll") for (int m = 0; m < 4; ++m) _Pragma("unroll") for (int n = 0; n < 2; ++n) _Pragma("unroll") for (int k = 0; k < 2; ++k) \
;         acc[ai][bj][m][n] = __builtin_amdgcn_mfma_f32_16x16x32_bf16(Bt[n][k], At[m][k], acc[ai][bj][m][n], 0, 0, 0); __builtin_amdgcn_s_setprio(0); } while (0)
; #define PG8_WAIT_V(n) asm volatile("s_waitcnt vmcnt(" #n ")" ::: "memory")
; #define PG8_BAR __builtin_amdgcn_s_barrier()
; template <class Epi, class Sched, bool ALIGN_EPI = false, bool SP2 = false>
; __device__ __forceinline__ void gemm_phase(PG8_LAS unsigned char* lds, const Gemm g, const Sched& S, const Epi& E, const int wid) {
;     ...
;         for (int t = 0; t < nt; t += 2) {
;             const bool last = (t == nt - 2);
;             const char* a1 = cA + (size_t)(t + 1) * kstep;
;             const char* a2 = last ? nA : cA + (size_t)(t + 2) * kstep; const char* b2 = last ? nB : cB + (size_t)(t + 2) * kstep;
;             const char* a3 = a2 + kstep; const char* b3 = b2 + kstep;
;             if (last && has_next) S.a_ready(nxt);
;             if constexpr (SP2) {
;             PG8_LDB(B0, 0, 0); PG8_LDB(B1, 0, 1); PG8_SCHED; PG8_LDA(At, 0, 0); PG8_STAGE(PG8_SA(1, 1), a1 + hstepA, voffA);
;             PG8_WAIT_V(8); PG8_WAIT_L(0); PG8_BAR; PG8_MMA(0, 0, At, B0); PG8_MMA(0, 1, At, B1); PG8_BAR; PG8_SCHED;
;             PG8_LDA(At, 0, 1); PG8_STAGE(PG8_SB(0, 0), b2, voffB); PG8_STAGE(PG8_SB(0, 1), b2 + hstepB, voffB); PG8_STAGE(PG8_SA(0, 0), a2, voffA);
;             PG8_WAIT_V(8); PG8_WAIT_L(0); PG8_BAR; PG8_MMA(1, 0, At, B0); PG8_MMA(1, 1, At, B1); PG8_BAR; PG8_SCHED;
.LBB0_1952:
	ds_read_b128 v[128:131], v190
	ds_read_b128 v[132:135], v190 offset:1024
	ds_read_b128 v[136:139], v190 offset:2048
	ds_read_b128 v[140:143], v190 offset:3072
	ds_read_b128 v[144:147], v191
	ds_read_b128 v[148:151], v191 offset:1024
	ds_read_b128 v[172:175], v191 offset:2048
	ds_read_b128 v[176:179], v191 offset:3072
	s_add_u32 s24, s22, 0x100
	s_addc_u32 s25, s23, 0
	s_cmp_eq_u32 s68, 40
	s_cselect_b32 s29, s7, s25
	s_cselect_b32 s28, s6, s24
	s_cselect_b32 s27, s21, s67
	s_cselect_b32 s26, s20, s66
	s_add_i32 m0, s34, 0xc000
	ds_read_b128 v[180:183], v192
	ds_read_b128 v[184:187], v192 offset:1024
	ds_read_b128 v[194:197], v192 offset:2048
	ds_read_b128 v[198:201], v192 offset:3072
	ds_read_b128 v[202:205], v192 offset:4096
	ds_read_b128 v[206:209], v192 offset:5120
	ds_read_b128 v[210:213], v192 offset:6144
	ds_read_b128 v[214:217], v192 offset:7168
	global_load_lds_dwordx4 v164, s[22:23]
	s_add_i32 m0, s34, 0xe000
	s_nop 0
	global_load_lds_dwordx4 v166, s[22:23]
	s_waitcnt vmcnt(8) lgkmcnt(0)
	s_barrier
	s_setprio 1
	v_mfma_f32_16x16x32_bf16 v[124:127], v[128:131], v[180:183], v[124:127]
	v_mfma_f32_16x16x32_bf16 v[120:123], v[136:139], v[180:183], v[120:123]
	v_mfma_f32_16x16x32_bf16 v[108:111], v[128:131], v[194:197], v[108:111]
	v_mfma_f32_16x16x32_bf16 v[104:107], v[136:139], v[194:197], v[104:107]
	v_mfma_f32_16x16x32_bf16 v[92:95], v[128:131], v[202:205], v[92:95]
	v_mfma_f32_16x16x32_bf16 v[88:91], v[136:139], v[202:205], v[88:91]
	v_mfma_f32_16x16x32_bf16 v[76:79], v[128:131], v[210:213], v[76:79]
	v_mfma_f32_16x16x32_bf16 v[72:75], v[136:139], v[210:213], v[72:75]
	v_mfma_f32_16x16x32_bf16 v[124:127], v[132:135], v[184:187], v[124:127]
	v_mfma_f32_16x16x32_bf16 v[120:123], v[140:143], v[184:187], v[120:123]
	v_mfma_f32_16x16x32_bf16 v[108:111], v[132:135], v[198:201], v[108:111]
	v_mfma_f32_16x16x32_bf16 v[104:107], v[140:143], v[198:201], v[104:107]
	v_mfma_f32_16x16x32_bf16 v[92:95], v[132:135], v[206:209], v[92:95]
	v_mfma_f32_16x16x32_bf16 v[88:91], v[140:143], v[206:209], v[88:91]
	v_mfma_f32_16x16x32_bf16 v[76:79], v[132:135], v[214:217], v[76:79]
	v_mfma_f32_16x16x32_bf16 v[72:75], v[140:143], v[214:217], v[72:75]
	s_setprio 0
	s_setprio 1
	v_mfma_f32_16x16x32_bf16 v[116:119], v[144:147], v[180:183], v[116:119]
	v_mfma_f32_16x16x32_bf16 v[112:115], v[172:175], v[180:183], v[112:115]
	v_mfma_f32_16x16x32_bf16 v[100:103], v[144:147], v[194:197], v[100:103]
	v_mfma_f32_16x16x32_bf16 v[96:99], v[172:175], v[194:197], v[96:99]
	v_mfma_f32_16x16x32_bf16 v[84:87], v[144:147], v[202:205], v[84:87]
	v_mfma_f32_16x16x32_bf16 v[80:83], v[172:175], v[202:205], v[80:83]
	v_mfma_f32_16x16x32_bf16 v[68:71], v[144:147], v[210:213], v[68:71]
	v_mfma_f32_16x16x32_bf16 v[64:67], v[172:175], v[210:213], v[64:67]
	v_mfma_f32_16x16x32_bf16 v[116:119], v[148:151], v[184:187], v[116:119]
	v_mfma_f32_16x16x32_bf16 v[112:115], v[176:179], v[184:187], v[112:115]
	v_mfma_f32_16x16x32_bf16 v[100:103], v[148:151], v[198:201], v[100:103]
	v_mfma_f32_16x16x32_bf16 v[96:99], v[176:179], v[198:201], v[96:99]
	v_mfma_f32_16x16x32_bf16 v[84:87], v[148:151], v[206:209], v[84:87]
	v_mfma_f32_16x16x32_bf16 v[80:83], v[176:179], v[206:209], v[80:83]
	v_mfma_f32_16x16x32_bf16 v[68:71], v[148:151], v[214:217], v[68:71]
	v_mfma_f32_16x16x32_bf16 v[64:67], v[176:179], v[214:217], v[64:67]
	s_setprio 0
	s_barrier
	s_add_i32 s22, s45, s33
	s_add_u32 s98, s26, 0x80
	s_addc_u32 s99, s27, 0
	s_mov_b32 m0, s22
	ds_read_b128 v[180:183], v192 offset:16384
	ds_read_b128 v[184:187], v192 offset:17408
	ds_read_b128 v[194:197], v192 offset:18432
	ds_read_b128 v[198:201], v192 offset:19456
	ds_read_b128 v[202:205], v192 offset:20480
	ds_read_b128 v[206:209], v192 offset:21504
	ds_read_b128 v[210:213], v192 offset:22528
	ds_read_b128 v[214:217], v192 offset:23552
	global_load_lds_dwordx4 v154, s[26:27]
	s_add_i32 m0, s22, 0x2000
	s_add_u32 s22, s26, 0xb0000
	s_addc_u32 s23, s27, 0
	s_add_i32 s69, s46, s33
	global_load_lds_dwordx4 v158, s[26:27]
	s_mov_b32 m0, s69
	s_add_u32 s100, s28, 0x80
	s_addc_u32 s101, s29, 0
	global_load_lds_dwordx4 v154, s[22:23]
	s_add_i32 m0, s69, 0x2000
	s_nop 0
	global_load_lds_dwordx4 v158, s[22:23]
	s_mov_b32 m0, s34
	s_nop 0
	global_load_lds_dwordx4 v152, s[28:29]
	s_mov_b32 m0, s35
	s_nop 0
	global_load_lds_dwordx4 v156, s[28:29]
	s_waitcnt vmcnt(8) lgkmcnt(0)
	s_barrier
	s_setprio 1
	v_mfma_f32_16x16x32_bf16 v[60:63], v[128:131], v[180:183], v[60:63]
	v_mfma_f32_16x16x32_bf16 v[56:59], v[136:139], v[180:183], v[56:59]
	v_mfma_f32_16x16x32_bf16 v[44:47], v[128:131], v[194:197], v[44:47]
	v_mfma_f32_16x16x32_bf16 v[40:43], v[136:139], v[194:197], v[40:43]
	v_mfma_f32_16x16x32_bf16 v[28:31], v[128:131], v[202:205], v[28:31]
	v_mfma_f32_16x16x32_bf16 v[24:27], v[136:139], v[202:205], v[24:27]
	v_mfma_f32_16x16x32_bf16 v[12:15], v[128:131], v[210:213], v[12:15]
	v_mfma_f32_16x16x32_bf16 v[8:11], v[136:139], v[210:213], v[8:11]
	v_mfma_f32_16x16x32_bf16 v[60:63], v[132:135], v[184:187], v[60:63]
	v_mfma_f32_16x16x32_bf16 v[56:59], v[140:143], v[184:187], v[56:59]
	v_mfma_f32_16x16x32_bf16 v[44:47], v[132:135], v[198:201], v[44:47]
	v_mfma_f32_16x16x32_bf16 v[40:43], v[140:143], v[198:201], v[40:43]
	v_mfma_f32_16x16x32_bf16 v[28:31], v[132:135], v[206:209], v[28:31]
	v_mfma_f32_16x16x32_bf16 v[24:27], v[140:143], v[206:209], v[24:27]
	v_mfma_f32_16x16x32_bf16 v[12:15], v[132:135], v[214:217], v[12:15]
	v_mfma_f32_16x16x32_bf16 v[8:11], v[140:143], v[214:217], v[8:11]
	s_setprio 0
	s_setprio 1
	v_mfma_f32_16x16x32_bf16 v[52:55], v[144:147], v[180:183], v[52:55]
	v_mfma_f32_16x16x32_bf16 v[48:51], v[172:175], v[180:183], v[48:51]
	v_mfma_f32_16x16x32_bf16 v[36:39], v[144:147], v[194:197], v[36:39]
	v_mfma_f32_16x16x32_bf16 v[32:35], v[172:175], v[194:197], v[32:35]
	v_mfma_f32_16x16x32_bf16 v[20:23], v[144:147], v[202:205], v[20:23]
	v_mfma_f32_16x16x32_bf16 v[16:19], v[172:175], v[202:205], v[16:19]
	v_mfma_f32_16x16x32_bf16 v[4:7], v[144:147], v[210:213], v[4:7]
	v_mfma_f32_16x16x32_bf16 v[0:3], v[172:175], v[210:213], v[0:3]
	v_mfma_f32_16x16x32_bf16 v[52:55], v[148:151], v[184:187], v[52:55]
	v_mfma_f32_16x16x32_bf16 v[48:51], v[176:179], v[184:187], v[48:51]
	v_mfma_f32_16x16x32_bf16 v[36:39], v[148:151], v[198:201], v[36:39]
	v_mfma_f32_16x16x32_bf16 v[32:35], v[176:179], v[198:201], v[32:35]
	v_mfma_f32_16x16x32_bf16 v[20:23], v[148:151], v[206:209], v[20:23]
	v_mfma_f32_16x16x32_bf16 v[16:19], v[176:179], v[206:209], v[16:19]
	v_mfma_f32_16x16x32_bf16 v[4:7], v[148:151], v[214:217], v[4:7]
	v_mfma_f32_16x16x32_bf16 v[0:3], v[176:179], v[214:217], v[0:3]
	s_setprio 0
	s_barrier
; #define PG8_STAGE(bufoff, gbase, voff) do { _Pragma("unroll") for (int _i = 0; _i < 2; ++_i) \
;         __builtin_amdgcn_global_load_lds((const unsigned*)((const char*)(gbase) + (voff)[_i]), (PG8_LAS unsigned*)(lds + (bufoff) + ldsw + _i * 8192), 16, 0, 0); } while (0)
; #define PG8_LDA(dst, b, h) do { _Pragma("unroll") for (int m = 0; m < 4; ++m) _Pragma("unroll") for (int k = 0; k < 2; ++k) dst[m][k] = *(const PG8_LAS bf16x8*)(lds + PG8_SA(b, h) + aoff + m * 2048 + k * 1024); } while (0)
; #define PG8_LDB(dst, b, h) do { _Pragma("unroll") for (int n = 0; n < 2; ++n) _Pragma("unroll") for (int k = 0; k < 2; ++k) dst[n][k] = *(const PG8_LAS bf16x8*)(lds + PG8_SB(b, h) + boff + n * 2048 + k * 1024); } while (0)
; #define PG8_MMA(ai, bj, At, Bt) do { __builtin_amdgcn_s_setprio(1); _Pragma("unroll") for (int m = 0; m < 4; ++m) _Pragma("unroll") for (int n = 0; n < 2; ++n) _Pragma("unroll") for (int k = 0; k < 2; ++k) \
;         acc[ai][bj][m][n] = __builtin_amdgcn_mfma_f32_16x16x32_bf16(Bt[n][k], At[m][k], acc[ai][bj][m][n], 0, 0, 0); __builtin_amdgcn_s_setprio(0); } while (0)
; #define PG8_WAIT_V(n) asm volatile("s_waitcnt vmcnt(" #n ")" ::: "memory")
; #define PG8_WAIT_L(n) asm volatile("s_waitcnt lgkmcnt(" #n ")" ::: "memory")
; #define PG8_BAR __builtin_amdgcn_s_barrier()
; #define PG8_SCHED __builtin_amdgcn_sched_barrier(0)
; template <class Epi, class Sched, bool ALIGN_EPI = false, bool SP2 = false>
; __device__ __forceinline__ void gemm_phase(PG8_LAS unsigned char* lds, const Gemm g, const Sched& S, const Epi& E, const int wid) {
;     ...
;             PG8_LDB(B0, 1, 0); PG8_LDB(B1, 1, 1); PG8_SCHED; PG8_LDA(At, 1, 0); PG8_STAGE(PG8_SA(0, 1), a2 + hstepA, voffA);
;             PG8_WAIT_V(8); PG8_WAIT_L(0); PG8_BAR; PG8_MMA(0, 0, At, B0); PG8_MMA(0, 1, At, B1); PG8_BAR; PG8_SCHED;
;             PG8_LDA(At, 1, 1); PG8_STAGE(PG8_SB(1, 0), b3, voffB); PG8_STAGE(PG8_SB(1, 1), b3 + hstepB, voffB); PG8_STAGE(PG8_SA(1, 0), a3, voffA);
;             PG8_WAIT_V(8); PG8_WAIT_L(0); PG8_BAR; PG8_MMA(1, 0, At, B0); PG8_MMA(1, 1, At, B1); PG8_BAR; PG8_SCHED;
;     ...
;         if constexpr (ALIGN_EPI) { if (wr == 0) PG8_BAR; }
	s_add_i32 s69, 0, 0x18000
	s_add_i32 s70, 0, 0x1c000
	ds_read_b128 v[128:131], v252
	ds_read_b128 v[132:135], v252 offset:1024
	ds_read_b128 v[136:139], v252 offset:2048
	ds_read_b128 v[140:143], v252 offset:3072
	ds_read_b128 v[144:147], v253
	ds_read_b128 v[148:151], v253 offset:1024
	ds_read_b128 v[172:175], v253 offset:2048
	ds_read_b128 v[176:179], v253 offset:3072
	s_add_u32 s22, s28, 0xb0000
	s_addc_u32 s23, s29, 0
	s_mov_b32 m0, s36
	ds_read_b128 v[180:183], v192 offset:32768
	ds_read_b128 v[184:187], v192 offset:33792
	ds_read_b128 v[194:197], v192 offset:34816
	ds_read_b128 v[198:201], v192 offset:35840
	ds_read_b128 v[202:205], v192 offset:36864
	ds_read_b128 v[206:209], v192 offset:37888
	ds_read_b128 v[210:213], v192 offset:38912
	ds_read_b128 v[214:217], v192 offset:39936
	global_load_lds_dwordx4 v152, s[22:23]
	s_mov_b32 m0, s37
	s_nop 0
	global_load_lds_dwordx4 v156, s[22:23]
	s_waitcnt vmcnt(8) lgkmcnt(0)
	s_barrier
	s_setprio 1
	v_mfma_f32_16x16x32_bf16 v[124:127], v[128:131], v[180:183], v[124:127]
	v_mfma_f32_16x16x32_bf16 v[120:123], v[136:139], v[180:183], v[120:123]
	v_mfma_f32_16x16x32_bf16 v[108:111], v[128:131], v[194:197], v[108:111]
	v_mfma_f32_16x16x32_bf16 v[104:107], v[136:139], v[194:197], v[104:107]
	v_mfma_f32_16x16x32_bf16 v[92:95], v[128:131], v[202:205], v[92:95]
	v_mfma_f32_16x16x32_bf16 v[88:91], v[136:139], v[202:205], v[88:91]
	v_mfma_f32_16x16x32_bf16 v[76:79], v[128:131], v[210:213], v[76:79]
	v_mfma_f32_16x16x32_bf16 v[72:75], v[136:139], v[210:213], v[72:75]
	v_mfma_f32_16x16x32_bf16 v[124:127], v[132:135], v[184:187], v[124:127]
	v_mfma_f32_16x16x32_bf16 v[120:123], v[140:143], v[184:187], v[120:123]
	v_mfma_f32_16x16x32_bf16 v[108:111], v[132:135], v[198:201], v[108:111]
	v_mfma_f32_16x16x32_bf16 v[104:107], v[140:143], v[198:201], v[104:107]
	v_mfma_f32_16x16x32_bf16 v[92:95], v[132:135], v[206:209], v[92:95]
	v_mfma_f32_16x16x32_bf16 v[88:91], v[140:143], v[206:209], v[88:91]
	v_mfma_f32_16x16x32_bf16 v[76:79], v[132:135], v[214:217], v[76:79]
	v_mfma_f32_16x16x32_bf16 v[72:75], v[140:143], v[214:217], v[72:75]
	s_setprio 0
	s_setprio 1
	v_mfma_f32_16x16x32_bf16 v[116:119], v[144:147], v[180:183], v[116:119]
	v_mfma_f32_16x16x32_bf16 v[112:115], v[172:175], v[180:183], v[112:115]
	v_mfma_f32_16x16x32_bf16 v[100:103], v[144:147], v[194:197], v[100:103]
	v_mfma_f32_16x16x32_bf16 v[96:99], v[172:175], v[194:197], v[96:99]
	v_mfma_f32_16x16x32_bf16 v[84:87], v[144:147], v[202:205], v[84:87]
	v_mfma_f32_16x16x32_bf16 v[80:83], v[172:175], v[202:205], v[80:83]
	v_mfma_f32_16x16x32_bf16 v[68:71], v[144:147], v[210:213], v[68:71]
	v_mfma_f32_16x16x32_bf16 v[64:67], v[172:175], v[210:213], v[64:67]
	v_mfma_f32_16x16x32_bf16 v[116:119], v[148:151], v[184:187], v[116:119]
	v_mfma_f32_16x16x32_bf16 v[112:115], v[176:179], v[184:187], v[112:115]
	v_mfma_f32_16x16x32_bf16 v[100:103], v[148:151], v[198:201], v[100:103]
	v_mfma_f32_16x16x32_bf16 v[96:99], v[176:179], v[198:201], v[96:99]
	v_mfma_f32_16x16x32_bf16 v[84:87], v[148:151], v[206:209], v[84:87]
	v_mfma_f32_16x16x32_bf16 v[80:83], v[176:179], v[206:209], v[80:83]
	v_mfma_f32_16x16x32_bf16 v[68:71], v[148:151], v[214:217], v[68:71]
	v_mfma_f32_16x16x32_bf16 v[64:67], v[176:179], v[214:217], v[64:67]
	s_setprio 0
	s_barrier
	s_add_i32 s22, s69, s33
	s_mov_b32 m0, s22
	ds_read_b128 v[180:183], v192 offset:49152
	ds_read_b128 v[184:187], v192 offset:50176
	ds_read_b128 v[194:197], v192 offset:51200
	ds_read_b128 v[198:201], v192 offset:52224
	ds_read_b128 v[202:205], v192 offset:53248
	ds_read_b128 v[206:209], v192 offset:54272
	ds_read_b128 v[210:213], v192 offset:55296
	ds_read_b128 v[214:217], v192 offset:56320
	global_load_lds_dwordx4 v154, s[98:99]
	s_add_i32 m0, s22, 0x2000
	s_add_u32 s22, s26, 0xb0080
	s_addc_u32 s23, s27, 0
	s_add_i32 s26, s70, s33
	global_load_lds_dwordx4 v158, s[98:99]
	s_mov_b32 m0, s26
	s_nop 0
	global_load_lds_dwordx4 v154, s[22:23]
	s_add_i32 m0, s26, 0x2000
	s_nop 0
	global_load_lds_dwordx4 v158, s[22:23]
	s_mov_b32 m0, s39
	s_nop 0
	global_load_lds_dwordx4 v152, s[100:101]
	s_mov_b32 m0, s40
	s_nop 0
	global_load_lds_dwordx4 v156, s[100:101]
	s_waitcnt vmcnt(8) lgkmcnt(0)
	s_barrier
	s_setprio 1
	v_mfma_f32_16x16x32_bf16 v[60:63], v[128:131], v[180:183], v[60:63]
	v_mfma_f32_16x16x32_bf16 v[56:59], v[136:139], v[180:183], v[56:59]
	v_mfma_f32_16x16x32_bf16 v[44:47], v[128:131], v[194:197], v[44:47]
	v_mfma_f32_16x16x32_bf16 v[40:43], v[136:139], v[194:197], v[40:43]
	v_mfma_f32_16x16x32_bf16 v[28:31], v[128:131], v[202:205], v[28:31]
	v_mfma_f32_16x16x32_bf16 v[24:27], v[136:139], v[202:205], v[24:27]
	v_mfma_f32_16x16x32_bf16 v[12:15], v[128:131], v[210:213], v[12:15]
	v_mfma_f32_16x16x32_bf16 v[8:11], v[136:139], v[210:213], v[8:11]
	v_mfma_f32_16x16x32_bf16 v[60:63], v[132:135], v[184:187], v[60:63]
	v_mfma_f32_16x16x32_bf16 v[56:59], v[140:143], v[184:187], v[56:59]
	v_mfma_f32_16x16x32_bf16 v[44:47], v[132:135], v[198:201], v[44:47]
	v_mfma_f32_16x16x32_bf16 v[40:43], v[140:143], v[198:201], v[40:43]
	v_mfma_f32_16x16x32_bf16 v[28:31], v[132:135], v[206:209], v[28:31]
	v_mfma_f32_16x16x32_bf16 v[24:27], v[140:143], v[206:209], v[24:27]
	v_mfma_f32_16x16x32_bf16 v[12:15], v[132:135], v[214:217], v[12:15]
	v_mfma_f32_16x16x32_bf16 v[8:11], v[140:143], v[214:217], v[8:11]
	s_setprio 0
	s_setprio 1
	v_mfma_f32_16x16x32_bf16 v[52:55], v[144:147], v[180:183], v[52:55]
	v_mfma_f32_16x16x32_bf16 v[48:51], v[172:175], v[180:183], v[48:51]
	v_mfma_f32_16x16x32_bf16 v[36:39], v[144:147], v[194:197], v[36:39]
	v_mfma_f32_16x16x32_bf16 v[32:35], v[172:175], v[194:197], v[32:35]
	v_mfma_f32_16x16x32_bf16 v[20:23], v[144:147], v[202:205], v[20:23]
	v_mfma_f32_16x16x32_bf16 v[16:19], v[172:175], v[202:205], v[16:19]
	v_mfma_f32_16x16x32_bf16 v[4:7], v[144:147], v[210:213], v[4:7]
	v_mfma_f32_16x16x32_bf16 v[0:3], v[172:175], v[210:213], v[0:3]
	v_mfma_f32_16x16x32_bf16 v[52:55], v[148:151], v[184:187], v[52:55]
	v_mfma_f32_16x16x32_bf16 v[48:51], v[176:179], v[184:187], v[48:51]
	v_mfma_f32_16x16x32_bf16 v[36:39], v[148:151], v[198:201], v[36:39]
	v_mfma_f32_16x16x32_bf16 v[32:35], v[176:179], v[198:201], v[32:35]
	v_mfma_f32_16x16x32_bf16 v[20:23], v[148:151], v[206:209], v[20:23]
	v_mfma_f32_16x16x32_bf16 v[16:19], v[176:179], v[206:209], v[16:19]
	v_mfma_f32_16x16x32_bf16 v[4:7], v[148:151], v[214:217], v[4:7]
	v_mfma_f32_16x16x32_bf16 v[0:3], v[176:179], v[214:217], v[0:3]
	s_setprio 0
	s_barrier
	s_add_i32 s68, s68, 2
	s_add_u32 s66, s66, 0x100
	s_addc_u32 s67, s67, 0
	s_cmp_gt_u32 s68, 41
	s_mov_b64 s[22:23], s[24:25]
	s_cbranch_scc0 .LBB0_1952
	s_and_b64 vcc, exec, s[18:19]
	s_cbranch_vccz .LBB0_1955
	s_barrier

; #define PG8_STAGE(bufoff, gbase, voff) do { _Pragma("unroll") for (int _i = 0; _i < 2; ++_i) \
;         __builtin_amdgcn_global_load_lds((const unsigned*)((const char*)(gbase) + (voff)[_i]), (PG8_LAS unsigned*)(lds + (bufoff) + ldsw + _i * 8192), 16, 0, 0); } while (0)
; #define PG8_LDA(dst, b, h) do { _Pragma("unroll") for (int m = 0; m < 4; ++m) _Pragma("unroll") for (int k = 0; k < 2; ++k) dst[m][k] = *(const PG8_LAS bf16x8*)(lds + PG8_SA(b, h) + aoff + m * 2048 + k * 1024); } while (0)
; #define PG8_LDB(dst, b, h) do { _Pragma("unroll") for (int n = 0; n < 2; ++n) _Pragma("unroll") for (int k = 0; k < 2; ++k) dst[n][k] = *(const PG8_LAS bf16x8*)(lds + PG8_SB(b, h) + boff + n * 2048 + k * 1024); } while (0)
; #define PG8_MMA(ai, bj, At, Bt) do { __builtin_amdgcn_s_setprio(1); _Pragma("unroll") for (int m = 0; m < 4; ++m) _Pragma("unroll") for (int n = 0; n < 2; ++n) _Pragma("unroll") for (int k = 0; k < 2; ++k) \
;         acc[ai][bj][m][n] = __builtin_amdgcn_mfma_f32_16x16x32_bf16(Bt[n][k], At[m][k], acc[ai][bj][m][n], 0, 0, 0); __builtin_amdgcn_s_setprio(0); } while (0)
; template <class Epi, class Sched, bool ALIGN_EPI = false, bool SP2 = false>
; __device__ __forceinline__ void gemm_phase(PG8_LAS unsigned char* lds, const Gemm g, const Sched& S, const Epi& E, const int wid) {
;     ...
;         const bool has_next = S.next(ui + 1, nxt);
;         const char* nA = has_next ? (const char*)g.A + (size_t)nxt.pm * tstepA : cA; const char* nB = has_next ? (const char*)g.Bt + (size_t)nxt.pn * tstepB : cB;
;         for (int t = 0; t < nt; t += 2) {
;             const bool last = (t == nt - 2);
;             const char* a1 = cA + (size_t)(t + 1) * kstep;
;             const char* a2 = last ? nA : cA + (size_t)(t + 2) * kstep; const char* b2 = last ? nB : cB + (size_t)(t + 2) * kstep;
;             const char* a3 = a2 + kstep; const char* b3 = b2 + kstep;
;             if (last && has_next) S.a_ready(nxt);
;             if constexpr (SP2) {
;             PG8_LDB(B0, 0, 0); PG8_LDB(B1, 0, 1); PG8_SCHED; PG8_LDA(At, 0, 0); PG8_STAGE(PG8_SA(1, 1), a1 + hstepA, voffA);
;             PG8_WAIT_V(8); PG8_WAIT_L(0); PG8_BAR; PG8_MMA(0, 0, At, B0); PG8_MMA(0, 1, At, B1); PG8_BAR; PG8_SCHED;
;             PG8_LDA(At, 0, 1); PG8_STAGE(PG8_SB(0, 0), b2, voffB); PG8_STAGE(PG8_SB(0, 1), b2 + hstepB, voffB); PG8_STAGE(PG8_SA(0, 0), a2, voffA);
.LBB0_2048:
	s_ashr_i32 s31, s30, 31
	s_lshl_b64 s[34:35], s[30:31], 19
	s_add_u32 s34, s0, s34
	s_addc_u32 s35, s1, s35
	s_and_b64 s[36:37], s[4:5], exec
	s_cselect_b32 s7, s35, s9
	s_cselect_b32 s11, s34, s8
	s_ashr_i32 s29, s28, 31
	s_lshl_b64 s[36:37], s[28:29], 19
	s_add_u32 s36, s33, s36
	s_addc_u32 s37, s44, s37
	s_and_b64 s[38:39], s[4:5], exec
	s_cselect_b32 s29, s37, s13
	s_cselect_b32 s31, s36, s12
	s_add_u32 s8, s8, 0x40080
	s_addc_u32 s9, s9, 0
	s_add_u32 s40, s12, 0x100
	s_addc_u32 s41, s13, 0
	s_mov_b32 s71, -2
	s_waitcnt lgkmcnt(0)
	v_add_u32_e32 v252, 0x18000, v174
	v_add_u32_e32 v253, 0x1c000, v174
	ds_read_b128 v[146:149], v179
	ds_read_b128 v[150:153], v179 offset:1024
	ds_read_b128 v[154:157], v179 offset:2048
	ds_read_b128 v[158:161], v179 offset:3072
	ds_read_b128 v[162:165], v180
	ds_read_b128 v[166:169], v180 offset:1024
	ds_read_b128 v[184:187], v180 offset:2048
	ds_read_b128 v[188:191], v180 offset:3072
	s_add_u32 s12, s8, 0xfffc0080
	s_addc_u32 s13, s9, -1
	s_cmp_eq_u32 s71, 12
	s_cselect_b32 s39, s7, s13
	s_cselect_b32 s38, s11, s12
	s_cselect_b32 s13, s29, s41
	s_cselect_b32 s12, s31, s40
	s_add_i32 m0, s46, 0xc000
	ds_read_b128 v[192:195], v181
	ds_read_b128 v[196:199], v181 offset:1024
	ds_read_b128 v[200:203], v181 offset:2048
	ds_read_b128 v[204:207], v181 offset:3072
	ds_read_b128 v[208:211], v181 offset:4096
	ds_read_b128 v[212:215], v181 offset:5120
	ds_read_b128 v[216:219], v181 offset:6144
	ds_read_b128 v[220:223], v181 offset:7168
	global_load_lds_dwordx4 v138, s[8:9]
	s_add_i32 m0, s46, 0xe000
	s_nop 0
	global_load_lds_dwordx4 v140, s[8:9]
	s_waitcnt vmcnt(8) lgkmcnt(0)
	s_barrier
	s_setprio 1
	v_mfma_f32_16x16x32_bf16 v[124:127], v[146:149], v[192:195], 0
	v_mfma_f32_16x16x32_bf16 v[120:123], v[154:157], v[192:195], 0
	v_mfma_f32_16x16x32_bf16 v[108:111], v[146:149], v[200:203], 0
	v_mfma_f32_16x16x32_bf16 v[104:107], v[154:157], v[200:203], 0
	v_mfma_f32_16x16x32_bf16 v[92:95], v[146:149], v[208:211], 0
	v_mfma_f32_16x16x32_bf16 v[88:91], v[154:157], v[208:211], 0
	v_mfma_f32_16x16x32_bf16 v[76:79], v[146:149], v[216:219], 0
	v_mfma_f32_16x16x32_bf16 v[72:75], v[154:157], v[216:219], 0
	v_mfma_f32_16x16x32_bf16 v[124:127], v[150:153], v[196:199], v[124:127]
	v_mfma_f32_16x16x32_bf16 v[120:123], v[158:161], v[196:199], v[120:123]
	v_mfma_f32_16x16x32_bf16 v[108:111], v[150:153], v[204:207], v[108:111]
	v_mfma_f32_16x16x32_bf16 v[104:107], v[158:161], v[204:207], v[104:107]
	v_mfma_f32_16x16x32_bf16 v[92:95], v[150:153], v[212:215], v[92:95]
	v_mfma_f32_16x16x32_bf16 v[88:91], v[158:161], v[212:215], v[88:91]
	v_mfma_f32_16x16x32_bf16 v[76:79], v[150:153], v[220:223], v[76:79]
	v_mfma_f32_16x16x32_bf16 v[72:75], v[158:161], v[220:223], v[72:75]
	s_setprio 0
	s_setprio 1
	v_mfma_f32_16x16x32_bf16 v[116:119], v[162:165], v[192:195], 0
	v_mfma_f32_16x16x32_bf16 v[112:115], v[184:187], v[192:195], 0
	v_mfma_f32_16x16x32_bf16 v[100:103], v[162:165], v[200:203], 0
	v_mfma_f32_16x16x32_bf16 v[96:99], v[184:187], v[200:203], 0
	v_mfma_f32_16x16x32_bf16 v[84:87], v[162:165], v[208:211], 0
	v_mfma_f32_16x16x32_bf16 v[80:83], v[184:187], v[208:211], 0
	v_mfma_f32_16x16x32_bf16 v[68:71], v[162:165], v[216:219], 0
	v_mfma_f32_16x16x32_bf16 v[64:67], v[184:187], v[216:219], 0
	v_mfma_f32_16x16x32_bf16 v[116:119], v[166:169], v[196:199], v[116:119]
	v_mfma_f32_16x16x32_bf16 v[112:115], v[188:191], v[196:199], v[112:115]
	v_mfma_f32_16x16x32_bf16 v[100:103], v[166:169], v[204:207], v[100:103]
	v_mfma_f32_16x16x32_bf16 v[96:99], v[188:191], v[204:207], v[96:99]
	v_mfma_f32_16x16x32_bf16 v[84:87], v[166:169], v[212:215], v[84:87]
	v_mfma_f32_16x16x32_bf16 v[80:83], v[188:191], v[212:215], v[80:83]
	v_mfma_f32_16x16x32_bf16 v[68:71], v[166:169], v[220:223], v[68:71]
	v_mfma_f32_16x16x32_bf16 v[64:67], v[188:191], v[220:223], v[64:67]
	s_setprio 0
	s_barrier
	s_add_i32 s72, s69, s45
	s_add_u32 s98, s12, 0x80
	s_addc_u32 s99, s13, 0
	s_mov_b32 m0, s72
	ds_read_b128 v[192:195], v181 offset:16384
	ds_read_b128 v[196:199], v181 offset:17408
	ds_read_b128 v[200:203], v181 offset:18432
	ds_read_b128 v[204:207], v181 offset:19456
	ds_read_b128 v[208:211], v181 offset:20480
	ds_read_b128 v[212:215], v181 offset:21504
	ds_read_b128 v[216:219], v181 offset:22528
	ds_read_b128 v[220:223], v181 offset:23552
	global_load_lds_dwordx4 v130, s[12:13]
	s_add_i32 m0, s72, 0x2000
	s_add_u32 s72, s12, 0x40000
	s_addc_u32 s73, s13, 0
	s_add_i32 s74, s70, s45
	global_load_lds_dwordx4 v134, s[12:13]
	s_mov_b32 m0, s74
	s_add_u32 s100, s38, 0x80
	s_addc_u32 s101, s39, 0
	global_load_lds_dwordx4 v130, s[72:73]
	s_add_i32 m0, s74, 0x2000
	s_nop 0
	global_load_lds_dwordx4 v134, s[72:73]
	s_mov_b32 m0, s46
	s_nop 0
	global_load_lds_dwordx4 v128, s[38:39]
	s_mov_b32 m0, s47
	s_nop 0
	global_load_lds_dwordx4 v132, s[38:39]
	s_waitcnt vmcnt(8) lgkmcnt(0)
	s_barrier
; #define PG8_STAGE(bufoff, gbase, voff) do { _Pragma("unroll") for (int _i = 0; _i < 2; ++_i) \
;         __builtin_amdgcn_global_load_lds((const unsigned*)((const char*)(gbase) + (voff)[_i]), (PG8_LAS unsigned*)(lds + (bufoff) + ldsw + _i * 8192), 16, 0, 0); } while (0)
; #define PG8_LDA(dst, b, h) do { _Pragma("unroll") for (int m = 0; m < 4; ++m) _Pragma("unroll") for (int k = 0; k < 2; ++k) dst[m][k] = *(const PG8_LAS bf16x8*)(lds + PG8_SA(b, h) + aoff + m * 2048 + k * 1024); } while (0)
; #define PG8_LDB(dst, b, h) do { _Pragma("unroll") for (int n = 0; n < 2; ++n) _Pragma("unroll") for (int k = 0; k < 2; ++k) dst[n][k] = *(const PG8_LAS bf16x8*)(lds + PG8_SB(b, h) + boff + n * 2048 + k * 1024); } while (0)
; #define PG8_MMA(ai, bj, At, Bt) do { __builtin_amdgcn_s_setprio(1); _Pragma("unroll") for (int m = 0; m < 4; ++m) _Pragma("unroll") for (int n = 0; n < 2; ++n) _Pragma("unroll") for (int k = 0; k < 2; ++k) \
;         acc[ai][bj][m][n] = __builtin_amdgcn_mfma_f32_16x16x32_bf16(Bt[n][k], At[m][k], acc[ai][bj][m][n], 0, 0, 0); __builtin_amdgcn_s_setprio(0); } while (0)
; #define PG8_WAIT_V(n) asm volatile("s_waitcnt vmcnt(" #n ")" ::: "memory")
; #define PG8_WAIT_L(n) asm volatile("s_waitcnt lgkmcnt(" #n ")" ::: "memory")
; #define PG8_BAR __builtin_amdgcn_s_barrier()
; #define PG8_SCHED __builtin_amdgcn_sched_barrier(0)
; template <class Epi, class Sched, bool ALIGN_EPI = false, bool SP2 = false>
; __device__ __forceinline__ void gemm_phase(PG8_LAS unsigned char* lds, const Gemm g, const Sched& S, const Epi& E, const int wid) {
;     ...
;             PG8_WAIT_V(8); PG8_WAIT_L(0); PG8_BAR; PG8_MMA(1, 0, At, B0); PG8_MMA(1, 1, At, B1); PG8_BAR; PG8_SCHED;
;             PG8_LDB(B0, 1, 0); PG8_LDB(B1, 1, 1); PG8_SCHED; PG8_LDA(At, 1, 0); PG8_STAGE(PG8_SA(0, 1), a2 + hstepA, voffA);
;             PG8_WAIT_V(8); PG8_WAIT_L(0); PG8_BAR; PG8_MMA(0, 0, At, B0); PG8_MMA(0, 1, At, B1); PG8_BAR; PG8_SCHED;
	s_setprio 1
	v_mfma_f32_16x16x32_bf16 v[60:63], v[146:149], v[192:195], 0
	v_mfma_f32_16x16x32_bf16 v[56:59], v[154:157], v[192:195], 0
	v_mfma_f32_16x16x32_bf16 v[44:47], v[146:149], v[200:203], 0
	v_mfma_f32_16x16x32_bf16 v[40:43], v[154:157], v[200:203], 0
	v_mfma_f32_16x16x32_bf16 v[28:31], v[146:149], v[208:211], 0
	v_mfma_f32_16x16x32_bf16 v[24:27], v[154:157], v[208:211], 0
	v_mfma_f32_16x16x32_bf16 v[12:15], v[146:149], v[216:219], 0
	v_mfma_f32_16x16x32_bf16 v[8:11], v[154:157], v[216:219], 0
	v_mfma_f32_16x16x32_bf16 v[60:63], v[150:153], v[196:199], v[60:63]
	v_mfma_f32_16x16x32_bf16 v[56:59], v[158:161], v[196:199], v[56:59]
	v_mfma_f32_16x16x32_bf16 v[44:47], v[150:153], v[204:207], v[44:47]
	v_mfma_f32_16x16x32_bf16 v[40:43], v[158:161], v[204:207], v[40:43]
	v_mfma_f32_16x16x32_bf16 v[28:31], v[150:153], v[212:215], v[28:31]
	v_mfma_f32_16x16x32_bf16 v[24:27], v[158:161], v[212:215], v[24:27]
	v_mfma_f32_16x16x32_bf16 v[12:15], v[150:153], v[220:223], v[12:15]
	v_mfma_f32_16x16x32_bf16 v[8:11], v[158:161], v[220:223], v[8:11]
	s_setprio 0
	s_setprio 1
	v_mfma_f32_16x16x32_bf16 v[52:55], v[162:165], v[192:195], 0
	v_mfma_f32_16x16x32_bf16 v[48:51], v[184:187], v[192:195], 0
	v_mfma_f32_16x16x32_bf16 v[36:39], v[162:165], v[200:203], 0
	v_mfma_f32_16x16x32_bf16 v[32:35], v[184:187], v[200:203], 0
	v_mfma_f32_16x16x32_bf16 v[20:23], v[162:165], v[208:211], 0
	v_mfma_f32_16x16x32_bf16 v[16:19], v[184:187], v[208:211], 0
	v_mfma_f32_16x16x32_bf16 v[4:7], v[162:165], v[216:219], 0
	v_mfma_f32_16x16x32_bf16 v[0:3], v[184:187], v[216:219], 0
	v_mfma_f32_16x16x32_bf16 v[52:55], v[166:169], v[196:199], v[52:55]
	v_mfma_f32_16x16x32_bf16 v[48:51], v[188:191], v[196:199], v[48:51]
	v_mfma_f32_16x16x32_bf16 v[36:39], v[166:169], v[204:207], v[36:39]
	v_mfma_f32_16x16x32_bf16 v[32:35], v[188:191], v[204:207], v[32:35]
	v_mfma_f32_16x16x32_bf16 v[20:23], v[166:169], v[212:215], v[20:23]
	v_mfma_f32_16x16x32_bf16 v[16:19], v[188:191], v[212:215], v[16:19]
	v_mfma_f32_16x16x32_bf16 v[4:7], v[166:169], v[220:223], v[4:7]
	v_mfma_f32_16x16x32_bf16 v[0:3], v[188:191], v[220:223], v[0:3]
	s_setprio 0
	s_barrier
	s_add_i32 s72, 0, 0x18000
	s_add_i32 s73, 0, 0x1c000
	ds_read_b128 v[146:149], v252
	ds_read_b128 v[150:153], v252 offset:1024
	ds_read_b128 v[154:157], v252 offset:2048
	ds_read_b128 v[158:161], v252 offset:3072
	ds_read_b128 v[162:165], v253
	ds_read_b128 v[166:169], v253 offset:1024
	ds_read_b128 v[184:187], v253 offset:2048
	ds_read_b128 v[188:191], v253 offset:3072
	s_add_u32 s38, s38, 0x40000
	s_addc_u32 s39, s39, 0
	s_mov_b32 m0, s48
	ds_read_b128 v[192:195], v181 offset:32768
	ds_read_b128 v[196:199], v181 offset:33792
	ds_read_b128 v[200:203], v181 offset:34816
	ds_read_b128 v[204:207], v181 offset:35840
	ds_read_b128 v[208:211], v181 offset:36864
	ds_read_b128 v[212:215], v181 offset:37888
	ds_read_b128 v[216:219], v181 offset:38912
	ds_read_b128 v[220:223], v181 offset:39936
	global_load_lds_dwordx4 v128, s[38:39]
	s_mov_b32 m0, s49
	s_nop 0
	global_load_lds_dwordx4 v132, s[38:39]
	s_waitcnt vmcnt(8) lgkmcnt(0)
	s_barrier
	s_setprio 1
	v_mfma_f32_16x16x32_bf16 v[124:127], v[146:149], v[192:195], v[124:127]
	v_mfma_f32_16x16x32_bf16 v[120:123], v[154:157], v[192:195], v[120:123]
	v_mfma_f32_16x16x32_bf16 v[108:111], v[146:149], v[200:203], v[108:111]
	v_mfma_f32_16x16x32_bf16 v[104:107], v[154:157], v[200:203], v[104:107]
	v_mfma_f32_16x16x32_bf16 v[92:95], v[146:149], v[208:211], v[92:95]
	v_mfma_f32_16x16x32_bf16 v[88:91], v[154:157], v[208:211], v[88:91]
	v_mfma_f32_16x16x32_bf16 v[76:79], v[146:149], v[216:219], v[76:79]
	v_mfma_f32_16x16x32_bf16 v[72:75], v[154:157], v[216:219], v[72:75]
	v_mfma_f32_16x16x32_bf16 v[124:127], v[150:153], v[196:199], v[124:127]
	v_mfma_f32_16x16x32_bf16 v[120:123], v[158:161], v[196:199], v[120:123]
	v_mfma_f32_16x16x32_bf16 v[108:111], v[150:153], v[204:207], v[108:111]
	v_mfma_f32_16x16x32_bf16 v[104:107], v[158:161], v[204:207], v[104:107]
	v_mfma_f32_16x16x32_bf16 v[92:95], v[150:153], v[212:215], v[92:95]
	v_mfma_f32_16x16x32_bf16 v[88:91], v[158:161], v[212:215], v[88:91]
	v_mfma_f32_16x16x32_bf16 v[76:79], v[150:153], v[220:223], v[76:79]
	v_mfma_f32_16x16x32_bf16 v[72:75], v[158:161], v[220:223], v[72:75]
	s_setprio 0
	s_setprio 1
	v_mfma_f32_16x16x32_bf16 v[116:119], v[162:165], v[192:195], v[116:119]
	v_mfma_f32_16x16x32_bf16 v[112:115], v[184:187], v[192:195], v[112:115]
	v_mfma_f32_16x16x32_bf16 v[100:103], v[162:165], v[200:203], v[100:103]
	v_mfma_f32_16x16x32_bf16 v[96:99], v[184:187], v[200:203], v[96:99]
	v_mfma_f32_16x16x32_bf16 v[84:87], v[162:165], v[208:211], v[84:87]
	v_mfma_f32_16x16x32_bf16 v[80:83], v[184:187], v[208:211], v[80:83]
	v_mfma_f32_16x16x32_bf16 v[68:71], v[162:165], v[216:219], v[68:71]
	v_mfma_f32_16x16x32_bf16 v[64:67], v[184:187], v[216:219], v[64:67]
	v_mfma_f32_16x16x32_bf16 v[116:119], v[166:169], v[196:199], v[116:119]
	v_mfma_f32_16x16x32_bf16 v[112:115], v[188:191], v[196:199], v[112:115]
	v_mfma_f32_16x16x32_bf16 v[100:103], v[166:169], v[204:207], v[100:103]
	v_mfma_f32_16x16x32_bf16 v[96:99], v[188:191], v[204:207], v[96:99]
	v_mfma_f32_16x16x32_bf16 v[84:87], v[166:169], v[212:215], v[84:87]
	v_mfma_f32_16x16x32_bf16 v[80:83], v[188:191], v[212:215], v[80:83]
	v_mfma_f32_16x16x32_bf16 v[68:71], v[166:169], v[220:223], v[68:71]
	v_mfma_f32_16x16x32_bf16 v[64:67], v[188:191], v[220:223], v[64:67]
	s_setprio 0
	s_barrier
; #define PG8_STAGE(bufoff, gbase, voff) do { _Pragma("unroll") for (int _i = 0; _i < 2; ++_i) \
;         __builtin_amdgcn_global_load_lds((const unsigned*)((const char*)(gbase) + (voff)[_i]), (PG8_LAS unsigned*)(lds + (bufoff) + ldsw + _i * 8192), 16, 0, 0); } while (0)
; #define PG8_LDA(dst, b, h) do { _Pragma("unroll") for (int m = 0; m < 4; ++m) _Pragma("unroll") for (int k = 0; k < 2; ++k) dst[m][k] = *(const PG8_LAS bf16x8*)(lds + PG8_SA(b, h) + aoff + m * 2048 + k * 1024); } while (0)
; #define PG8_WAIT_V(n) asm volatile("s_waitcnt vmcnt(" #n ")" ::: "memory")
; #define PG8_WAIT_L(n) asm volatile("s_waitcnt lgkmcnt(" #n ")" ::: "memory")
; #define PG8_BAR __builtin_amdgcn_s_barrier()
; template <class Epi, class Sched, bool ALIGN_EPI = false, bool SP2 = false>
; __device__ __forceinline__ void gemm_phase(PG8_LAS unsigned char* lds, const Gemm g, const Sched& S, const Epi& E, const int wid) {
;     ...
;         for (int t = 0; t < nt; t += 2) {
;             const bool last = (t == nt - 2);
;             const char* a1 = cA + (size_t)(t + 1) * kstep;
;             const char* a2 = last ? nA : cA + (size_t)(t + 2) * kstep; const char* b2 = last ? nB : cB + (size_t)(t + 2) * kstep;
;             const char* a3 = a2 + kstep; const char* b3 = b2 + kstep;
;             if (last && has_next) S.a_ready(nxt);
;             if constexpr (SP2) {
;             PG8_LDB(B0, 0, 0); PG8_LDB(B1, 0, 1); PG8_SCHED; PG8_LDA(At, 0, 0); PG8_STAGE(PG8_SA(1, 1), a1 + hstepA, voffA);
;             PG8_WAIT_V(8); PG8_WAIT_L(0); PG8_BAR; PG8_MMA(0, 0, At, B0); PG8_MMA(0, 1, At, B1); PG8_BAR; PG8_SCHED;
;             PG8_LDA(At, 0, 1); PG8_STAGE(PG8_SB(0, 0), b2, voffB); PG8_STAGE(PG8_SB(0, 1), b2 + hstepB, voffB); PG8_STAGE(PG8_SA(0, 0), a2, voffA);
;             PG8_WAIT_V(8); PG8_WAIT_L(0); PG8_BAR; PG8_MMA(1, 0, At, B0); PG8_MMA(1, 1, At, B1); PG8_BAR; PG8_SCHED;
;             PG8_LDB(B0, 1, 0); PG8_LDB(B1, 1, 1); PG8_SCHED; PG8_LDA(At, 1, 0); PG8_STAGE(PG8_SA(0, 1), a2 + hstepA, voffA);
;             PG8_WAIT_V(8); PG8_WAIT_L(0); PG8_BAR; PG8_MMA(0, 0, At, B0); PG8_MMA(0, 1, At, B1); PG8_BAR; PG8_SCHED;
;             PG8_LDA(At, 1, 1); PG8_STAGE(PG8_SB(1, 0), b3, voffB); PG8_STAGE(PG8_SB(1, 1), b3 + hstepB, voffB); PG8_STAGE(PG8_SA(1, 0), a3, voffA);
;             PG8_WAIT_V(8); PG8_WAIT_L(0); PG8_BAR; PG8_MMA(1, 0, At, B0); PG8_MMA(1, 1, At, B1); PG8_BAR; PG8_SCHED;
	s_add_i32 s38, s72, s45
	s_mov_b32 m0, s38
	ds_read_b128 v[192:195], v181 offset:49152
	ds_read_b128 v[196:199], v181 offset:50176
	ds_read_b128 v[200:203], v181 offset:51200
	ds_read_b128 v[204:207], v181 offset:52224
	ds_read_b128 v[208:211], v181 offset:53248
	ds_read_b128 v[212:215], v181 offset:54272
	ds_read_b128 v[216:219], v181 offset:55296
	ds_read_b128 v[220:223], v181 offset:56320
	global_load_lds_dwordx4 v130, s[98:99]
	s_add_i32 m0, s38, 0x2000
	s_add_u32 s12, s12, 0x40080
	s_addc_u32 s13, s13, 0
	s_add_i32 s38, s73, s45
	global_load_lds_dwordx4 v134, s[98:99]
	s_mov_b32 m0, s38
	s_nop 0
	global_load_lds_dwordx4 v130, s[12:13]
	s_add_i32 m0, s38, 0x2000
	s_nop 0
	global_load_lds_dwordx4 v134, s[12:13]
	s_mov_b32 m0, s65
	s_nop 0
	global_load_lds_dwordx4 v128, s[100:101]
	s_mov_b32 m0, s66
	s_nop 0
	global_load_lds_dwordx4 v132, s[100:101]
	s_waitcnt vmcnt(8) lgkmcnt(0)
	s_barrier
	s_setprio 1
	v_mfma_f32_16x16x32_bf16 v[60:63], v[146:149], v[192:195], v[60:63]
	v_mfma_f32_16x16x32_bf16 v[56:59], v[154:157], v[192:195], v[56:59]
	v_mfma_f32_16x16x32_bf16 v[44:47], v[146:149], v[200:203], v[44:47]
	v_mfma_f32_16x16x32_bf16 v[40:43], v[154:157], v[200:203], v[40:43]
	v_mfma_f32_16x16x32_bf16 v[28:31], v[146:149], v[208:211], v[28:31]
	v_mfma_f32_16x16x32_bf16 v[24:27], v[154:157], v[208:211], v[24:27]
	v_mfma_f32_16x16x32_bf16 v[12:15], v[146:149], v[216:219], v[12:15]
	v_mfma_f32_16x16x32_bf16 v[8:11], v[154:157], v[216:219], v[8:11]
	v_mfma_f32_16x16x32_bf16 v[60:63], v[150:153], v[196:199], v[60:63]
	v_mfma_f32_16x16x32_bf16 v[56:59], v[158:161], v[196:199], v[56:59]
	v_mfma_f32_16x16x32_bf16 v[44:47], v[150:153], v[204:207], v[44:47]
	v_mfma_f32_16x16x32_bf16 v[40:43], v[158:161], v[204:207], v[40:43]
	v_mfma_f32_16x16x32_bf16 v[28:31], v[150:153], v[212:215], v[28:31]
	v_mfma_f32_16x16x32_bf16 v[24:27], v[158:161], v[212:215], v[24:27]
	v_mfma_f32_16x16x32_bf16 v[12:15], v[150:153], v[220:223], v[12:15]
	v_mfma_f32_16x16x32_bf16 v[8:11], v[158:161], v[220:223], v[8:11]
	s_setprio 0
	s_setprio 1
	v_mfma_f32_16x16x32_bf16 v[52:55], v[162:165], v[192:195], v[52:55]
	v_mfma_f32_16x16x32_bf16 v[48:51], v[184:187], v[192:195], v[48:51]
	v_mfma_f32_16x16x32_bf16 v[36:39], v[162:165], v[200:203], v[36:39]
	v_mfma_f32_16x16x32_bf16 v[32:35], v[184:187], v[200:203], v[32:35]
	v_mfma_f32_16x16x32_bf16 v[20:23], v[162:165], v[208:211], v[20:23]
	v_mfma_f32_16x16x32_bf16 v[16:19], v[184:187], v[208:211], v[16:19]
	v_mfma_f32_16x16x32_bf16 v[4:7], v[162:165], v[216:219], v[4:7]
	v_mfma_f32_16x16x32_bf16 v[0:3], v[184:187], v[216:219], v[0:3]
	v_mfma_f32_16x16x32_bf16 v[52:55], v[166:169], v[196:199], v[52:55]
	v_mfma_f32_16x16x32_bf16 v[48:51], v[188:191], v[196:199], v[48:51]
	v_mfma_f32_16x16x32_bf16 v[36:39], v[166:169], v[204:207], v[36:39]
	v_mfma_f32_16x16x32_bf16 v[32:35], v[188:191], v[204:207], v[32:35]
	v_mfma_f32_16x16x32_bf16 v[20:23], v[166:169], v[212:215], v[20:23]
	v_mfma_f32_16x16x32_bf16 v[16:19], v[188:191], v[212:215], v[16:19]
	v_mfma_f32_16x16x32_bf16 v[4:7], v[166:169], v[220:223], v[4:7]
	v_mfma_f32_16x16x32_bf16 v[0:3], v[188:191], v[220:223], v[0:3]
	s_setprio 0
	s_barrier
	s_add_i32 s71, s71, 2
	s_add_u32 s8, s8, 0x100
	s_addc_u32 s9, s9, 0
	s_add_u32 s40, s40, 0x100
	s_addc_u32 s41, s41, 0
	s_cmp_gt_u32 s71, 13
.LBB0_2049:
	ds_read_b128 v[146:149], v179
	ds_read_b128 v[150:153], v179 offset:1024
	ds_read_b128 v[154:157], v179 offset:2048
	ds_read_b128 v[158:161], v179 offset:3072
	ds_read_b128 v[162:165], v180
	ds_read_b128 v[166:169], v180 offset:1024
	ds_read_b128 v[184:187], v180 offset:2048
	ds_read_b128 v[188:191], v180 offset:3072
	s_add_u32 s12, s8, 0xfffc0080
	s_addc_u32 s13, s9, -1
	s_cmp_eq_u32 s71, 12
	s_cselect_b32 s39, s7, s13
	s_cselect_b32 s38, s11, s12
	s_cselect_b32 s13, s29, s41
	s_cselect_b32 s12, s31, s40
	s_add_i32 m0, s46, 0xc000
	ds_read_b128 v[192:195], v181
	ds_read_b128 v[196:199], v181 offset:1024
	ds_read_b128 v[200:203], v181 offset:2048
	ds_read_b128 v[204:207], v181 offset:3072
	ds_read_b128 v[208:211], v181 offset:4096
	ds_read_b128 v[212:215], v181 offset:5120
	ds_read_b128 v[216:219], v181 offset:6144
	ds_read_b128 v[220:223], v181 offset:7168
	global_load_lds_dwordx4 v138, s[8:9]
	s_add_i32 m0, s46, 0xe000
	s_nop 0
	global_load_lds_dwordx4 v140, s[8:9]
	s_waitcnt vmcnt(8) lgkmcnt(0)
	s_barrier
	s_setprio 1
	v_mfma_f32_16x16x32_bf16 v[124:127], v[146:149], v[192:195], v[124:127]
	v_mfma_f32_16x16x32_bf16 v[120:123], v[154:157], v[192:195], v[120:123]
	v_mfma_f32_16x16x32_bf16 v[108:111], v[146:149], v[200:203], v[108:111]
	v_mfma_f32_16x16x32_bf16 v[104:107], v[154:157], v[200:203], v[104:107]
	v_mfma_f32_16x16x32_bf16 v[92:95], v[146:149], v[208:211], v[92:95]
	v_mfma_f32_16x16x32_bf16 v[88:91], v[154:157], v[208:211], v[88:91]
	v_mfma_f32_16x16x32_bf16 v[76:79], v[146:149], v[216:219], v[76:79]
	v_mfma_f32_16x16x32_bf16 v[72:75], v[154:157], v[216:219], v[72:75]
	v_mfma_f32_16x16x32_bf16 v[124:127], v[150:153], v[196:199], v[124:127]
	v_mfma_f32_16x16x32_bf16 v[120:123], v[158:161], v[196:199], v[120:123]
	v_mfma_f32_16x16x32_bf16 v[108:111], v[150:153], v[204:207], v[108:111]
	v_mfma_f32_16x16x32_bf16 v[104:107], v[158:161], v[204:207], v[104:107]
	v_mfma_f32_16x16x32_bf16 v[92:95], v[150:153], v[212:215], v[92:95]
	v_mfma_f32_16x16x32_bf16 v[88:91], v[158:161], v[212:215], v[88:91]
	v_mfma_f32_16x16x32_bf16 v[76:79], v[150:153], v[220:223], v[76:79]
	v_mfma_f32_16x16x32_bf16 v[72:75], v[158:161], v[220:223], v[72:75]
	s_setprio 0
	s_setprio 1
	v_mfma_f32_16x16x32_bf16 v[116:119], v[162:165], v[192:195], v[116:119]
	v_mfma_f32_16x16x32_bf16 v[112:115], v[184:187], v[192:195], v[112:115]
	v_mfma_f32_16x16x32_bf16 v[100:103], v[162:165], v[200:203], v[100:103]
	v_mfma_f32_16x16x32_bf16 v[96:99], v[184:187], v[200:203], v[96:99]
	v_mfma_f32_16x16x32_bf16 v[84:87], v[162:165], v[208:211], v[84:87]
	v_mfma_f32_16x16x32_bf16 v[80:83], v[184:187], v[208:211], v[80:83]
	v_mfma_f32_16x16x32_bf16 v[68:71], v[162:165], v[216:219], v[68:71]
	v_mfma_f32_16x16x32_bf16 v[64:67], v[184:187], v[216:219], v[64:67]
	v_mfma_f32_16x16x32_bf16 v[116:119], v[166:169], v[196:199], v[116:119]
	v_mfma_f32_16x16x32_bf16 v[112:115], v[188:191], v[196:199], v[112:115]
	v_mfma_f32_16x16x32_bf16 v[100:103], v[166:169], v[204:207], v[100:103]
	v_mfma_f32_16x16x32_bf16 v[96:99], v[188:191], v[204:207], v[96:99]
	v_mfma_f32_16x16x32_bf16 v[84:87], v[166:169], v[212:215], v[84:87]
	v_mfma_f32_16x16x32_bf16 v[80:83], v[188:191], v[212:215], v[80:83]
	v_mfma_f32_16x16x32_bf16 v[68:71], v[166:169], v[220:223], v[68:71]
	v_mfma_f32_16x16x32_bf16 v[64:67], v[188:191], v[220:223], v[64:67]
	s_setprio 0
	s_barrier
; #define PG8_STAGE(bufoff, gbase, voff) do { _Pragma("unroll") for (int _i = 0; _i < 2; ++_i) \
;         __builtin_amdgcn_global_load_lds((const unsigned*)((const char*)(gbase) + (voff)[_i]), (PG8_LAS unsigned*)(lds + (bufoff) + ldsw + _i * 8192), 16, 0, 0); } while (0)
; #define PG8_LDA(dst, b, h) do { _Pragma("unroll") for (int m = 0; m < 4; ++m) _Pragma("unroll") for (int k = 0; k < 2; ++k) dst[m][k] = *(const PG8_LAS bf16x8*)(lds + PG8_SA(b, h) + aoff + m * 2048 + k * 1024); } while (0)
; #define PG8_LDB(dst, b, h) do { _Pragma("unroll") for (int n = 0; n < 2; ++n) _Pragma("unroll") for (int k = 0; k < 2; ++k) dst[n][k] = *(const PG8_LAS bf16x8*)(lds + PG8_SB(b, h) + boff + n * 2048 + k * 1024); } while (0)
; #define PG8_MMA(ai, bj, At, Bt) do { __builtin_amdgcn_s_setprio(1); _Pragma("unroll") for (int m = 0; m < 4; ++m) _Pragma("unroll") for (int n = 0; n < 2; ++n) _Pragma("unroll") for (int k = 0; k < 2; ++k) \
;         acc[ai][bj][m][n] = __builtin_amdgcn_mfma_f32_16x16x32_bf16(Bt[n][k], At[m][k], acc[ai][bj][m][n], 0, 0, 0); __builtin_amdgcn_s_setprio(0); } while (0)
; #define PG8_WAIT_V(n) asm volatile("s_waitcnt vmcnt(" #n ")" ::: "memory")
; #define PG8_WAIT_L(n) asm volatile("s_waitcnt lgkmcnt(" #n ")" ::: "memory")
; #define PG8_BAR __builtin_amdgcn_s_barrier()
; #define PG8_SCHED __builtin_amdgcn_sched_barrier(0)
; template <class Epi, class Sched, bool ALIGN_EPI = false, bool SP2 = false>
; __device__ __forceinline__ void gemm_phase(PG8_LAS unsigned char* lds, const Gemm g, const Sched& S, const Epi& E, const int wid) {
;     ...
;             PG8_LDA(At, 0, 1); PG8_STAGE(PG8_SB(0, 0), b2, voffB); PG8_STAGE(PG8_SB(0, 1), b2 + hstepB, voffB); PG8_STAGE(PG8_SA(0, 0), a2, voffA);
;             PG8_WAIT_V(8); PG8_WAIT_L(0); PG8_BAR; PG8_MMA(1, 0, At, B0); PG8_MMA(1, 1, At, B1); PG8_BAR; PG8_SCHED;
;             PG8_LDB(B0, 1, 0); PG8_LDB(B1, 1, 1); PG8_SCHED; PG8_LDA(At, 1, 0); PG8_STAGE(PG8_SA(0, 1), a2 + hstepA, voffA);
	s_add_i32 s72, s69, s45
	s_add_u32 s98, s12, 0x80
	s_addc_u32 s99, s13, 0
	s_mov_b32 m0, s72
	ds_read_b128 v[192:195], v181 offset:16384
	ds_read_b128 v[196:199], v181 offset:17408
	ds_read_b128 v[200:203], v181 offset:18432
	ds_read_b128 v[204:207], v181 offset:19456
	ds_read_b128 v[208:211], v181 offset:20480
	ds_read_b128 v[212:215], v181 offset:21504
	ds_read_b128 v[216:219], v181 offset:22528
	ds_read_b128 v[220:223], v181 offset:23552
	global_load_lds_dwordx4 v130, s[12:13]
	s_add_i32 m0, s72, 0x2000
	s_add_u32 s72, s12, 0x40000
	s_addc_u32 s73, s13, 0
	s_add_i32 s74, s70, s45
	global_load_lds_dwordx4 v134, s[12:13]
	s_mov_b32 m0, s74
	s_add_u32 s100, s38, 0x80
	s_addc_u32 s101, s39, 0
	global_load_lds_dwordx4 v130, s[72:73]
	s_add_i32 m0, s74, 0x2000
	s_nop 0
	global_load_lds_dwordx4 v134, s[72:73]
	s_mov_b32 m0, s46
	s_nop 0
	global_load_lds_dwordx4 v128, s[38:39]
	s_mov_b32 m0, s47
	s_nop 0
	global_load_lds_dwordx4 v132, s[38:39]
	s_waitcnt vmcnt(8) lgkmcnt(0)
	s_barrier
	s_setprio 1
	v_mfma_f32_16x16x32_bf16 v[60:63], v[146:149], v[192:195], v[60:63]
	v_mfma_f32_16x16x32_bf16 v[56:59], v[154:157], v[192:195], v[56:59]
	v_mfma_f32_16x16x32_bf16 v[44:47], v[146:149], v[200:203], v[44:47]
	v_mfma_f32_16x16x32_bf16 v[40:43], v[154:157], v[200:203], v[40:43]
	v_mfma_f32_16x16x32_bf16 v[28:31], v[146:149], v[208:211], v[28:31]
	v_mfma_f32_16x16x32_bf16 v[24:27], v[154:157], v[208:211], v[24:27]
	v_mfma_f32_16x16x32_bf16 v[12:15], v[146:149], v[216:219], v[12:15]
	v_mfma_f32_16x16x32_bf16 v[8:11], v[154:157], v[216:219], v[8:11]
	v_mfma_f32_16x16x32_bf16 v[60:63], v[150:153], v[196:199], v[60:63]
	v_mfma_f32_16x16x32_bf16 v[56:59], v[158:161], v[196:199], v[56:59]
	v_mfma_f32_16x16x32_bf16 v[44:47], v[150:153], v[204:207], v[44:47]
	v_mfma_f32_16x16x32_bf16 v[40:43], v[158:161], v[204:207], v[40:43]
	v_mfma_f32_16x16x32_bf16 v[28:31], v[150:153], v[212:215], v[28:31]
	v_mfma_f32_16x16x32_bf16 v[24:27], v[158:161], v[212:215], v[24:27]
	v_mfma_f32_16x16x32_bf16 v[12:15], v[150:153], v[220:223], v[12:15]
	v_mfma_f32_16x16x32_bf16 v[8:11], v[158:161], v[220:223], v[8:11]
	s_setprio 0
	s_setprio 1
	v_mfma_f32_16x16x32_bf16 v[52:55], v[162:165], v[192:195], v[52:55]
	v_mfma_f32_16x16x32_bf16 v[48:51], v[184:187], v[192:195], v[48:51]
	v_mfma_f32_16x16x32_bf16 v[36:39], v[162:165], v[200:203], v[36:39]
	v_mfma_f32_16x16x32_bf16 v[32:35], v[184:187], v[200:203], v[32:35]
	v_mfma_f32_16x16x32_bf16 v[20:23], v[162:165], v[208:211], v[20:23]
	v_mfma_f32_16x16x32_bf16 v[16:19], v[184:187], v[208:211], v[16:19]
	v_mfma_f32_16x16x32_bf16 v[4:7], v[162:165], v[216:219], v[4:7]
	v_mfma_f32_16x16x32_bf16 v[0:3], v[184:187], v[216:219], v[0:3]
	v_mfma_f32_16x16x32_bf16 v[52:55], v[166:169], v[196:199], v[52:55]
	v_mfma_f32_16x16x32_bf16 v[48:51], v[188:191], v[196:199], v[48:51]
	v_mfma_f32_16x16x32_bf16 v[36:39], v[166:169], v[204:207], v[36:39]
	v_mfma_f32_16x16x32_bf16 v[32:35], v[188:191], v[204:207], v[32:35]
	v_mfma_f32_16x16x32_bf16 v[20:23], v[166:169], v[212:215], v[20:23]
	v_mfma_f32_16x16x32_bf16 v[16:19], v[188:191], v[212:215], v[16:19]
	v_mfma_f32_16x16x32_bf16 v[4:7], v[166:169], v[220:223], v[4:7]
	v_mfma_f32_16x16x32_bf16 v[0:3], v[188:191], v[220:223], v[0:3]
	s_setprio 0
	s_barrier
	s_add_i32 s72, 0, 0x18000
	s_add_i32 s73, 0, 0x1c000
	ds_read_b128 v[146:149], v252
	ds_read_b128 v[150:153], v252 offset:1024
	ds_read_b128 v[154:157], v252 offset:2048
	ds_read_b128 v[158:161], v252 offset:3072
	ds_read_b128 v[162:165], v253
	ds_read_b128 v[166:169], v253 offset:1024
	ds_read_b128 v[184:187], v253 offset:2048
	ds_read_b128 v[188:191], v253 offset:3072
	s_add_u32 s38, s38, 0x40000
	s_addc_u32 s39, s39, 0
	s_mov_b32 m0, s48
	ds_read_b128 v[192:195], v181 offset:32768
	ds_read_b128 v[196:199], v181 offset:33792
	ds_read_b128 v[200:203], v181 offset:34816
	ds_read_b128 v[204:207], v181 offset:35840
	ds_read_b128 v[208:211], v181 offset:36864
	ds_read_b128 v[212:215], v181 offset:37888
	ds_read_b128 v[216:219], v181 offset:38912
	ds_read_b128 v[220:223], v181 offset:39936
	global_load_lds_dwordx4 v128, s[38:39]
	s_mov_b32 m0, s49
	s_nop 0
	global_load_lds_dwordx4 v132, s[38:39]
	s_waitcnt vmcnt(8) lgkmcnt(0)
	s_barrier
; #define PG8_STAGE(bufoff, gbase, voff) do { _Pragma("unroll") for (int _i = 0; _i < 2; ++_i) \
;         __builtin_amdgcn_global_load_lds((const unsigned*)((const char*)(gbase) + (voff)[_i]), (PG8_LAS unsigned*)(lds + (bufoff) + ldsw + _i * 8192), 16, 0, 0); } while (0)
; #define PG8_LDA(dst, b, h) do { _Pragma("unroll") for (int m = 0; m < 4; ++m) _Pragma("unroll") for (int k = 0; k < 2; ++k) dst[m][k] = *(const PG8_LAS bf16x8*)(lds + PG8_SA(b, h) + aoff + m * 2048 + k * 1024); } while (0)
; #define PG8_MMA(ai, bj, At, Bt) do { __builtin_amdgcn_s_setprio(1); _Pragma("unroll") for (int m = 0; m < 4; ++m) _Pragma("unroll") for (int n = 0; n < 2; ++n) _Pragma("unroll") for (int k = 0; k < 2; ++k) \
;         acc[ai][bj][m][n] = __builtin_amdgcn_mfma_f32_16x16x32_bf16(Bt[n][k], At[m][k], acc[ai][bj][m][n], 0, 0, 0); __builtin_amdgcn_s_setprio(0); } while (0)
; #define PG8_WAIT_V(n) asm volatile("s_waitcnt vmcnt(" #n ")" ::: "memory")
; #define PG8_WAIT_L(n) asm volatile("s_waitcnt lgkmcnt(" #n ")" ::: "memory")
; #define PG8_BAR __builtin_amdgcn_s_barrier()
; #define PG8_SCHED __builtin_amdgcn_sched_barrier(0)
; template <class Epi, class Sched, bool ALIGN_EPI = false, bool SP2 = false>
; __device__ __forceinline__ void gemm_phase(PG8_LAS unsigned char* lds, const Gemm g, const Sched& S, const Epi& E, const int wid) {
;     ...
;             PG8_WAIT_V(8); PG8_WAIT_L(0); PG8_BAR; PG8_MMA(0, 0, At, B0); PG8_MMA(0, 1, At, B1); PG8_BAR; PG8_SCHED;
;             PG8_LDA(At, 1, 1); PG8_STAGE(PG8_SB(1, 0), b3, voffB); PG8_STAGE(PG8_SB(1, 1), b3 + hstepB, voffB); PG8_STAGE(PG8_SA(1, 0), a3, voffA);
;             PG8_WAIT_V(8); PG8_WAIT_L(0); PG8_BAR; PG8_MMA(1, 0, At, B0); PG8_MMA(1, 1, At, B1); PG8_BAR; PG8_SCHED;
;     ...
;         if constexpr (ALIGN_EPI) { if (wr == 0) PG8_BAR; }
	s_setprio 1
	v_mfma_f32_16x16x32_bf16 v[124:127], v[146:149], v[192:195], v[124:127]
	v_mfma_f32_16x16x32_bf16 v[120:123], v[154:157], v[192:195], v[120:123]
	v_mfma_f32_16x16x32_bf16 v[108:111], v[146:149], v[200:203], v[108:111]
	v_mfma_f32_16x16x32_bf16 v[104:107], v[154:157], v[200:203], v[104:107]
	v_mfma_f32_16x16x32_bf16 v[92:95], v[146:149], v[208:211], v[92:95]
	v_mfma_f32_16x16x32_bf16 v[88:91], v[154:157], v[208:211], v[88:91]
	v_mfma_f32_16x16x32_bf16 v[76:79], v[146:149], v[216:219], v[76:79]
	v_mfma_f32_16x16x32_bf16 v[72:75], v[154:157], v[216:219], v[72:75]
	v_mfma_f32_16x16x32_bf16 v[124:127], v[150:153], v[196:199], v[124:127]
	v_mfma_f32_16x16x32_bf16 v[120:123], v[158:161], v[196:199], v[120:123]
	v_mfma_f32_16x16x32_bf16 v[108:111], v[150:153], v[204:207], v[108:111]
	v_mfma_f32_16x16x32_bf16 v[104:107], v[158:161], v[204:207], v[104:107]
	v_mfma_f32_16x16x32_bf16 v[92:95], v[150:153], v[212:215], v[92:95]
	v_mfma_f32_16x16x32_bf16 v[88:91], v[158:161], v[212:215], v[88:91]
	v_mfma_f32_16x16x32_bf16 v[76:79], v[150:153], v[220:223], v[76:79]
	v_mfma_f32_16x16x32_bf16 v[72:75], v[158:161], v[220:223], v[72:75]
	s_setprio 0
	s_setprio 1
	v_mfma_f32_16x16x32_bf16 v[116:119], v[162:165], v[192:195], v[116:119]
	v_mfma_f32_16x16x32_bf16 v[112:115], v[184:187], v[192:195], v[112:115]
	v_mfma_f32_16x16x32_bf16 v[100:103], v[162:165], v[200:203], v[100:103]
	v_mfma_f32_16x16x32_bf16 v[96:99], v[184:187], v[200:203], v[96:99]
	v_mfma_f32_16x16x32_bf16 v[84:87], v[162:165], v[208:211], v[84:87]
	v_mfma_f32_16x16x32_bf16 v[80:83], v[184:187], v[208:211], v[80:83]
	v_mfma_f32_16x16x32_bf16 v[68:71], v[162:165], v[216:219], v[68:71]
	v_mfma_f32_16x16x32_bf16 v[64:67], v[184:187], v[216:219], v[64:67]
	v_mfma_f32_16x16x32_bf16 v[116:119], v[166:169], v[196:199], v[116:119]
	v_mfma_f32_16x16x32_bf16 v[112:115], v[188:191], v[196:199], v[112:115]
	v_mfma_f32_16x16x32_bf16 v[100:103], v[166:169], v[204:207], v[100:103]
	v_mfma_f32_16x16x32_bf16 v[96:99], v[188:191], v[204:207], v[96:99]
	v_mfma_f32_16x16x32_bf16 v[84:87], v[166:169], v[212:215], v[84:87]
	v_mfma_f32_16x16x32_bf16 v[80:83], v[188:191], v[212:215], v[80:83]
	v_mfma_f32_16x16x32_bf16 v[68:71], v[166:169], v[220:223], v[68:71]
	v_mfma_f32_16x16x32_bf16 v[64:67], v[188:191], v[220:223], v[64:67]
	s_setprio 0
	s_barrier
	s_add_i32 s38, s72, s45
	s_mov_b32 m0, s38
	ds_read_b128 v[192:195], v181 offset:49152
	ds_read_b128 v[196:199], v181 offset:50176
	ds_read_b128 v[200:203], v181 offset:51200
	ds_read_b128 v[204:207], v181 offset:52224
	ds_read_b128 v[208:211], v181 offset:53248
	ds_read_b128 v[212:215], v181 offset:54272
	ds_read_b128 v[216:219], v181 offset:55296
	ds_read_b128 v[220:223], v181 offset:56320
	global_load_lds_dwordx4 v130, s[98:99]
	s_add_i32 m0, s38, 0x2000
	s_add_u32 s12, s12, 0x40080
	s_addc_u32 s13, s13, 0
	s_add_i32 s38, s73, s45
	global_load_lds_dwordx4 v134, s[98:99]
	s_mov_b32 m0, s38
	s_nop 0
	global_load_lds_dwordx4 v130, s[12:13]
	s_add_i32 m0, s38, 0x2000
	s_nop 0
	global_load_lds_dwordx4 v134, s[12:13]
	s_mov_b32 m0, s65
	s_nop 0
	global_load_lds_dwordx4 v128, s[100:101]
	s_mov_b32 m0, s66
	s_nop 0
	global_load_lds_dwordx4 v132, s[100:101]
	s_waitcnt vmcnt(8) lgkmcnt(0)
	s_barrier
	s_setprio 1
	v_mfma_f32_16x16x32_bf16 v[60:63], v[146:149], v[192:195], v[60:63]
	v_mfma_f32_16x16x32_bf16 v[56:59], v[154:157], v[192:195], v[56:59]
	v_mfma_f32_16x16x32_bf16 v[44:47], v[146:149], v[200:203], v[44:47]
	v_mfma_f32_16x16x32_bf16 v[40:43], v[154:157], v[200:203], v[40:43]
	v_mfma_f32_16x16x32_bf16 v[28:31], v[146:149], v[208:211], v[28:31]
	v_mfma_f32_16x16x32_bf16 v[24:27], v[154:157], v[208:211], v[24:27]
	v_mfma_f32_16x16x32_bf16 v[12:15], v[146:149], v[216:219], v[12:15]
	v_mfma_f32_16x16x32_bf16 v[8:11], v[154:157], v[216:219], v[8:11]
	v_mfma_f32_16x16x32_bf16 v[60:63], v[150:153], v[196:199], v[60:63]
	v_mfma_f32_16x16x32_bf16 v[56:59], v[158:161], v[196:199], v[56:59]
	v_mfma_f32_16x16x32_bf16 v[44:47], v[150:153], v[204:207], v[44:47]
	v_mfma_f32_16x16x32_bf16 v[40:43], v[158:161], v[204:207], v[40:43]
	v_mfma_f32_16x16x32_bf16 v[28:31], v[150:153], v[212:215], v[28:31]
	v_mfma_f32_16x16x32_bf16 v[24:27], v[158:161], v[212:215], v[24:27]
	v_mfma_f32_16x16x32_bf16 v[12:15], v[150:153], v[220:223], v[12:15]
	v_mfma_f32_16x16x32_bf16 v[8:11], v[158:161], v[220:223], v[8:11]
	s_setprio 0
	s_setprio 1
	v_mfma_f32_16x16x32_bf16 v[52:55], v[162:165], v[192:195], v[52:55]
	v_mfma_f32_16x16x32_bf16 v[48:51], v[184:187], v[192:195], v[48:51]
	v_mfma_f32_16x16x32_bf16 v[36:39], v[162:165], v[200:203], v[36:39]
	v_mfma_f32_16x16x32_bf16 v[32:35], v[184:187], v[200:203], v[32:35]
	v_mfma_f32_16x16x32_bf16 v[20:23], v[162:165], v[208:211], v[20:23]
	v_mfma_f32_16x16x32_bf16 v[16:19], v[184:187], v[208:211], v[16:19]
	v_mfma_f32_16x16x32_bf16 v[4:7], v[162:165], v[216:219], v[4:7]
	v_mfma_f32_16x16x32_bf16 v[0:3], v[184:187], v[216:219], v[0:3]
	v_mfma_f32_16x16x32_bf16 v[52:55], v[166:169], v[196:199], v[52:55]
	v_mfma_f32_16x16x32_bf16 v[48:51], v[188:191], v[196:199], v[48:51]
	v_mfma_f32_16x16x32_bf16 v[36:39], v[166:169], v[204:207], v[36:39]
	v_mfma_f32_16x16x32_bf16 v[32:35], v[188:191], v[204:207], v[32:35]
	v_mfma_f32_16x16x32_bf16 v[20:23], v[166:169], v[212:215], v[20:23]
	v_mfma_f32_16x16x32_bf16 v[16:19], v[188:191], v[212:215], v[16:19]
	v_mfma_f32_16x16x32_bf16 v[4:7], v[166:169], v[220:223], v[4:7]
	v_mfma_f32_16x16x32_bf16 v[0:3], v[188:191], v[220:223], v[0:3]
	s_setprio 0
	s_barrier
	s_add_i32 s71, s71, 2
	s_add_u32 s8, s8, 0x100
	s_addc_u32 s9, s9, 0
	s_add_u32 s40, s40, 0x100
	s_addc_u32 s41, s41, 0
	s_cmp_gt_u32 s71, 13
	s_cbranch_scc0 .LBB0_2049
	s_and_b64 vcc, exec, s[20:21]
	s_cbranch_vccz .LBB0_2052
	s_barrier

; #define PG8_STAGE(bufoff, gbase, voff) do { _Pragma("unroll") for (int _i = 0; _i < 2; ++_i) \
;         __builtin_amdgcn_global_load_lds((const unsigned*)((const char*)(gbase) + (voff)[_i]), (PG8_LAS unsigned*)(lds + (bufoff) + ldsw + _i * 8192), 16, 0, 0); } while (0)
; #define PG8_LDA(dst, b, h) do { _Pragma("unroll") for (int m = 0; m < 4; ++m) _Pragma("unroll") for (int k = 0; k < 2; ++k) dst[m][k] = *(const PG8_LAS bf16x8*)(lds + PG8_SA(b, h) + aoff + m * 2048 + k * 1024); } while (0)
; #define PG8_LDB(dst, b, h) do { _Pragma("unroll") for (int n = 0; n < 2; ++n) _Pragma("unroll") for (int k = 0; k < 2; ++k) dst[n][k] = *(const PG8_LAS bf16x8*)(lds + PG8_SB(b, h) + boff + n * 2048 + k * 1024); } while (0)
; #define PG8_MMA(ai, bj, At, Bt) do { __builtin_amdgcn_s_setprio(1); _Pragma("unroll") for (int m = 0; m < 4; ++m) _Pragma("unroll") for (int n = 0; n < 2; ++n) _Pragma("unroll") for (int k = 0; k < 2; ++k) \
;         acc[ai][bj][m][n] = __builtin_amdgcn_mfma_f32_16x16x32_bf16(Bt[n][k], At[m][k], acc[ai][bj][m][n], 0, 0, 0); __builtin_amdgcn_s_setprio(0); } while (0)
; template <class Epi, class Sched, bool ALIGN_EPI = false, bool SP2 = false>
; __device__ __forceinline__ void gemm_phase(PG8_LAS unsigned char* lds, const Gemm g, const Sched& S, const Epi& E, const int wid) {
;     ...
;         const bool has_next = S.next(ui + 1, nxt);
;         const char* nA = has_next ? (const char*)g.A + (size_t)nxt.pm * tstepA : cA; const char* nB = has_next ? (const char*)g.Bt + (size_t)nxt.pn * tstepB : cB;
;         for (int t = 0; t < nt; t += 2) {
;             const bool last = (t == nt - 2);
;             const char* a1 = cA + (size_t)(t + 1) * kstep;
;             const char* a2 = last ? nA : cA + (size_t)(t + 2) * kstep; const char* b2 = last ? nB : cB + (size_t)(t + 2) * kstep;
;             const char* a3 = a2 + kstep; const char* b3 = b2 + kstep;
;             if (last && has_next) S.a_ready(nxt);
;             if constexpr (SP2) {
;             PG8_LDB(B0, 0, 0); PG8_LDB(B1, 0, 1); PG8_SCHED; PG8_LDA(At, 0, 0); PG8_STAGE(PG8_SA(1, 1), a1 + hstepA, voffA);
;             PG8_WAIT_V(8); PG8_WAIT_L(0); PG8_BAR; PG8_MMA(0, 0, At, B0); PG8_MMA(0, 1, At, B1); PG8_BAR; PG8_SCHED;
;             PG8_LDA(At, 0, 1); PG8_STAGE(PG8_SB(0, 0), b2, voffB); PG8_STAGE(PG8_SB(0, 1), b2 + hstepB, voffB); PG8_STAGE(PG8_SA(0, 0), a2, voffA);
.LBB0_2279:
	s_ashr_i32 s19, s18, 31
	s_lshl_b64 s[20:21], s[18:19], 20
	s_add_u32 s20, s65, s20
	s_addc_u32 s21, s66, s21
	s_and_b64 s[22:23], s[2:3], exec
	s_cselect_b32 s19, s21, s29
	s_cselect_b32 s81, s20, s28
	s_ashr_i32 s17, s16, 31
	s_lshl_b64 s[22:23], s[16:17], 17
	s_add_u32 s22, s67, s22
	s_addc_u32 s23, s68, s23
	s_and_b64 s[30:31], s[2:3], exec
	s_cselect_b32 s17, s23, s27
	s_cselect_b32 s82, s22, s26
	s_mov_b32 s36, 0
	s_mov_b64 s[30:31], -1
	s_mov_b64 s[34:35], 0
	v_add_u32_e32 v252, 0x18000, v156
	v_add_u32_e32 v253, 0x1c000, v156
	s_add_u32 s37, s28, s36
	s_addc_u32 s44, s29, 0
	s_add_u32 s40, s37, 0x100
	s_addc_u32 s41, s44, 0
	s_and_b64 s[38:39], s[34:35], exec
	s_cselect_b32 s39, s19, s41
	s_cselect_b32 s38, s81, s40
	s_add_u32 s36, s26, s36
	s_addc_u32 s40, s27, 0
	s_add_u32 s36, s36, 0x100
	s_addc_u32 s40, s40, 0
	s_and_b64 s[34:35], s[34:35], exec
	s_cselect_b32 s41, s17, s40
	s_cselect_b32 s40, s82, s36
	s_add_u32 s46, s37, 0x80080
	ds_read_b128 v[142:145], v157
	ds_read_b128 v[146:149], v157 offset:1024
	ds_read_b128 v[150:153], v157 offset:2048
	ds_read_b128 v[162:165], v157 offset:3072
	ds_read_b128 v[166:169], v158
	ds_read_b128 v[170:173], v158 offset:1024
	ds_read_b128 v[174:177], v158 offset:2048
	ds_read_b128 v[178:181], v158 offset:3072
	s_addc_u32 s47, s44, 0
	s_add_i32 s93, s77, s0
	s_add_i32 m0, s70, 0xc000
	s_add_i32 s94, s70, 0xe000
	s_add_i32 s89, s93, 0x2000
	s_add_u32 s44, s40, 0x10000
	s_addc_u32 s45, s41, 0
	s_add_i32 s92, s78, s0
	s_add_i32 s91, s92, 0x2000
	s_add_i32 s88, 0, 0x18000
	s_add_i32 s87, 0, 0x1c000
	s_add_u32 s36, s38, 0x80000
	s_addc_u32 s37, s39, 0
	s_add_i32 s86, s88, s0
	s_add_i32 s84, s86, 0x2000
	s_add_u32 s34, s40, 0x10080
	s_addc_u32 s35, s41, 0
	s_add_i32 s85, s87, s0
	s_add_i32 s83, s85, 0x2000
	ds_read_b128 v[182:185], v159
	ds_read_b128 v[186:189], v159 offset:1024
	ds_read_b128 v[190:193], v159 offset:2048
	ds_read_b128 v[194:197], v159 offset:3072
	ds_read_b128 v[198:201], v159 offset:4096
	ds_read_b128 v[202:205], v159 offset:5120
	ds_read_b128 v[206:209], v159 offset:6144
	ds_read_b128 v[210:213], v159 offset:7168
	global_load_lds_dwordx4 v134, s[46:47]
	s_mov_b32 m0, s94
	s_nop 0
	global_load_lds_dwordx4 v130, s[46:47]
	s_waitcnt vmcnt(8) lgkmcnt(0)
	s_barrier
	s_setprio 1
	v_mfma_f32_16x16x32_bf16 v[124:127], v[142:145], v[182:185], 0
	v_mfma_f32_16x16x32_bf16 v[120:123], v[150:153], v[182:185], 0
	v_mfma_f32_16x16x32_bf16 v[116:119], v[142:145], v[190:193], 0
	v_mfma_f32_16x16x32_bf16 v[112:115], v[150:153], v[190:193], 0
	v_mfma_f32_16x16x32_bf16 v[100:103], v[142:145], v[198:201], 0
	v_mfma_f32_16x16x32_bf16 v[96:99], v[150:153], v[198:201], 0
	v_mfma_f32_16x16x32_bf16 v[84:87], v[142:145], v[206:209], 0
	v_mfma_f32_16x16x32_bf16 v[80:83], v[150:153], v[206:209], 0
	v_mfma_f32_16x16x32_bf16 v[124:127], v[146:149], v[186:189], v[124:127]
	v_mfma_f32_16x16x32_bf16 v[120:123], v[162:165], v[186:189], v[120:123]
	v_mfma_f32_16x16x32_bf16 v[116:119], v[146:149], v[194:197], v[116:119]
	v_mfma_f32_16x16x32_bf16 v[112:115], v[162:165], v[194:197], v[112:115]
	v_mfma_f32_16x16x32_bf16 v[100:103], v[146:149], v[202:205], v[100:103]
	v_mfma_f32_16x16x32_bf16 v[96:99], v[162:165], v[202:205], v[96:99]
	v_mfma_f32_16x16x32_bf16 v[84:87], v[146:149], v[210:213], v[84:87]
	v_mfma_f32_16x16x32_bf16 v[80:83], v[162:165], v[210:213], v[80:83]
	s_setprio 0
	s_setprio 1
	v_mfma_f32_16x16x32_bf16 v[108:111], v[166:169], v[182:185], 0
	v_mfma_f32_16x16x32_bf16 v[104:107], v[174:177], v[182:185], 0
	v_mfma_f32_16x16x32_bf16 v[92:95], v[166:169], v[190:193], 0
	v_mfma_f32_16x16x32_bf16 v[88:91], v[174:177], v[190:193], 0
	v_mfma_f32_16x16x32_bf16 v[76:79], v[166:169], v[198:201], 0
	v_mfma_f32_16x16x32_bf16 v[72:75], v[174:177], v[198:201], 0
	v_mfma_f32_16x16x32_bf16 v[68:71], v[166:169], v[206:209], 0
	v_mfma_f32_16x16x32_bf16 v[64:67], v[174:177], v[206:209], 0
	v_mfma_f32_16x16x32_bf16 v[108:111], v[170:173], v[186:189], v[108:111]
	v_mfma_f32_16x16x32_bf16 v[104:107], v[178:181], v[186:189], v[104:107]
	v_mfma_f32_16x16x32_bf16 v[92:95], v[170:173], v[194:197], v[92:95]
	v_mfma_f32_16x16x32_bf16 v[88:91], v[178:181], v[194:197], v[88:91]
	v_mfma_f32_16x16x32_bf16 v[76:79], v[170:173], v[202:205], v[76:79]
	v_mfma_f32_16x16x32_bf16 v[72:75], v[178:181], v[202:205], v[72:75]
	v_mfma_f32_16x16x32_bf16 v[68:71], v[170:173], v[210:213], v[68:71]
	v_mfma_f32_16x16x32_bf16 v[64:67], v[178:181], v[210:213], v[64:67]
	s_setprio 0
	s_barrier
	s_mov_b32 m0, s93
	s_add_u32 s98, s40, 0x80
	s_addc_u32 s99, s41, 0
	ds_read_b128 v[182:185], v159 offset:16384
	ds_read_b128 v[186:189], v159 offset:17408
	ds_read_b128 v[190:193], v159 offset:18432
	ds_read_b128 v[194:197], v159 offset:19456
	ds_read_b128 v[198:201], v159 offset:20480
	ds_read_b128 v[202:205], v159 offset:21504
	ds_read_b128 v[206:209], v159 offset:22528
	ds_read_b128 v[210:213], v159 offset:23552
	global_load_lds_dwordx4 v132, s[40:41]
	s_mov_b32 m0, s89
	s_nop 0
	global_load_lds_dwordx4 v128, s[40:41]
	s_mov_b32 m0, s92
	s_add_u32 s100, s38, 0x80
	s_addc_u32 s101, s39, 0
	global_load_lds_dwordx4 v132, s[44:45]
	s_mov_b32 m0, s91
	s_nop 0
	global_load_lds_dwordx4 v128, s[44:45]
	s_mov_b32 m0, s70
	s_nop 0
	global_load_lds_dwordx4 v134, s[38:39]
	s_mov_b32 m0, s71
	s_nop 0
	global_load_lds_dwordx4 v130, s[38:39]
	s_waitcnt vmcnt(8) lgkmcnt(0)
	s_barrier
; #define PG8_STAGE(bufoff, gbase, voff) do { _Pragma("unroll") for (int _i = 0; _i < 2; ++_i) \
;         __builtin_amdgcn_global_load_lds((const unsigned*)((const char*)(gbase) + (voff)[_i]), (PG8_LAS unsigned*)(lds + (bufoff) + ldsw + _i * 8192), 16, 0, 0); } while (0)
; #define PG8_LDA(dst, b, h) do { _Pragma("unroll") for (int m = 0; m < 4; ++m) _Pragma("unroll") for (int k = 0; k < 2; ++k) dst[m][k] = *(const PG8_LAS bf16x8*)(lds + PG8_SA(b, h) + aoff + m * 2048 + k * 1024); } while (0)
; #define PG8_LDB(dst, b, h) do { _Pragma("unroll") for (int n = 0; n < 2; ++n) _Pragma("unroll") for (int k = 0; k < 2; ++k) dst[n][k] = *(const PG8_LAS bf16x8*)(lds + PG8_SB(b, h) + boff + n * 2048 + k * 1024); } while (0)
; #define PG8_MMA(ai, bj, At, Bt) do { __builtin_amdgcn_s_setprio(1); _Pragma("unroll") for (int m = 0; m < 4; ++m) _Pragma("unroll") for (int n = 0; n < 2; ++n) _Pragma("unroll") for (int k = 0; k < 2; ++k) \
;         acc[ai][bj][m][n] = __builtin_amdgcn_mfma_f32_16x16x32_bf16(Bt[n][k], At[m][k], acc[ai][bj][m][n], 0, 0, 0); __builtin_amdgcn_s_setprio(0); } while (0)
; #define PG8_WAIT_V(n) asm volatile("s_waitcnt vmcnt(" #n ")" ::: "memory")
; #define PG8_WAIT_L(n) asm volatile("s_waitcnt lgkmcnt(" #n ")" ::: "memory")
; #define PG8_BAR __builtin_amdgcn_s_barrier()
; #define PG8_SCHED __builtin_amdgcn_sched_barrier(0)
; template <class Epi, class Sched, bool ALIGN_EPI = false, bool SP2 = false>
; __device__ __forceinline__ void gemm_phase(PG8_LAS unsigned char* lds, const Gemm g, const Sched& S, const Epi& E, const int wid) {
;     ...
;             PG8_WAIT_V(8); PG8_WAIT_L(0); PG8_BAR; PG8_MMA(1, 0, At, B0); PG8_MMA(1, 1, At, B1); PG8_BAR; PG8_SCHED;
;             PG8_LDB(B0, 1, 0); PG8_LDB(B1, 1, 1); PG8_SCHED; PG8_LDA(At, 1, 0); PG8_STAGE(PG8_SA(0, 1), a2 + hstepA, voffA);
;             PG8_WAIT_V(8); PG8_WAIT_L(0); PG8_BAR; PG8_MMA(0, 0, At, B0); PG8_MMA(0, 1, At, B1); PG8_BAR; PG8_SCHED;
	s_setprio 1
	v_mfma_f32_16x16x32_bf16 v[60:63], v[142:145], v[182:185], 0
	v_mfma_f32_16x16x32_bf16 v[56:59], v[150:153], v[182:185], 0
	v_mfma_f32_16x16x32_bf16 v[52:55], v[142:145], v[190:193], 0
	v_mfma_f32_16x16x32_bf16 v[48:51], v[150:153], v[190:193], 0
	v_mfma_f32_16x16x32_bf16 v[36:39], v[142:145], v[198:201], 0
	v_mfma_f32_16x16x32_bf16 v[32:35], v[150:153], v[198:201], 0
	v_mfma_f32_16x16x32_bf16 v[20:23], v[142:145], v[206:209], 0
	v_mfma_f32_16x16x32_bf16 v[16:19], v[150:153], v[206:209], 0
	v_mfma_f32_16x16x32_bf16 v[60:63], v[146:149], v[186:189], v[60:63]
	v_mfma_f32_16x16x32_bf16 v[56:59], v[162:165], v[186:189], v[56:59]
	v_mfma_f32_16x16x32_bf16 v[52:55], v[146:149], v[194:197], v[52:55]
	v_mfma_f32_16x16x32_bf16 v[48:51], v[162:165], v[194:197], v[48:51]
	v_mfma_f32_16x16x32_bf16 v[36:39], v[146:149], v[202:205], v[36:39]
	v_mfma_f32_16x16x32_bf16 v[32:35], v[162:165], v[202:205], v[32:35]
	v_mfma_f32_16x16x32_bf16 v[20:23], v[146:149], v[210:213], v[20:23]
	v_mfma_f32_16x16x32_bf16 v[16:19], v[162:165], v[210:213], v[16:19]
	s_setprio 0
	s_setprio 1
	v_mfma_f32_16x16x32_bf16 v[44:47], v[166:169], v[182:185], 0
	v_mfma_f32_16x16x32_bf16 v[40:43], v[174:177], v[182:185], 0
	v_mfma_f32_16x16x32_bf16 v[28:31], v[166:169], v[190:193], 0
	v_mfma_f32_16x16x32_bf16 v[24:27], v[174:177], v[190:193], 0
	v_mfma_f32_16x16x32_bf16 v[12:15], v[166:169], v[198:201], 0
	v_mfma_f32_16x16x32_bf16 v[8:11], v[174:177], v[198:201], 0
	v_mfma_f32_16x16x32_bf16 v[4:7], v[166:169], v[206:209], 0
	v_mfma_f32_16x16x32_bf16 v[0:3], v[174:177], v[206:209], 0
	v_mfma_f32_16x16x32_bf16 v[44:47], v[170:173], v[186:189], v[44:47]
	v_mfma_f32_16x16x32_bf16 v[40:43], v[178:181], v[186:189], v[40:43]
	v_mfma_f32_16x16x32_bf16 v[28:31], v[170:173], v[194:197], v[28:31]
	v_mfma_f32_16x16x32_bf16 v[24:27], v[178:181], v[194:197], v[24:27]
	v_mfma_f32_16x16x32_bf16 v[12:15], v[170:173], v[202:205], v[12:15]
	v_mfma_f32_16x16x32_bf16 v[8:11], v[178:181], v[202:205], v[8:11]
	v_mfma_f32_16x16x32_bf16 v[4:7], v[170:173], v[210:213], v[4:7]
	v_mfma_f32_16x16x32_bf16 v[0:3], v[178:181], v[210:213], v[0:3]
	s_setprio 0
	s_barrier
	ds_read_b128 v[142:145], v252
	ds_read_b128 v[146:149], v252 offset:1024
	ds_read_b128 v[150:153], v252 offset:2048
	ds_read_b128 v[162:165], v252 offset:3072
	ds_read_b128 v[166:169], v253
	ds_read_b128 v[170:173], v253 offset:1024
	ds_read_b128 v[174:177], v253 offset:2048
	ds_read_b128 v[178:181], v253 offset:3072
	s_mov_b32 m0, s72
	ds_read_b128 v[182:185], v159 offset:32768
	ds_read_b128 v[186:189], v159 offset:33792
	ds_read_b128 v[190:193], v159 offset:34816
	ds_read_b128 v[194:197], v159 offset:35840
	ds_read_b128 v[198:201], v159 offset:36864
	ds_read_b128 v[202:205], v159 offset:37888
	ds_read_b128 v[206:209], v159 offset:38912
	ds_read_b128 v[210:213], v159 offset:39936
	global_load_lds_dwordx4 v134, s[36:37]
	s_mov_b32 m0, s73
	s_nop 0
	global_load_lds_dwordx4 v130, s[36:37]
	s_waitcnt vmcnt(8) lgkmcnt(0)
	s_barrier
	s_setprio 1
	v_mfma_f32_16x16x32_bf16 v[124:127], v[142:145], v[182:185], v[124:127]
	v_mfma_f32_16x16x32_bf16 v[120:123], v[150:153], v[182:185], v[120:123]
	v_mfma_f32_16x16x32_bf16 v[116:119], v[142:145], v[190:193], v[116:119]
	v_mfma_f32_16x16x32_bf16 v[112:115], v[150:153], v[190:193], v[112:115]
	v_mfma_f32_16x16x32_bf16 v[100:103], v[142:145], v[198:201], v[100:103]
	v_mfma_f32_16x16x32_bf16 v[96:99], v[150:153], v[198:201], v[96:99]
	v_mfma_f32_16x16x32_bf16 v[84:87], v[142:145], v[206:209], v[84:87]
	v_mfma_f32_16x16x32_bf16 v[80:83], v[150:153], v[206:209], v[80:83]
	v_mfma_f32_16x16x32_bf16 v[124:127], v[146:149], v[186:189], v[124:127]
	v_mfma_f32_16x16x32_bf16 v[120:123], v[162:165], v[186:189], v[120:123]
	v_mfma_f32_16x16x32_bf16 v[116:119], v[146:149], v[194:197], v[116:119]
	v_mfma_f32_16x16x32_bf16 v[112:115], v[162:165], v[194:197], v[112:115]
	v_mfma_f32_16x16x32_bf16 v[100:103], v[146:149], v[202:205], v[100:103]
	v_mfma_f32_16x16x32_bf16 v[96:99], v[162:165], v[202:205], v[96:99]
	v_mfma_f32_16x16x32_bf16 v[84:87], v[146:149], v[210:213], v[84:87]
	v_mfma_f32_16x16x32_bf16 v[80:83], v[162:165], v[210:213], v[80:83]
	s_setprio 0
	s_setprio 1
	v_mfma_f32_16x16x32_bf16 v[108:111], v[166:169], v[182:185], v[108:111]
	v_mfma_f32_16x16x32_bf16 v[104:107], v[174:177], v[182:185], v[104:107]
	v_mfma_f32_16x16x32_bf16 v[92:95], v[166:169], v[190:193], v[92:95]
	v_mfma_f32_16x16x32_bf16 v[88:91], v[174:177], v[190:193], v[88:91]
	v_mfma_f32_16x16x32_bf16 v[76:79], v[166:169], v[198:201], v[76:79]
	v_mfma_f32_16x16x32_bf16 v[72:75], v[174:177], v[198:201], v[72:75]
	v_mfma_f32_16x16x32_bf16 v[68:71], v[166:169], v[206:209], v[68:71]
	v_mfma_f32_16x16x32_bf16 v[64:67], v[174:177], v[206:209], v[64:67]
	v_mfma_f32_16x16x32_bf16 v[108:111], v[170:173], v[186:189], v[108:111]
	v_mfma_f32_16x16x32_bf16 v[104:107], v[178:181], v[186:189], v[104:107]
	v_mfma_f32_16x16x32_bf16 v[92:95], v[170:173], v[194:197], v[92:95]
	v_mfma_f32_16x16x32_bf16 v[88:91], v[178:181], v[194:197], v[88:91]
	v_mfma_f32_16x16x32_bf16 v[76:79], v[170:173], v[202:205], v[76:79]
	v_mfma_f32_16x16x32_bf16 v[72:75], v[178:181], v[202:205], v[72:75]
	v_mfma_f32_16x16x32_bf16 v[68:71], v[170:173], v[210:213], v[68:71]
	v_mfma_f32_16x16x32_bf16 v[64:67], v[178:181], v[210:213], v[64:67]
	s_setprio 0
	s_barrier
; #define PG8_STAGE(bufoff, gbase, voff) do { _Pragma("unroll") for (int _i = 0; _i < 2; ++_i) \
;         __builtin_amdgcn_global_load_lds((const unsigned*)((const char*)(gbase) + (voff)[_i]), (PG8_LAS unsigned*)(lds + (bufoff) + ldsw + _i * 8192), 16, 0, 0); } while (0)
; #define PG8_LDA(dst, b, h) do { _Pragma("unroll") for (int m = 0; m < 4; ++m) _Pragma("unroll") for (int k = 0; k < 2; ++k) dst[m][k] = *(const PG8_LAS bf16x8*)(lds + PG8_SA(b, h) + aoff + m * 2048 + k * 1024); } while (0)
; #define PG8_WAIT_V(n) asm volatile("s_waitcnt vmcnt(" #n ")" ::: "memory")
; #define PG8_WAIT_L(n) asm volatile("s_waitcnt lgkmcnt(" #n ")" ::: "memory")
; #define PG8_BAR __builtin_amdgcn_s_barrier()
; template <class Epi, class Sched, bool ALIGN_EPI = false, bool SP2 = false>
; __device__ __forceinline__ void gemm_phase(PG8_LAS unsigned char* lds, const Gemm g, const Sched& S, const Epi& E, const int wid) {
;     ...
;         for (int t = 0; t < nt; t += 2) {
;             const bool last = (t == nt - 2);
;             const char* a1 = cA + (size_t)(t + 1) * kstep;
;             const char* a2 = last ? nA : cA + (size_t)(t + 2) * kstep; const char* b2 = last ? nB : cB + (size_t)(t + 2) * kstep;
;             const char* a3 = a2 + kstep; const char* b3 = b2 + kstep;
;             if (last && has_next) S.a_ready(nxt);
;             if constexpr (SP2) {
;             PG8_LDB(B0, 0, 0); PG8_LDB(B1, 0, 1); PG8_SCHED; PG8_LDA(At, 0, 0); PG8_STAGE(PG8_SA(1, 1), a1 + hstepA, voffA);
;             PG8_WAIT_V(8); PG8_WAIT_L(0); PG8_BAR; PG8_MMA(0, 0, At, B0); PG8_MMA(0, 1, At, B1); PG8_BAR; PG8_SCHED;
;             PG8_LDA(At, 0, 1); PG8_STAGE(PG8_SB(0, 0), b2, voffB); PG8_STAGE(PG8_SB(0, 1), b2 + hstepB, voffB); PG8_STAGE(PG8_SA(0, 0), a2, voffA);
;             PG8_WAIT_V(8); PG8_WAIT_L(0); PG8_BAR; PG8_MMA(1, 0, At, B0); PG8_MMA(1, 1, At, B1); PG8_BAR; PG8_SCHED;
;             PG8_LDB(B0, 1, 0); PG8_LDB(B1, 1, 1); PG8_SCHED; PG8_LDA(At, 1, 0); PG8_STAGE(PG8_SA(0, 1), a2 + hstepA, voffA);
;             PG8_WAIT_V(8); PG8_WAIT_L(0); PG8_BAR; PG8_MMA(0, 0, At, B0); PG8_MMA(0, 1, At, B1); PG8_BAR; PG8_SCHED;
;             PG8_LDA(At, 1, 1); PG8_STAGE(PG8_SB(1, 0), b3, voffB); PG8_STAGE(PG8_SB(1, 1), b3 + hstepB, voffB); PG8_STAGE(PG8_SA(1, 0), a3, voffA);
;             PG8_WAIT_V(8); PG8_WAIT_L(0); PG8_BAR; PG8_MMA(1, 0, At, B0); PG8_MMA(1, 1, At, B1); PG8_BAR; PG8_SCHED;
	s_mov_b32 m0, s86
	ds_read_b128 v[182:185], v159 offset:49152
	ds_read_b128 v[186:189], v159 offset:50176
	ds_read_b128 v[190:193], v159 offset:51200
	ds_read_b128 v[194:197], v159 offset:52224
	ds_read_b128 v[198:201], v159 offset:53248
	ds_read_b128 v[202:205], v159 offset:54272
	ds_read_b128 v[206:209], v159 offset:55296
	ds_read_b128 v[210:213], v159 offset:56320
	global_load_lds_dwordx4 v132, s[98:99]
	s_mov_b32 m0, s84
	s_nop 0
	global_load_lds_dwordx4 v128, s[98:99]
	s_mov_b32 m0, s85
	s_nop 0
	global_load_lds_dwordx4 v132, s[34:35]
	s_mov_b32 m0, s83
	s_nop 0
	global_load_lds_dwordx4 v128, s[34:35]
	s_mov_b32 m0, s74
	s_nop 0
	global_load_lds_dwordx4 v134, s[100:101]
	s_mov_b32 m0, s75
	s_nop 0
	global_load_lds_dwordx4 v130, s[100:101]
	s_waitcnt vmcnt(8) lgkmcnt(0)
	s_barrier
	s_setprio 1
	v_mfma_f32_16x16x32_bf16 v[60:63], v[142:145], v[182:185], v[60:63]
	v_mfma_f32_16x16x32_bf16 v[56:59], v[150:153], v[182:185], v[56:59]
	v_mfma_f32_16x16x32_bf16 v[52:55], v[142:145], v[190:193], v[52:55]
	v_mfma_f32_16x16x32_bf16 v[48:51], v[150:153], v[190:193], v[48:51]
	v_mfma_f32_16x16x32_bf16 v[36:39], v[142:145], v[198:201], v[36:39]
	v_mfma_f32_16x16x32_bf16 v[32:35], v[150:153], v[198:201], v[32:35]
	v_mfma_f32_16x16x32_bf16 v[20:23], v[142:145], v[206:209], v[20:23]
	v_mfma_f32_16x16x32_bf16 v[16:19], v[150:153], v[206:209], v[16:19]
	v_mfma_f32_16x16x32_bf16 v[60:63], v[146:149], v[186:189], v[60:63]
	v_mfma_f32_16x16x32_bf16 v[56:59], v[162:165], v[186:189], v[56:59]
	v_mfma_f32_16x16x32_bf16 v[52:55], v[146:149], v[194:197], v[52:55]
	v_mfma_f32_16x16x32_bf16 v[48:51], v[162:165], v[194:197], v[48:51]
	v_mfma_f32_16x16x32_bf16 v[36:39], v[146:149], v[202:205], v[36:39]
	v_mfma_f32_16x16x32_bf16 v[32:35], v[162:165], v[202:205], v[32:35]
	v_mfma_f32_16x16x32_bf16 v[20:23], v[146:149], v[210:213], v[20:23]
	v_mfma_f32_16x16x32_bf16 v[16:19], v[162:165], v[210:213], v[16:19]
	s_setprio 0
	s_setprio 1
	v_mfma_f32_16x16x32_bf16 v[44:47], v[166:169], v[182:185], v[44:47]
	v_mfma_f32_16x16x32_bf16 v[40:43], v[174:177], v[182:185], v[40:43]
	v_mfma_f32_16x16x32_bf16 v[28:31], v[166:169], v[190:193], v[28:31]
	v_mfma_f32_16x16x32_bf16 v[24:27], v[174:177], v[190:193], v[24:27]
	v_mfma_f32_16x16x32_bf16 v[12:15], v[166:169], v[198:201], v[12:15]
	v_mfma_f32_16x16x32_bf16 v[8:11], v[174:177], v[198:201], v[8:11]
	v_mfma_f32_16x16x32_bf16 v[4:7], v[166:169], v[206:209], v[4:7]
	v_mfma_f32_16x16x32_bf16 v[0:3], v[174:177], v[206:209], v[0:3]
	v_mfma_f32_16x16x32_bf16 v[44:47], v[170:173], v[186:189], v[44:47]
	v_mfma_f32_16x16x32_bf16 v[40:43], v[178:181], v[186:189], v[40:43]
	v_mfma_f32_16x16x32_bf16 v[28:31], v[170:173], v[194:197], v[28:31]
	v_mfma_f32_16x16x32_bf16 v[24:27], v[178:181], v[194:197], v[24:27]
	v_mfma_f32_16x16x32_bf16 v[12:15], v[170:173], v[202:205], v[12:15]
	v_mfma_f32_16x16x32_bf16 v[8:11], v[178:181], v[202:205], v[8:11]
	v_mfma_f32_16x16x32_bf16 v[4:7], v[170:173], v[210:213], v[4:7]
	v_mfma_f32_16x16x32_bf16 v[0:3], v[178:181], v[210:213], v[0:3]
	s_setprio 0
	s_barrier
	s_movk_i32 s36, 0x100
	s_andn2_b64 vcc, exec, s[30:31]
	s_mov_b64 s[34:35], -1
	s_mov_b64 s[30:31], 0
.LBB0_2280:
	s_add_u32 s37, s28, s36
	s_addc_u32 s44, s29, 0
	s_add_u32 s40, s37, 0x100
	s_addc_u32 s41, s44, 0
	s_and_b64 s[38:39], s[34:35], exec
	s_cselect_b32 s39, s19, s41
	s_cselect_b32 s38, s81, s40
	s_add_u32 s36, s26, s36
	s_addc_u32 s40, s27, 0
	s_add_u32 s36, s36, 0x100
	s_addc_u32 s40, s40, 0
	s_and_b64 s[34:35], s[34:35], exec
	s_cselect_b32 s41, s17, s40
	s_cselect_b32 s40, s82, s36
	s_add_u32 s46, s37, 0x80080
	ds_read_b128 v[142:145], v157
	ds_read_b128 v[146:149], v157 offset:1024
	ds_read_b128 v[150:153], v157 offset:2048
	ds_read_b128 v[162:165], v157 offset:3072
	ds_read_b128 v[166:169], v158
	ds_read_b128 v[170:173], v158 offset:1024
	ds_read_b128 v[174:177], v158 offset:2048
	ds_read_b128 v[178:181], v158 offset:3072
	s_addc_u32 s47, s44, 0
	s_add_i32 s93, s77, s0
	s_add_i32 m0, s70, 0xc000
	s_add_i32 s94, s70, 0xe000
	s_add_i32 s89, s93, 0x2000
	s_add_u32 s44, s40, 0x10000
	s_addc_u32 s45, s41, 0
	s_add_i32 s92, s78, s0
	s_add_i32 s91, s92, 0x2000
	s_add_i32 s88, 0, 0x18000
	s_add_i32 s87, 0, 0x1c000
	s_add_u32 s36, s38, 0x80000
	s_addc_u32 s37, s39, 0
	s_add_i32 s86, s88, s0
	s_add_i32 s84, s86, 0x2000
	s_add_u32 s34, s40, 0x10080
	s_addc_u32 s35, s41, 0
	s_add_i32 s85, s87, s0
	s_add_i32 s83, s85, 0x2000
	ds_read_b128 v[182:185], v159
	ds_read_b128 v[186:189], v159 offset:1024
	ds_read_b128 v[190:193], v159 offset:2048
	ds_read_b128 v[194:197], v159 offset:3072
	ds_read_b128 v[198:201], v159 offset:4096
	ds_read_b128 v[202:205], v159 offset:5120
	ds_read_b128 v[206:209], v159 offset:6144
	ds_read_b128 v[210:213], v159 offset:7168
	global_load_lds_dwordx4 v134, s[46:47]
	s_mov_b32 m0, s94
	s_nop 0
	global_load_lds_dwordx4 v130, s[46:47]
	s_waitcnt vmcnt(8) lgkmcnt(0)
	s_barrier
; #define PG8_STAGE(bufoff, gbase, voff) do { _Pragma("unroll") for (int _i = 0; _i < 2; ++_i) \
;         __builtin_amdgcn_global_load_lds((const unsigned*)((const char*)(gbase) + (voff)[_i]), (PG8_LAS unsigned*)(lds + (bufoff) + ldsw + _i * 8192), 16, 0, 0); } while (0)
; #define PG8_LDA(dst, b, h) do { _Pragma("unroll") for (int m = 0; m < 4; ++m) _Pragma("unroll") for (int k = 0; k < 2; ++k) dst[m][k] = *(const PG8_LAS bf16x8*)(lds + PG8_SA(b, h) + aoff + m * 2048 + k * 1024); } while (0)
; #define PG8_MMA(ai, bj, At, Bt) do { __builtin_amdgcn_s_setprio(1); _Pragma("unroll") for (int m = 0; m < 4; ++m) _Pragma("unroll") for (int n = 0; n < 2; ++n) _Pragma("unroll") for (int k = 0; k < 2; ++k) \
;         acc[ai][bj][m][n] = __builtin_amdgcn_mfma_f32_16x16x32_bf16(Bt[n][k], At[m][k], acc[ai][bj][m][n], 0, 0, 0); __builtin_amdgcn_s_setprio(0); } while (0)
; #define PG8_WAIT_V(n) asm volatile("s_waitcnt vmcnt(" #n ")" ::: "memory")
; #define PG8_WAIT_L(n) asm volatile("s_waitcnt lgkmcnt(" #n ")" ::: "memory")
; #define PG8_BAR __builtin_amdgcn_s_barrier()
; #define PG8_SCHED __builtin_amdgcn_sched_barrier(0)
; template <class Epi, class Sched, bool ALIGN_EPI = false, bool SP2 = false>
; __device__ __forceinline__ void gemm_phase(PG8_LAS unsigned char* lds, const Gemm g, const Sched& S, const Epi& E, const int wid) {
;     ...
;             PG8_WAIT_V(8); PG8_WAIT_L(0); PG8_BAR; PG8_MMA(0, 0, At, B0); PG8_MMA(0, 1, At, B1); PG8_BAR; PG8_SCHED;
;             PG8_LDA(At, 0, 1); PG8_STAGE(PG8_SB(0, 0), b2, voffB); PG8_STAGE(PG8_SB(0, 1), b2 + hstepB, voffB); PG8_STAGE(PG8_SA(0, 0), a2, voffA);
;             PG8_WAIT_V(8); PG8_WAIT_L(0); PG8_BAR; PG8_MMA(1, 0, At, B0); PG8_MMA(1, 1, At, B1); PG8_BAR; PG8_SCHED;
	s_setprio 1
	v_mfma_f32_16x16x32_bf16 v[124:127], v[142:145], v[182:185], v[124:127]
	v_mfma_f32_16x16x32_bf16 v[120:123], v[150:153], v[182:185], v[120:123]
	v_mfma_f32_16x16x32_bf16 v[116:119], v[142:145], v[190:193], v[116:119]
	v_mfma_f32_16x16x32_bf16 v[112:115], v[150:153], v[190:193], v[112:115]
	v_mfma_f32_16x16x32_bf16 v[100:103], v[142:145], v[198:201], v[100:103]
	v_mfma_f32_16x16x32_bf16 v[96:99], v[150:153], v[198:201], v[96:99]
	v_mfma_f32_16x16x32_bf16 v[84:87], v[142:145], v[206:209], v[84:87]
	v_mfma_f32_16x16x32_bf16 v[80:83], v[150:153], v[206:209], v[80:83]
	v_mfma_f32_16x16x32_bf16 v[124:127], v[146:149], v[186:189], v[124:127]
	v_mfma_f32_16x16x32_bf16 v[120:123], v[162:165], v[186:189], v[120:123]
	v_mfma_f32_16x16x32_bf16 v[116:119], v[146:149], v[194:197], v[116:119]
	v_mfma_f32_16x16x32_bf16 v[112:115], v[162:165], v[194:197], v[112:115]
	v_mfma_f32_16x16x32_bf16 v[100:103], v[146:149], v[202:205], v[100:103]
	v_mfma_f32_16x16x32_bf16 v[96:99], v[162:165], v[202:205], v[96:99]
	v_mfma_f32_16x16x32_bf16 v[84:87], v[146:149], v[210:213], v[84:87]
	v_mfma_f32_16x16x32_bf16 v[80:83], v[162:165], v[210:213], v[80:83]
	s_setprio 0
	s_setprio 1
	v_mfma_f32_16x16x32_bf16 v[108:111], v[166:169], v[182:185], v[108:111]
	v_mfma_f32_16x16x32_bf16 v[104:107], v[174:177], v[182:185], v[104:107]
	v_mfma_f32_16x16x32_bf16 v[92:95], v[166:169], v[190:193], v[92:95]
	v_mfma_f32_16x16x32_bf16 v[88:91], v[174:177], v[190:193], v[88:91]
	v_mfma_f32_16x16x32_bf16 v[76:79], v[166:169], v[198:201], v[76:79]
	v_mfma_f32_16x16x32_bf16 v[72:75], v[174:177], v[198:201], v[72:75]
	v_mfma_f32_16x16x32_bf16 v[68:71], v[166:169], v[206:209], v[68:71]
	v_mfma_f32_16x16x32_bf16 v[64:67], v[174:177], v[206:209], v[64:67]
	v_mfma_f32_16x16x32_bf16 v[108:111], v[170:173], v[186:189], v[108:111]
	v_mfma_f32_16x16x32_bf16 v[104:107], v[178:181], v[186:189], v[104:107]
	v_mfma_f32_16x16x32_bf16 v[92:95], v[170:173], v[194:197], v[92:95]
	v_mfma_f32_16x16x32_bf16 v[88:91], v[178:181], v[194:197], v[88:91]
	v_mfma_f32_16x16x32_bf16 v[76:79], v[170:173], v[202:205], v[76:79]
	v_mfma_f32_16x16x32_bf16 v[72:75], v[178:181], v[202:205], v[72:75]
	v_mfma_f32_16x16x32_bf16 v[68:71], v[170:173], v[210:213], v[68:71]
	v_mfma_f32_16x16x32_bf16 v[64:67], v[178:181], v[210:213], v[64:67]
	s_setprio 0
	s_barrier
	s_mov_b32 m0, s93
	s_add_u32 s98, s40, 0x80
	s_addc_u32 s99, s41, 0
	ds_read_b128 v[182:185], v159 offset:16384
	ds_read_b128 v[186:189], v159 offset:17408
	ds_read_b128 v[190:193], v159 offset:18432
	ds_read_b128 v[194:197], v159 offset:19456
	ds_read_b128 v[198:201], v159 offset:20480
	ds_read_b128 v[202:205], v159 offset:21504
	ds_read_b128 v[206:209], v159 offset:22528
	ds_read_b128 v[210:213], v159 offset:23552
	global_load_lds_dwordx4 v132, s[40:41]
	s_mov_b32 m0, s89
	s_nop 0
	global_load_lds_dwordx4 v128, s[40:41]
	s_mov_b32 m0, s92
	s_add_u32 s100, s38, 0x80
	s_addc_u32 s101, s39, 0
	global_load_lds_dwordx4 v132, s[44:45]
	s_mov_b32 m0, s91
	s_nop 0
	global_load_lds_dwordx4 v128, s[44:45]
	s_mov_b32 m0, s70
	s_nop 0
	global_load_lds_dwordx4 v134, s[38:39]
	s_mov_b32 m0, s71
	s_nop 0
	global_load_lds_dwordx4 v130, s[38:39]
	s_waitcnt vmcnt(8) lgkmcnt(0)
	s_barrier
	s_setprio 1
	v_mfma_f32_16x16x32_bf16 v[60:63], v[142:145], v[182:185], v[60:63]
	v_mfma_f32_16x16x32_bf16 v[56:59], v[150:153], v[182:185], v[56:59]
	v_mfma_f32_16x16x32_bf16 v[52:55], v[142:145], v[190:193], v[52:55]
	v_mfma_f32_16x16x32_bf16 v[48:51], v[150:153], v[190:193], v[48:51]
	v_mfma_f32_16x16x32_bf16 v[36:39], v[142:145], v[198:201], v[36:39]
	v_mfma_f32_16x16x32_bf16 v[32:35], v[150:153], v[198:201], v[32:35]
	v_mfma_f32_16x16x32_bf16 v[20:23], v[142:145], v[206:209], v[20:23]
	v_mfma_f32_16x16x32_bf16 v[16:19], v[150:153], v[206:209], v[16:19]
	v_mfma_f32_16x16x32_bf16 v[60:63], v[146:149], v[186:189], v[60:63]
	v_mfma_f32_16x16x32_bf16 v[56:59], v[162:165], v[186:189], v[56:59]
	v_mfma_f32_16x16x32_bf16 v[52:55], v[146:149], v[194:197], v[52:55]
	v_mfma_f32_16x16x32_bf16 v[48:51], v[162:165], v[194:197], v[48:51]
	v_mfma_f32_16x16x32_bf16 v[36:39], v[146:149], v[202:205], v[36:39]
	v_mfma_f32_16x16x32_bf16 v[32:35], v[162:165], v[202:205], v[32:35]
	v_mfma_f32_16x16x32_bf16 v[20:23], v[146:149], v[210:213], v[20:23]
	v_mfma_f32_16x16x32_bf16 v[16:19], v[162:165], v[210:213], v[16:19]
	s_setprio 0
	s_setprio 1
	v_mfma_f32_16x16x32_bf16 v[44:47], v[166:169], v[182:185], v[44:47]
	v_mfma_f32_16x16x32_bf16 v[40:43], v[174:177], v[182:185], v[40:43]
	v_mfma_f32_16x16x32_bf16 v[28:31], v[166:169], v[190:193], v[28:31]
	v_mfma_f32_16x16x32_bf16 v[24:27], v[174:177], v[190:193], v[24:27]
	v_mfma_f32_16x16x32_bf16 v[12:15], v[166:169], v[198:201], v[12:15]
	v_mfma_f32_16x16x32_bf16 v[8:11], v[174:177], v[198:201], v[8:11]
	v_mfma_f32_16x16x32_bf16 v[4:7], v[166:169], v[206:209], v[4:7]
	v_mfma_f32_16x16x32_bf16 v[0:3], v[174:177], v[206:209], v[0:3]
	v_mfma_f32_16x16x32_bf16 v[44:47], v[170:173], v[186:189], v[44:47]
	v_mfma_f32_16x16x32_bf16 v[40:43], v[178:181], v[186:189], v[40:43]
	v_mfma_f32_16x16x32_bf16 v[28:31], v[170:173], v[194:197], v[28:31]
	v_mfma_f32_16x16x32_bf16 v[24:27], v[178:181], v[194:197], v[24:27]
	v_mfma_f32_16x16x32_bf16 v[12:15], v[170:173], v[202:205], v[12:15]
	v_mfma_f32_16x16x32_bf16 v[8:11], v[178:181], v[202:205], v[8:11]
	v_mfma_f32_16x16x32_bf16 v[4:7], v[170:173], v[210:213], v[4:7]
	v_mfma_f32_16x16x32_bf16 v[0:3], v[178:181], v[210:213], v[0:3]
	s_setprio 0
	s_barrier
; #define PG8_STAGE(bufoff, gbase, voff) do { _Pragma("unroll") for (int _i = 0; _i < 2; ++_i) \
;         __builtin_amdgcn_global_load_lds((const unsigned*)((const char*)(gbase) + (voff)[_i]), (PG8_LAS unsigned*)(lds + (bufoff) + ldsw + _i * 8192), 16, 0, 0); } while (0)
; #define PG8_LDA(dst, b, h) do { _Pragma("unroll") for (int m = 0; m < 4; ++m) _Pragma("unroll") for (int k = 0; k < 2; ++k) dst[m][k] = *(const PG8_LAS bf16x8*)(lds + PG8_SA(b, h) + aoff + m * 2048 + k * 1024); } while (0)
; #define PG8_LDB(dst, b, h) do { _Pragma("unroll") for (int n = 0; n < 2; ++n) _Pragma("unroll") for (int k = 0; k < 2; ++k) dst[n][k] = *(const PG8_LAS bf16x8*)(lds + PG8_SB(b, h) + boff + n * 2048 + k * 1024); } while (0)
; #define PG8_MMA(ai, bj, At, Bt) do { __builtin_amdgcn_s_setprio(1); _Pragma("unroll") for (int m = 0; m < 4; ++m) _Pragma("unroll") for (int n = 0; n < 2; ++n) _Pragma("unroll") for (int k = 0; k < 2; ++k) \
;         acc[ai][bj][m][n] = __builtin_amdgcn_mfma_f32_16x16x32_bf16(Bt[n][k], At[m][k], acc[ai][bj][m][n], 0, 0, 0); __builtin_amdgcn_s_setprio(0); } while (0)
; #define PG8_WAIT_V(n) asm volatile("s_waitcnt vmcnt(" #n ")" ::: "memory")
; #define PG8_WAIT_L(n) asm volatile("s_waitcnt lgkmcnt(" #n ")" ::: "memory")
; #define PG8_BAR __builtin_amdgcn_s_barrier()
; #define PG8_SCHED __builtin_amdgcn_sched_barrier(0)
; template <class Epi, class Sched, bool ALIGN_EPI = false, bool SP2 = false>
; __device__ __forceinline__ void gemm_phase(PG8_LAS unsigned char* lds, const Gemm g, const Sched& S, const Epi& E, const int wid) {
;     ...
;             PG8_LDB(B0, 1, 0); PG8_LDB(B1, 1, 1); PG8_SCHED; PG8_LDA(At, 1, 0); PG8_STAGE(PG8_SA(0, 1), a2 + hstepA, voffA);
;             PG8_WAIT_V(8); PG8_WAIT_L(0); PG8_BAR; PG8_MMA(0, 0, At, B0); PG8_MMA(0, 1, At, B1); PG8_BAR; PG8_SCHED;
;             PG8_LDA(At, 1, 1); PG8_STAGE(PG8_SB(1, 0), b3, voffB); PG8_STAGE(PG8_SB(1, 1), b3 + hstepB, voffB); PG8_STAGE(PG8_SA(1, 0), a3, voffA);
;             PG8_WAIT_V(8); PG8_WAIT_L(0); PG8_BAR; PG8_MMA(1, 0, At, B0); PG8_MMA(1, 1, At, B1); PG8_BAR; PG8_SCHED;
;     ...
;         if constexpr (ALIGN_EPI) { if (wr == 0) PG8_BAR; }
	ds_read_b128 v[142:145], v252
	ds_read_b128 v[146:149], v252 offset:1024
	ds_read_b128 v[150:153], v252 offset:2048
	ds_read_b128 v[162:165], v252 offset:3072
	ds_read_b128 v[166:169], v253
	ds_read_b128 v[170:173], v253 offset:1024
	ds_read_b128 v[174:177], v253 offset:2048
	ds_read_b128 v[178:181], v253 offset:3072
	s_mov_b32 m0, s72
	ds_read_b128 v[182:185], v159 offset:32768
	ds_read_b128 v[186:189], v159 offset:33792
	ds_read_b128 v[190:193], v159 offset:34816
	ds_read_b128 v[194:197], v159 offset:35840
	ds_read_b128 v[198:201], v159 offset:36864
	ds_read_b128 v[202:205], v159 offset:37888
	ds_read_b128 v[206:209], v159 offset:38912
	ds_read_b128 v[210:213], v159 offset:39936
	global_load_lds_dwordx4 v134, s[36:37]
	s_mov_b32 m0, s73
	s_nop 0
	global_load_lds_dwordx4 v130, s[36:37]
	s_waitcnt vmcnt(8) lgkmcnt(0)
	s_barrier
	s_setprio 1
	v_mfma_f32_16x16x32_bf16 v[124:127], v[142:145], v[182:185], v[124:127]
	v_mfma_f32_16x16x32_bf16 v[120:123], v[150:153], v[182:185], v[120:123]
	v_mfma_f32_16x16x32_bf16 v[116:119], v[142:145], v[190:193], v[116:119]
	v_mfma_f32_16x16x32_bf16 v[112:115], v[150:153], v[190:193], v[112:115]
	v_mfma_f32_16x16x32_bf16 v[100:103], v[142:145], v[198:201], v[100:103]
	v_mfma_f32_16x16x32_bf16 v[96:99], v[150:153], v[198:201], v[96:99]
	v_mfma_f32_16x16x32_bf16 v[84:87], v[142:145], v[206:209], v[84:87]
	v_mfma_f32_16x16x32_bf16 v[80:83], v[150:153], v[206:209], v[80:83]
	v_mfma_f32_16x16x32_bf16 v[124:127], v[146:149], v[186:189], v[124:127]
	v_mfma_f32_16x16x32_bf16 v[120:123], v[162:165], v[186:189], v[120:123]
	v_mfma_f32_16x16x32_bf16 v[116:119], v[146:149], v[194:197], v[116:119]
	v_mfma_f32_16x16x32_bf16 v[112:115], v[162:165], v[194:197], v[112:115]
	v_mfma_f32_16x16x32_bf16 v[100:103], v[146:149], v[202:205], v[100:103]
	v_mfma_f32_16x16x32_bf16 v[96:99], v[162:165], v[202:205], v[96:99]
	v_mfma_f32_16x16x32_bf16 v[84:87], v[146:149], v[210:213], v[84:87]
	v_mfma_f32_16x16x32_bf16 v[80:83], v[162:165], v[210:213], v[80:83]
	s_setprio 0
	s_setprio 1
	v_mfma_f32_16x16x32_bf16 v[108:111], v[166:169], v[182:185], v[108:111]
	v_mfma_f32_16x16x32_bf16 v[104:107], v[174:177], v[182:185], v[104:107]
	v_mfma_f32_16x16x32_bf16 v[92:95], v[166:169], v[190:193], v[92:95]
	v_mfma_f32_16x16x32_bf16 v[88:91], v[174:177], v[190:193], v[88:91]
	v_mfma_f32_16x16x32_bf16 v[76:79], v[166:169], v[198:201], v[76:79]
	v_mfma_f32_16x16x32_bf16 v[72:75], v[174:177], v[198:201], v[72:75]
	v_mfma_f32_16x16x32_bf16 v[68:71], v[166:169], v[206:209], v[68:71]
	v_mfma_f32_16x16x32_bf16 v[64:67], v[174:177], v[206:209], v[64:67]
	v_mfma_f32_16x16x32_bf16 v[108:111], v[170:173], v[186:189], v[108:111]
	v_mfma_f32_16x16x32_bf16 v[104:107], v[178:181], v[186:189], v[104:107]
	v_mfma_f32_16x16x32_bf16 v[92:95], v[170:173], v[194:197], v[92:95]
	v_mfma_f32_16x16x32_bf16 v[88:91], v[178:181], v[194:197], v[88:91]
	v_mfma_f32_16x16x32_bf16 v[76:79], v[170:173], v[202:205], v[76:79]
	v_mfma_f32_16x16x32_bf16 v[72:75], v[178:181], v[202:205], v[72:75]
	v_mfma_f32_16x16x32_bf16 v[68:71], v[170:173], v[210:213], v[68:71]
	v_mfma_f32_16x16x32_bf16 v[64:67], v[178:181], v[210:213], v[64:67]
	s_setprio 0
	s_barrier
	s_mov_b32 m0, s86
	ds_read_b128 v[182:185], v159 offset:49152
	ds_read_b128 v[186:189], v159 offset:50176
	ds_read_b128 v[190:193], v159 offset:51200
	ds_read_b128 v[194:197], v159 offset:52224
	ds_read_b128 v[198:201], v159 offset:53248
	ds_read_b128 v[202:205], v159 offset:54272
	ds_read_b128 v[206:209], v159 offset:55296
	ds_read_b128 v[210:213], v159 offset:56320
	global_load_lds_dwordx4 v132, s[98:99]
	s_mov_b32 m0, s84
	s_nop 0
	global_load_lds_dwordx4 v128, s[98:99]
	s_mov_b32 m0, s85
	s_nop 0
	global_load_lds_dwordx4 v132, s[34:35]
	s_mov_b32 m0, s83
	s_nop 0
	global_load_lds_dwordx4 v128, s[34:35]
	s_mov_b32 m0, s74
	s_nop 0
	global_load_lds_dwordx4 v134, s[100:101]
	s_mov_b32 m0, s75
	s_nop 0
	global_load_lds_dwordx4 v130, s[100:101]
	s_waitcnt vmcnt(8) lgkmcnt(0)
	s_barrier
	s_setprio 1
	v_mfma_f32_16x16x32_bf16 v[60:63], v[142:145], v[182:185], v[60:63]
	v_mfma_f32_16x16x32_bf16 v[56:59], v[150:153], v[182:185], v[56:59]
	v_mfma_f32_16x16x32_bf16 v[52:55], v[142:145], v[190:193], v[52:55]
	v_mfma_f32_16x16x32_bf16 v[48:51], v[150:153], v[190:193], v[48:51]
	v_mfma_f32_16x16x32_bf16 v[36:39], v[142:145], v[198:201], v[36:39]
	v_mfma_f32_16x16x32_bf16 v[32:35], v[150:153], v[198:201], v[32:35]
	v_mfma_f32_16x16x32_bf16 v[20:23], v[142:145], v[206:209], v[20:23]
	v_mfma_f32_16x16x32_bf16 v[16:19], v[150:153], v[206:209], v[16:19]
	v_mfma_f32_16x16x32_bf16 v[60:63], v[146:149], v[186:189], v[60:63]
	v_mfma_f32_16x16x32_bf16 v[56:59], v[162:165], v[186:189], v[56:59]
	v_mfma_f32_16x16x32_bf16 v[52:55], v[146:149], v[194:197], v[52:55]
	v_mfma_f32_16x16x32_bf16 v[48:51], v[162:165], v[194:197], v[48:51]
	v_mfma_f32_16x16x32_bf16 v[36:39], v[146:149], v[202:205], v[36:39]
	v_mfma_f32_16x16x32_bf16 v[32:35], v[162:165], v[202:205], v[32:35]
	v_mfma_f32_16x16x32_bf16 v[20:23], v[146:149], v[210:213], v[20:23]
	v_mfma_f32_16x16x32_bf16 v[16:19], v[162:165], v[210:213], v[16:19]
	s_setprio 0
	s_setprio 1
	v_mfma_f32_16x16x32_bf16 v[44:47], v[166:169], v[182:185], v[44:47]
	v_mfma_f32_16x16x32_bf16 v[40:43], v[174:177], v[182:185], v[40:43]
	v_mfma_f32_16x16x32_bf16 v[28:31], v[166:169], v[190:193], v[28:31]
	v_mfma_f32_16x16x32_bf16 v[24:27], v[174:177], v[190:193], v[24:27]
	v_mfma_f32_16x16x32_bf16 v[12:15], v[166:169], v[198:201], v[12:15]
	v_mfma_f32_16x16x32_bf16 v[8:11], v[174:177], v[198:201], v[8:11]
	v_mfma_f32_16x16x32_bf16 v[4:7], v[166:169], v[206:209], v[4:7]
	v_mfma_f32_16x16x32_bf16 v[0:3], v[174:177], v[206:209], v[0:3]
	v_mfma_f32_16x16x32_bf16 v[44:47], v[170:173], v[186:189], v[44:47]
	v_mfma_f32_16x16x32_bf16 v[40:43], v[178:181], v[186:189], v[40:43]
	v_mfma_f32_16x16x32_bf16 v[28:31], v[170:173], v[194:197], v[28:31]
	v_mfma_f32_16x16x32_bf16 v[24:27], v[178:181], v[194:197], v[24:27]
	v_mfma_f32_16x16x32_bf16 v[12:15], v[170:173], v[202:205], v[12:15]
	v_mfma_f32_16x16x32_bf16 v[8:11], v[178:181], v[202:205], v[8:11]
	v_mfma_f32_16x16x32_bf16 v[4:7], v[170:173], v[210:213], v[4:7]
	v_mfma_f32_16x16x32_bf16 v[0:3], v[178:181], v[210:213], v[0:3]
	s_setprio 0
	s_barrier
	s_movk_i32 s36, 0x100
	s_andn2_b64 vcc, exec, s[30:31]
	s_mov_b64 s[34:35], -1
	s_mov_b64 s[30:31], 0
	s_cbranch_vccz .LBB0_2280
	s_and_b64 vcc, exec, s[14:15]
	s_cbranch_vccz .LBB0_2283
	s_barrier

; #define PG8_STAGE(bufoff, gbase, voff) do { _Pragma("unroll") for (int _i = 0; _i < 2; ++_i) \
;         __builtin_amdgcn_global_load_lds((const unsigned*)((const char*)(gbase) + (voff)[_i]), (PG8_LAS unsigned*)(lds + (bufoff) + ldsw + _i * 8192), 16, 0, 0); } while (0)
; #define PG8_LDA(dst, b, h) do { _Pragma("unroll") for (int m = 0; m < 4; ++m) _Pragma("unroll") for (int k = 0; k < 2; ++k) dst[m][k] = *(const PG8_LAS bf16x8*)(lds + PG8_SA(b, h) + aoff + m * 2048 + k * 1024); } while (0)
; #define PG8_LDB(dst, b, h) do { _Pragma("unroll") for (int n = 0; n < 2; ++n) _Pragma("unroll") for (int k = 0; k < 2; ++k) dst[n][k] = *(const PG8_LAS bf16x8*)(lds + PG8_SB(b, h) + boff + n * 2048 + k * 1024); } while (0)
; #define PG8_MMA(ai, bj, At, Bt) do { __builtin_amdgcn_s_setprio(1); _Pragma("unroll") for (int m = 0; m < 4; ++m) _Pragma("unroll") for (int n = 0; n < 2; ++n) _Pragma("unroll") for (int k = 0; k < 2; ++k) \
;         acc[ai][bj][m][n] = __builtin_amdgcn_mfma_f32_16x16x32_bf16(Bt[n][k], At[m][k], acc[ai][bj][m][n], 0, 0, 0); __builtin_amdgcn_s_setprio(0); } while (0)
; template <class Epi, class Sched, bool ALIGN_EPI = false, bool SP2 = false>
; __device__ __forceinline__ void gemm_phase(PG8_LAS unsigned char* lds, const Gemm g, const Sched& S, const Epi& E, const int wid) {
;     ...
;         const bool has_next = S.next(ui + 1, nxt);
;         const char* nA = has_next ? (const char*)g.A + (size_t)nxt.pm * tstepA : cA; const char* nB = has_next ? (const char*)g.Bt + (size_t)nxt.pn * tstepB : cB;
;         for (int t = 0; t < nt; t += 2) {
;             const bool last = (t == nt - 2);
;             const char* a1 = cA + (size_t)(t + 1) * kstep;
;             const char* a2 = last ? nA : cA + (size_t)(t + 2) * kstep; const char* b2 = last ? nB : cB + (size_t)(t + 2) * kstep;
;             const char* a3 = a2 + kstep; const char* b3 = b2 + kstep;
;             if (last && has_next) S.a_ready(nxt);
;             if constexpr (SP2) {
;             PG8_LDB(B0, 0, 0); PG8_LDB(B1, 0, 1); PG8_SCHED; PG8_LDA(At, 0, 0); PG8_STAGE(PG8_SA(1, 1), a1 + hstepA, voffA);
;             PG8_WAIT_V(8); PG8_WAIT_L(0); PG8_BAR; PG8_MMA(0, 0, At, B0); PG8_MMA(0, 1, At, B1); PG8_BAR; PG8_SCHED;
;             PG8_LDA(At, 0, 1); PG8_STAGE(PG8_SB(0, 0), b2, voffB); PG8_STAGE(PG8_SB(0, 1), b2 + hstepB, voffB); PG8_STAGE(PG8_SA(0, 0), a2, voffA);
.LBB0_2724:
	s_ashr_i32 s21, s20, 31
	s_lshl_b64 s[22:23], s[20:21], 19
	s_add_u32 s22, s0, s22
	s_addc_u32 s23, s1, s23
	s_and_b64 s[24:25], s[4:5], exec
	s_cselect_b32 s21, s23, s31
	s_cselect_b32 s27, s22, s30
	s_ashr_i32 s19, s18, 31
	s_lshl_b64 s[24:25], s[18:19], 19
	s_add_u32 s24, s33, s24
	s_addc_u32 s25, s38, s25
	s_and_b64 s[36:37], s[4:5], exec
	s_cselect_b32 s19, s25, s35
	s_cselect_b32 s29, s24, s34
	s_add_u32 s30, s30, 0x40080
	s_addc_u32 s31, s31, 0
	s_add_u32 s58, s34, 0x100
	s_addc_u32 s59, s35, 0
	s_mov_b32 s60, -2
	s_waitcnt lgkmcnt(0)
	v_add_u32_e32 v252, 0x18000, v189
	v_add_u32_e32 v253, 0x1c000, v189
	ds_read_b128 v[128:131], v190
	ds_read_b128 v[132:135], v190 offset:1024
	ds_read_b128 v[136:139], v190 offset:2048
	ds_read_b128 v[140:143], v190 offset:3072
	ds_read_b128 v[144:147], v191
	ds_read_b128 v[148:151], v191 offset:1024
	ds_read_b128 v[172:175], v191 offset:2048
	ds_read_b128 v[176:179], v191 offset:3072
	s_add_u32 s34, s30, 0xfffc0080
	s_addc_u32 s35, s31, -1
	s_cmp_eq_u32 s60, 12
	s_cselect_b32 s37, s21, s35
	s_cselect_b32 s36, s27, s34
	s_cselect_b32 s35, s19, s59
	s_cselect_b32 s34, s29, s58
	s_add_i32 m0, s40, 0xc000
	ds_read_b128 v[180:183], v192
	ds_read_b128 v[184:187], v192 offset:1024
	ds_read_b128 v[194:197], v192 offset:2048
	ds_read_b128 v[198:201], v192 offset:3072
	ds_read_b128 v[202:205], v192 offset:4096
	ds_read_b128 v[206:209], v192 offset:5120
	ds_read_b128 v[210:213], v192 offset:6144
	ds_read_b128 v[214:217], v192 offset:7168
	global_load_lds_dwordx4 v164, s[30:31]
	s_add_i32 m0, s40, 0xe000
	s_nop 0
	global_load_lds_dwordx4 v166, s[30:31]
	s_waitcnt vmcnt(8) lgkmcnt(0)
	s_barrier
	s_setprio 1
	v_mfma_f32_16x16x32_bf16 v[124:127], v[128:131], v[180:183], 0
	v_mfma_f32_16x16x32_bf16 v[120:123], v[136:139], v[180:183], 0
	v_mfma_f32_16x16x32_bf16 v[108:111], v[128:131], v[194:197], 0
	v_mfma_f32_16x16x32_bf16 v[104:107], v[136:139], v[194:197], 0
	v_mfma_f32_16x16x32_bf16 v[92:95], v[128:131], v[202:205], 0
	v_mfma_f32_16x16x32_bf16 v[88:91], v[136:139], v[202:205], 0
	v_mfma_f32_16x16x32_bf16 v[76:79], v[128:131], v[210:213], 0
	v_mfma_f32_16x16x32_bf16 v[72:75], v[136:139], v[210:213], 0
	v_mfma_f32_16x16x32_bf16 v[124:127], v[132:135], v[184:187], v[124:127]
	v_mfma_f32_16x16x32_bf16 v[120:123], v[140:143], v[184:187], v[120:123]
	v_mfma_f32_16x16x32_bf16 v[108:111], v[132:135], v[198:201], v[108:111]
	v_mfma_f32_16x16x32_bf16 v[104:107], v[140:143], v[198:201], v[104:107]
	v_mfma_f32_16x16x32_bf16 v[92:95], v[132:135], v[206:209], v[92:95]
	v_mfma_f32_16x16x32_bf16 v[88:91], v[140:143], v[206:209], v[88:91]
	v_mfma_f32_16x16x32_bf16 v[76:79], v[132:135], v[214:217], v[76:79]
	v_mfma_f32_16x16x32_bf16 v[72:75], v[140:143], v[214:217], v[72:75]
	s_setprio 0
	s_setprio 1
	v_mfma_f32_16x16x32_bf16 v[116:119], v[144:147], v[180:183], 0
	v_mfma_f32_16x16x32_bf16 v[112:115], v[172:175], v[180:183], 0
	v_mfma_f32_16x16x32_bf16 v[100:103], v[144:147], v[194:197], 0
	v_mfma_f32_16x16x32_bf16 v[96:99], v[172:175], v[194:197], 0
	v_mfma_f32_16x16x32_bf16 v[84:87], v[144:147], v[202:205], 0
	v_mfma_f32_16x16x32_bf16 v[80:83], v[172:175], v[202:205], 0
	v_mfma_f32_16x16x32_bf16 v[68:71], v[144:147], v[210:213], 0
	v_mfma_f32_16x16x32_bf16 v[64:67], v[172:175], v[210:213], 0
	v_mfma_f32_16x16x32_bf16 v[116:119], v[148:151], v[184:187], v[116:119]
	v_mfma_f32_16x16x32_bf16 v[112:115], v[176:179], v[184:187], v[112:115]
	v_mfma_f32_16x16x32_bf16 v[100:103], v[148:151], v[198:201], v[100:103]
	v_mfma_f32_16x16x32_bf16 v[96:99], v[176:179], v[198:201], v[96:99]
	v_mfma_f32_16x16x32_bf16 v[84:87], v[148:151], v[206:209], v[84:87]
	v_mfma_f32_16x16x32_bf16 v[80:83], v[176:179], v[206:209], v[80:83]
	v_mfma_f32_16x16x32_bf16 v[68:71], v[148:151], v[214:217], v[68:71]
	v_mfma_f32_16x16x32_bf16 v[64:67], v[176:179], v[214:217], v[64:67]
	s_setprio 0
	s_barrier
	s_add_i32 s61, s49, s39
	s_add_u32 s98, s34, 0x80
	s_addc_u32 s99, s35, 0
	s_mov_b32 m0, s61
	ds_read_b128 v[180:183], v192 offset:16384
	ds_read_b128 v[184:187], v192 offset:17408
	ds_read_b128 v[194:197], v192 offset:18432
	ds_read_b128 v[198:201], v192 offset:19456
	ds_read_b128 v[202:205], v192 offset:20480
	ds_read_b128 v[206:209], v192 offset:21504
	ds_read_b128 v[210:213], v192 offset:22528
	ds_read_b128 v[214:217], v192 offset:23552
	global_load_lds_dwordx4 v154, s[34:35]
	s_add_i32 m0, s61, 0x2000
	s_add_u32 s62, s34, 0x40000
	s_addc_u32 s63, s35, 0
	s_add_i32 s61, s56, s39
	global_load_lds_dwordx4 v158, s[34:35]
	s_mov_b32 m0, s61
	s_add_u32 s100, s36, 0x80
	s_addc_u32 s101, s37, 0
	global_load_lds_dwordx4 v154, s[62:63]
	s_add_i32 m0, s61, 0x2000
	s_nop 0
	global_load_lds_dwordx4 v158, s[62:63]
	s_mov_b32 m0, s40
	s_nop 0
	global_load_lds_dwordx4 v152, s[36:37]
	s_mov_b32 m0, s41
	s_nop 0
	global_load_lds_dwordx4 v156, s[36:37]
	s_waitcnt vmcnt(8) lgkmcnt(0)
	s_barrier
; #define PG8_STAGE(bufoff, gbase, voff) do { _Pragma("unroll") for (int _i = 0; _i < 2; ++_i) \
;         __builtin_amdgcn_global_load_lds((const unsigned*)((const char*)(gbase) + (voff)[_i]), (PG8_LAS unsigned*)(lds + (bufoff) + ldsw + _i * 8192), 16, 0, 0); } while (0)
; #define PG8_LDA(dst, b, h) do { _Pragma("unroll") for (int m = 0; m < 4; ++m) _Pragma("unroll") for (int k = 0; k < 2; ++k) dst[m][k] = *(const PG8_LAS bf16x8*)(lds + PG8_SA(b, h) + aoff + m * 2048 + k * 1024); } while (0)
; #define PG8_LDB(dst, b, h) do { _Pragma("unroll") for (int n = 0; n < 2; ++n) _Pragma("unroll") for (int k = 0; k < 2; ++k) dst[n][k] = *(const PG8_LAS bf16x8*)(lds + PG8_SB(b, h) + boff + n * 2048 + k * 1024); } while (0)
; #define PG8_MMA(ai, bj, At, Bt) do { __builtin_amdgcn_s_setprio(1); _Pragma("unroll") for (int m = 0; m < 4; ++m) _Pragma("unroll") for (int n = 0; n < 2; ++n) _Pragma("unroll") for (int k = 0; k < 2; ++k) \
;         acc[ai][bj][m][n] = __builtin_amdgcn_mfma_f32_16x16x32_bf16(Bt[n][k], At[m][k], acc[ai][bj][m][n], 0, 0, 0); __builtin_amdgcn_s_setprio(0); } while (0)
; #define PG8_WAIT_V(n) asm volatile("s_waitcnt vmcnt(" #n ")" ::: "memory")
; #define PG8_WAIT_L(n) asm volatile("s_waitcnt lgkmcnt(" #n ")" ::: "memory")
; #define PG8_BAR __builtin_amdgcn_s_barrier()
; #define PG8_SCHED __builtin_amdgcn_sched_barrier(0)
; template <class Epi, class Sched, bool ALIGN_EPI = false, bool SP2 = false>
; __device__ __forceinline__ void gemm_phase(PG8_LAS unsigned char* lds, const Gemm g, const Sched& S, const Epi& E, const int wid) {
;     ...
;             PG8_WAIT_V(8); PG8_WAIT_L(0); PG8_BAR; PG8_MMA(1, 0, At, B0); PG8_MMA(1, 1, At, B1); PG8_BAR; PG8_SCHED;
;             PG8_LDB(B0, 1, 0); PG8_LDB(B1, 1, 1); PG8_SCHED; PG8_LDA(At, 1, 0); PG8_STAGE(PG8_SA(0, 1), a2 + hstepA, voffA);
;             PG8_WAIT_V(8); PG8_WAIT_L(0); PG8_BAR; PG8_MMA(0, 0, At, B0); PG8_MMA(0, 1, At, B1); PG8_BAR; PG8_SCHED;
	s_setprio 1
	v_mfma_f32_16x16x32_bf16 v[60:63], v[128:131], v[180:183], 0
	v_mfma_f32_16x16x32_bf16 v[56:59], v[136:139], v[180:183], 0
	v_mfma_f32_16x16x32_bf16 v[44:47], v[128:131], v[194:197], 0
	v_mfma_f32_16x16x32_bf16 v[40:43], v[136:139], v[194:197], 0
	v_mfma_f32_16x16x32_bf16 v[28:31], v[128:131], v[202:205], 0
	v_mfma_f32_16x16x32_bf16 v[24:27], v[136:139], v[202:205], 0
	v_mfma_f32_16x16x32_bf16 v[12:15], v[128:131], v[210:213], 0
	v_mfma_f32_16x16x32_bf16 v[8:11], v[136:139], v[210:213], 0
	v_mfma_f32_16x16x32_bf16 v[60:63], v[132:135], v[184:187], v[60:63]
	v_mfma_f32_16x16x32_bf16 v[56:59], v[140:143], v[184:187], v[56:59]
	v_mfma_f32_16x16x32_bf16 v[44:47], v[132:135], v[198:201], v[44:47]
	v_mfma_f32_16x16x32_bf16 v[40:43], v[140:143], v[198:201], v[40:43]
	v_mfma_f32_16x16x32_bf16 v[28:31], v[132:135], v[206:209], v[28:31]
	v_mfma_f32_16x16x32_bf16 v[24:27], v[140:143], v[206:209], v[24:27]
	v_mfma_f32_16x16x32_bf16 v[12:15], v[132:135], v[214:217], v[12:15]
	v_mfma_f32_16x16x32_bf16 v[8:11], v[140:143], v[214:217], v[8:11]
	s_setprio 0
	s_setprio 1
	v_mfma_f32_16x16x32_bf16 v[52:55], v[144:147], v[180:183], 0
	v_mfma_f32_16x16x32_bf16 v[48:51], v[172:175], v[180:183], 0
	v_mfma_f32_16x16x32_bf16 v[36:39], v[144:147], v[194:197], 0
	v_mfma_f32_16x16x32_bf16 v[32:35], v[172:175], v[194:197], 0
	v_mfma_f32_16x16x32_bf16 v[20:23], v[144:147], v[202:205], 0
	v_mfma_f32_16x16x32_bf16 v[16:19], v[172:175], v[202:205], 0
	v_mfma_f32_16x16x32_bf16 v[4:7], v[144:147], v[210:213], 0
	v_mfma_f32_16x16x32_bf16 v[0:3], v[172:175], v[210:213], 0
	v_mfma_f32_16x16x32_bf16 v[52:55], v[148:151], v[184:187], v[52:55]
	v_mfma_f32_16x16x32_bf16 v[48:51], v[176:179], v[184:187], v[48:51]
	v_mfma_f32_16x16x32_bf16 v[36:39], v[148:151], v[198:201], v[36:39]
	v_mfma_f32_16x16x32_bf16 v[32:35], v[176:179], v[198:201], v[32:35]
	v_mfma_f32_16x16x32_bf16 v[20:23], v[148:151], v[206:209], v[20:23]
	v_mfma_f32_16x16x32_bf16 v[16:19], v[176:179], v[206:209], v[16:19]
	v_mfma_f32_16x16x32_bf16 v[4:7], v[148:151], v[214:217], v[4:7]
	v_mfma_f32_16x16x32_bf16 v[0:3], v[176:179], v[214:217], v[0:3]
	s_setprio 0
	s_barrier
	s_add_i32 s61, 0, 0x18000
	s_add_i32 s62, 0, 0x1c000
	ds_read_b128 v[128:131], v252
	ds_read_b128 v[132:135], v252 offset:1024
	ds_read_b128 v[136:139], v252 offset:2048
	ds_read_b128 v[140:143], v252 offset:3072
	ds_read_b128 v[144:147], v253
	ds_read_b128 v[148:151], v253 offset:1024
	ds_read_b128 v[172:175], v253 offset:2048
	ds_read_b128 v[176:179], v253 offset:3072
	s_add_u32 s36, s36, 0x40000
	s_addc_u32 s37, s37, 0
	s_mov_b32 m0, s42
	ds_read_b128 v[180:183], v192 offset:32768
	ds_read_b128 v[184:187], v192 offset:33792
	ds_read_b128 v[194:197], v192 offset:34816
	ds_read_b128 v[198:201], v192 offset:35840
	ds_read_b128 v[202:205], v192 offset:36864
	ds_read_b128 v[206:209], v192 offset:37888
	ds_read_b128 v[210:213], v192 offset:38912
	ds_read_b128 v[214:217], v192 offset:39936
	global_load_lds_dwordx4 v152, s[36:37]
	s_mov_b32 m0, s43
	s_nop 0
	global_load_lds_dwordx4 v156, s[36:37]
	s_waitcnt vmcnt(8) lgkmcnt(0)
	s_barrier
	s_setprio 1
	v_mfma_f32_16x16x32_bf16 v[124:127], v[128:131], v[180:183], v[124:127]
	v_mfma_f32_16x16x32_bf16 v[120:123], v[136:139], v[180:183], v[120:123]
	v_mfma_f32_16x16x32_bf16 v[108:111], v[128:131], v[194:197], v[108:111]
	v_mfma_f32_16x16x32_bf16 v[104:107], v[136:139], v[194:197], v[104:107]
	v_mfma_f32_16x16x32_bf16 v[92:95], v[128:131], v[202:205], v[92:95]
	v_mfma_f32_16x16x32_bf16 v[88:91], v[136:139], v[202:205], v[88:91]
	v_mfma_f32_16x16x32_bf16 v[76:79], v[128:131], v[210:213], v[76:79]
	v_mfma_f32_16x16x32_bf16 v[72:75], v[136:139], v[210:213], v[72:75]
	v_mfma_f32_16x16x32_bf16 v[124:127], v[132:135], v[184:187], v[124:127]
	v_mfma_f32_16x16x32_bf16 v[120:123], v[140:143], v[184:187], v[120:123]
	v_mfma_f32_16x16x32_bf16 v[108:111], v[132:135], v[198:201], v[108:111]
	v_mfma_f32_16x16x32_bf16 v[104:107], v[140:143], v[198:201], v[104:107]
	v_mfma_f32_16x16x32_bf16 v[92:95], v[132:135], v[206:209], v[92:95]
	v_mfma_f32_16x16x32_bf16 v[88:91], v[140:143], v[206:209], v[88:91]
	v_mfma_f32_16x16x32_bf16 v[76:79], v[132:135], v[214:217], v[76:79]
	v_mfma_f32_16x16x32_bf16 v[72:75], v[140:143], v[214:217], v[72:75]
	s_setprio 0
	s_setprio 1
	v_mfma_f32_16x16x32_bf16 v[116:119], v[144:147], v[180:183], v[116:119]
	v_mfma_f32_16x16x32_bf16 v[112:115], v[172:175], v[180:183], v[112:115]
	v_mfma_f32_16x16x32_bf16 v[100:103], v[144:147], v[194:197], v[100:103]
	v_mfma_f32_16x16x32_bf16 v[96:99], v[172:175], v[194:197], v[96:99]
	v_mfma_f32_16x16x32_bf16 v[84:87], v[144:147], v[202:205], v[84:87]
	v_mfma_f32_16x16x32_bf16 v[80:83], v[172:175], v[202:205], v[80:83]
	v_mfma_f32_16x16x32_bf16 v[68:71], v[144:147], v[210:213], v[68:71]
	v_mfma_f32_16x16x32_bf16 v[64:67], v[172:175], v[210:213], v[64:67]
	v_mfma_f32_16x16x32_bf16 v[116:119], v[148:151], v[184:187], v[116:119]
	v_mfma_f32_16x16x32_bf16 v[112:115], v[176:179], v[184:187], v[112:115]
	v_mfma_f32_16x16x32_bf16 v[100:103], v[148:151], v[198:201], v[100:103]
	v_mfma_f32_16x16x32_bf16 v[96:99], v[176:179], v[198:201], v[96:99]
	v_mfma_f32_16x16x32_bf16 v[84:87], v[148:151], v[206:209], v[84:87]
	v_mfma_f32_16x16x32_bf16 v[80:83], v[176:179], v[206:209], v[80:83]
	v_mfma_f32_16x16x32_bf16 v[68:71], v[148:151], v[214:217], v[68:71]
	v_mfma_f32_16x16x32_bf16 v[64:67], v[176:179], v[214:217], v[64:67]
	s_setprio 0
	s_barrier
; #define PG8_STAGE(bufoff, gbase, voff) do { _Pragma("unroll") for (int _i = 0; _i < 2; ++_i) \
;         __builtin_amdgcn_global_load_lds((const unsigned*)((const char*)(gbase) + (voff)[_i]), (PG8_LAS unsigned*)(lds + (bufoff) + ldsw + _i * 8192), 16, 0, 0); } while (0)
; #define PG8_LDA(dst, b, h) do { _Pragma("unroll") for (int m = 0; m < 4; ++m) _Pragma("unroll") for (int k = 0; k < 2; ++k) dst[m][k] = *(const PG8_LAS bf16x8*)(lds + PG8_SA(b, h) + aoff + m * 2048 + k * 1024); } while (0)
; #define PG8_WAIT_V(n) asm volatile("s_waitcnt vmcnt(" #n ")" ::: "memory")
; #define PG8_WAIT_L(n) asm volatile("s_waitcnt lgkmcnt(" #n ")" ::: "memory")
; #define PG8_BAR __builtin_amdgcn_s_barrier()
; template <class Epi, class Sched, bool ALIGN_EPI = false, bool SP2 = false>
; __device__ __forceinline__ void gemm_phase(PG8_LAS unsigned char* lds, const Gemm g, const Sched& S, const Epi& E, const int wid) {
;     ...
;         for (int t = 0; t < nt; t += 2) {
;             const bool last = (t == nt - 2);
;             const char* a1 = cA + (size_t)(t + 1) * kstep;
;             const char* a2 = last ? nA : cA + (size_t)(t + 2) * kstep; const char* b2 = last ? nB : cB + (size_t)(t + 2) * kstep;
;             const char* a3 = a2 + kstep; const char* b3 = b2 + kstep;
;             if (last && has_next) S.a_ready(nxt);
;             if constexpr (SP2) {
;             PG8_LDB(B0, 0, 0); PG8_LDB(B1, 0, 1); PG8_SCHED; PG8_LDA(At, 0, 0); PG8_STAGE(PG8_SA(1, 1), a1 + hstepA, voffA);
;             PG8_WAIT_V(8); PG8_WAIT_L(0); PG8_BAR; PG8_MMA(0, 0, At, B0); PG8_MMA(0, 1, At, B1); PG8_BAR; PG8_SCHED;
;             PG8_LDA(At, 0, 1); PG8_STAGE(PG8_SB(0, 0), b2, voffB); PG8_STAGE(PG8_SB(0, 1), b2 + hstepB, voffB); PG8_STAGE(PG8_SA(0, 0), a2, voffA);
;             PG8_WAIT_V(8); PG8_WAIT_L(0); PG8_BAR; PG8_MMA(1, 0, At, B0); PG8_MMA(1, 1, At, B1); PG8_BAR; PG8_SCHED;
;             PG8_LDB(B0, 1, 0); PG8_LDB(B1, 1, 1); PG8_SCHED; PG8_LDA(At, 1, 0); PG8_STAGE(PG8_SA(0, 1), a2 + hstepA, voffA);
;             PG8_WAIT_V(8); PG8_WAIT_L(0); PG8_BAR; PG8_MMA(0, 0, At, B0); PG8_MMA(0, 1, At, B1); PG8_BAR; PG8_SCHED;
;             PG8_LDA(At, 1, 1); PG8_STAGE(PG8_SB(1, 0), b3, voffB); PG8_STAGE(PG8_SB(1, 1), b3 + hstepB, voffB); PG8_STAGE(PG8_SA(1, 0), a3, voffA);
;             PG8_WAIT_V(8); PG8_WAIT_L(0); PG8_BAR; PG8_MMA(1, 0, At, B0); PG8_MMA(1, 1, At, B1); PG8_BAR; PG8_SCHED;
	s_add_i32 s36, s61, s39
	s_mov_b32 m0, s36
	ds_read_b128 v[180:183], v192 offset:49152
	ds_read_b128 v[184:187], v192 offset:50176
	ds_read_b128 v[194:197], v192 offset:51200
	ds_read_b128 v[198:201], v192 offset:52224
	ds_read_b128 v[202:205], v192 offset:53248
	ds_read_b128 v[206:209], v192 offset:54272
	ds_read_b128 v[210:213], v192 offset:55296
	ds_read_b128 v[214:217], v192 offset:56320
	global_load_lds_dwordx4 v154, s[98:99]
	s_add_i32 m0, s36, 0x2000
	s_add_u32 s34, s34, 0x40080
	s_addc_u32 s35, s35, 0
	s_add_i32 s36, s62, s39
	global_load_lds_dwordx4 v158, s[98:99]
	s_mov_b32 m0, s36
	s_nop 0
	global_load_lds_dwordx4 v154, s[34:35]
	s_add_i32 m0, s36, 0x2000
	s_nop 0
	global_load_lds_dwordx4 v158, s[34:35]
	s_mov_b32 m0, s45
	s_nop 0
	global_load_lds_dwordx4 v152, s[100:101]
	s_mov_b32 m0, s46
	s_nop 0
	global_load_lds_dwordx4 v156, s[100:101]
	s_waitcnt vmcnt(8) lgkmcnt(0)
	s_barrier
	s_setprio 1
	v_mfma_f32_16x16x32_bf16 v[60:63], v[128:131], v[180:183], v[60:63]
	v_mfma_f32_16x16x32_bf16 v[56:59], v[136:139], v[180:183], v[56:59]
	v_mfma_f32_16x16x32_bf16 v[44:47], v[128:131], v[194:197], v[44:47]
	v_mfma_f32_16x16x32_bf16 v[40:43], v[136:139], v[194:197], v[40:43]
	v_mfma_f32_16x16x32_bf16 v[28:31], v[128:131], v[202:205], v[28:31]
	v_mfma_f32_16x16x32_bf16 v[24:27], v[136:139], v[202:205], v[24:27]
	v_mfma_f32_16x16x32_bf16 v[12:15], v[128:131], v[210:213], v[12:15]
	v_mfma_f32_16x16x32_bf16 v[8:11], v[136:139], v[210:213], v[8:11]
	v_mfma_f32_16x16x32_bf16 v[60:63], v[132:135], v[184:187], v[60:63]
	v_mfma_f32_16x16x32_bf16 v[56:59], v[140:143], v[184:187], v[56:59]
	v_mfma_f32_16x16x32_bf16 v[44:47], v[132:135], v[198:201], v[44:47]
	v_mfma_f32_16x16x32_bf16 v[40:43], v[140:143], v[198:201], v[40:43]
	v_mfma_f32_16x16x32_bf16 v[28:31], v[132:135], v[206:209], v[28:31]
	v_mfma_f32_16x16x32_bf16 v[24:27], v[140:143], v[206:209], v[24:27]
	v_mfma_f32_16x16x32_bf16 v[12:15], v[132:135], v[214:217], v[12:15]
	v_mfma_f32_16x16x32_bf16 v[8:11], v[140:143], v[214:217], v[8:11]
	s_setprio 0
	s_setprio 1
	v_mfma_f32_16x16x32_bf16 v[52:55], v[144:147], v[180:183], v[52:55]
	v_mfma_f32_16x16x32_bf16 v[48:51], v[172:175], v[180:183], v[48:51]
	v_mfma_f32_16x16x32_bf16 v[36:39], v[144:147], v[194:197], v[36:39]
	v_mfma_f32_16x16x32_bf16 v[32:35], v[172:175], v[194:197], v[32:35]
	v_mfma_f32_16x16x32_bf16 v[20:23], v[144:147], v[202:205], v[20:23]
	v_mfma_f32_16x16x32_bf16 v[16:19], v[172:175], v[202:205], v[16:19]
	v_mfma_f32_16x16x32_bf16 v[4:7], v[144:147], v[210:213], v[4:7]
	v_mfma_f32_16x16x32_bf16 v[0:3], v[172:175], v[210:213], v[0:3]
	v_mfma_f32_16x16x32_bf16 v[52:55], v[148:151], v[184:187], v[52:55]
	v_mfma_f32_16x16x32_bf16 v[48:51], v[176:179], v[184:187], v[48:51]
	v_mfma_f32_16x16x32_bf16 v[36:39], v[148:151], v[198:201], v[36:39]
	v_mfma_f32_16x16x32_bf16 v[32:35], v[176:179], v[198:201], v[32:35]
	v_mfma_f32_16x16x32_bf16 v[20:23], v[148:151], v[206:209], v[20:23]
	v_mfma_f32_16x16x32_bf16 v[16:19], v[176:179], v[206:209], v[16:19]
	v_mfma_f32_16x16x32_bf16 v[4:7], v[148:151], v[214:217], v[4:7]
	v_mfma_f32_16x16x32_bf16 v[0:3], v[176:179], v[214:217], v[0:3]
	s_setprio 0
	s_barrier
	s_add_i32 s60, s60, 2
	s_add_u32 s30, s30, 0x100
	s_addc_u32 s31, s31, 0
	s_add_u32 s58, s58, 0x100
	s_addc_u32 s59, s59, 0
	s_cmp_gt_u32 s60, 13
.LBB0_2725:
	ds_read_b128 v[128:131], v190
	ds_read_b128 v[132:135], v190 offset:1024
	ds_read_b128 v[136:139], v190 offset:2048
	ds_read_b128 v[140:143], v190 offset:3072
	ds_read_b128 v[144:147], v191
	ds_read_b128 v[148:151], v191 offset:1024
	ds_read_b128 v[172:175], v191 offset:2048
	ds_read_b128 v[176:179], v191 offset:3072
	s_add_u32 s34, s30, 0xfffc0080
	s_addc_u32 s35, s31, -1
	s_cmp_eq_u32 s60, 12
	s_cselect_b32 s37, s21, s35
	s_cselect_b32 s36, s27, s34
	s_cselect_b32 s35, s19, s59
	s_cselect_b32 s34, s29, s58
	s_add_i32 m0, s40, 0xc000
	ds_read_b128 v[180:183], v192
	ds_read_b128 v[184:187], v192 offset:1024
	ds_read_b128 v[194:197], v192 offset:2048
	ds_read_b128 v[198:201], v192 offset:3072
	ds_read_b128 v[202:205], v192 offset:4096
	ds_read_b128 v[206:209], v192 offset:5120
	ds_read_b128 v[210:213], v192 offset:6144
	ds_read_b128 v[214:217], v192 offset:7168
	global_load_lds_dwordx4 v164, s[30:31]
	s_add_i32 m0, s40, 0xe000
	s_nop 0
	global_load_lds_dwordx4 v166, s[30:31]
	s_waitcnt vmcnt(8) lgkmcnt(0)
	s_barrier
	s_setprio 1
	v_mfma_f32_16x16x32_bf16 v[124:127], v[128:131], v[180:183], v[124:127]
	v_mfma_f32_16x16x32_bf16 v[120:123], v[136:139], v[180:183], v[120:123]
	v_mfma_f32_16x16x32_bf16 v[108:111], v[128:131], v[194:197], v[108:111]
	v_mfma_f32_16x16x32_bf16 v[104:107], v[136:139], v[194:197], v[104:107]
	v_mfma_f32_16x16x32_bf16 v[92:95], v[128:131], v[202:205], v[92:95]
	v_mfma_f32_16x16x32_bf16 v[88:91], v[136:139], v[202:205], v[88:91]
	v_mfma_f32_16x16x32_bf16 v[76:79], v[128:131], v[210:213], v[76:79]
	v_mfma_f32_16x16x32_bf16 v[72:75], v[136:139], v[210:213], v[72:75]
	v_mfma_f32_16x16x32_bf16 v[124:127], v[132:135], v[184:187], v[124:127]
	v_mfma_f32_16x16x32_bf16 v[120:123], v[140:143], v[184:187], v[120:123]
	v_mfma_f32_16x16x32_bf16 v[108:111], v[132:135], v[198:201], v[108:111]
	v_mfma_f32_16x16x32_bf16 v[104:107], v[140:143], v[198:201], v[104:107]
	v_mfma_f32_16x16x32_bf16 v[92:95], v[132:135], v[206:209], v[92:95]
	v_mfma_f32_16x16x32_bf16 v[88:91], v[140:143], v[206:209], v[88:91]
	v_mfma_f32_16x16x32_bf16 v[76:79], v[132:135], v[214:217], v[76:79]
	v_mfma_f32_16x16x32_bf16 v[72:75], v[140:143], v[214:217], v[72:75]
	s_setprio 0
	s_setprio 1
	v_mfma_f32_16x16x32_bf16 v[116:119], v[144:147], v[180:183], v[116:119]
	v_mfma_f32_16x16x32_bf16 v[112:115], v[172:175], v[180:183], v[112:115]
	v_mfma_f32_16x16x32_bf16 v[100:103], v[144:147], v[194:197], v[100:103]
	v_mfma_f32_16x16x32_bf16 v[96:99], v[172:175], v[194:197], v[96:99]
	v_mfma_f32_16x16x32_bf16 v[84:87], v[144:147], v[202:205], v[84:87]
	v_mfma_f32_16x16x32_bf16 v[80:83], v[172:175], v[202:205], v[80:83]
	v_mfma_f32_16x16x32_bf16 v[68:71], v[144:147], v[210:213], v[68:71]
	v_mfma_f32_16x16x32_bf16 v[64:67], v[172:175], v[210:213], v[64:67]
	v_mfma_f32_16x16x32_bf16 v[116:119], v[148:151], v[184:187], v[116:119]
	v_mfma_f32_16x16x32_bf16 v[112:115], v[176:179], v[184:187], v[112:115]
	v_mfma_f32_16x16x32_bf16 v[100:103], v[148:151], v[198:201], v[100:103]
	v_mfma_f32_16x16x32_bf16 v[96:99], v[176:179], v[198:201], v[96:99]
	v_mfma_f32_16x16x32_bf16 v[84:87], v[148:151], v[206:209], v[84:87]
	v_mfma_f32_16x16x32_bf16 v[80:83], v[176:179], v[206:209], v[80:83]
	v_mfma_f32_16x16x32_bf16 v[68:71], v[148:151], v[214:217], v[68:71]
	v_mfma_f32_16x16x32_bf16 v[64:67], v[176:179], v[214:217], v[64:67]
	s_setprio 0
	s_barrier
; #define PG8_STAGE(bufoff, gbase, voff) do { _Pragma("unroll") for (int _i = 0; _i < 2; ++_i) \
;         __builtin_amdgcn_global_load_lds((const unsigned*)((const char*)(gbase) + (voff)[_i]), (PG8_LAS unsigned*)(lds + (bufoff) + ldsw + _i * 8192), 16, 0, 0); } while (0)
; #define PG8_LDA(dst, b, h) do { _Pragma("unroll") for (int m = 0; m < 4; ++m) _Pragma("unroll") for (int k = 0; k < 2; ++k) dst[m][k] = *(const PG8_LAS bf16x8*)(lds + PG8_SA(b, h) + aoff + m * 2048 + k * 1024); } while (0)
; #define PG8_LDB(dst, b, h) do { _Pragma("unroll") for (int n = 0; n < 2; ++n) _Pragma("unroll") for (int k = 0; k < 2; ++k) dst[n][k] = *(const PG8_LAS bf16x8*)(lds + PG8_SB(b, h) + boff + n * 2048 + k * 1024); } while (0)
; #define PG8_MMA(ai, bj, At, Bt) do { __builtin_amdgcn_s_setprio(1); _Pragma("unroll") for (int m = 0; m < 4; ++m) _Pragma("unroll") for (int n = 0; n < 2; ++n) _Pragma("unroll") for (int k = 0; k < 2; ++k) \
;         acc[ai][bj][m][n] = __builtin_amdgcn_mfma_f32_16x16x32_bf16(Bt[n][k], At[m][k], acc[ai][bj][m][n], 0, 0, 0); __builtin_amdgcn_s_setprio(0); } while (0)
; #define PG8_WAIT_V(n) asm volatile("s_waitcnt vmcnt(" #n ")" ::: "memory")
; #define PG8_WAIT_L(n) asm volatile("s_waitcnt lgkmcnt(" #n ")" ::: "memory")
; #define PG8_BAR __builtin_amdgcn_s_barrier()
; #define PG8_SCHED __builtin_amdgcn_sched_barrier(0)
; template <class Epi, class Sched, bool ALIGN_EPI = false, bool SP2 = false>
; __device__ __forceinline__ void gemm_phase(PG8_LAS unsigned char* lds, const Gemm g, const Sched& S, const Epi& E, const int wid) {
;     ...
;             PG8_LDA(At, 0, 1); PG8_STAGE(PG8_SB(0, 0), b2, voffB); PG8_STAGE(PG8_SB(0, 1), b2 + hstepB, voffB); PG8_STAGE(PG8_SA(0, 0), a2, voffA);
;             PG8_WAIT_V(8); PG8_WAIT_L(0); PG8_BAR; PG8_MMA(1, 0, At, B0); PG8_MMA(1, 1, At, B1); PG8_BAR; PG8_SCHED;
;             PG8_LDB(B0, 1, 0); PG8_LDB(B1, 1, 1); PG8_SCHED; PG8_LDA(At, 1, 0); PG8_STAGE(PG8_SA(0, 1), a2 + hstepA, voffA);
	s_add_i32 s61, s49, s39
	s_add_u32 s98, s34, 0x80
	s_addc_u32 s99, s35, 0
	s_mov_b32 m0, s61
	ds_read_b128 v[180:183], v192 offset:16384
	ds_read_b128 v[184:187], v192 offset:17408
	ds_read_b128 v[194:197], v192 offset:18432
	ds_read_b128 v[198:201], v192 offset:19456
	ds_read_b128 v[202:205], v192 offset:20480
	ds_read_b128 v[206:209], v192 offset:21504
	ds_read_b128 v[210:213], v192 offset:22528
	ds_read_b128 v[214:217], v192 offset:23552
	global_load_lds_dwordx4 v154, s[34:35]
	s_add_i32 m0, s61, 0x2000
	s_add_u32 s62, s34, 0x40000
	s_addc_u32 s63, s35, 0
	s_add_i32 s61, s56, s39
	global_load_lds_dwordx4 v158, s[34:35]
	s_mov_b32 m0, s61
	s_add_u32 s100, s36, 0x80
	s_addc_u32 s101, s37, 0
	global_load_lds_dwordx4 v154, s[62:63]
	s_add_i32 m0, s61, 0x2000
	s_nop 0
	global_load_lds_dwordx4 v158, s[62:63]
	s_mov_b32 m0, s40
	s_nop 0
	global_load_lds_dwordx4 v152, s[36:37]
	s_mov_b32 m0, s41
	s_nop 0
	global_load_lds_dwordx4 v156, s[36:37]
	s_waitcnt vmcnt(8) lgkmcnt(0)
	s_barrier
	s_setprio 1
	v_mfma_f32_16x16x32_bf16 v[60:63], v[128:131], v[180:183], v[60:63]
	v_mfma_f32_16x16x32_bf16 v[56:59], v[136:139], v[180:183], v[56:59]
	v_mfma_f32_16x16x32_bf16 v[44:47], v[128:131], v[194:197], v[44:47]
	v_mfma_f32_16x16x32_bf16 v[40:43], v[136:139], v[194:197], v[40:43]
	v_mfma_f32_16x16x32_bf16 v[28:31], v[128:131], v[202:205], v[28:31]
	v_mfma_f32_16x16x32_bf16 v[24:27], v[136:139], v[202:205], v[24:27]
	v_mfma_f32_16x16x32_bf16 v[12:15], v[128:131], v[210:213], v[12:15]
	v_mfma_f32_16x16x32_bf16 v[8:11], v[136:139], v[210:213], v[8:11]
	v_mfma_f32_16x16x32_bf16 v[60:63], v[132:135], v[184:187], v[60:63]
	v_mfma_f32_16x16x32_bf16 v[56:59], v[140:143], v[184:187], v[56:59]
	v_mfma_f32_16x16x32_bf16 v[44:47], v[132:135], v[198:201], v[44:47]
	v_mfma_f32_16x16x32_bf16 v[40:43], v[140:143], v[198:201], v[40:43]
	v_mfma_f32_16x16x32_bf16 v[28:31], v[132:135], v[206:209], v[28:31]
	v_mfma_f32_16x16x32_bf16 v[24:27], v[140:143], v[206:209], v[24:27]
	v_mfma_f32_16x16x32_bf16 v[12:15], v[132:135], v[214:217], v[12:15]
	v_mfma_f32_16x16x32_bf16 v[8:11], v[140:143], v[214:217], v[8:11]
	s_setprio 0
	s_setprio 1
	v_mfma_f32_16x16x32_bf16 v[52:55], v[144:147], v[180:183], v[52:55]
	v_mfma_f32_16x16x32_bf16 v[48:51], v[172:175], v[180:183], v[48:51]
	v_mfma_f32_16x16x32_bf16 v[36:39], v[144:147], v[194:197], v[36:39]
	v_mfma_f32_16x16x32_bf16 v[32:35], v[172:175], v[194:197], v[32:35]
	v_mfma_f32_16x16x32_bf16 v[20:23], v[144:147], v[202:205], v[20:23]
	v_mfma_f32_16x16x32_bf16 v[16:19], v[172:175], v[202:205], v[16:19]
	v_mfma_f32_16x16x32_bf16 v[4:7], v[144:147], v[210:213], v[4:7]
	v_mfma_f32_16x16x32_bf16 v[0:3], v[172:175], v[210:213], v[0:3]
	v_mfma_f32_16x16x32_bf16 v[52:55], v[148:151], v[184:187], v[52:55]
	v_mfma_f32_16x16x32_bf16 v[48:51], v[176:179], v[184:187], v[48:51]
	v_mfma_f32_16x16x32_bf16 v[36:39], v[148:151], v[198:201], v[36:39]
	v_mfma_f32_16x16x32_bf16 v[32:35], v[176:179], v[198:201], v[32:35]
	v_mfma_f32_16x16x32_bf16 v[20:23], v[148:151], v[206:209], v[20:23]
	v_mfma_f32_16x16x32_bf16 v[16:19], v[176:179], v[206:209], v[16:19]
	v_mfma_f32_16x16x32_bf16 v[4:7], v[148:151], v[214:217], v[4:7]
	v_mfma_f32_16x16x32_bf16 v[0:3], v[176:179], v[214:217], v[0:3]
	s_setprio 0
	s_barrier
	s_add_i32 s61, 0, 0x18000
	s_add_i32 s62, 0, 0x1c000
	ds_read_b128 v[128:131], v252
	ds_read_b128 v[132:135], v252 offset:1024
	ds_read_b128 v[136:139], v252 offset:2048
	ds_read_b128 v[140:143], v252 offset:3072
	ds_read_b128 v[144:147], v253
	ds_read_b128 v[148:151], v253 offset:1024
	ds_read_b128 v[172:175], v253 offset:2048
	ds_read_b128 v[176:179], v253 offset:3072
	s_add_u32 s36, s36, 0x40000
	s_addc_u32 s37, s37, 0
	s_mov_b32 m0, s42
	ds_read_b128 v[180:183], v192 offset:32768
	ds_read_b128 v[184:187], v192 offset:33792
	ds_read_b128 v[194:197], v192 offset:34816
	ds_read_b128 v[198:201], v192 offset:35840
	ds_read_b128 v[202:205], v192 offset:36864
	ds_read_b128 v[206:209], v192 offset:37888
	ds_read_b128 v[210:213], v192 offset:38912
	ds_read_b128 v[214:217], v192 offset:39936
	global_load_lds_dwordx4 v152, s[36:37]
	s_mov_b32 m0, s43
	s_nop 0
	global_load_lds_dwordx4 v156, s[36:37]
	s_waitcnt vmcnt(8) lgkmcnt(0)
	s_barrier
; #define PG8_STAGE(bufoff, gbase, voff) do { _Pragma("unroll") for (int _i = 0; _i < 2; ++_i) \
;         __builtin_amdgcn_global_load_lds((const unsigned*)((const char*)(gbase) + (voff)[_i]), (PG8_LAS unsigned*)(lds + (bufoff) + ldsw + _i * 8192), 16, 0, 0); } while (0)
; #define PG8_LDA(dst, b, h) do { _Pragma("unroll") for (int m = 0; m < 4; ++m) _Pragma("unroll") for (int k = 0; k < 2; ++k) dst[m][k] = *(const PG8_LAS bf16x8*)(lds + PG8_SA(b, h) + aoff + m * 2048 + k * 1024); } while (0)
; #define PG8_MMA(ai, bj, At, Bt) do { __builtin_amdgcn_s_setprio(1); _Pragma("unroll") for (int m = 0; m < 4; ++m) _Pragma("unroll") for (int n = 0; n < 2; ++n) _Pragma("unroll") for (int k = 0; k < 2; ++k) \
;         acc[ai][bj][m][n] = __builtin_amdgcn_mfma_f32_16x16x32_bf16(Bt[n][k], At[m][k], acc[ai][bj][m][n], 0, 0, 0); __builtin_amdgcn_s_setprio(0); } while (0)
; #define PG8_WAIT_V(n) asm volatile("s_waitcnt vmcnt(" #n ")" ::: "memory")
; #define PG8_WAIT_L(n) asm volatile("s_waitcnt lgkmcnt(" #n ")" ::: "memory")
; #define PG8_BAR __builtin_amdgcn_s_barrier()
; #define PG8_SCHED __builtin_amdgcn_sched_barrier(0)
; template <class Epi, class Sched, bool ALIGN_EPI = false, bool SP2 = false>
; __device__ __forceinline__ void gemm_phase(PG8_LAS unsigned char* lds, const Gemm g, const Sched& S, const Epi& E, const int wid) {
;     ...
;             PG8_WAIT_V(8); PG8_WAIT_L(0); PG8_BAR; PG8_MMA(0, 0, At, B0); PG8_MMA(0, 1, At, B1); PG8_BAR; PG8_SCHED;
;             PG8_LDA(At, 1, 1); PG8_STAGE(PG8_SB(1, 0), b3, voffB); PG8_STAGE(PG8_SB(1, 1), b3 + hstepB, voffB); PG8_STAGE(PG8_SA(1, 0), a3, voffA);
;             PG8_WAIT_V(8); PG8_WAIT_L(0); PG8_BAR; PG8_MMA(1, 0, At, B0); PG8_MMA(1, 1, At, B1); PG8_BAR; PG8_SCHED;
;     ...
;         if constexpr (ALIGN_EPI) { if (wr == 0) PG8_BAR; }
	s_setprio 1
	v_mfma_f32_16x16x32_bf16 v[124:127], v[128:131], v[180:183], v[124:127]
	v_mfma_f32_16x16x32_bf16 v[120:123], v[136:139], v[180:183], v[120:123]
	v_mfma_f32_16x16x32_bf16 v[108:111], v[128:131], v[194:197], v[108:111]
	v_mfma_f32_16x16x32_bf16 v[104:107], v[136:139], v[194:197], v[104:107]
	v_mfma_f32_16x16x32_bf16 v[92:95], v[128:131], v[202:205], v[92:95]
	v_mfma_f32_16x16x32_bf16 v[88:91], v[136:139], v[202:205], v[88:91]
	v_mfma_f32_16x16x32_bf16 v[76:79], v[128:131], v[210:213], v[76:79]
	v_mfma_f32_16x16x32_bf16 v[72:75], v[136:139], v[210:213], v[72:75]
	v_mfma_f32_16x16x32_bf16 v[124:127], v[132:135], v[184:187], v[124:127]
	v_mfma_f32_16x16x32_bf16 v[120:123], v[140:143], v[184:187], v[120:123]
	v_mfma_f32_16x16x32_bf16 v[108:111], v[132:135], v[198:201], v[108:111]
	v_mfma_f32_16x16x32_bf16 v[104:107], v[140:143], v[198:201], v[104:107]
	v_mfma_f32_16x16x32_bf16 v[92:95], v[132:135], v[206:209], v[92:95]
	v_mfma_f32_16x16x32_bf16 v[88:91], v[140:143], v[206:209], v[88:91]
	v_mfma_f32_16x16x32_bf16 v[76:79], v[132:135], v[214:217], v[76:79]
	v_mfma_f32_16x16x32_bf16 v[72:75], v[140:143], v[214:217], v[72:75]
	s_setprio 0
	s_setprio 1
	v_mfma_f32_16x16x32_bf16 v[116:119], v[144:147], v[180:183], v[116:119]
	v_mfma_f32_16x16x32_bf16 v[112:115], v[172:175], v[180:183], v[112:115]
	v_mfma_f32_16x16x32_bf16 v[100:103], v[144:147], v[194:197], v[100:103]
	v_mfma_f32_16x16x32_bf16 v[96:99], v[172:175], v[194:197], v[96:99]
	v_mfma_f32_16x16x32_bf16 v[84:87], v[144:147], v[202:205], v[84:87]
	v_mfma_f32_16x16x32_bf16 v[80:83], v[172:175], v[202:205], v[80:83]
	v_mfma_f32_16x16x32_bf16 v[68:71], v[144:147], v[210:213], v[68:71]
	v_mfma_f32_16x16x32_bf16 v[64:67], v[172:175], v[210:213], v[64:67]
	v_mfma_f32_16x16x32_bf16 v[116:119], v[148:151], v[184:187], v[116:119]
	v_mfma_f32_16x16x32_bf16 v[112:115], v[176:179], v[184:187], v[112:115]
	v_mfma_f32_16x16x32_bf16 v[100:103], v[148:151], v[198:201], v[100:103]
	v_mfma_f32_16x16x32_bf16 v[96:99], v[176:179], v[198:201], v[96:99]
	v_mfma_f32_16x16x32_bf16 v[84:87], v[148:151], v[206:209], v[84:87]
	v_mfma_f32_16x16x32_bf16 v[80:83], v[176:179], v[206:209], v[80:83]
	v_mfma_f32_16x16x32_bf16 v[68:71], v[148:151], v[214:217], v[68:71]
	v_mfma_f32_16x16x32_bf16 v[64:67], v[176:179], v[214:217], v[64:67]
	s_setprio 0
	s_barrier
	s_add_i32 s36, s61, s39
	s_mov_b32 m0, s36
	ds_read_b128 v[180:183], v192 offset:49152
	ds_read_b128 v[184:187], v192 offset:50176
	ds_read_b128 v[194:197], v192 offset:51200
	ds_read_b128 v[198:201], v192 offset:52224
	ds_read_b128 v[202:205], v192 offset:53248
	ds_read_b128 v[206:209], v192 offset:54272
	ds_read_b128 v[210:213], v192 offset:55296
	ds_read_b128 v[214:217], v192 offset:56320
	global_load_lds_dwordx4 v154, s[98:99]
	s_add_i32 m0, s36, 0x2000
	s_add_u32 s34, s34, 0x40080
	s_addc_u32 s35, s35, 0
	s_add_i32 s36, s62, s39
	global_load_lds_dwordx4 v158, s[98:99]
	s_mov_b32 m0, s36
	s_nop 0
	global_load_lds_dwordx4 v154, s[34:35]
	s_add_i32 m0, s36, 0x2000
	s_nop 0
	global_load_lds_dwordx4 v158, s[34:35]
	s_mov_b32 m0, s45
	s_nop 0
	global_load_lds_dwordx4 v152, s[100:101]
	s_mov_b32 m0, s46
	s_nop 0
	global_load_lds_dwordx4 v156, s[100:101]
	s_waitcnt vmcnt(8) lgkmcnt(0)
	s_barrier
	s_setprio 1
	v_mfma_f32_16x16x32_bf16 v[60:63], v[128:131], v[180:183], v[60:63]
	v_mfma_f32_16x16x32_bf16 v[56:59], v[136:139], v[180:183], v[56:59]
	v_mfma_f32_16x16x32_bf16 v[44:47], v[128:131], v[194:197], v[44:47]
	v_mfma_f32_16x16x32_bf16 v[40:43], v[136:139], v[194:197], v[40:43]
	v_mfma_f32_16x16x32_bf16 v[28:31], v[128:131], v[202:205], v[28:31]
	v_mfma_f32_16x16x32_bf16 v[24:27], v[136:139], v[202:205], v[24:27]
	v_mfma_f32_16x16x32_bf16 v[12:15], v[128:131], v[210:213], v[12:15]
	v_mfma_f32_16x16x32_bf16 v[8:11], v[136:139], v[210:213], v[8:11]
	v_mfma_f32_16x16x32_bf16 v[60:63], v[132:135], v[184:187], v[60:63]
	v_mfma_f32_16x16x32_bf16 v[56:59], v[140:143], v[184:187], v[56:59]
	v_mfma_f32_16x16x32_bf16 v[44:47], v[132:135], v[198:201], v[44:47]
	v_mfma_f32_16x16x32_bf16 v[40:43], v[140:143], v[198:201], v[40:43]
	v_mfma_f32_16x16x32_bf16 v[28:31], v[132:135], v[206:209], v[28:31]
	v_mfma_f32_16x16x32_bf16 v[24:27], v[140:143], v[206:209], v[24:27]
	v_mfma_f32_16x16x32_bf16 v[12:15], v[132:135], v[214:217], v[12:15]
	v_mfma_f32_16x16x32_bf16 v[8:11], v[140:143], v[214:217], v[8:11]
	s_setprio 0
	s_setprio 1
	v_mfma_f32_16x16x32_bf16 v[52:55], v[144:147], v[180:183], v[52:55]
	v_mfma_f32_16x16x32_bf16 v[48:51], v[172:175], v[180:183], v[48:51]
	v_mfma_f32_16x16x32_bf16 v[36:39], v[144:147], v[194:197], v[36:39]
	v_mfma_f32_16x16x32_bf16 v[32:35], v[172:175], v[194:197], v[32:35]
	v_mfma_f32_16x16x32_bf16 v[20:23], v[144:147], v[202:205], v[20:23]
	v_mfma_f32_16x16x32_bf16 v[16:19], v[172:175], v[202:205], v[16:19]
	v_mfma_f32_16x16x32_bf16 v[4:7], v[144:147], v[210:213], v[4:7]
	v_mfma_f32_16x16x32_bf16 v[0:3], v[172:175], v[210:213], v[0:3]
	v_mfma_f32_16x16x32_bf16 v[52:55], v[148:151], v[184:187], v[52:55]
	v_mfma_f32_16x16x32_bf16 v[48:51], v[176:179], v[184:187], v[48:51]
	v_mfma_f32_16x16x32_bf16 v[36:39], v[148:151], v[198:201], v[36:39]
	v_mfma_f32_16x16x32_bf16 v[32:35], v[176:179], v[198:201], v[32:35]
	v_mfma_f32_16x16x32_bf16 v[20:23], v[148:151], v[206:209], v[20:23]
	v_mfma_f32_16x16x32_bf16 v[16:19], v[176:179], v[206:209], v[16:19]
	v_mfma_f32_16x16x32_bf16 v[4:7], v[148:151], v[214:217], v[4:7]
	v_mfma_f32_16x16x32_bf16 v[0:3], v[176:179], v[214:217], v[0:3]
	s_setprio 0
	s_barrier
	s_add_i32 s60, s60, 2
	s_add_u32 s30, s30, 0x100
	s_addc_u32 s31, s31, 0
	s_add_u32 s58, s58, 0x100
	s_addc_u32 s59, s59, 0
	s_cmp_gt_u32 s60, 13
	s_cbranch_scc0 .LBB0_2725
	s_and_b64 vcc, exec, s[16:17]
	s_cbranch_vccz .LBB0_2728
	s_barrier

; #define PG8_STAGE(bufoff, gbase, voff) do { _Pragma("unroll") for (int _i = 0; _i < 2; ++_i) \
;         __builtin_amdgcn_global_load_lds((const unsigned*)((const char*)(gbase) + (voff)[_i]), (PG8_LAS unsigned*)(lds + (bufoff) + ldsw + _i * 8192), 16, 0, 0); } while (0)
; #define PG8_LDA(dst, b, h) do { _Pragma("unroll") for (int m = 0; m < 4; ++m) _Pragma("unroll") for (int k = 0; k < 2; ++k) dst[m][k] = *(const PG8_LAS bf16x8*)(lds + PG8_SA(b, h) + aoff + m * 2048 + k * 1024); } while (0)
; #define PG8_LDB(dst, b, h) do { _Pragma("unroll") for (int n = 0; n < 2; ++n) _Pragma("unroll") for (int k = 0; k < 2; ++k) dst[n][k] = *(const PG8_LAS bf16x8*)(lds + PG8_SB(b, h) + boff + n * 2048 + k * 1024); } while (0)
; #define PG8_MMA(ai, bj, At, Bt) do { __builtin_amdgcn_s_setprio(1); _Pragma("unroll") for (int m = 0; m < 4; ++m) _Pragma("unroll") for (int n = 0; n < 2; ++n) _Pragma("unroll") for (int k = 0; k < 2; ++k) \
;         acc[ai][bj][m][n] = __builtin_amdgcn_mfma_f32_16x16x32_bf16(Bt[n][k], At[m][k], acc[ai][bj][m][n], 0, 0, 0); __builtin_amdgcn_s_setprio(0); } while (0)
; template <class Epi, class Sched, bool ALIGN_EPI = false, bool SP2 = false>
; __device__ __forceinline__ void gemm_phase(PG8_LAS unsigned char* lds, const Gemm g, const Sched& S, const Epi& E, const int wid) {
;     ...
;         const bool has_next = S.next(ui + 1, nxt);
;         const char* nA = has_next ? (const char*)g.A + (size_t)nxt.pm * tstepA : cA; const char* nB = has_next ? (const char*)g.Bt + (size_t)nxt.pn * tstepB : cB;
;         for (int t = 0; t < nt; t += 2) {
;             const bool last = (t == nt - 2);
;             const char* a1 = cA + (size_t)(t + 1) * kstep;
;             const char* a2 = last ? nA : cA + (size_t)(t + 2) * kstep; const char* b2 = last ? nB : cB + (size_t)(t + 2) * kstep;
;             const char* a3 = a2 + kstep; const char* b3 = b2 + kstep;
;             if (last && has_next) S.a_ready(nxt);
;             if constexpr (SP2) {
;             PG8_LDB(B0, 0, 0); PG8_LDB(B1, 0, 1); PG8_SCHED; PG8_LDA(At, 0, 0); PG8_STAGE(PG8_SA(1, 1), a1 + hstepA, voffA);
;             PG8_WAIT_V(8); PG8_WAIT_L(0); PG8_BAR; PG8_MMA(0, 0, At, B0); PG8_MMA(0, 1, At, B1); PG8_BAR; PG8_SCHED;
;             PG8_LDA(At, 0, 1); PG8_STAGE(PG8_SB(0, 0), b2, voffB); PG8_STAGE(PG8_SB(0, 1), b2 + hstepB, voffB); PG8_STAGE(PG8_SA(0, 0), a2, voffA);
.LBB0_2811:
	s_ashr_i32 s17, s16, 31
	s_lshl_b64 s[18:19], s[16:17], 19
	s_add_u32 s18, s0, s18
	s_addc_u32 s19, s1, s19
	s_and_b64 s[20:21], s[2:3], exec
	s_cselect_b32 s17, s19, s25
	s_cselect_b32 s47, s18, s24
	s_ashr_i32 s15, s14, 31
	s_lshl_b64 s[20:21], s[14:15], 19
	s_add_u32 s20, s30, s20
	s_addc_u32 s21, s31, s21
	s_and_b64 s[28:29], s[2:3], exec
	s_cselect_b32 s15, s21, s27
	s_cselect_b32 s48, s20, s26
	s_add_u32 s24, s24, 0x40080
	s_addc_u32 s25, s25, 0
	s_add_u32 s49, s26, 0x100
	s_addc_u32 s56, s27, 0
	s_mov_b32 s57, -2
	v_add_u32_e32 v252, 0x18000, v165
	v_add_u32_e32 v253, 0x1c000, v165
	ds_read_b128 v[148:151], v166
	ds_read_b128 v[152:155], v166 offset:1024
	ds_read_b128 v[156:159], v166 offset:2048
	ds_read_b128 v[160:163], v166 offset:3072
	ds_read_b128 v[172:175], v167
	ds_read_b128 v[176:179], v167 offset:1024
	ds_read_b128 v[180:183], v167 offset:2048
	ds_read_b128 v[184:187], v167 offset:3072
	s_add_u32 s26, s24, 0xfffc0080
	s_addc_u32 s27, s25, -1
	s_cmp_eq_u32 s57, 12
	s_cselect_b32 s29, s17, s27
	s_cselect_b32 s28, s47, s26
	s_cselect_b32 s27, s15, s56
	s_cselect_b32 s26, s48, s49
	s_add_i32 m0, s36, 0xc000
	ds_read_b128 v[188:191], v168
	ds_read_b128 v[192:195], v168 offset:1024
	ds_read_b128 v[196:199], v168 offset:2048
	ds_read_b128 v[200:203], v168 offset:3072
	ds_read_b128 v[204:207], v168 offset:4096
	ds_read_b128 v[208:211], v168 offset:5120
	ds_read_b128 v[212:215], v168 offset:6144
	ds_read_b128 v[216:219], v168 offset:7168
	global_load_lds_dwordx4 v140, s[24:25]
	s_add_i32 m0, s36, 0xe000
	s_nop 0
	global_load_lds_dwordx4 v142, s[24:25]
	s_waitcnt vmcnt(8) lgkmcnt(0)
	s_barrier
	s_setprio 1
	v_mfma_f32_16x16x32_bf16 v[124:127], v[148:151], v[188:191], 0
	v_mfma_f32_16x16x32_bf16 v[116:119], v[156:159], v[188:191], 0
	v_mfma_f32_16x16x32_bf16 v[108:111], v[148:151], v[196:199], 0
	v_mfma_f32_16x16x32_bf16 v[100:103], v[156:159], v[196:199], 0
	v_mfma_f32_16x16x32_bf16 v[92:95], v[148:151], v[204:207], 0
	v_mfma_f32_16x16x32_bf16 v[84:87], v[156:159], v[204:207], 0
	v_mfma_f32_16x16x32_bf16 v[76:79], v[148:151], v[212:215], 0
	v_mfma_f32_16x16x32_bf16 v[68:71], v[156:159], v[212:215], 0
	v_mfma_f32_16x16x32_bf16 v[124:127], v[152:155], v[192:195], v[124:127]
	v_mfma_f32_16x16x32_bf16 v[116:119], v[160:163], v[192:195], v[116:119]
	v_mfma_f32_16x16x32_bf16 v[108:111], v[152:155], v[200:203], v[108:111]
	v_mfma_f32_16x16x32_bf16 v[100:103], v[160:163], v[200:203], v[100:103]
	v_mfma_f32_16x16x32_bf16 v[92:95], v[152:155], v[208:211], v[92:95]
	v_mfma_f32_16x16x32_bf16 v[84:87], v[160:163], v[208:211], v[84:87]
	v_mfma_f32_16x16x32_bf16 v[76:79], v[152:155], v[216:219], v[76:79]
	v_mfma_f32_16x16x32_bf16 v[68:71], v[160:163], v[216:219], v[68:71]
	s_setprio 0
	s_setprio 1
	v_mfma_f32_16x16x32_bf16 v[120:123], v[172:175], v[188:191], 0
	v_mfma_f32_16x16x32_bf16 v[112:115], v[180:183], v[188:191], 0
	v_mfma_f32_16x16x32_bf16 v[104:107], v[172:175], v[196:199], 0
	v_mfma_f32_16x16x32_bf16 v[96:99], v[180:183], v[196:199], 0
	v_mfma_f32_16x16x32_bf16 v[88:91], v[172:175], v[204:207], 0
	v_mfma_f32_16x16x32_bf16 v[80:83], v[180:183], v[204:207], 0
	v_mfma_f32_16x16x32_bf16 v[72:75], v[172:175], v[212:215], 0
	v_mfma_f32_16x16x32_bf16 v[64:67], v[180:183], v[212:215], 0
	v_mfma_f32_16x16x32_bf16 v[120:123], v[176:179], v[192:195], v[120:123]
	v_mfma_f32_16x16x32_bf16 v[112:115], v[184:187], v[192:195], v[112:115]
	v_mfma_f32_16x16x32_bf16 v[104:107], v[176:179], v[200:203], v[104:107]
	v_mfma_f32_16x16x32_bf16 v[96:99], v[184:187], v[200:203], v[96:99]
	v_mfma_f32_16x16x32_bf16 v[88:91], v[176:179], v[208:211], v[88:91]
	v_mfma_f32_16x16x32_bf16 v[80:83], v[184:187], v[208:211], v[80:83]
	v_mfma_f32_16x16x32_bf16 v[72:75], v[176:179], v[216:219], v[72:75]
	v_mfma_f32_16x16x32_bf16 v[64:67], v[184:187], v[216:219], v[64:67]
	s_setprio 0
	s_barrier
	s_add_i32 s58, s43, s33
	s_add_u32 s98, s26, 0x80
	s_addc_u32 s99, s27, 0
	s_mov_b32 m0, s58
	ds_read_b128 v[188:191], v168 offset:16384
	ds_read_b128 v[192:195], v168 offset:17408
	ds_read_b128 v[196:199], v168 offset:18432
	ds_read_b128 v[200:203], v168 offset:19456
	ds_read_b128 v[204:207], v168 offset:20480
	ds_read_b128 v[208:211], v168 offset:21504
	ds_read_b128 v[212:215], v168 offset:22528
	ds_read_b128 v[216:219], v168 offset:23552
	global_load_lds_dwordx4 v132, s[26:27]
	s_add_i32 m0, s58, 0x2000
	s_add_u32 s58, s26, 0x40000
	s_addc_u32 s59, s27, 0
	s_add_i32 s60, s44, s33
	global_load_lds_dwordx4 v128, s[26:27]
	s_mov_b32 m0, s60
	s_add_u32 s100, s28, 0x80
	s_addc_u32 s101, s29, 0
	global_load_lds_dwordx4 v132, s[58:59]
	s_add_i32 m0, s60, 0x2000
	s_nop 0
	global_load_lds_dwordx4 v128, s[58:59]
	s_mov_b32 m0, s36
	s_nop 0
	global_load_lds_dwordx4 v134, s[28:29]
	s_mov_b32 m0, s37
	s_nop 0
	global_load_lds_dwordx4 v130, s[28:29]
	s_waitcnt vmcnt(8) lgkmcnt(0)
	s_barrier
; #define PG8_STAGE(bufoff, gbase, voff) do { _Pragma("unroll") for (int _i = 0; _i < 2; ++_i) \
;         __builtin_amdgcn_global_load_lds((const unsigned*)((const char*)(gbase) + (voff)[_i]), (PG8_LAS unsigned*)(lds + (bufoff) + ldsw + _i * 8192), 16, 0, 0); } while (0)
; #define PG8_LDA(dst, b, h) do { _Pragma("unroll") for (int m = 0; m < 4; ++m) _Pragma("unroll") for (int k = 0; k < 2; ++k) dst[m][k] = *(const PG8_LAS bf16x8*)(lds + PG8_SA(b, h) + aoff + m * 2048 + k * 1024); } while (0)
; #define PG8_LDB(dst, b, h) do { _Pragma("unroll") for (int n = 0; n < 2; ++n) _Pragma("unroll") for (int k = 0; k < 2; ++k) dst[n][k] = *(const PG8_LAS bf16x8*)(lds + PG8_SB(b, h) + boff + n * 2048 + k * 1024); } while (0)
; #define PG8_MMA(ai, bj, At, Bt) do { __builtin_amdgcn_s_setprio(1); _Pragma("unroll") for (int m = 0; m < 4; ++m) _Pragma("unroll") for (int n = 0; n < 2; ++n) _Pragma("unroll") for (int k = 0; k < 2; ++k) \
;         acc[ai][bj][m][n] = __builtin_amdgcn_mfma_f32_16x16x32_bf16(Bt[n][k], At[m][k], acc[ai][bj][m][n], 0, 0, 0); __builtin_amdgcn_s_setprio(0); } while (0)
; #define PG8_WAIT_V(n) asm volatile("s_waitcnt vmcnt(" #n ")" ::: "memory")
; #define PG8_WAIT_L(n) asm volatile("s_waitcnt lgkmcnt(" #n ")" ::: "memory")
; #define PG8_BAR __builtin_amdgcn_s_barrier()
; #define PG8_SCHED __builtin_amdgcn_sched_barrier(0)
; template <class Epi, class Sched, bool ALIGN_EPI = false, bool SP2 = false>
; __device__ __forceinline__ void gemm_phase(PG8_LAS unsigned char* lds, const Gemm g, const Sched& S, const Epi& E, const int wid) {
;     ...
;             PG8_WAIT_V(8); PG8_WAIT_L(0); PG8_BAR; PG8_MMA(1, 0, At, B0); PG8_MMA(1, 1, At, B1); PG8_BAR; PG8_SCHED;
;             PG8_LDB(B0, 1, 0); PG8_LDB(B1, 1, 1); PG8_SCHED; PG8_LDA(At, 1, 0); PG8_STAGE(PG8_SA(0, 1), a2 + hstepA, voffA);
;             PG8_WAIT_V(8); PG8_WAIT_L(0); PG8_BAR; PG8_MMA(0, 0, At, B0); PG8_MMA(0, 1, At, B1); PG8_BAR; PG8_SCHED;
	s_setprio 1
	v_mfma_f32_16x16x32_bf16 v[60:63], v[148:151], v[188:191], 0
	v_mfma_f32_16x16x32_bf16 v[52:55], v[156:159], v[188:191], 0
	v_mfma_f32_16x16x32_bf16 v[44:47], v[148:151], v[196:199], 0
	v_mfma_f32_16x16x32_bf16 v[36:39], v[156:159], v[196:199], 0
	v_mfma_f32_16x16x32_bf16 v[28:31], v[148:151], v[204:207], 0
	v_mfma_f32_16x16x32_bf16 v[20:23], v[156:159], v[204:207], 0
	v_mfma_f32_16x16x32_bf16 v[12:15], v[148:151], v[212:215], 0
	v_mfma_f32_16x16x32_bf16 v[4:7], v[156:159], v[212:215], 0
	v_mfma_f32_16x16x32_bf16 v[60:63], v[152:155], v[192:195], v[60:63]
	v_mfma_f32_16x16x32_bf16 v[52:55], v[160:163], v[192:195], v[52:55]
	v_mfma_f32_16x16x32_bf16 v[44:47], v[152:155], v[200:203], v[44:47]
	v_mfma_f32_16x16x32_bf16 v[36:39], v[160:163], v[200:203], v[36:39]
	v_mfma_f32_16x16x32_bf16 v[28:31], v[152:155], v[208:211], v[28:31]
	v_mfma_f32_16x16x32_bf16 v[20:23], v[160:163], v[208:211], v[20:23]
	v_mfma_f32_16x16x32_bf16 v[12:15], v[152:155], v[216:219], v[12:15]
	v_mfma_f32_16x16x32_bf16 v[4:7], v[160:163], v[216:219], v[4:7]
	s_setprio 0
	s_setprio 1
	v_mfma_f32_16x16x32_bf16 v[56:59], v[172:175], v[188:191], 0
	v_mfma_f32_16x16x32_bf16 v[48:51], v[180:183], v[188:191], 0
	v_mfma_f32_16x16x32_bf16 v[40:43], v[172:175], v[196:199], 0
	v_mfma_f32_16x16x32_bf16 v[32:35], v[180:183], v[196:199], 0
	v_mfma_f32_16x16x32_bf16 v[24:27], v[172:175], v[204:207], 0
	v_mfma_f32_16x16x32_bf16 v[16:19], v[180:183], v[204:207], 0
	v_mfma_f32_16x16x32_bf16 v[8:11], v[172:175], v[212:215], 0
	v_mfma_f32_16x16x32_bf16 v[0:3], v[180:183], v[212:215], 0
	v_mfma_f32_16x16x32_bf16 v[56:59], v[176:179], v[192:195], v[56:59]
	v_mfma_f32_16x16x32_bf16 v[48:51], v[184:187], v[192:195], v[48:51]
	v_mfma_f32_16x16x32_bf16 v[40:43], v[176:179], v[200:203], v[40:43]
	v_mfma_f32_16x16x32_bf16 v[32:35], v[184:187], v[200:203], v[32:35]
	v_mfma_f32_16x16x32_bf16 v[24:27], v[176:179], v[208:211], v[24:27]
	v_mfma_f32_16x16x32_bf16 v[16:19], v[184:187], v[208:211], v[16:19]
	v_mfma_f32_16x16x32_bf16 v[8:11], v[176:179], v[216:219], v[8:11]
	v_mfma_f32_16x16x32_bf16 v[0:3], v[184:187], v[216:219], v[0:3]
	s_setprio 0
	s_barrier
	s_add_i32 s58, 0, 0x18000
	s_add_i32 s59, 0, 0x1c000
	ds_read_b128 v[148:151], v252
	ds_read_b128 v[152:155], v252 offset:1024
	ds_read_b128 v[156:159], v252 offset:2048
	ds_read_b128 v[160:163], v252 offset:3072
	ds_read_b128 v[172:175], v253
	ds_read_b128 v[176:179], v253 offset:1024
	ds_read_b128 v[180:183], v253 offset:2048
	ds_read_b128 v[184:187], v253 offset:3072
	s_add_u32 s28, s28, 0x40000
	s_addc_u32 s29, s29, 0
	s_mov_b32 m0, s38
	ds_read_b128 v[188:191], v168 offset:32768
	ds_read_b128 v[192:195], v168 offset:33792
	ds_read_b128 v[196:199], v168 offset:34816
	ds_read_b128 v[200:203], v168 offset:35840
	ds_read_b128 v[204:207], v168 offset:36864
	ds_read_b128 v[208:211], v168 offset:37888
	ds_read_b128 v[212:215], v168 offset:38912
	ds_read_b128 v[216:219], v168 offset:39936
	global_load_lds_dwordx4 v134, s[28:29]
	s_mov_b32 m0, s39
	s_nop 0
	global_load_lds_dwordx4 v130, s[28:29]
	s_waitcnt vmcnt(8) lgkmcnt(0)
	s_barrier
	s_setprio 1
	v_mfma_f32_16x16x32_bf16 v[124:127], v[148:151], v[188:191], v[124:127]
	v_mfma_f32_16x16x32_bf16 v[116:119], v[156:159], v[188:191], v[116:119]
	v_mfma_f32_16x16x32_bf16 v[108:111], v[148:151], v[196:199], v[108:111]
	v_mfma_f32_16x16x32_bf16 v[100:103], v[156:159], v[196:199], v[100:103]
	v_mfma_f32_16x16x32_bf16 v[92:95], v[148:151], v[204:207], v[92:95]
	v_mfma_f32_16x16x32_bf16 v[84:87], v[156:159], v[204:207], v[84:87]
	v_mfma_f32_16x16x32_bf16 v[76:79], v[148:151], v[212:215], v[76:79]
	v_mfma_f32_16x16x32_bf16 v[68:71], v[156:159], v[212:215], v[68:71]
	v_mfma_f32_16x16x32_bf16 v[124:127], v[152:155], v[192:195], v[124:127]
	v_mfma_f32_16x16x32_bf16 v[116:119], v[160:163], v[192:195], v[116:119]
	v_mfma_f32_16x16x32_bf16 v[108:111], v[152:155], v[200:203], v[108:111]
	v_mfma_f32_16x16x32_bf16 v[100:103], v[160:163], v[200:203], v[100:103]
	v_mfma_f32_16x16x32_bf16 v[92:95], v[152:155], v[208:211], v[92:95]
	v_mfma_f32_16x16x32_bf16 v[84:87], v[160:163], v[208:211], v[84:87]
	v_mfma_f32_16x16x32_bf16 v[76:79], v[152:155], v[216:219], v[76:79]
	v_mfma_f32_16x16x32_bf16 v[68:71], v[160:163], v[216:219], v[68:71]
	s_setprio 0
	s_setprio 1
	v_mfma_f32_16x16x32_bf16 v[120:123], v[172:175], v[188:191], v[120:123]
	v_mfma_f32_16x16x32_bf16 v[112:115], v[180:183], v[188:191], v[112:115]
	v_mfma_f32_16x16x32_bf16 v[104:107], v[172:175], v[196:199], v[104:107]
	v_mfma_f32_16x16x32_bf16 v[96:99], v[180:183], v[196:199], v[96:99]
	v_mfma_f32_16x16x32_bf16 v[88:91], v[172:175], v[204:207], v[88:91]
	v_mfma_f32_16x16x32_bf16 v[80:83], v[180:183], v[204:207], v[80:83]
	v_mfma_f32_16x16x32_bf16 v[72:75], v[172:175], v[212:215], v[72:75]
	v_mfma_f32_16x16x32_bf16 v[64:67], v[180:183], v[212:215], v[64:67]
	v_mfma_f32_16x16x32_bf16 v[120:123], v[176:179], v[192:195], v[120:123]
	v_mfma_f32_16x16x32_bf16 v[112:115], v[184:187], v[192:195], v[112:115]
	v_mfma_f32_16x16x32_bf16 v[104:107], v[176:179], v[200:203], v[104:107]
	v_mfma_f32_16x16x32_bf16 v[96:99], v[184:187], v[200:203], v[96:99]
	v_mfma_f32_16x16x32_bf16 v[88:91], v[176:179], v[208:211], v[88:91]
	v_mfma_f32_16x16x32_bf16 v[80:83], v[184:187], v[208:211], v[80:83]
	v_mfma_f32_16x16x32_bf16 v[72:75], v[176:179], v[216:219], v[72:75]
	v_mfma_f32_16x16x32_bf16 v[64:67], v[184:187], v[216:219], v[64:67]
	s_setprio 0
	s_barrier
; #define PG8_STAGE(bufoff, gbase, voff) do { _Pragma("unroll") for (int _i = 0; _i < 2; ++_i) \
;         __builtin_amdgcn_global_load_lds((const unsigned*)((const char*)(gbase) + (voff)[_i]), (PG8_LAS unsigned*)(lds + (bufoff) + ldsw + _i * 8192), 16, 0, 0); } while (0)
; #define PG8_LDA(dst, b, h) do { _Pragma("unroll") for (int m = 0; m < 4; ++m) _Pragma("unroll") for (int k = 0; k < 2; ++k) dst[m][k] = *(const PG8_LAS bf16x8*)(lds + PG8_SA(b, h) + aoff + m * 2048 + k * 1024); } while (0)
; #define PG8_WAIT_V(n) asm volatile("s_waitcnt vmcnt(" #n ")" ::: "memory")
; #define PG8_WAIT_L(n) asm volatile("s_waitcnt lgkmcnt(" #n ")" ::: "memory")
; #define PG8_BAR __builtin_amdgcn_s_barrier()
; template <class Epi, class Sched, bool ALIGN_EPI = false, bool SP2 = false>
; __device__ __forceinline__ void gemm_phase(PG8_LAS unsigned char* lds, const Gemm g, const Sched& S, const Epi& E, const int wid) {
;     ...
;         for (int t = 0; t < nt; t += 2) {
;             const bool last = (t == nt - 2);
;             const char* a1 = cA + (size_t)(t + 1) * kstep;
;             const char* a2 = last ? nA : cA + (size_t)(t + 2) * kstep; const char* b2 = last ? nB : cB + (size_t)(t + 2) * kstep;
;             const char* a3 = a2 + kstep; const char* b3 = b2 + kstep;
;             if (last && has_next) S.a_ready(nxt);
;             if constexpr (SP2) {
;             PG8_LDB(B0, 0, 0); PG8_LDB(B1, 0, 1); PG8_SCHED; PG8_LDA(At, 0, 0); PG8_STAGE(PG8_SA(1, 1), a1 + hstepA, voffA);
;             PG8_WAIT_V(8); PG8_WAIT_L(0); PG8_BAR; PG8_MMA(0, 0, At, B0); PG8_MMA(0, 1, At, B1); PG8_BAR; PG8_SCHED;
;             PG8_LDA(At, 0, 1); PG8_STAGE(PG8_SB(0, 0), b2, voffB); PG8_STAGE(PG8_SB(0, 1), b2 + hstepB, voffB); PG8_STAGE(PG8_SA(0, 0), a2, voffA);
;             PG8_WAIT_V(8); PG8_WAIT_L(0); PG8_BAR; PG8_MMA(1, 0, At, B0); PG8_MMA(1, 1, At, B1); PG8_BAR; PG8_SCHED;
;             PG8_LDB(B0, 1, 0); PG8_LDB(B1, 1, 1); PG8_SCHED; PG8_LDA(At, 1, 0); PG8_STAGE(PG8_SA(0, 1), a2 + hstepA, voffA);
;             PG8_WAIT_V(8); PG8_WAIT_L(0); PG8_BAR; PG8_MMA(0, 0, At, B0); PG8_MMA(0, 1, At, B1); PG8_BAR; PG8_SCHED;
;             PG8_LDA(At, 1, 1); PG8_STAGE(PG8_SB(1, 0), b3, voffB); PG8_STAGE(PG8_SB(1, 1), b3 + hstepB, voffB); PG8_STAGE(PG8_SA(1, 0), a3, voffA);
;             PG8_WAIT_V(8); PG8_WAIT_L(0); PG8_BAR; PG8_MMA(1, 0, At, B0); PG8_MMA(1, 1, At, B1); PG8_BAR; PG8_SCHED;
	s_add_i32 s28, s58, s33
	s_mov_b32 m0, s28
	ds_read_b128 v[188:191], v168 offset:49152
	ds_read_b128 v[192:195], v168 offset:50176
	ds_read_b128 v[196:199], v168 offset:51200
	ds_read_b128 v[200:203], v168 offset:52224
	ds_read_b128 v[204:207], v168 offset:53248
	ds_read_b128 v[208:211], v168 offset:54272
	ds_read_b128 v[212:215], v168 offset:55296
	ds_read_b128 v[216:219], v168 offset:56320
	global_load_lds_dwordx4 v132, s[98:99]
	s_add_i32 m0, s28, 0x2000
	s_add_u32 s26, s26, 0x40080
	s_addc_u32 s27, s27, 0
	s_add_i32 s28, s59, s33
	global_load_lds_dwordx4 v128, s[98:99]
	s_mov_b32 m0, s28
	s_nop 0
	global_load_lds_dwordx4 v132, s[26:27]
	s_add_i32 m0, s28, 0x2000
	s_nop 0
	global_load_lds_dwordx4 v128, s[26:27]
	s_mov_b32 m0, s40
	s_nop 0
	global_load_lds_dwordx4 v134, s[100:101]
	s_mov_b32 m0, s41
	s_nop 0
	global_load_lds_dwordx4 v130, s[100:101]
	s_waitcnt vmcnt(8) lgkmcnt(0)
	s_barrier
	s_setprio 1
	v_mfma_f32_16x16x32_bf16 v[60:63], v[148:151], v[188:191], v[60:63]
	v_mfma_f32_16x16x32_bf16 v[52:55], v[156:159], v[188:191], v[52:55]
	v_mfma_f32_16x16x32_bf16 v[44:47], v[148:151], v[196:199], v[44:47]
	v_mfma_f32_16x16x32_bf16 v[36:39], v[156:159], v[196:199], v[36:39]
	v_mfma_f32_16x16x32_bf16 v[28:31], v[148:151], v[204:207], v[28:31]
	v_mfma_f32_16x16x32_bf16 v[20:23], v[156:159], v[204:207], v[20:23]
	v_mfma_f32_16x16x32_bf16 v[12:15], v[148:151], v[212:215], v[12:15]
	v_mfma_f32_16x16x32_bf16 v[4:7], v[156:159], v[212:215], v[4:7]
	v_mfma_f32_16x16x32_bf16 v[60:63], v[152:155], v[192:195], v[60:63]
	v_mfma_f32_16x16x32_bf16 v[52:55], v[160:163], v[192:195], v[52:55]
	v_mfma_f32_16x16x32_bf16 v[44:47], v[152:155], v[200:203], v[44:47]
	v_mfma_f32_16x16x32_bf16 v[36:39], v[160:163], v[200:203], v[36:39]
	v_mfma_f32_16x16x32_bf16 v[28:31], v[152:155], v[208:211], v[28:31]
	v_mfma_f32_16x16x32_bf16 v[20:23], v[160:163], v[208:211], v[20:23]
	v_mfma_f32_16x16x32_bf16 v[12:15], v[152:155], v[216:219], v[12:15]
	v_mfma_f32_16x16x32_bf16 v[4:7], v[160:163], v[216:219], v[4:7]
	s_setprio 0
	s_setprio 1
	v_mfma_f32_16x16x32_bf16 v[56:59], v[172:175], v[188:191], v[56:59]
	v_mfma_f32_16x16x32_bf16 v[48:51], v[180:183], v[188:191], v[48:51]
	v_mfma_f32_16x16x32_bf16 v[40:43], v[172:175], v[196:199], v[40:43]
	v_mfma_f32_16x16x32_bf16 v[32:35], v[180:183], v[196:199], v[32:35]
	v_mfma_f32_16x16x32_bf16 v[24:27], v[172:175], v[204:207], v[24:27]
	v_mfma_f32_16x16x32_bf16 v[16:19], v[180:183], v[204:207], v[16:19]
	v_mfma_f32_16x16x32_bf16 v[8:11], v[172:175], v[212:215], v[8:11]
	v_mfma_f32_16x16x32_bf16 v[0:3], v[180:183], v[212:215], v[0:3]
	v_mfma_f32_16x16x32_bf16 v[56:59], v[176:179], v[192:195], v[56:59]
	v_mfma_f32_16x16x32_bf16 v[48:51], v[184:187], v[192:195], v[48:51]
	v_mfma_f32_16x16x32_bf16 v[40:43], v[176:179], v[200:203], v[40:43]
	v_mfma_f32_16x16x32_bf16 v[32:35], v[184:187], v[200:203], v[32:35]
	v_mfma_f32_16x16x32_bf16 v[24:27], v[176:179], v[208:211], v[24:27]
	v_mfma_f32_16x16x32_bf16 v[16:19], v[184:187], v[208:211], v[16:19]
	v_mfma_f32_16x16x32_bf16 v[8:11], v[176:179], v[216:219], v[8:11]
	v_mfma_f32_16x16x32_bf16 v[0:3], v[184:187], v[216:219], v[0:3]
	s_setprio 0
	s_barrier
	s_add_i32 s57, s57, 2
	s_add_u32 s24, s24, 0x100
	s_addc_u32 s25, s25, 0
	s_add_u32 s49, s49, 0x100
	s_addc_u32 s56, s56, 0
	s_cmp_gt_u32 s57, 13
.LBB0_2812:
	ds_read_b128 v[148:151], v166
	ds_read_b128 v[152:155], v166 offset:1024
	ds_read_b128 v[156:159], v166 offset:2048
	ds_read_b128 v[160:163], v166 offset:3072
	ds_read_b128 v[172:175], v167
	ds_read_b128 v[176:179], v167 offset:1024
	ds_read_b128 v[180:183], v167 offset:2048
	ds_read_b128 v[184:187], v167 offset:3072
	s_add_u32 s26, s24, 0xfffc0080
	s_addc_u32 s27, s25, -1
	s_cmp_eq_u32 s57, 12
	s_cselect_b32 s29, s17, s27
	s_cselect_b32 s28, s47, s26
	s_cselect_b32 s27, s15, s56
	s_cselect_b32 s26, s48, s49
	s_add_i32 m0, s36, 0xc000
	ds_read_b128 v[188:191], v168
	ds_read_b128 v[192:195], v168 offset:1024
	ds_read_b128 v[196:199], v168 offset:2048
	ds_read_b128 v[200:203], v168 offset:3072
	ds_read_b128 v[204:207], v168 offset:4096
	ds_read_b128 v[208:211], v168 offset:5120
	ds_read_b128 v[212:215], v168 offset:6144
	ds_read_b128 v[216:219], v168 offset:7168
	global_load_lds_dwordx4 v140, s[24:25]
	s_add_i32 m0, s36, 0xe000
	s_nop 0
	global_load_lds_dwordx4 v142, s[24:25]
	s_waitcnt vmcnt(8) lgkmcnt(0)
	s_barrier
	s_setprio 1
	v_mfma_f32_16x16x32_bf16 v[124:127], v[148:151], v[188:191], v[124:127]
	v_mfma_f32_16x16x32_bf16 v[116:119], v[156:159], v[188:191], v[116:119]
	v_mfma_f32_16x16x32_bf16 v[108:111], v[148:151], v[196:199], v[108:111]
	v_mfma_f32_16x16x32_bf16 v[100:103], v[156:159], v[196:199], v[100:103]
	v_mfma_f32_16x16x32_bf16 v[92:95], v[148:151], v[204:207], v[92:95]
	v_mfma_f32_16x16x32_bf16 v[84:87], v[156:159], v[204:207], v[84:87]
	v_mfma_f32_16x16x32_bf16 v[76:79], v[148:151], v[212:215], v[76:79]
	v_mfma_f32_16x16x32_bf16 v[68:71], v[156:159], v[212:215], v[68:71]
	v_mfma_f32_16x16x32_bf16 v[124:127], v[152:155], v[192:195], v[124:127]
	v_mfma_f32_16x16x32_bf16 v[116:119], v[160:163], v[192:195], v[116:119]
	v_mfma_f32_16x16x32_bf16 v[108:111], v[152:155], v[200:203], v[108:111]
	v_mfma_f32_16x16x32_bf16 v[100:103], v[160:163], v[200:203], v[100:103]
	v_mfma_f32_16x16x32_bf16 v[92:95], v[152:155], v[208:211], v[92:95]
	v_mfma_f32_16x16x32_bf16 v[84:87], v[160:163], v[208:211], v[84:87]
	v_mfma_f32_16x16x32_bf16 v[76:79], v[152:155], v[216:219], v[76:79]
	v_mfma_f32_16x16x32_bf16 v[68:71], v[160:163], v[216:219], v[68:71]
	s_setprio 0
	s_setprio 1
	v_mfma_f32_16x16x32_bf16 v[120:123], v[172:175], v[188:191], v[120:123]
	v_mfma_f32_16x16x32_bf16 v[112:115], v[180:183], v[188:191], v[112:115]
	v_mfma_f32_16x16x32_bf16 v[104:107], v[172:175], v[196:199], v[104:107]
	v_mfma_f32_16x16x32_bf16 v[96:99], v[180:183], v[196:199], v[96:99]
	v_mfma_f32_16x16x32_bf16 v[88:91], v[172:175], v[204:207], v[88:91]
	v_mfma_f32_16x16x32_bf16 v[80:83], v[180:183], v[204:207], v[80:83]
	v_mfma_f32_16x16x32_bf16 v[72:75], v[172:175], v[212:215], v[72:75]
	v_mfma_f32_16x16x32_bf16 v[64:67], v[180:183], v[212:215], v[64:67]
	v_mfma_f32_16x16x32_bf16 v[120:123], v[176:179], v[192:195], v[120:123]
	v_mfma_f32_16x16x32_bf16 v[112:115], v[184:187], v[192:195], v[112:115]
	v_mfma_f32_16x16x32_bf16 v[104:107], v[176:179], v[200:203], v[104:107]
	v_mfma_f32_16x16x32_bf16 v[96:99], v[184:187], v[200:203], v[96:99]
	v_mfma_f32_16x16x32_bf16 v[88:91], v[176:179], v[208:211], v[88:91]
	v_mfma_f32_16x16x32_bf16 v[80:83], v[184:187], v[208:211], v[80:83]
	v_mfma_f32_16x16x32_bf16 v[72:75], v[176:179], v[216:219], v[72:75]
	v_mfma_f32_16x16x32_bf16 v[64:67], v[184:187], v[216:219], v[64:67]
	s_setprio 0
	s_barrier
; #define PG8_STAGE(bufoff, gbase, voff) do { _Pragma("unroll") for (int _i = 0; _i < 2; ++_i) \
;         __builtin_amdgcn_global_load_lds((const unsigned*)((const char*)(gbase) + (voff)[_i]), (PG8_LAS unsigned*)(lds + (bufoff) + ldsw + _i * 8192), 16, 0, 0); } while (0)
; #define PG8_LDA(dst, b, h) do { _Pragma("unroll") for (int m = 0; m < 4; ++m) _Pragma("unroll") for (int k = 0; k < 2; ++k) dst[m][k] = *(const PG8_LAS bf16x8*)(lds + PG8_SA(b, h) + aoff + m * 2048 + k * 1024); } while (0)
; #define PG8_LDB(dst, b, h) do { _Pragma("unroll") for (int n = 0; n < 2; ++n) _Pragma("unroll") for (int k = 0; k < 2; ++k) dst[n][k] = *(const PG8_LAS bf16x8*)(lds + PG8_SB(b, h) + boff + n * 2048 + k * 1024); } while (0)
; #define PG8_MMA(ai, bj, At, Bt) do { __builtin_amdgcn_s_setprio(1); _Pragma("unroll") for (int m = 0; m < 4; ++m) _Pragma("unroll") for (int n = 0; n < 2; ++n) _Pragma("unroll") for (int k = 0; k < 2; ++k) \
;         acc[ai][bj][m][n] = __builtin_amdgcn_mfma_f32_16x16x32_bf16(Bt[n][k], At[m][k], acc[ai][bj][m][n], 0, 0, 0); __builtin_amdgcn_s_setprio(0); } while (0)
; #define PG8_BAR __builtin_amdgcn_s_barrier()
; template <class Epi, class Sched, bool ALIGN_EPI = false, bool SP2 = false>
; __device__ __forceinline__ void gemm_phase(PG8_LAS unsigned char* lds, const Gemm g, const Sched& S, const Epi& E, const int wid) {
;     ...
;             PG8_LDB(B0, 0, 0); PG8_LDB(B1, 0, 1); PG8_SCHED; PG8_LDA(At, 0, 0); PG8_STAGE(PG8_SA(1, 1), a1 + hstepA, voffA);
;             PG8_WAIT_V(8); PG8_WAIT_L(0); PG8_BAR; PG8_MMA(0, 0, At, B0); PG8_MMA(0, 1, At, B1); PG8_BAR; PG8_SCHED;
;             PG8_LDA(At, 0, 1); PG8_STAGE(PG8_SB(0, 0), b2, voffB); PG8_STAGE(PG8_SB(0, 1), b2 + hstepB, voffB); PG8_STAGE(PG8_SA(0, 0), a2, voffA);
;             PG8_WAIT_V(8); PG8_WAIT_L(0); PG8_BAR; PG8_MMA(1, 0, At, B0); PG8_MMA(1, 1, At, B1); PG8_BAR; PG8_SCHED;
;             PG8_LDB(B0, 1, 0); PG8_LDB(B1, 1, 1); PG8_SCHED; PG8_LDA(At, 1, 0); PG8_STAGE(PG8_SA(0, 1), a2 + hstepA, voffA);
;             PG8_WAIT_V(8); PG8_WAIT_L(0); PG8_BAR; PG8_MMA(0, 0, At, B0); PG8_MMA(0, 1, At, B1); PG8_BAR; PG8_SCHED;
;             PG8_LDA(At, 1, 1); PG8_STAGE(PG8_SB(1, 0), b3, voffB); PG8_STAGE(PG8_SB(1, 1), b3 + hstepB, voffB); PG8_STAGE(PG8_SA(1, 0), a3, voffA);
;             PG8_WAIT_V(8); PG8_WAIT_L(0); PG8_BAR; PG8_MMA(1, 0, At, B0); PG8_MMA(1, 1, At, B1); PG8_BAR; PG8_SCHED;
	s_add_i32 s58, s43, s33
	s_add_u32 s98, s26, 0x80
	s_addc_u32 s99, s27, 0
	s_mov_b32 m0, s58
	ds_read_b128 v[188:191], v168 offset:16384
	ds_read_b128 v[192:195], v168 offset:17408
	ds_read_b128 v[196:199], v168 offset:18432
	ds_read_b128 v[200:203], v168 offset:19456
	ds_read_b128 v[204:207], v168 offset:20480
	ds_read_b128 v[208:211], v168 offset:21504
	ds_read_b128 v[212:215], v168 offset:22528
	ds_read_b128 v[216:219], v168 offset:23552
	global_load_lds_dwordx4 v132, s[26:27]
	s_add_i32 m0, s58, 0x2000
	s_add_u32 s58, s26, 0x40000
	s_addc_u32 s59, s27, 0
	s_add_i32 s60, s44, s33
	global_load_lds_dwordx4 v128, s[26:27]
	s_mov_b32 m0, s60
	s_add_u32 s100, s28, 0x80
	s_addc_u32 s101, s29, 0
	global_load_lds_dwordx4 v132, s[58:59]
	s_add_i32 m0, s60, 0x2000
	s_nop 0
	global_load_lds_dwordx4 v128, s[58:59]
	s_mov_b32 m0, s36
	s_nop 0
	global_load_lds_dwordx4 v134, s[28:29]
	s_mov_b32 m0, s37
	s_nop 0
	global_load_lds_dwordx4 v130, s[28:29]
	s_waitcnt vmcnt(8) lgkmcnt(0)
	s_barrier
	s_setprio 1
	v_mfma_f32_16x16x32_bf16 v[60:63], v[148:151], v[188:191], v[60:63]
	v_mfma_f32_16x16x32_bf16 v[52:55], v[156:159], v[188:191], v[52:55]
	v_mfma_f32_16x16x32_bf16 v[44:47], v[148:151], v[196:199], v[44:47]
	v_mfma_f32_16x16x32_bf16 v[36:39], v[156:159], v[196:199], v[36:39]
	v_mfma_f32_16x16x32_bf16 v[28:31], v[148:151], v[204:207], v[28:31]
	v_mfma_f32_16x16x32_bf16 v[20:23], v[156:159], v[204:207], v[20:23]
	v_mfma_f32_16x16x32_bf16 v[12:15], v[148:151], v[212:215], v[12:15]
	v_mfma_f32_16x16x32_bf16 v[4:7], v[156:159], v[212:215], v[4:7]
	v_mfma_f32_16x16x32_bf16 v[60:63], v[152:155], v[192:195], v[60:63]
	v_mfma_f32_16x16x32_bf16 v[52:55], v[160:163], v[192:195], v[52:55]
	v_mfma_f32_16x16x32_bf16 v[44:47], v[152:155], v[200:203], v[44:47]
	v_mfma_f32_16x16x32_bf16 v[36:39], v[160:163], v[200:203], v[36:39]
	v_mfma_f32_16x16x32_bf16 v[28:31], v[152:155], v[208:211], v[28:31]
	v_mfma_f32_16x16x32_bf16 v[20:23], v[160:163], v[208:211], v[20:23]
	v_mfma_f32_16x16x32_bf16 v[12:15], v[152:155], v[216:219], v[12:15]
	v_mfma_f32_16x16x32_bf16 v[4:7], v[160:163], v[216:219], v[4:7]
	s_setprio 0
	s_setprio 1
	v_mfma_f32_16x16x32_bf16 v[56:59], v[172:175], v[188:191], v[56:59]
	v_mfma_f32_16x16x32_bf16 v[48:51], v[180:183], v[188:191], v[48:51]
	v_mfma_f32_16x16x32_bf16 v[40:43], v[172:175], v[196:199], v[40:43]
	v_mfma_f32_16x16x32_bf16 v[32:35], v[180:183], v[196:199], v[32:35]
	v_mfma_f32_16x16x32_bf16 v[24:27], v[172:175], v[204:207], v[24:27]
	v_mfma_f32_16x16x32_bf16 v[16:19], v[180:183], v[204:207], v[16:19]
	v_mfma_f32_16x16x32_bf16 v[8:11], v[172:175], v[212:215], v[8:11]
	v_mfma_f32_16x16x32_bf16 v[0:3], v[180:183], v[212:215], v[0:3]
	v_mfma_f32_16x16x32_bf16 v[56:59], v[176:179], v[192:195], v[56:59]
	v_mfma_f32_16x16x32_bf16 v[48:51], v[184:187], v[192:195], v[48:51]
	v_mfma_f32_16x16x32_bf16 v[40:43], v[176:179], v[200:203], v[40:43]
	v_mfma_f32_16x16x32_bf16 v[32:35], v[184:187], v[200:203], v[32:35]
	v_mfma_f32_16x16x32_bf16 v[24:27], v[176:179], v[208:211], v[24:27]
	v_mfma_f32_16x16x32_bf16 v[16:19], v[184:187], v[208:211], v[16:19]
	v_mfma_f32_16x16x32_bf16 v[8:11], v[176:179], v[216:219], v[8:11]
	v_mfma_f32_16x16x32_bf16 v[0:3], v[184:187], v[216:219], v[0:3]
	s_setprio 0
	s_barrier
	s_add_i32 s58, 0, 0x18000
	s_add_i32 s59, 0, 0x1c000
	ds_read_b128 v[148:151], v252
	ds_read_b128 v[152:155], v252 offset:1024
	ds_read_b128 v[156:159], v252 offset:2048
	ds_read_b128 v[160:163], v252 offset:3072
	ds_read_b128 v[172:175], v253
	ds_read_b128 v[176:179], v253 offset:1024
	ds_read_b128 v[180:183], v253 offset:2048
	ds_read_b128 v[184:187], v253 offset:3072
	s_add_u32 s28, s28, 0x40000
	s_addc_u32 s29, s29, 0
	s_mov_b32 m0, s38
	ds_read_b128 v[188:191], v168 offset:32768
	ds_read_b128 v[192:195], v168 offset:33792
	ds_read_b128 v[196:199], v168 offset:34816
	ds_read_b128 v[200:203], v168 offset:35840
	ds_read_b128 v[204:207], v168 offset:36864
	ds_read_b128 v[208:211], v168 offset:37888
	ds_read_b128 v[212:215], v168 offset:38912
	ds_read_b128 v[216:219], v168 offset:39936
	global_load_lds_dwordx4 v134, s[28:29]
	s_mov_b32 m0, s39
	s_nop 0
	global_load_lds_dwordx4 v130, s[28:29]
	s_waitcnt vmcnt(8) lgkmcnt(0)
	s_barrier
; #define PG8_STAGE(bufoff, gbase, voff) do { _Pragma("unroll") for (int _i = 0; _i < 2; ++_i) \
;         __builtin_amdgcn_global_load_lds((const unsigned*)((const char*)(gbase) + (voff)[_i]), (PG8_LAS unsigned*)(lds + (bufoff) + ldsw + _i * 8192), 16, 0, 0); } while (0)
; #define PG8_LDA(dst, b, h) do { _Pragma("unroll") for (int m = 0; m < 4; ++m) _Pragma("unroll") for (int k = 0; k < 2; ++k) dst[m][k] = *(const PG8_LAS bf16x8*)(lds + PG8_SA(b, h) + aoff + m * 2048 + k * 1024); } while (0)
; #define PG8_LDB(dst, b, h) do { _Pragma("unroll") for (int n = 0; n < 2; ++n) _Pragma("unroll") for (int k = 0; k < 2; ++k) dst[n][k] = *(const PG8_LAS bf16x8*)(lds + PG8_SB(b, h) + boff + n * 2048 + k * 1024); } while (0)
; #define PG8_WAIT_V(n) asm volatile("s_waitcnt vmcnt(" #n ")" ::: "memory")
; #define PG8_WAIT_L(n) asm volatile("s_waitcnt lgkmcnt(" #n ")" ::: "memory")
; #define PG8_BAR __builtin_amdgcn_s_barrier()
; template <class Epi, class Sched, bool ALIGN_EPI = false, bool SP2 = false>
; __device__ __forceinline__ void gemm_phase(PG8_LAS unsigned char* lds, const Gemm g, const Sched& S, const Epi& E, const int wid) {
;     ...
;             PG8_LDB(B0, 0, 0); PG8_LDB(B1, 0, 1); PG8_SCHED; PG8_LDA(At, 0, 0); PG8_STAGE(PG8_SA(1, 1), a1 + hstepA, voffA);
;             PG8_WAIT_V(8); PG8_WAIT_L(0); PG8_BAR; PG8_MMA(0, 0, At, B0); PG8_MMA(0, 1, At, B1); PG8_BAR; PG8_SCHED;
;             PG8_LDA(At, 0, 1); PG8_STAGE(PG8_SB(0, 0), b2, voffB); PG8_STAGE(PG8_SB(0, 1), b2 + hstepB, voffB); PG8_STAGE(PG8_SA(0, 0), a2, voffA);
;             PG8_WAIT_V(8); PG8_WAIT_L(0); PG8_BAR; PG8_MMA(1, 0, At, B0); PG8_MMA(1, 1, At, B1); PG8_BAR; PG8_SCHED;
;             PG8_LDB(B0, 1, 0); PG8_LDB(B1, 1, 1); PG8_SCHED; PG8_LDA(At, 1, 0); PG8_STAGE(PG8_SA(0, 1), a2 + hstepA, voffA);
;             PG8_WAIT_V(8); PG8_WAIT_L(0); PG8_BAR; PG8_MMA(0, 0, At, B0); PG8_MMA(0, 1, At, B1); PG8_BAR; PG8_SCHED;
;             PG8_LDA(At, 1, 1); PG8_STAGE(PG8_SB(1, 0), b3, voffB); PG8_STAGE(PG8_SB(1, 1), b3 + hstepB, voffB); PG8_STAGE(PG8_SA(1, 0), a3, voffA);
;             PG8_WAIT_V(8); PG8_WAIT_L(0); PG8_BAR; PG8_MMA(1, 0, At, B0); PG8_MMA(1, 1, At, B1); PG8_BAR; PG8_SCHED;
;     ...
;         if constexpr (ALIGN_EPI) { if (wr == 0) PG8_BAR; }
;         if constexpr (!Epi::AFTER_DRAIN) { E(acc, cur, wr, wc, fr, fq); S.done(cur); }
;         if (!has_next) break;
	s_setprio 1
	v_mfma_f32_16x16x32_bf16 v[124:127], v[148:151], v[188:191], v[124:127]
	v_mfma_f32_16x16x32_bf16 v[116:119], v[156:159], v[188:191], v[116:119]
	v_mfma_f32_16x16x32_bf16 v[108:111], v[148:151], v[196:199], v[108:111]
	v_mfma_f32_16x16x32_bf16 v[100:103], v[156:159], v[196:199], v[100:103]
	v_mfma_f32_16x16x32_bf16 v[92:95], v[148:151], v[204:207], v[92:95]
	v_mfma_f32_16x16x32_bf16 v[84:87], v[156:159], v[204:207], v[84:87]
	v_mfma_f32_16x16x32_bf16 v[76:79], v[148:151], v[212:215], v[76:79]
	v_mfma_f32_16x16x32_bf16 v[68:71], v[156:159], v[212:215], v[68:71]
	v_mfma_f32_16x16x32_bf16 v[124:127], v[152:155], v[192:195], v[124:127]
	v_mfma_f32_16x16x32_bf16 v[116:119], v[160:163], v[192:195], v[116:119]
	v_mfma_f32_16x16x32_bf16 v[108:111], v[152:155], v[200:203], v[108:111]
	v_mfma_f32_16x16x32_bf16 v[100:103], v[160:163], v[200:203], v[100:103]
	v_mfma_f32_16x16x32_bf16 v[92:95], v[152:155], v[208:211], v[92:95]
	v_mfma_f32_16x16x32_bf16 v[84:87], v[160:163], v[208:211], v[84:87]
	v_mfma_f32_16x16x32_bf16 v[76:79], v[152:155], v[216:219], v[76:79]
	v_mfma_f32_16x16x32_bf16 v[68:71], v[160:163], v[216:219], v[68:71]
	s_setprio 0
	s_setprio 1
	v_mfma_f32_16x16x32_bf16 v[120:123], v[172:175], v[188:191], v[120:123]
	v_mfma_f32_16x16x32_bf16 v[112:115], v[180:183], v[188:191], v[112:115]
	v_mfma_f32_16x16x32_bf16 v[104:107], v[172:175], v[196:199], v[104:107]
	v_mfma_f32_16x16x32_bf16 v[96:99], v[180:183], v[196:199], v[96:99]
	v_mfma_f32_16x16x32_bf16 v[88:91], v[172:175], v[204:207], v[88:91]
	v_mfma_f32_16x16x32_bf16 v[80:83], v[180:183], v[204:207], v[80:83]
	v_mfma_f32_16x16x32_bf16 v[72:75], v[172:175], v[212:215], v[72:75]
	v_mfma_f32_16x16x32_bf16 v[64:67], v[180:183], v[212:215], v[64:67]
	v_mfma_f32_16x16x32_bf16 v[120:123], v[176:179], v[192:195], v[120:123]
	v_mfma_f32_16x16x32_bf16 v[112:115], v[184:187], v[192:195], v[112:115]
	v_mfma_f32_16x16x32_bf16 v[104:107], v[176:179], v[200:203], v[104:107]
	v_mfma_f32_16x16x32_bf16 v[96:99], v[184:187], v[200:203], v[96:99]
	v_mfma_f32_16x16x32_bf16 v[88:91], v[176:179], v[208:211], v[88:91]
	v_mfma_f32_16x16x32_bf16 v[80:83], v[184:187], v[208:211], v[80:83]
	v_mfma_f32_16x16x32_bf16 v[72:75], v[176:179], v[216:219], v[72:75]
	v_mfma_f32_16x16x32_bf16 v[64:67], v[184:187], v[216:219], v[64:67]
	s_setprio 0
	s_barrier
	s_add_i32 s28, s58, s33
	s_mov_b32 m0, s28
	ds_read_b128 v[188:191], v168 offset:49152
	ds_read_b128 v[192:195], v168 offset:50176
	ds_read_b128 v[196:199], v168 offset:51200
	ds_read_b128 v[200:203], v168 offset:52224
	ds_read_b128 v[204:207], v168 offset:53248
	ds_read_b128 v[208:211], v168 offset:54272
	ds_read_b128 v[212:215], v168 offset:55296
	ds_read_b128 v[216:219], v168 offset:56320
	global_load_lds_dwordx4 v132, s[98:99]
	s_add_i32 m0, s28, 0x2000
	s_add_u32 s26, s26, 0x40080
	s_addc_u32 s27, s27, 0
	s_add_i32 s28, s59, s33
	global_load_lds_dwordx4 v128, s[98:99]
	s_mov_b32 m0, s28
	s_nop 0
	global_load_lds_dwordx4 v132, s[26:27]
	s_add_i32 m0, s28, 0x2000
	s_nop 0
	global_load_lds_dwordx4 v128, s[26:27]
	s_mov_b32 m0, s40
	s_nop 0
	global_load_lds_dwordx4 v134, s[100:101]
	s_mov_b32 m0, s41
	s_nop 0
	global_load_lds_dwordx4 v130, s[100:101]
	s_waitcnt vmcnt(8) lgkmcnt(0)
	s_barrier
	s_setprio 1
	v_mfma_f32_16x16x32_bf16 v[60:63], v[148:151], v[188:191], v[60:63]
	v_mfma_f32_16x16x32_bf16 v[52:55], v[156:159], v[188:191], v[52:55]
	v_mfma_f32_16x16x32_bf16 v[44:47], v[148:151], v[196:199], v[44:47]
	v_mfma_f32_16x16x32_bf16 v[36:39], v[156:159], v[196:199], v[36:39]
	v_mfma_f32_16x16x32_bf16 v[28:31], v[148:151], v[204:207], v[28:31]
	v_mfma_f32_16x16x32_bf16 v[20:23], v[156:159], v[204:207], v[20:23]
	v_mfma_f32_16x16x32_bf16 v[12:15], v[148:151], v[212:215], v[12:15]
	v_mfma_f32_16x16x32_bf16 v[4:7], v[156:159], v[212:215], v[4:7]
	v_mfma_f32_16x16x32_bf16 v[60:63], v[152:155], v[192:195], v[60:63]
	v_mfma_f32_16x16x32_bf16 v[52:55], v[160:163], v[192:195], v[52:55]
	v_mfma_f32_16x16x32_bf16 v[44:47], v[152:155], v[200:203], v[44:47]
	v_mfma_f32_16x16x32_bf16 v[36:39], v[160:163], v[200:203], v[36:39]
	v_mfma_f32_16x16x32_bf16 v[28:31], v[152:155], v[208:211], v[28:31]
	v_mfma_f32_16x16x32_bf16 v[20:23], v[160:163], v[208:211], v[20:23]
	v_mfma_f32_16x16x32_bf16 v[12:15], v[152:155], v[216:219], v[12:15]
	v_mfma_f32_16x16x32_bf16 v[4:7], v[160:163], v[216:219], v[4:7]
	s_setprio 0
	s_setprio 1
	v_mfma_f32_16x16x32_bf16 v[56:59], v[172:175], v[188:191], v[56:59]
	v_mfma_f32_16x16x32_bf16 v[48:51], v[180:183], v[188:191], v[48:51]
	v_mfma_f32_16x16x32_bf16 v[40:43], v[172:175], v[196:199], v[40:43]
	v_mfma_f32_16x16x32_bf16 v[32:35], v[180:183], v[196:199], v[32:35]
	v_mfma_f32_16x16x32_bf16 v[24:27], v[172:175], v[204:207], v[24:27]
	v_mfma_f32_16x16x32_bf16 v[16:19], v[180:183], v[204:207], v[16:19]
	v_mfma_f32_16x16x32_bf16 v[8:11], v[172:175], v[212:215], v[8:11]
	v_mfma_f32_16x16x32_bf16 v[0:3], v[180:183], v[212:215], v[0:3]
	v_mfma_f32_16x16x32_bf16 v[56:59], v[176:179], v[192:195], v[56:59]
	v_mfma_f32_16x16x32_bf16 v[48:51], v[184:187], v[192:195], v[48:51]
	v_mfma_f32_16x16x32_bf16 v[40:43], v[176:179], v[200:203], v[40:43]
	v_mfma_f32_16x16x32_bf16 v[32:35], v[184:187], v[200:203], v[32:35]
	v_mfma_f32_16x16x32_bf16 v[24:27], v[176:179], v[208:211], v[24:27]
	v_mfma_f32_16x16x32_bf16 v[16:19], v[184:187], v[208:211], v[16:19]
	v_mfma_f32_16x16x32_bf16 v[8:11], v[176:179], v[216:219], v[8:11]
	v_mfma_f32_16x16x32_bf16 v[0:3], v[184:187], v[216:219], v[0:3]
	s_setprio 0
	s_barrier
	s_add_i32 s57, s57, 2
	s_add_u32 s24, s24, 0x100
	s_addc_u32 s25, s25, 0
	s_add_u32 s49, s49, 0x100
	s_addc_u32 s56, s56, 0
	s_cmp_gt_u32 s57, 13
	s_cbranch_scc0 .LBB0_2812
	s_and_b64 vcc, exec, s[12:13]
	s_cbranch_vccz .LBB0_2815
	s_barrier

; #define PG8_STAGE(bufoff, gbase, voff) do { _Pragma("unroll") for (int _i = 0; _i < 2; ++_i) \
;         __builtin_amdgcn_global_load_lds((const unsigned*)((const char*)(gbase) + (voff)[_i]), (PG8_LAS unsigned*)(lds + (bufoff) + ldsw + _i * 8192), 16, 0, 0); } while (0)
; #define PG8_LDA(dst, b, h) do { _Pragma("unroll") for (int m = 0; m < 4; ++m) _Pragma("unroll") for (int k = 0; k < 2; ++k) dst[m][k] = *(const PG8_LAS bf16x8*)(lds + PG8_SA(b, h) + aoff + m * 2048 + k * 1024); } while (0)
; #define PG8_LDB(dst, b, h) do { _Pragma("unroll") for (int n = 0; n < 2; ++n) _Pragma("unroll") for (int k = 0; k < 2; ++k) dst[n][k] = *(const PG8_LAS bf16x8*)(lds + PG8_SB(b, h) + boff + n * 2048 + k * 1024); } while (0)
; #define PG8_MMA(ai, bj, At, Bt) do { __builtin_amdgcn_s_setprio(1); _Pragma("unroll") for (int m = 0; m < 4; ++m) _Pragma("unroll") for (int n = 0; n < 2; ++n) _Pragma("unroll") for (int k = 0; k < 2; ++k) \
;         acc[ai][bj][m][n] = __builtin_amdgcn_mfma_f32_16x16x32_bf16(Bt[n][k], At[m][k], acc[ai][bj][m][n], 0, 0, 0); __builtin_amdgcn_s_setprio(0); } while (0)
; #define PG8_WAIT_V(n) asm volatile("s_waitcnt vmcnt(" #n ")" ::: "memory")
; #define PG8_WAIT_L(n) asm volatile("s_waitcnt lgkmcnt(" #n ")" ::: "memory")
; #define PG8_BAR __builtin_amdgcn_s_barrier()
; #define PG8_SCHED __builtin_amdgcn_sched_barrier(0)
; template <class Epi, class Sched, bool ALIGN_EPI = false, bool SP2 = false>
; __device__ __forceinline__ void gemm_phase(PG8_LAS unsigned char* lds, const Gemm g, const Sched& S, const Epi& E, const int wid) {
;     ...
;     f32x4 acc[2][2][4][2];
; #pragma unroll
;     for (int a = 0; a < 2; ++a)
; #pragma unroll
;         for (int b = 0; b < 2; ++b)
; #pragma unroll
;             for (int m = 0; m < 4; ++m)
; #pragma unroll
;                 for (int n = 0; n < 2; ++n) acc[a][b][m][n] = (f32x4){0.f, 0.f, 0.f, 0.f};
;     ...
;             PG8_LDB(B0, 0, 0); PG8_LDB(B1, 0, 1); PG8_SCHED; PG8_LDA(At, 0, 0); PG8_STAGE(PG8_SA(1, 1), a1 + hstepA, voffA);
;             PG8_WAIT_V(8); PG8_WAIT_L(0); PG8_BAR; PG8_MMA(0, 0, At, B0); PG8_MMA(0, 1, At, B1); PG8_BAR; PG8_SCHED;
;             PG8_LDA(At, 0, 1); PG8_STAGE(PG8_SB(0, 0), b2, voffB); PG8_STAGE(PG8_SB(0, 1), b2 + hstepB, voffB); PG8_STAGE(PG8_SA(0, 0), a2, voffA);
;             PG8_WAIT_V(8); PG8_WAIT_L(0); PG8_BAR; PG8_MMA(1, 0, At, B0); PG8_MMA(1, 1, At, B1); PG8_BAR; PG8_SCHED;
.LBB0_2896:
	s_add_u32 s56, s24, 0x100
	s_addc_u32 s57, s25, 0
	s_mov_b32 s58, -2
	s_waitcnt lgkmcnt(0)
	v_add_u32_e32 v252, 0x18000, v189
	v_add_u32_e32 v253, 0x1c000, v189
	ds_read_b128 v[128:131], v190
	ds_read_b128 v[132:135], v190 offset:1024
	ds_read_b128 v[136:139], v190 offset:2048
	ds_read_b128 v[140:143], v190 offset:3072
	ds_read_b128 v[144:147], v191
	ds_read_b128 v[148:151], v191 offset:1024
	ds_read_b128 v[172:175], v191 offset:2048
	ds_read_b128 v[176:179], v191 offset:3072
	s_add_u32 s24, s22, 0x100
	s_addc_u32 s25, s23, 0
	s_cmp_eq_u32 s58, 40
	s_cselect_b32 s29, s7, s25
	s_cselect_b32 s28, s6, s24
	s_cselect_b32 s27, s21, s57
	s_cselect_b32 s26, s20, s56
	s_add_i32 m0, s34, 0xc000
	ds_read_b128 v[180:183], v192
	ds_read_b128 v[184:187], v192 offset:1024
	ds_read_b128 v[194:197], v192 offset:2048
	ds_read_b128 v[198:201], v192 offset:3072
	ds_read_b128 v[202:205], v192 offset:4096
	ds_read_b128 v[206:209], v192 offset:5120
	ds_read_b128 v[210:213], v192 offset:6144
	ds_read_b128 v[214:217], v192 offset:7168
	global_load_lds_dwordx4 v164, s[22:23]
	s_add_i32 m0, s34, 0xe000
	s_nop 0
	global_load_lds_dwordx4 v166, s[22:23]
	s_waitcnt vmcnt(8) lgkmcnt(0)
	s_barrier
	s_setprio 1
	v_mfma_f32_16x16x32_bf16 v[124:127], v[128:131], v[180:183], 0
	v_mfma_f32_16x16x32_bf16 v[120:123], v[136:139], v[180:183], 0
	v_mfma_f32_16x16x32_bf16 v[108:111], v[128:131], v[194:197], 0
	v_mfma_f32_16x16x32_bf16 v[104:107], v[136:139], v[194:197], 0
	v_mfma_f32_16x16x32_bf16 v[92:95], v[128:131], v[202:205], 0
	v_mfma_f32_16x16x32_bf16 v[88:91], v[136:139], v[202:205], 0
	v_mfma_f32_16x16x32_bf16 v[76:79], v[128:131], v[210:213], 0
	v_mfma_f32_16x16x32_bf16 v[72:75], v[136:139], v[210:213], 0
	v_mfma_f32_16x16x32_bf16 v[124:127], v[132:135], v[184:187], v[124:127]
	v_mfma_f32_16x16x32_bf16 v[120:123], v[140:143], v[184:187], v[120:123]
	v_mfma_f32_16x16x32_bf16 v[108:111], v[132:135], v[198:201], v[108:111]
	v_mfma_f32_16x16x32_bf16 v[104:107], v[140:143], v[198:201], v[104:107]
	v_mfma_f32_16x16x32_bf16 v[92:95], v[132:135], v[206:209], v[92:95]
	v_mfma_f32_16x16x32_bf16 v[88:91], v[140:143], v[206:209], v[88:91]
	v_mfma_f32_16x16x32_bf16 v[76:79], v[132:135], v[214:217], v[76:79]
	v_mfma_f32_16x16x32_bf16 v[72:75], v[140:143], v[214:217], v[72:75]
	s_setprio 0
	s_setprio 1
	v_mfma_f32_16x16x32_bf16 v[116:119], v[144:147], v[180:183], 0
	v_mfma_f32_16x16x32_bf16 v[112:115], v[172:175], v[180:183], 0
	v_mfma_f32_16x16x32_bf16 v[100:103], v[144:147], v[194:197], 0
	v_mfma_f32_16x16x32_bf16 v[96:99], v[172:175], v[194:197], 0
	v_mfma_f32_16x16x32_bf16 v[84:87], v[144:147], v[202:205], 0
	v_mfma_f32_16x16x32_bf16 v[80:83], v[172:175], v[202:205], 0
	v_mfma_f32_16x16x32_bf16 v[68:71], v[144:147], v[210:213], 0
	v_mfma_f32_16x16x32_bf16 v[64:67], v[172:175], v[210:213], 0
	v_mfma_f32_16x16x32_bf16 v[116:119], v[148:151], v[184:187], v[116:119]
	v_mfma_f32_16x16x32_bf16 v[112:115], v[176:179], v[184:187], v[112:115]
	v_mfma_f32_16x16x32_bf16 v[100:103], v[148:151], v[198:201], v[100:103]
	v_mfma_f32_16x16x32_bf16 v[96:99], v[176:179], v[198:201], v[96:99]
	v_mfma_f32_16x16x32_bf16 v[84:87], v[148:151], v[206:209], v[84:87]
	v_mfma_f32_16x16x32_bf16 v[80:83], v[176:179], v[206:209], v[80:83]
	v_mfma_f32_16x16x32_bf16 v[68:71], v[148:151], v[214:217], v[68:71]
	v_mfma_f32_16x16x32_bf16 v[64:67], v[176:179], v[214:217], v[64:67]
	s_setprio 0
	s_barrier
	s_add_i32 s22, s43, s33
	s_add_u32 s98, s26, 0x80
	s_addc_u32 s99, s27, 0
	s_mov_b32 m0, s22
	ds_read_b128 v[180:183], v192 offset:16384
	ds_read_b128 v[184:187], v192 offset:17408
	ds_read_b128 v[194:197], v192 offset:18432
	ds_read_b128 v[198:201], v192 offset:19456
	ds_read_b128 v[202:205], v192 offset:20480
	ds_read_b128 v[206:209], v192 offset:21504
	ds_read_b128 v[210:213], v192 offset:22528
	ds_read_b128 v[214:217], v192 offset:23552
	global_load_lds_dwordx4 v154, s[26:27]
	s_add_i32 m0, s22, 0x2000
	s_add_u32 s22, s26, 0xb0000
	s_addc_u32 s23, s27, 0
	s_add_i32 s59, s44, s33
	global_load_lds_dwordx4 v158, s[26:27]
	s_mov_b32 m0, s59
	s_add_u32 s100, s28, 0x80
	s_addc_u32 s101, s29, 0
	global_load_lds_dwordx4 v154, s[22:23]
	s_add_i32 m0, s59, 0x2000
	s_nop 0
	global_load_lds_dwordx4 v158, s[22:23]
	s_mov_b32 m0, s34
	s_nop 0
	global_load_lds_dwordx4 v152, s[28:29]
	s_mov_b32 m0, s35
	s_nop 0
	global_load_lds_dwordx4 v156, s[28:29]
	s_waitcnt vmcnt(8) lgkmcnt(0)
	s_barrier
	s_setprio 1
	v_mfma_f32_16x16x32_bf16 v[60:63], v[128:131], v[180:183], 0
	v_mfma_f32_16x16x32_bf16 v[56:59], v[136:139], v[180:183], 0
	v_mfma_f32_16x16x32_bf16 v[44:47], v[128:131], v[194:197], 0
	v_mfma_f32_16x16x32_bf16 v[40:43], v[136:139], v[194:197], 0
	v_mfma_f32_16x16x32_bf16 v[28:31], v[128:131], v[202:205], 0
	v_mfma_f32_16x16x32_bf16 v[24:27], v[136:139], v[202:205], 0
	v_mfma_f32_16x16x32_bf16 v[12:15], v[128:131], v[210:213], 0
	v_mfma_f32_16x16x32_bf16 v[8:11], v[136:139], v[210:213], 0
	v_mfma_f32_16x16x32_bf16 v[60:63], v[132:135], v[184:187], v[60:63]
	v_mfma_f32_16x16x32_bf16 v[56:59], v[140:143], v[184:187], v[56:59]
	v_mfma_f32_16x16x32_bf16 v[44:47], v[132:135], v[198:201], v[44:47]
	v_mfma_f32_16x16x32_bf16 v[40:43], v[140:143], v[198:201], v[40:43]
	v_mfma_f32_16x16x32_bf16 v[28:31], v[132:135], v[206:209], v[28:31]
	v_mfma_f32_16x16x32_bf16 v[24:27], v[140:143], v[206:209], v[24:27]
	v_mfma_f32_16x16x32_bf16 v[12:15], v[132:135], v[214:217], v[12:15]
	v_mfma_f32_16x16x32_bf16 v[8:11], v[140:143], v[214:217], v[8:11]
	s_setprio 0
	s_setprio 1
	v_mfma_f32_16x16x32_bf16 v[52:55], v[144:147], v[180:183], 0
	v_mfma_f32_16x16x32_bf16 v[48:51], v[172:175], v[180:183], 0
	v_mfma_f32_16x16x32_bf16 v[36:39], v[144:147], v[194:197], 0
	v_mfma_f32_16x16x32_bf16 v[32:35], v[172:175], v[194:197], 0
	v_mfma_f32_16x16x32_bf16 v[20:23], v[144:147], v[202:205], 0
	v_mfma_f32_16x16x32_bf16 v[16:19], v[172:175], v[202:205], 0
	v_mfma_f32_16x16x32_bf16 v[4:7], v[144:147], v[210:213], 0
	v_mfma_f32_16x16x32_bf16 v[0:3], v[172:175], v[210:213], 0
	v_mfma_f32_16x16x32_bf16 v[52:55], v[148:151], v[184:187], v[52:55]
	v_mfma_f32_16x16x32_bf16 v[48:51], v[176:179], v[184:187], v[48:51]
	v_mfma_f32_16x16x32_bf16 v[36:39], v[148:151], v[198:201], v[36:39]
	v_mfma_f32_16x16x32_bf16 v[32:35], v[176:179], v[198:201], v[32:35]
	v_mfma_f32_16x16x32_bf16 v[20:23], v[148:151], v[206:209], v[20:23]
	v_mfma_f32_16x16x32_bf16 v[16:19], v[176:179], v[206:209], v[16:19]
	v_mfma_f32_16x16x32_bf16 v[4:7], v[148:151], v[214:217], v[4:7]
	v_mfma_f32_16x16x32_bf16 v[0:3], v[176:179], v[214:217], v[0:3]
	s_setprio 0
	s_barrier
; #define PG8_STAGE(bufoff, gbase, voff) do { _Pragma("unroll") for (int _i = 0; _i < 2; ++_i) \
;         __builtin_amdgcn_global_load_lds((const unsigned*)((const char*)(gbase) + (voff)[_i]), (PG8_LAS unsigned*)(lds + (bufoff) + ldsw + _i * 8192), 16, 0, 0); } while (0)
; #define PG8_LDA(dst, b, h) do { _Pragma("unroll") for (int m = 0; m < 4; ++m) _Pragma("unroll") for (int k = 0; k < 2; ++k) dst[m][k] = *(const PG8_LAS bf16x8*)(lds + PG8_SA(b, h) + aoff + m * 2048 + k * 1024); } while (0)
; #define PG8_LDB(dst, b, h) do { _Pragma("unroll") for (int n = 0; n < 2; ++n) _Pragma("unroll") for (int k = 0; k < 2; ++k) dst[n][k] = *(const PG8_LAS bf16x8*)(lds + PG8_SB(b, h) + boff + n * 2048 + k * 1024); } while (0)
; #define PG8_MMA(ai, bj, At, Bt) do { __builtin_amdgcn_s_setprio(1); _Pragma("unroll") for (int m = 0; m < 4; ++m) _Pragma("unroll") for (int n = 0; n < 2; ++n) _Pragma("unroll") for (int k = 0; k < 2; ++k) \
;         acc[ai][bj][m][n] = __builtin_amdgcn_mfma_f32_16x16x32_bf16(Bt[n][k], At[m][k], acc[ai][bj][m][n], 0, 0, 0); __builtin_amdgcn_s_setprio(0); } while (0)
; #define PG8_WAIT_V(n) asm volatile("s_waitcnt vmcnt(" #n ")" ::: "memory")
; #define PG8_WAIT_L(n) asm volatile("s_waitcnt lgkmcnt(" #n ")" ::: "memory")
; #define PG8_BAR __builtin_amdgcn_s_barrier()
; #define PG8_SCHED __builtin_amdgcn_sched_barrier(0)
; template <class Epi, class Sched, bool ALIGN_EPI = false, bool SP2 = false>
; __device__ __forceinline__ void gemm_phase(PG8_LAS unsigned char* lds, const Gemm g, const Sched& S, const Epi& E, const int wid) {
;     ...
;             PG8_LDB(B0, 1, 0); PG8_LDB(B1, 1, 1); PG8_SCHED; PG8_LDA(At, 1, 0); PG8_STAGE(PG8_SA(0, 1), a2 + hstepA, voffA);
;             PG8_WAIT_V(8); PG8_WAIT_L(0); PG8_BAR; PG8_MMA(0, 0, At, B0); PG8_MMA(0, 1, At, B1); PG8_BAR; PG8_SCHED;
;             PG8_LDA(At, 1, 1); PG8_STAGE(PG8_SB(1, 0), b3, voffB); PG8_STAGE(PG8_SB(1, 1), b3 + hstepB, voffB); PG8_STAGE(PG8_SA(1, 0), a3, voffA);
;             PG8_WAIT_V(8); PG8_WAIT_L(0); PG8_BAR; PG8_MMA(1, 0, At, B0); PG8_MMA(1, 1, At, B1); PG8_BAR; PG8_SCHED;
	s_add_i32 s59, 0, 0x18000
	s_add_i32 s60, 0, 0x1c000
	ds_read_b128 v[128:131], v252
	ds_read_b128 v[132:135], v252 offset:1024
	ds_read_b128 v[136:139], v252 offset:2048
	ds_read_b128 v[140:143], v252 offset:3072
	ds_read_b128 v[144:147], v253
	ds_read_b128 v[148:151], v253 offset:1024
	ds_read_b128 v[172:175], v253 offset:2048
	ds_read_b128 v[176:179], v253 offset:3072
	s_add_u32 s22, s28, 0xb0000
	s_addc_u32 s23, s29, 0
	s_mov_b32 m0, s36
	ds_read_b128 v[180:183], v192 offset:32768
	ds_read_b128 v[184:187], v192 offset:33792
	ds_read_b128 v[194:197], v192 offset:34816
	ds_read_b128 v[198:201], v192 offset:35840
	ds_read_b128 v[202:205], v192 offset:36864
	ds_read_b128 v[206:209], v192 offset:37888
	ds_read_b128 v[210:213], v192 offset:38912
	ds_read_b128 v[214:217], v192 offset:39936
	global_load_lds_dwordx4 v152, s[22:23]
	s_mov_b32 m0, s37
	s_nop 0
	global_load_lds_dwordx4 v156, s[22:23]
	s_waitcnt vmcnt(8) lgkmcnt(0)
	s_barrier
	s_setprio 1
	v_mfma_f32_16x16x32_bf16 v[124:127], v[128:131], v[180:183], v[124:127]
	v_mfma_f32_16x16x32_bf16 v[120:123], v[136:139], v[180:183], v[120:123]
	v_mfma_f32_16x16x32_bf16 v[108:111], v[128:131], v[194:197], v[108:111]
	v_mfma_f32_16x16x32_bf16 v[104:107], v[136:139], v[194:197], v[104:107]
	v_mfma_f32_16x16x32_bf16 v[92:95], v[128:131], v[202:205], v[92:95]
	v_mfma_f32_16x16x32_bf16 v[88:91], v[136:139], v[202:205], v[88:91]
	v_mfma_f32_16x16x32_bf16 v[76:79], v[128:131], v[210:213], v[76:79]
	v_mfma_f32_16x16x32_bf16 v[72:75], v[136:139], v[210:213], v[72:75]
	v_mfma_f32_16x16x32_bf16 v[124:127], v[132:135], v[184:187], v[124:127]
	v_mfma_f32_16x16x32_bf16 v[120:123], v[140:143], v[184:187], v[120:123]
	v_mfma_f32_16x16x32_bf16 v[108:111], v[132:135], v[198:201], v[108:111]
	v_mfma_f32_16x16x32_bf16 v[104:107], v[140:143], v[198:201], v[104:107]
	v_mfma_f32_16x16x32_bf16 v[92:95], v[132:135], v[206:209], v[92:95]
	v_mfma_f32_16x16x32_bf16 v[88:91], v[140:143], v[206:209], v[88:91]
	v_mfma_f32_16x16x32_bf16 v[76:79], v[132:135], v[214:217], v[76:79]
	v_mfma_f32_16x16x32_bf16 v[72:75], v[140:143], v[214:217], v[72:75]
	s_setprio 0
	s_setprio 1
	v_mfma_f32_16x16x32_bf16 v[116:119], v[144:147], v[180:183], v[116:119]
	v_mfma_f32_16x16x32_bf16 v[112:115], v[172:175], v[180:183], v[112:115]
	v_mfma_f32_16x16x32_bf16 v[100:103], v[144:147], v[194:197], v[100:103]
	v_mfma_f32_16x16x32_bf16 v[96:99], v[172:175], v[194:197], v[96:99]
	v_mfma_f32_16x16x32_bf16 v[84:87], v[144:147], v[202:205], v[84:87]
	v_mfma_f32_16x16x32_bf16 v[80:83], v[172:175], v[202:205], v[80:83]
	v_mfma_f32_16x16x32_bf16 v[68:71], v[144:147], v[210:213], v[68:71]
	v_mfma_f32_16x16x32_bf16 v[64:67], v[172:175], v[210:213], v[64:67]
	v_mfma_f32_16x16x32_bf16 v[116:119], v[148:151], v[184:187], v[116:119]
	v_mfma_f32_16x16x32_bf16 v[112:115], v[176:179], v[184:187], v[112:115]
	v_mfma_f32_16x16x32_bf16 v[100:103], v[148:151], v[198:201], v[100:103]
	v_mfma_f32_16x16x32_bf16 v[96:99], v[176:179], v[198:201], v[96:99]
	v_mfma_f32_16x16x32_bf16 v[84:87], v[148:151], v[206:209], v[84:87]
	v_mfma_f32_16x16x32_bf16 v[80:83], v[176:179], v[206:209], v[80:83]
	v_mfma_f32_16x16x32_bf16 v[68:71], v[148:151], v[214:217], v[68:71]
	v_mfma_f32_16x16x32_bf16 v[64:67], v[176:179], v[214:217], v[64:67]
	s_setprio 0
	s_barrier
	s_add_i32 s22, s59, s33
	s_mov_b32 m0, s22
	ds_read_b128 v[180:183], v192 offset:49152
	ds_read_b128 v[184:187], v192 offset:50176
	ds_read_b128 v[194:197], v192 offset:51200
	ds_read_b128 v[198:201], v192 offset:52224
	ds_read_b128 v[202:205], v192 offset:53248
	ds_read_b128 v[206:209], v192 offset:54272
	ds_read_b128 v[210:213], v192 offset:55296
	ds_read_b128 v[214:217], v192 offset:56320
	global_load_lds_dwordx4 v154, s[98:99]
	s_add_i32 m0, s22, 0x2000
	s_add_u32 s22, s26, 0xb0080
	s_addc_u32 s23, s27, 0
	s_add_i32 s26, s60, s33
	global_load_lds_dwordx4 v158, s[98:99]
	s_mov_b32 m0, s26
	s_nop 0
	global_load_lds_dwordx4 v154, s[22:23]
	s_add_i32 m0, s26, 0x2000
	s_nop 0
	global_load_lds_dwordx4 v158, s[22:23]
	s_mov_b32 m0, s39
	s_nop 0
	global_load_lds_dwordx4 v152, s[100:101]
	s_mov_b32 m0, s40
	s_nop 0
	global_load_lds_dwordx4 v156, s[100:101]
	s_waitcnt vmcnt(8) lgkmcnt(0)
	s_barrier
	s_setprio 1
	v_mfma_f32_16x16x32_bf16 v[60:63], v[128:131], v[180:183], v[60:63]
	v_mfma_f32_16x16x32_bf16 v[56:59], v[136:139], v[180:183], v[56:59]
	v_mfma_f32_16x16x32_bf16 v[44:47], v[128:131], v[194:197], v[44:47]
	v_mfma_f32_16x16x32_bf16 v[40:43], v[136:139], v[194:197], v[40:43]
	v_mfma_f32_16x16x32_bf16 v[28:31], v[128:131], v[202:205], v[28:31]
	v_mfma_f32_16x16x32_bf16 v[24:27], v[136:139], v[202:205], v[24:27]
	v_mfma_f32_16x16x32_bf16 v[12:15], v[128:131], v[210:213], v[12:15]
	v_mfma_f32_16x16x32_bf16 v[8:11], v[136:139], v[210:213], v[8:11]
	v_mfma_f32_16x16x32_bf16 v[60:63], v[132:135], v[184:187], v[60:63]
	v_mfma_f32_16x16x32_bf16 v[56:59], v[140:143], v[184:187], v[56:59]
	v_mfma_f32_16x16x32_bf16 v[44:47], v[132:135], v[198:201], v[44:47]
	v_mfma_f32_16x16x32_bf16 v[40:43], v[140:143], v[198:201], v[40:43]
	v_mfma_f32_16x16x32_bf16 v[28:31], v[132:135], v[206:209], v[28:31]
	v_mfma_f32_16x16x32_bf16 v[24:27], v[140:143], v[206:209], v[24:27]
	v_mfma_f32_16x16x32_bf16 v[12:15], v[132:135], v[214:217], v[12:15]
	v_mfma_f32_16x16x32_bf16 v[8:11], v[140:143], v[214:217], v[8:11]
	s_setprio 0
	s_setprio 1
	v_mfma_f32_16x16x32_bf16 v[52:55], v[144:147], v[180:183], v[52:55]
	v_mfma_f32_16x16x32_bf16 v[48:51], v[172:175], v[180:183], v[48:51]
	v_mfma_f32_16x16x32_bf16 v[36:39], v[144:147], v[194:197], v[36:39]
	v_mfma_f32_16x16x32_bf16 v[32:35], v[172:175], v[194:197], v[32:35]
	v_mfma_f32_16x16x32_bf16 v[20:23], v[144:147], v[202:205], v[20:23]
	v_mfma_f32_16x16x32_bf16 v[16:19], v[172:175], v[202:205], v[16:19]
	v_mfma_f32_16x16x32_bf16 v[4:7], v[144:147], v[210:213], v[4:7]
	v_mfma_f32_16x16x32_bf16 v[0:3], v[172:175], v[210:213], v[0:3]
	v_mfma_f32_16x16x32_bf16 v[52:55], v[148:151], v[184:187], v[52:55]
	v_mfma_f32_16x16x32_bf16 v[48:51], v[176:179], v[184:187], v[48:51]
	v_mfma_f32_16x16x32_bf16 v[36:39], v[148:151], v[198:201], v[36:39]
	v_mfma_f32_16x16x32_bf16 v[32:35], v[176:179], v[198:201], v[32:35]
	v_mfma_f32_16x16x32_bf16 v[20:23], v[148:151], v[206:209], v[20:23]
	v_mfma_f32_16x16x32_bf16 v[16:19], v[176:179], v[206:209], v[16:19]
	v_mfma_f32_16x16x32_bf16 v[4:7], v[148:151], v[214:217], v[4:7]
	v_mfma_f32_16x16x32_bf16 v[0:3], v[176:179], v[214:217], v[0:3]
	s_setprio 0
	s_barrier
	s_add_i32 s58, s58, 2
	s_add_u32 s56, s56, 0x100
	s_addc_u32 s57, s57, 0
	s_cmp_gt_u32 s58, 41
	s_mov_b64 s[22:23], s[24:25]
; #define PG8_STAGE(bufoff, gbase, voff) do { _Pragma("unroll") for (int _i = 0; _i < 2; ++_i) \
;         __builtin_amdgcn_global_load_lds((const unsigned*)((const char*)(gbase) + (voff)[_i]), (PG8_LAS unsigned*)(lds + (bufoff) + ldsw + _i * 8192), 16, 0, 0); } while (0)
; #define PG8_LDA(dst, b, h) do { _Pragma("unroll") for (int m = 0; m < 4; ++m) _Pragma("unroll") for (int k = 0; k < 2; ++k) dst[m][k] = *(const PG8_LAS bf16x8*)(lds + PG8_SA(b, h) + aoff + m * 2048 + k * 1024); } while (0)
; #define PG8_LDB(dst, b, h) do { _Pragma("unroll") for (int n = 0; n < 2; ++n) _Pragma("unroll") for (int k = 0; k < 2; ++k) dst[n][k] = *(const PG8_LAS bf16x8*)(lds + PG8_SB(b, h) + boff + n * 2048 + k * 1024); } while (0)
; #define PG8_MMA(ai, bj, At, Bt) do { __builtin_amdgcn_s_setprio(1); _Pragma("unroll") for (int m = 0; m < 4; ++m) _Pragma("unroll") for (int n = 0; n < 2; ++n) _Pragma("unroll") for (int k = 0; k < 2; ++k) \
;         acc[ai][bj][m][n] = __builtin_amdgcn_mfma_f32_16x16x32_bf16(Bt[n][k], At[m][k], acc[ai][bj][m][n], 0, 0, 0); __builtin_amdgcn_s_setprio(0); } while (0)
; #define PG8_WAIT_V(n) asm volatile("s_waitcnt vmcnt(" #n ")" ::: "memory")
; #define PG8_WAIT_L(n) asm volatile("s_waitcnt lgkmcnt(" #n ")" ::: "memory")
; #define PG8_BAR __builtin_amdgcn_s_barrier()
; #define PG8_SCHED __builtin_amdgcn_sched_barrier(0)
; template <class Epi, class Sched, bool ALIGN_EPI = false, bool SP2 = false>
; __device__ __forceinline__ void gemm_phase(PG8_LAS unsigned char* lds, const Gemm g, const Sched& S, const Epi& E, const int wid) {
;     ...
;             PG8_LDB(B0, 0, 0); PG8_LDB(B1, 0, 1); PG8_SCHED; PG8_LDA(At, 0, 0); PG8_STAGE(PG8_SA(1, 1), a1 + hstepA, voffA);
;             PG8_WAIT_V(8); PG8_WAIT_L(0); PG8_BAR; PG8_MMA(0, 0, At, B0); PG8_MMA(0, 1, At, B1); PG8_BAR; PG8_SCHED;
;             PG8_LDA(At, 0, 1); PG8_STAGE(PG8_SB(0, 0), b2, voffB); PG8_STAGE(PG8_SB(0, 1), b2 + hstepB, voffB); PG8_STAGE(PG8_SA(0, 0), a2, voffA);
;             PG8_WAIT_V(8); PG8_WAIT_L(0); PG8_BAR; PG8_MMA(1, 0, At, B0); PG8_MMA(1, 1, At, B1); PG8_BAR; PG8_SCHED;
.LBB0_2897:
	ds_read_b128 v[128:131], v190
	ds_read_b128 v[132:135], v190 offset:1024
	ds_read_b128 v[136:139], v190 offset:2048
	ds_read_b128 v[140:143], v190 offset:3072
	ds_read_b128 v[144:147], v191
	ds_read_b128 v[148:151], v191 offset:1024
	ds_read_b128 v[172:175], v191 offset:2048
	ds_read_b128 v[176:179], v191 offset:3072
	s_add_u32 s24, s22, 0x100
	s_addc_u32 s25, s23, 0
	s_cmp_eq_u32 s58, 40
	s_cselect_b32 s29, s7, s25
	s_cselect_b32 s28, s6, s24
	s_cselect_b32 s27, s21, s57
	s_cselect_b32 s26, s20, s56
	s_add_i32 m0, s34, 0xc000
	ds_read_b128 v[180:183], v192
	ds_read_b128 v[184:187], v192 offset:1024
	ds_read_b128 v[194:197], v192 offset:2048
	ds_read_b128 v[198:201], v192 offset:3072
	ds_read_b128 v[202:205], v192 offset:4096
	ds_read_b128 v[206:209], v192 offset:5120
	ds_read_b128 v[210:213], v192 offset:6144
	ds_read_b128 v[214:217], v192 offset:7168
	global_load_lds_dwordx4 v164, s[22:23]
	s_add_i32 m0, s34, 0xe000
	s_nop 0
	global_load_lds_dwordx4 v166, s[22:23]
	s_waitcnt vmcnt(8) lgkmcnt(0)
	s_barrier
	s_setprio 1
	v_mfma_f32_16x16x32_bf16 v[124:127], v[128:131], v[180:183], v[124:127]
	v_mfma_f32_16x16x32_bf16 v[120:123], v[136:139], v[180:183], v[120:123]
	v_mfma_f32_16x16x32_bf16 v[108:111], v[128:131], v[194:197], v[108:111]
	v_mfma_f32_16x16x32_bf16 v[104:107], v[136:139], v[194:197], v[104:107]
	v_mfma_f32_16x16x32_bf16 v[92:95], v[128:131], v[202:205], v[92:95]
	v_mfma_f32_16x16x32_bf16 v[88:91], v[136:139], v[202:205], v[88:91]
	v_mfma_f32_16x16x32_bf16 v[76:79], v[128:131], v[210:213], v[76:79]
	v_mfma_f32_16x16x32_bf16 v[72:75], v[136:139], v[210:213], v[72:75]
	v_mfma_f32_16x16x32_bf16 v[124:127], v[132:135], v[184:187], v[124:127]
	v_mfma_f32_16x16x32_bf16 v[120:123], v[140:143], v[184:187], v[120:123]
	v_mfma_f32_16x16x32_bf16 v[108:111], v[132:135], v[198:201], v[108:111]
	v_mfma_f32_16x16x32_bf16 v[104:107], v[140:143], v[198:201], v[104:107]
	v_mfma_f32_16x16x32_bf16 v[92:95], v[132:135], v[206:209], v[92:95]
	v_mfma_f32_16x16x32_bf16 v[88:91], v[140:143], v[206:209], v[88:91]
	v_mfma_f32_16x16x32_bf16 v[76:79], v[132:135], v[214:217], v[76:79]
	v_mfma_f32_16x16x32_bf16 v[72:75], v[140:143], v[214:217], v[72:75]
	s_setprio 0
	s_setprio 1
	v_mfma_f32_16x16x32_bf16 v[116:119], v[144:147], v[180:183], v[116:119]
	v_mfma_f32_16x16x32_bf16 v[112:115], v[172:175], v[180:183], v[112:115]
	v_mfma_f32_16x16x32_bf16 v[100:103], v[144:147], v[194:197], v[100:103]
	v_mfma_f32_16x16x32_bf16 v[96:99], v[172:175], v[194:197], v[96:99]
	v_mfma_f32_16x16x32_bf16 v[84:87], v[144:147], v[202:205], v[84:87]
	v_mfma_f32_16x16x32_bf16 v[80:83], v[172:175], v[202:205], v[80:83]
	v_mfma_f32_16x16x32_bf16 v[68:71], v[144:147], v[210:213], v[68:71]
	v_mfma_f32_16x16x32_bf16 v[64:67], v[172:175], v[210:213], v[64:67]
	v_mfma_f32_16x16x32_bf16 v[116:119], v[148:151], v[184:187], v[116:119]
	v_mfma_f32_16x16x32_bf16 v[112:115], v[176:179], v[184:187], v[112:115]
	v_mfma_f32_16x16x32_bf16 v[100:103], v[148:151], v[198:201], v[100:103]
	v_mfma_f32_16x16x32_bf16 v[96:99], v[176:179], v[198:201], v[96:99]
	v_mfma_f32_16x16x32_bf16 v[84:87], v[148:151], v[206:209], v[84:87]
	v_mfma_f32_16x16x32_bf16 v[80:83], v[176:179], v[206:209], v[80:83]
	v_mfma_f32_16x16x32_bf16 v[68:71], v[148:151], v[214:217], v[68:71]
	v_mfma_f32_16x16x32_bf16 v[64:67], v[176:179], v[214:217], v[64:67]
	s_setprio 0
	s_barrier
	s_add_i32 s22, s43, s33
	s_add_u32 s98, s26, 0x80
	s_addc_u32 s99, s27, 0
	s_mov_b32 m0, s22
	ds_read_b128 v[180:183], v192 offset:16384
	ds_read_b128 v[184:187], v192 offset:17408
	ds_read_b128 v[194:197], v192 offset:18432
	ds_read_b128 v[198:201], v192 offset:19456
	ds_read_b128 v[202:205], v192 offset:20480
	ds_read_b128 v[206:209], v192 offset:21504
	ds_read_b128 v[210:213], v192 offset:22528
	ds_read_b128 v[214:217], v192 offset:23552
	global_load_lds_dwordx4 v154, s[26:27]
	s_add_i32 m0, s22, 0x2000
	s_add_u32 s22, s26, 0xb0000
	s_addc_u32 s23, s27, 0
	s_add_i32 s59, s44, s33
	global_load_lds_dwordx4 v158, s[26:27]
	s_mov_b32 m0, s59
	s_add_u32 s100, s28, 0x80
	s_addc_u32 s101, s29, 0
	global_load_lds_dwordx4 v154, s[22:23]
	s_add_i32 m0, s59, 0x2000
	s_nop 0
	global_load_lds_dwordx4 v158, s[22:23]
	s_mov_b32 m0, s34
	s_nop 0
	global_load_lds_dwordx4 v152, s[28:29]
	s_mov_b32 m0, s35
	s_nop 0
	global_load_lds_dwordx4 v156, s[28:29]
	s_waitcnt vmcnt(8) lgkmcnt(0)
	s_barrier
	s_setprio 1
	v_mfma_f32_16x16x32_bf16 v[60:63], v[128:131], v[180:183], v[60:63]
	v_mfma_f32_16x16x32_bf16 v[56:59], v[136:139], v[180:183], v[56:59]
	v_mfma_f32_16x16x32_bf16 v[44:47], v[128:131], v[194:197], v[44:47]
	v_mfma_f32_16x16x32_bf16 v[40:43], v[136:139], v[194:197], v[40:43]
	v_mfma_f32_16x16x32_bf16 v[28:31], v[128:131], v[202:205], v[28:31]
	v_mfma_f32_16x16x32_bf16 v[24:27], v[136:139], v[202:205], v[24:27]
	v_mfma_f32_16x16x32_bf16 v[12:15], v[128:131], v[210:213], v[12:15]
	v_mfma_f32_16x16x32_bf16 v[8:11], v[136:139], v[210:213], v[8:11]
	v_mfma_f32_16x16x32_bf16 v[60:63], v[132:135], v[184:187], v[60:63]
	v_mfma_f32_16x16x32_bf16 v[56:59], v[140:143], v[184:187], v[56:59]
	v_mfma_f32_16x16x32_bf16 v[44:47], v[132:135], v[198:201], v[44:47]
	v_mfma_f32_16x16x32_bf16 v[40:43], v[140:143], v[198:201], v[40:43]
	v_mfma_f32_16x16x32_bf16 v[28:31], v[132:135], v[206:209], v[28:31]
	v_mfma_f32_16x16x32_bf16 v[24:27], v[140:143], v[206:209], v[24:27]
	v_mfma_f32_16x16x32_bf16 v[12:15], v[132:135], v[214:217], v[12:15]
	v_mfma_f32_16x16x32_bf16 v[8:11], v[140:143], v[214:217], v[8:11]
	s_setprio 0
	s_setprio 1
	v_mfma_f32_16x16x32_bf16 v[52:55], v[144:147], v[180:183], v[52:55]
	v_mfma_f32_16x16x32_bf16 v[48:51], v[172:175], v[180:183], v[48:51]
	v_mfma_f32_16x16x32_bf16 v[36:39], v[144:147], v[194:197], v[36:39]
	v_mfma_f32_16x16x32_bf16 v[32:35], v[172:175], v[194:197], v[32:35]
	v_mfma_f32_16x16x32_bf16 v[20:23], v[144:147], v[202:205], v[20:23]
	v_mfma_f32_16x16x32_bf16 v[16:19], v[172:175], v[202:205], v[16:19]
	v_mfma_f32_16x16x32_bf16 v[4:7], v[144:147], v[210:213], v[4:7]
	v_mfma_f32_16x16x32_bf16 v[0:3], v[172:175], v[210:213], v[0:3]
	v_mfma_f32_16x16x32_bf16 v[52:55], v[148:151], v[184:187], v[52:55]
	v_mfma_f32_16x16x32_bf16 v[48:51], v[176:179], v[184:187], v[48:51]
	v_mfma_f32_16x16x32_bf16 v[36:39], v[148:151], v[198:201], v[36:39]
	v_mfma_f32_16x16x32_bf16 v[32:35], v[176:179], v[198:201], v[32:35]
	v_mfma_f32_16x16x32_bf16 v[20:23], v[148:151], v[206:209], v[20:23]
	v_mfma_f32_16x16x32_bf16 v[16:19], v[176:179], v[206:209], v[16:19]
	v_mfma_f32_16x16x32_bf16 v[4:7], v[148:151], v[214:217], v[4:7]
	v_mfma_f32_16x16x32_bf16 v[0:3], v[176:179], v[214:217], v[0:3]
	s_setprio 0
	s_barrier
; #define PG8_STAGE(bufoff, gbase, voff) do { _Pragma("unroll") for (int _i = 0; _i < 2; ++_i) \
;         __builtin_amdgcn_global_load_lds((const unsigned*)((const char*)(gbase) + (voff)[_i]), (PG8_LAS unsigned*)(lds + (bufoff) + ldsw + _i * 8192), 16, 0, 0); } while (0)
; #define PG8_LDA(dst, b, h) do { _Pragma("unroll") for (int m = 0; m < 4; ++m) _Pragma("unroll") for (int k = 0; k < 2; ++k) dst[m][k] = *(const PG8_LAS bf16x8*)(lds + PG8_SA(b, h) + aoff + m * 2048 + k * 1024); } while (0)
; #define PG8_LDB(dst, b, h) do { _Pragma("unroll") for (int n = 0; n < 2; ++n) _Pragma("unroll") for (int k = 0; k < 2; ++k) dst[n][k] = *(const PG8_LAS bf16x8*)(lds + PG8_SB(b, h) + boff + n * 2048 + k * 1024); } while (0)
; #define PG8_MMA(ai, bj, At, Bt) do { __builtin_amdgcn_s_setprio(1); _Pragma("unroll") for (int m = 0; m < 4; ++m) _Pragma("unroll") for (int n = 0; n < 2; ++n) _Pragma("unroll") for (int k = 0; k < 2; ++k) \
;         acc[ai][bj][m][n] = __builtin_amdgcn_mfma_f32_16x16x32_bf16(Bt[n][k], At[m][k], acc[ai][bj][m][n], 0, 0, 0); __builtin_amdgcn_s_setprio(0); } while (0)
; #define PG8_WAIT_V(n) asm volatile("s_waitcnt vmcnt(" #n ")" ::: "memory")
; #define PG8_WAIT_L(n) asm volatile("s_waitcnt lgkmcnt(" #n ")" ::: "memory")
; #define PG8_BAR __builtin_amdgcn_s_barrier()
; #define PG8_SCHED __builtin_amdgcn_sched_barrier(0)
; template <class Epi, class Sched, bool ALIGN_EPI = false, bool SP2 = false>
; __device__ __forceinline__ void gemm_phase(PG8_LAS unsigned char* lds, const Gemm g, const Sched& S, const Epi& E, const int wid) {
;     ...
;             PG8_LDB(B0, 1, 0); PG8_LDB(B1, 1, 1); PG8_SCHED; PG8_LDA(At, 1, 0); PG8_STAGE(PG8_SA(0, 1), a2 + hstepA, voffA);
;             PG8_WAIT_V(8); PG8_WAIT_L(0); PG8_BAR; PG8_MMA(0, 0, At, B0); PG8_MMA(0, 1, At, B1); PG8_BAR; PG8_SCHED;
;             PG8_LDA(At, 1, 1); PG8_STAGE(PG8_SB(1, 0), b3, voffB); PG8_STAGE(PG8_SB(1, 1), b3 + hstepB, voffB); PG8_STAGE(PG8_SA(1, 0), a3, voffA);
;             PG8_WAIT_V(8); PG8_WAIT_L(0); PG8_BAR; PG8_MMA(1, 0, At, B0); PG8_MMA(1, 1, At, B1); PG8_BAR; PG8_SCHED;
;     ...
;         if constexpr (ALIGN_EPI) { if (wr == 0) PG8_BAR; }
;         if constexpr (!Epi::AFTER_DRAIN) { E(acc, cur, wr, wc, fr, fq); S.done(cur); }
;         if (!has_next) break;
	s_add_i32 s59, 0, 0x18000
	s_add_i32 s60, 0, 0x1c000
	ds_read_b128 v[128:131], v252
	ds_read_b128 v[132:135], v252 offset:1024
	ds_read_b128 v[136:139], v252 offset:2048
	ds_read_b128 v[140:143], v252 offset:3072
	ds_read_b128 v[144:147], v253
	ds_read_b128 v[148:151], v253 offset:1024
	ds_read_b128 v[172:175], v253 offset:2048
	ds_read_b128 v[176:179], v253 offset:3072
	s_add_u32 s22, s28, 0xb0000
	s_addc_u32 s23, s29, 0
	s_mov_b32 m0, s36
	ds_read_b128 v[180:183], v192 offset:32768
	ds_read_b128 v[184:187], v192 offset:33792
	ds_read_b128 v[194:197], v192 offset:34816
	ds_read_b128 v[198:201], v192 offset:35840
	ds_read_b128 v[202:205], v192 offset:36864
	ds_read_b128 v[206:209], v192 offset:37888
	ds_read_b128 v[210:213], v192 offset:38912
	ds_read_b128 v[214:217], v192 offset:39936
	global_load_lds_dwordx4 v152, s[22:23]
	s_mov_b32 m0, s37
	s_nop 0
	global_load_lds_dwordx4 v156, s[22:23]
	s_waitcnt vmcnt(8) lgkmcnt(0)
	s_barrier
	s_setprio 1
	v_mfma_f32_16x16x32_bf16 v[124:127], v[128:131], v[180:183], v[124:127]
	v_mfma_f32_16x16x32_bf16 v[120:123], v[136:139], v[180:183], v[120:123]
	v_mfma_f32_16x16x32_bf16 v[108:111], v[128:131], v[194:197], v[108:111]
	v_mfma_f32_16x16x32_bf16 v[104:107], v[136:139], v[194:197], v[104:107]
	v_mfma_f32_16x16x32_bf16 v[92:95], v[128:131], v[202:205], v[92:95]
	v_mfma_f32_16x16x32_bf16 v[88:91], v[136:139], v[202:205], v[88:91]
	v_mfma_f32_16x16x32_bf16 v[76:79], v[128:131], v[210:213], v[76:79]
	v_mfma_f32_16x16x32_bf16 v[72:75], v[136:139], v[210:213], v[72:75]
	v_mfma_f32_16x16x32_bf16 v[124:127], v[132:135], v[184:187], v[124:127]
	v_mfma_f32_16x16x32_bf16 v[120:123], v[140:143], v[184:187], v[120:123]
	v_mfma_f32_16x16x32_bf16 v[108:111], v[132:135], v[198:201], v[108:111]
	v_mfma_f32_16x16x32_bf16 v[104:107], v[140:143], v[198:201], v[104:107]
	v_mfma_f32_16x16x32_bf16 v[92:95], v[132:135], v[206:209], v[92:95]
	v_mfma_f32_16x16x32_bf16 v[88:91], v[140:143], v[206:209], v[88:91]
	v_mfma_f32_16x16x32_bf16 v[76:79], v[132:135], v[214:217], v[76:79]
	v_mfma_f32_16x16x32_bf16 v[72:75], v[140:143], v[214:217], v[72:75]
	s_setprio 0
	s_setprio 1
	v_mfma_f32_16x16x32_bf16 v[116:119], v[144:147], v[180:183], v[116:119]
	v_mfma_f32_16x16x32_bf16 v[112:115], v[172:175], v[180:183], v[112:115]
	v_mfma_f32_16x16x32_bf16 v[100:103], v[144:147], v[194:197], v[100:103]
	v_mfma_f32_16x16x32_bf16 v[96:99], v[172:175], v[194:197], v[96:99]
	v_mfma_f32_16x16x32_bf16 v[84:87], v[144:147], v[202:205], v[84:87]
	v_mfma_f32_16x16x32_bf16 v[80:83], v[172:175], v[202:205], v[80:83]
	v_mfma_f32_16x16x32_bf16 v[68:71], v[144:147], v[210:213], v[68:71]
	v_mfma_f32_16x16x32_bf16 v[64:67], v[172:175], v[210:213], v[64:67]
	v_mfma_f32_16x16x32_bf16 v[116:119], v[148:151], v[184:187], v[116:119]
	v_mfma_f32_16x16x32_bf16 v[112:115], v[176:179], v[184:187], v[112:115]
	v_mfma_f32_16x16x32_bf16 v[100:103], v[148:151], v[198:201], v[100:103]
	v_mfma_f32_16x16x32_bf16 v[96:99], v[176:179], v[198:201], v[96:99]
	v_mfma_f32_16x16x32_bf16 v[84:87], v[148:151], v[206:209], v[84:87]
	v_mfma_f32_16x16x32_bf16 v[80:83], v[176:179], v[206:209], v[80:83]
	v_mfma_f32_16x16x32_bf16 v[68:71], v[148:151], v[214:217], v[68:71]
	v_mfma_f32_16x16x32_bf16 v[64:67], v[176:179], v[214:217], v[64:67]
	s_setprio 0
	s_barrier
	s_add_i32 s22, s59, s33
	s_mov_b32 m0, s22
	ds_read_b128 v[180:183], v192 offset:49152
	ds_read_b128 v[184:187], v192 offset:50176
	ds_read_b128 v[194:197], v192 offset:51200
	ds_read_b128 v[198:201], v192 offset:52224
	ds_read_b128 v[202:205], v192 offset:53248
	ds_read_b128 v[206:209], v192 offset:54272
	ds_read_b128 v[210:213], v192 offset:55296
	ds_read_b128 v[214:217], v192 offset:56320
	global_load_lds_dwordx4 v154, s[98:99]
	s_add_i32 m0, s22, 0x2000
	s_add_u32 s22, s26, 0xb0080
	s_addc_u32 s23, s27, 0
	s_add_i32 s26, s60, s33
	global_load_lds_dwordx4 v158, s[98:99]
	s_mov_b32 m0, s26
	s_nop 0
	global_load_lds_dwordx4 v154, s[22:23]
	s_add_i32 m0, s26, 0x2000
	s_nop 0
	global_load_lds_dwordx4 v158, s[22:23]
	s_mov_b32 m0, s39
	s_nop 0
	global_load_lds_dwordx4 v152, s[100:101]
	s_mov_b32 m0, s40
	s_nop 0
	global_load_lds_dwordx4 v156, s[100:101]
	s_waitcnt vmcnt(8) lgkmcnt(0)
	s_barrier
	s_setprio 1
	v_mfma_f32_16x16x32_bf16 v[60:63], v[128:131], v[180:183], v[60:63]
	v_mfma_f32_16x16x32_bf16 v[56:59], v[136:139], v[180:183], v[56:59]
	v_mfma_f32_16x16x32_bf16 v[44:47], v[128:131], v[194:197], v[44:47]
	v_mfma_f32_16x16x32_bf16 v[40:43], v[136:139], v[194:197], v[40:43]
	v_mfma_f32_16x16x32_bf16 v[28:31], v[128:131], v[202:205], v[28:31]
	v_mfma_f32_16x16x32_bf16 v[24:27], v[136:139], v[202:205], v[24:27]
	v_mfma_f32_16x16x32_bf16 v[12:15], v[128:131], v[210:213], v[12:15]
	v_mfma_f32_16x16x32_bf16 v[8:11], v[136:139], v[210:213], v[8:11]
	v_mfma_f32_16x16x32_bf16 v[60:63], v[132:135], v[184:187], v[60:63]
	v_mfma_f32_16x16x32_bf16 v[56:59], v[140:143], v[184:187], v[56:59]
	v_mfma_f32_16x16x32_bf16 v[44:47], v[132:135], v[198:201], v[44:47]
	v_mfma_f32_16x16x32_bf16 v[40:43], v[140:143], v[198:201], v[40:43]
	v_mfma_f32_16x16x32_bf16 v[28:31], v[132:135], v[206:209], v[28:31]
	v_mfma_f32_16x16x32_bf16 v[24:27], v[140:143], v[206:209], v[24:27]
	v_mfma_f32_16x16x32_bf16 v[12:15], v[132:135], v[214:217], v[12:15]
	v_mfma_f32_16x16x32_bf16 v[8:11], v[140:143], v[214:217], v[8:11]
	s_setprio 0
	s_setprio 1
	v_mfma_f32_16x16x32_bf16 v[52:55], v[144:147], v[180:183], v[52:55]
	v_mfma_f32_16x16x32_bf16 v[48:51], v[172:175], v[180:183], v[48:51]
	v_mfma_f32_16x16x32_bf16 v[36:39], v[144:147], v[194:197], v[36:39]
	v_mfma_f32_16x16x32_bf16 v[32:35], v[172:175], v[194:197], v[32:35]
	v_mfma_f32_16x16x32_bf16 v[20:23], v[144:147], v[202:205], v[20:23]
	v_mfma_f32_16x16x32_bf16 v[16:19], v[172:175], v[202:205], v[16:19]
	v_mfma_f32_16x16x32_bf16 v[4:7], v[144:147], v[210:213], v[4:7]
	v_mfma_f32_16x16x32_bf16 v[0:3], v[172:175], v[210:213], v[0:3]
	v_mfma_f32_16x16x32_bf16 v[52:55], v[148:151], v[184:187], v[52:55]
	v_mfma_f32_16x16x32_bf16 v[48:51], v[176:179], v[184:187], v[48:51]
	v_mfma_f32_16x16x32_bf16 v[36:39], v[148:151], v[198:201], v[36:39]
	v_mfma_f32_16x16x32_bf16 v[32:35], v[176:179], v[198:201], v[32:35]
	v_mfma_f32_16x16x32_bf16 v[20:23], v[148:151], v[206:209], v[20:23]
	v_mfma_f32_16x16x32_bf16 v[16:19], v[176:179], v[206:209], v[16:19]
	v_mfma_f32_16x16x32_bf16 v[4:7], v[148:151], v[214:217], v[4:7]
	v_mfma_f32_16x16x32_bf16 v[0:3], v[176:179], v[214:217], v[0:3]
	s_setprio 0
	s_barrier
	s_add_i32 s58, s58, 2
	s_add_u32 s56, s56, 0x100
	s_addc_u32 s57, s57, 0
	s_cmp_gt_u32 s58, 41
	s_mov_b64 s[22:23], s[24:25]
	s_cbranch_scc0 .LBB0_2897
	s_and_b64 vcc, exec, s[18:19]
	s_cbranch_vccz .LBB0_2900
	s_barrier
